# v28: v26 + static priority raise (s_setprio 1) for the lagging wave half in GEMM calls and attention tile loops, per-segment s_setprio toggles removed
# baseline (speedup 1.0000x reference)
.LBB0_238:
	v_lshl_add_u32 v0, v2, 4, s73
	v_ashrrev_i32_e32 v3, 31, v0
	v_lshrrev_b32_e32 v3, 22, v3
	v_add_u32_e32 v3, v0, v3
	v_ashrrev_i32_e32 v3, 10, v3
	v_mul_i32_i24_e32 v4, 0x400, v3
	v_sub_u32_e32 v4, v0, v4
	v_lshrrev_b32_e32 v5, 4, v4
	v_bitop3_b32 v4, v5, v4, 32 bitop3:0x6c
	v_ashrrev_i32_e32 v6, 31, v4
	v_lshrrev_b32_e32 v6, 26, v6
	v_add_u32_e32 v6, v4, v6
	v_lshrrev_b32_e32 v7, 6, v6
	v_and_b32_e32 v6, 0xc0, v6
	v_lshlrev_b32_e32 v5, 3, v3
	v_lshlrev_b32_e32 v3, 5, v3
	v_sub_u32_e32 v4, v4, v6
	v_and_b32_e32 v5, 0x1ffff0, v5
	v_and_b32_e32 v3, 32, v3
	v_ashrrev_i16_sdwa v4, v203, sext(v4) dst_sel:DWORD dst_unused:UNUSED_PAD src0_sel:DWORD src1_sel:BYTE_0
	v_add_u32_sdwa v3, v3, sext(v4) dst_sel:DWORD dst_unused:UNUSED_PAD src0_sel:DWORD src1_sel:WORD_0
	v_add_lshl_u32 v4, v7, v5, 11
	v_add_u32_e32 v0, 0x2000, v0
	v_lshl_add_u32 v136, v3, 1, v4
	v_ashrrev_i32_e32 v3, 31, v0
	v_lshrrev_b32_e32 v3, 22, v3
	v_add_u32_e32 v3, v0, v3
	v_ashrrev_i32_e32 v3, 10, v3
	v_mul_i32_i24_e32 v4, 0x400, v3
	v_sub_u32_e32 v0, v0, v4
	v_lshrrev_b32_e32 v4, 4, v0
	s_add_i32 s1, s1, s4
	v_bitop3_b32 v0, v4, v0, 32 bitop3:0x6c
	s_ashr_i32 s4, s1, 31
	v_ashrrev_i32_e32 v5, 31, v0
	s_lshr_b32 s4, s4, 26
	v_lshrrev_b32_e32 v5, 26, v5
	s_add_i32 s4, s1, s4
	v_add_u32_e32 v5, v0, v5
	s_ashr_i32 s5, s4, 6
	v_lshrrev_b32_e32 v6, 6, v5
	v_and_b32_e32 v5, 0xffc0, v5
	s_lshl_b32 s5, s5, 3
	v_sub_u32_e32 v0, v0, v5
	s_sub_i32 s6, 64, s5
	v_lshrrev_b16_e32 v5, 7, v0
	s_min_i32 s6, s6, 8
	v_and_b32_e32 v5, 1, v5
	s_abs_i32 s7, s6
	v_add_u16_e32 v0, v0, v5
	v_cvt_f32_u32_e32 v5, s7
	v_lshlrev_b32_e32 v4, 3, v3
	v_lshlrev_b32_e32 v3, 5, v3
	v_and_b32_e32 v4, 0x1ffff0, v4
	v_and_b32_e32 v3, 32, v3
	v_ashrrev_i16_sdwa v0, v203, sext(v0) dst_sel:DWORD dst_unused:UNUSED_PAD src0_sel:DWORD src1_sel:BYTE_0
	v_add_u32_sdwa v0, v3, sext(v0) dst_sel:DWORD dst_unused:UNUSED_PAD src0_sel:DWORD src1_sel:WORD_0
	v_add_lshl_u32 v3, v6, v4, 11
	v_lshl_add_u32 v137, v0, 1, v3
	v_rcp_iflag_f32_e32 v0, v5
	s_sub_i32 s9, 0, s7
	s_andn2_b32 s4, s4, 63
	s_sub_i32 s1, s1, s4
	v_mul_f32_e32 v0, 0x4f7ffffe, v0
	v_cvt_u32_f32_e32 v0, v0
	s_abs_i32 s8, s1
	s_xor_b32 s4, s1, s6
	s_ashr_i32 s4, s4, 31
	v_readfirstlane_b32 s10, v0
	s_mul_i32 s9, s9, s10
	s_mul_hi_u32 s9, s10, s9
	s_add_i32 s10, s10, s9
	s_mul_hi_u32 s9, s8, s10
	s_mul_i32 s10, s9, s7
	s_sub_i32 s8, s8, s10
	s_add_i32 s10, s9, 1
	s_sub_i32 s11, s8, s7
	s_cmp_ge_u32 s8, s7
	s_cselect_b32 s9, s10, s9
	s_cselect_b32 s8, s11, s8
	s_add_i32 s10, s9, 1
	s_cmp_ge_u32 s8, s7
	s_cselect_b32 s7, s10, s9
	s_xor_b32 s7, s7, s4
	s_sub_i32 s4, s7, s4
	s_mul_i32 s6, s4, s6
	s_sub_i32 s1, s1, s6
	s_add_i32 s12, s5, s1
	s_cmp_lt_i32 s4, 4
	s_cselect_b32 s1, 8, 16
	s_ashr_i32 s13, s12, 31
	s_add_i32 s24, s1, s4
	s_lshl_b64 s[4:5], s[12:13], 19
	v_readlane_b32 s1, v252, 22
	s_add_u32 s26, s1, s4
	v_readlane_b32 s1, v252, 24
	s_addc_u32 s27, s1, s5
	s_ashr_i32 s25, s24, 31
	s_lshl_b64 s[4:5], s[24:25], 19
	v_readlane_b32 s1, v252, 26
	s_add_u32 s46, s1, s4
	v_readlane_b32 s1, v252, 28
	s_addc_u32 s47, s1, s5
	v_mov_b32_e32 v0, v136
	s_add_i32 s1, s73, 0
	s_add_i32 m0, s1, 0x10000
	s_add_i32 s13, s1, 0x2000
	global_load_lds_dwordx4 v0, s[46:47]
	v_mov_b32_e32 v0, v137
	s_add_i32 m0, s1, 0x12000
	s_add_u32 s4, s46, 0x40000
	global_load_lds_dwordx4 v0, s[46:47]
	v_mov_b32_e32 v0, v136
	s_mov_b32 m0, s1
	s_addc_u32 s5, s47, 0
	global_load_lds_dwordx4 v0, s[26:27]
	v_mov_b32_e32 v0, v137
	s_mov_b32 m0, s13
	s_nop 0
	global_load_lds_dwordx4 v0, s[26:27]
	v_mov_b32_e32 v0, v136
	s_add_i32 m0, s1, 0x14000
	s_nop 0
	global_load_lds_dwordx4 v0, s[4:5]
	v_mov_b32_e32 v0, v137
	s_add_i32 m0, s1, 0x16000
	s_nop 0
	global_load_lds_dwordx4 v0, s[4:5]
	s_add_u32 s4, s26, 0x40000
	s_addc_u32 s5, s27, 0
	v_mov_b32_e32 v0, v136
	s_add_i32 s14, s1, 0x4000
	s_mov_b32 m0, s14
	s_add_i32 s15, s1, 0x6000
	global_load_lds_dwordx4 v0, s[4:5]
	v_mov_b32_e32 v0, v137
	s_mov_b32 m0, s15
	s_nop 0
	global_load_lds_dwordx4 v0, s[4:5]
	v_readlane_b32 s4, v252, 48
	v_readlane_b32 s5, v252, 49
	s_andn2_b64 vcc, exec, s[4:5]
	s_cbranch_vccnz .LBB0_240
	s_setprio 1
	s_barrier

.Lpeel_0:
	s_add_u32 s31, s26, 0xfffc0080
	s_addc_u32 s33, s27, -1
	s_add_i32 s34, 0, 0x10000
	v_add_u32_e32 v0, s34, v138
	ds_read_b128 v[140:143], v0
	ds_read_b128 v[144:147], v0 offset:1024
	ds_read_b128 v[148:151], v0 offset:2048
	ds_read_b128 v[152:155], v0 offset:3072
	s_cmp_eq_u32 s30, 12
	s_cselect_b32 s49, s3, s33
	s_cselect_b32 s48, s5, s31
	s_cselect_b32 s47, s20, s25
	s_cselect_b32 s46, s21, s22
	v_mov_b32_e32 v0, v136
	ds_read_b128 v[156:159], v139
	ds_read_b128 v[160:163], v139 offset:1024
	ds_read_b128 v[172:175], v139 offset:2048
	ds_read_b128 v[176:179], v139 offset:3072
	ds_read_b128 v[180:183], v139 offset:4096
	ds_read_b128 v[184:187], v139 offset:5120
	ds_read_b128 v[188:191], v139 offset:6144
	ds_read_b128 v[192:195], v139 offset:7168
	s_nop 0
	v_mov_b32_e32 v0, v137
	s_nop 0
	s_waitcnt lgkmcnt(8)
	s_barrier
	s_waitcnt lgkmcnt(0)
	v_mov_b64_e32 v[50:51], v[164:165]
	s_waitcnt lgkmcnt(0)
	v_mfma_scale_f32_16x16x128_f8f6f4 v[98:101], v[156:163], v[148:155], 0, v202, v202 op_sel_hi:[0,0,0]
	v_mov_b64_e32 v[52:53], v[166:167]
	v_mfma_scale_f32_16x16x128_f8f6f4 v[164:167], v[172:179], v[140:147], 0, v202, v202 op_sel_hi:[0,0,0]
	s_add_i32 m0, s1, 0xc000
	v_mfma_scale_f32_16x16x128_f8f6f4 v[90:93], v[180:187], v[148:155], 0, v202, v202 op_sel_hi:[0,0,0]
	global_load_lds_dwordx4 v136, s[26:27]
	v_mfma_scale_f32_16x16x128_f8f6f4 v[130:133], v[156:163], v[140:147], 0, v202, v202 op_sel_hi:[0,0,0]
	v_mfma_scale_f32_16x16x128_f8f6f4 v[168:171], v[172:179], v[148:155], 0, v202, v202 op_sel_hi:[0,0,0]
	s_add_i32 m0, s1, 0xe000
	v_mfma_scale_f32_16x16x128_f8f6f4 v[196:199], v[180:187], v[140:147], 0, v202, v202 op_sel_hi:[0,0,0]
	global_load_lds_dwordx4 v137, s[26:27]
	v_mfma_scale_f32_16x16x128_f8f6f4 v[206:209], v[188:195], v[140:147], 0, v202, v202 op_sel_hi:[0,0,0]
	v_mfma_scale_f32_16x16x128_f8f6f4 v[210:213], v[188:195], v[148:155], 0, v202, v202 op_sel_hi:[0,0,0]
	s_barrier
	s_add_i32 s31, 0, 0x14000
	v_add_u32_e32 v0, s31, v138
	s_nop 2
	ds_read_b128 v[82:85], v0
	ds_read_b128 v[86:89], v0 offset:1024
	ds_read_b128 v[114:117], v0 offset:2048
	ds_read_b128 v[118:121], v0 offset:3072
	v_mov_b32_e32 v0, v136
	s_add_i32 s33, s34, s73
	s_nop 0
	v_mov_b32_e32 v0, v137
	s_nop 0
	s_barrier
	s_waitcnt lgkmcnt(0)
	s_waitcnt lgkmcnt(0)
	v_mfma_scale_f32_16x16x128_f8f6f4 v[66:69], v[156:163], v[82:89], 0, v202, v202 op_sel_hi:[0,0,0]
	v_mfma_scale_f32_16x16x128_f8f6f4 v[38:41], v[156:163], v[114:121], 0, v202, v202 op_sel_hi:[0,0,0]
	s_mov_b32 m0, s33
	v_mfma_scale_f32_16x16x128_f8f6f4 v[58:61], v[180:187], v[82:89], 0, v202, v202 op_sel_hi:[0,0,0]
	global_load_lds_dwordx4 v136, s[46:47]
	v_mfma_scale_f32_16x16x128_f8f6f4 v[214:217], v[172:179], v[82:89], 0, v202, v202 op_sel_hi:[0,0,0]
	v_mfma_scale_f32_16x16x128_f8f6f4 v[172:175], v[172:179], v[114:121], 0, v202, v202 op_sel_hi:[0,0,0]
	s_add_i32 m0, s33, 0x2000
	v_mfma_scale_f32_16x16x128_f8f6f4 v[176:179], v[180:187], v[114:121], 0, v202, v202 op_sel_hi:[0,0,0]
	global_load_lds_dwordx4 v137, s[46:47]
	v_mfma_scale_f32_16x16x128_f8f6f4 v[180:183], v[188:195], v[82:89], 0, v202, v202 op_sel_hi:[0,0,0]
	v_mfma_scale_f32_16x16x128_f8f6f4 v[184:187], v[188:195], v[114:121], 0, v202, v202 op_sel_hi:[0,0,0]
	v_mov_b32_e32 v0, v136
	s_barrier
	s_nop 1
	ds_read_b128 v[18:21], v139 offset:16384
	ds_read_b128 v[22:25], v139 offset:17408
	ds_read_b128 v[50:53], v139 offset:18432
	ds_read_b128 v[54:57], v139 offset:19456
	ds_read_b128 v[122:125], v139 offset:20480
	ds_read_b128 v[126:129], v139 offset:21504
	ds_read_b128 v[156:159], v139 offset:22528
	ds_read_b128 v[160:163], v139 offset:23552
	s_nop 0
	v_mov_b32_e32 v0, v137
	s_nop 0
	s_barrier
	s_waitcnt lgkmcnt(0)
	s_waitcnt lgkmcnt(0)
	v_mfma_scale_f32_16x16x128_f8f6f4 v[110:113], v[18:25], v[140:147], 0, v202, v202 op_sel_hi:[0,0,0]
	v_mfma_scale_f32_16x16x128_f8f6f4 v[78:81], v[18:25], v[148:155], 0, v202, v202 op_sel_hi:[0,0,0]
	s_mov_b32 m0, s1
	v_mfma_scale_f32_16x16x128_f8f6f4 v[102:105], v[50:57], v[140:147], 0, v202, v202 op_sel_hi:[0,0,0]
	global_load_lds_dwordx4 v136, s[48:49]
	v_mfma_scale_f32_16x16x128_f8f6f4 v[106:109], v[122:129], v[140:147], 0, v202, v202 op_sel_hi:[0,0,0]
	v_mfma_scale_f32_16x16x128_f8f6f4 v[94:97], v[156:163], v[140:147], 0, v202, v202 op_sel_hi:[0,0,0]
	s_mov_b32 m0, s13
	v_mfma_scale_f32_16x16x128_f8f6f4 v[62:65], v[156:163], v[148:155], 0, v202, v202 op_sel_hi:[0,0,0]
	global_load_lds_dwordx4 v137, s[48:49]
	v_mfma_scale_f32_16x16x128_f8f6f4 v[218:221], v[50:57], v[148:155], 0, v202, v202 op_sel_hi:[0,0,0]
	v_mfma_scale_f32_16x16x128_f8f6f4 v[222:225], v[122:129], v[148:155], 0, v202, v202 op_sel_hi:[0,0,0]
	s_barrier
	s_add_u32 s34, s46, 0x40000
	s_addc_u32 s35, s47, 0
	v_mov_b32_e32 v0, v136
	s_add_i32 s31, s31, s73
	s_mov_b32 s100, s31
	s_nop 0
	v_mov_b32_e32 v0, v137
	s_add_i32 s101, s31, 0x2000
	s_nop 0
	s_waitcnt vmcnt(4)
	s_barrier
	v_mfma_scale_f32_16x16x128_f8f6f4 v[34:37], v[50:57], v[82:89], 0, v202, v202 op_sel_hi:[0,0,0]
	v_mfma_scale_f32_16x16x128_f8f6f4 v[226:229], v[18:25], v[82:89], 0, v202, v202 op_sel_hi:[0,0,0]
	s_mov_b32 m0, s100
	v_mfma_scale_f32_16x16x128_f8f6f4 v[230:233], v[18:25], v[114:121], 0, v202, v202 op_sel_hi:[0,0,0]
	global_load_lds_dwordx4 v136, s[34:35]
	v_mfma_scale_f32_16x16x128_f8f6f4 v[234:237], v[50:57], v[114:121], 0, v202, v202 op_sel_hi:[0,0,0]
	v_mfma_scale_f32_16x16x128_f8f6f4 v[238:241], v[122:129], v[82:89], 0, v202, v202 op_sel_hi:[0,0,0]
	s_mov_b32 m0, s101
	v_mfma_scale_f32_16x16x128_f8f6f4 v[242:245], v[122:129], v[114:121], 0, v202, v202 op_sel_hi:[0,0,0]
	global_load_lds_dwordx4 v137, s[34:35]
	v_mfma_scale_f32_16x16x128_f8f6f4 v[246:249], v[156:163], v[82:89], 0, v202, v202 op_sel_hi:[0,0,0]
	v_mfma_scale_f32_16x16x128_f8f6f4 v[50:53], v[156:163], v[114:121], 0, v202, v202 op_sel_hi:[0,0,0]
	s_add_i32 s31, 0, 0x18000
	v_add_u32_e32 v0, s31, v138
	s_barrier
	s_nop 2
	ds_read_b128 v[2:5], v0
	ds_read_b128 v[6:9], v0 offset:1024
	ds_read_b128 v[10:13], v0 offset:2048
	ds_read_b128 v[14:17], v0 offset:3072
	s_add_u32 s34, s48, 0x40000
	v_mov_b32_e32 v0, v136
	ds_read_b128 v[18:21], v139 offset:32768
	ds_read_b128 v[22:25], v139 offset:33792
	ds_read_b128 v[26:29], v139 offset:34816
	ds_read_b128 v[30:33], v139 offset:35840
	ds_read_b128 v[42:45], v139 offset:36864
	ds_read_b128 v[46:49], v139 offset:37888
	ds_read_b128 v[70:73], v139 offset:38912
	ds_read_b128 v[74:77], v139 offset:39936
	s_addc_u32 s35, s49, 0
	s_nop 0
	v_mov_b32_e32 v0, v137
	s_nop 0
	s_waitcnt lgkmcnt(8)
	s_barrier
	s_waitcnt lgkmcnt(0)
	s_waitcnt lgkmcnt(0)
	v_mfma_scale_f32_16x16x128_f8f6f4 v[126:129], v[18:25], v[2:9], v[130:133], v202, v202 op_sel_hi:[0,0,0]
	v_mfma_scale_f32_16x16x128_f8f6f4 v[98:101], v[18:25], v[10:17], v[98:101], v202, v202 op_sel_hi:[0,0,0]
	s_mov_b32 m0, s14
	v_mfma_scale_f32_16x16x128_f8f6f4 v[118:121], v[26:33], v[2:9], v[164:167], v202, v202 op_sel_hi:[0,0,0]
	global_load_lds_dwordx4 v136, s[34:35]
	v_mfma_scale_f32_16x16x128_f8f6f4 v[86:89], v[26:33], v[10:17], v[168:171], v202, v202 op_sel_hi:[0,0,0]
	v_mfma_scale_f32_16x16x128_f8f6f4 v[122:125], v[42:49], v[2:9], v[196:199], v202, v202 op_sel_hi:[0,0,0]
	s_mov_b32 m0, s15
	v_mfma_scale_f32_16x16x128_f8f6f4 v[90:93], v[42:49], v[10:17], v[90:93], v202, v202 op_sel_hi:[0,0,0]
	global_load_lds_dwordx4 v137, s[34:35]
	v_mfma_scale_f32_16x16x128_f8f6f4 v[114:117], v[70:77], v[2:9], v[206:209], v202, v202 op_sel_hi:[0,0,0]
	v_mfma_scale_f32_16x16x128_f8f6f4 v[82:85], v[70:77], v[10:17], v[210:213], v202, v202 op_sel_hi:[0,0,0]
	s_barrier
	s_add_i32 s33, 0, 0x1c000
	v_add_u32_e32 v0, s33, v138
	ds_read_b128 v[140:143], v0
	ds_read_b128 v[144:147], v0 offset:1024
	ds_read_b128 v[148:151], v0 offset:2048
	ds_read_b128 v[152:155], v0 offset:3072
	v_mov_b32_e32 v0, v136
	s_add_i32 s31, s31, s73
	v_lshl_add_u64 v[54:55], s[46:47], 0, v[0:1]
	v_lshl_add_u64 v[54:55], v[54:55], 0, s[66:67]
	v_mov_b32_e32 v0, v137
	v_lshl_add_u64 v[54:55], s[46:47], 0, v[0:1]
	v_lshl_add_u64 v[54:55], v[54:55], 0, s[66:67]
	s_barrier
	s_waitcnt lgkmcnt(0)
	s_waitcnt lgkmcnt(0)
	v_mfma_scale_f32_16x16x128_f8f6f4 v[66:69], v[18:25], v[140:147], v[66:69], v202, v202 op_sel_hi:[0,0,0]
	v_mfma_scale_f32_16x16x128_f8f6f4 v[38:41], v[18:25], v[148:155], v[38:41], v202, v202 op_sel_hi:[0,0,0]
	s_add_u32 s98, s46, s66
	s_addc_u32 s99, s47, s67
	s_mov_b32 m0, s31
	v_mfma_scale_f32_16x16x128_f8f6f4 v[54:57], v[26:33], v[140:147], v[214:217], v202, v202 op_sel_hi:[0,0,0]
	global_load_lds_dwordx4 v136, s[98:99]
	v_mfma_scale_f32_16x16x128_f8f6f4 v[22:25], v[26:33], v[148:155], v[172:175], v202, v202 op_sel_hi:[0,0,0]
	v_mfma_scale_f32_16x16x128_f8f6f4 v[58:61], v[42:49], v[140:147], v[58:61], v202, v202 op_sel_hi:[0,0,0]
	s_add_i32 m0, s31, 0x2000
	v_mfma_scale_f32_16x16x128_f8f6f4 v[30:33], v[42:49], v[148:155], v[176:179], v202, v202 op_sel_hi:[0,0,0]
	global_load_lds_dwordx4 v137, s[98:99]
	v_mfma_scale_f32_16x16x128_f8f6f4 v[18:21], v[70:77], v[140:147], v[180:183], v202, v202 op_sel_hi:[0,0,0]
	v_mfma_scale_f32_16x16x128_f8f6f4 v[164:167], v[70:77], v[148:155], v[184:187], v202, v202 op_sel_hi:[0,0,0]
	v_mov_b32_e32 v0, v136
	s_barrier
	ds_read_b128 v[156:159], v139 offset:49152
	ds_read_b128 v[160:163], v139 offset:50176
	ds_read_b128 v[172:175], v139 offset:51200
	ds_read_b128 v[176:179], v139 offset:52224
	ds_read_b128 v[180:183], v139 offset:53248
	ds_read_b128 v[184:187], v139 offset:54272
	ds_read_b128 v[188:191], v139 offset:55296
	ds_read_b128 v[192:195], v139 offset:56320
	v_lshl_add_u64 v[26:27], s[48:49], 0, v[0:1]
	v_lshl_add_u64 v[26:27], v[26:27], 0, s[66:67]
	v_mov_b32_e32 v0, v137
	v_lshl_add_u64 v[26:27], s[48:49], 0, v[0:1]
	v_lshl_add_u64 v[26:27], v[26:27], 0, s[66:67]
	s_barrier
	s_waitcnt lgkmcnt(0)
	s_waitcnt lgkmcnt(0)
	v_mfma_scale_f32_16x16x128_f8f6f4 v[110:113], v[156:163], v[2:9], v[110:113], v202, v202 op_sel_hi:[0,0,0]
	v_mfma_scale_f32_16x16x128_f8f6f4 v[78:81], v[156:163], v[10:17], v[78:81], v202, v202 op_sel_hi:[0,0,0]
	s_add_u32 s98, s48, s66
	s_addc_u32 s99, s49, s67
	s_mov_b32 m0, s17
	v_mfma_scale_f32_16x16x128_f8f6f4 v[102:105], v[172:179], v[2:9], v[102:105], v202, v202 op_sel_hi:[0,0,0]
	global_load_lds_dwordx4 v136, s[98:99]
	v_mfma_scale_f32_16x16x128_f8f6f4 v[70:73], v[172:179], v[10:17], v[218:221], v202, v202 op_sel_hi:[0,0,0]
	v_mfma_scale_f32_16x16x128_f8f6f4 v[106:109], v[180:187], v[2:9], v[106:109], v202, v202 op_sel_hi:[0,0,0]
	s_mov_b32 m0, s18
	v_mfma_scale_f32_16x16x128_f8f6f4 v[74:77], v[180:187], v[10:17], v[222:225], v202, v202 op_sel_hi:[0,0,0]
	global_load_lds_dwordx4 v137, s[98:99]
	v_mfma_scale_f32_16x16x128_f8f6f4 v[94:97], v[188:195], v[2:9], v[94:97], v202, v202 op_sel_hi:[0,0,0]
	v_mfma_scale_f32_16x16x128_f8f6f4 v[62:65], v[188:195], v[10:17], v[62:65], v202, v202 op_sel_hi:[0,0,0]
	s_barrier
	s_add_u32 s34, s46, 0x40080
	s_addc_u32 s35, s47, 0
	v_mov_b32_e32 v0, v136
	s_add_i32 s31, s33, s73
	s_nop 0
	v_mov_b32_e32 v0, v137
	s_nop 0
	s_waitcnt vmcnt(4)
	s_barrier
	v_mfma_scale_f32_16x16x128_f8f6f4 v[46:49], v[156:163], v[140:147], v[226:229], v202, v202 op_sel_hi:[0,0,0]
	v_mfma_scale_f32_16x16x128_f8f6f4 v[14:17], v[156:163], v[148:155], v[230:233], v202, v202 op_sel_hi:[0,0,0]
	s_mov_b32 m0, s31
	v_mfma_scale_f32_16x16x128_f8f6f4 v[34:37], v[172:179], v[140:147], v[34:37], v202, v202 op_sel_hi:[0,0,0]
	global_load_lds_dwordx4 v136, s[34:35]
	v_mfma_scale_f32_16x16x128_f8f6f4 v[6:9], v[172:179], v[148:155], v[234:237], v202, v202 op_sel_hi:[0,0,0]
	v_mfma_scale_f32_16x16x128_f8f6f4 v[42:45], v[180:187], v[140:147], v[238:241], v202, v202 op_sel_hi:[0,0,0]
	s_add_i32 m0, s31, 0x2000
	v_mfma_scale_f32_16x16x128_f8f6f4 v[10:13], v[180:187], v[148:155], v[242:245], v202, v202 op_sel_hi:[0,0,0]
	global_load_lds_dwordx4 v137, s[34:35]
	v_mfma_scale_f32_16x16x128_f8f6f4 v[26:29], v[188:195], v[140:147], v[246:249], v202, v202 op_sel_hi:[0,0,0]
	v_mfma_scale_f32_16x16x128_f8f6f4 v[2:5], v[188:195], v[148:155], v[50:53], v202, v202 op_sel_hi:[0,0,0]
	s_add_i32 s30, s30, 2
	s_add_u32 s26, s26, 0x100
	s_addc_u32 s27, s27, 0
	s_add_u32 s22, s22, 0x100
	s_addc_u32 s25, s25, 0
	s_cmp_gt_u32 s30, 13
	s_barrier
	s_cbranch_scc0 .LBB0_249
	s_branch .Lpeel_exit_0
.LBB0_249:
	s_add_u32 s31, s26, 0xfffc0080
	s_addc_u32 s33, s27, -1
	s_add_i32 s34, 0, 0x10000
	v_add_u32_e32 v0, s34, v138
	ds_read_b128 v[140:143], v0
	ds_read_b128 v[144:147], v0 offset:1024
	ds_read_b128 v[148:151], v0 offset:2048
	ds_read_b128 v[152:155], v0 offset:3072
	s_cmp_eq_u32 s30, 12
	s_cselect_b32 s49, s3, s33
	s_cselect_b32 s48, s5, s31
	s_cselect_b32 s47, s20, s25
	s_cselect_b32 s46, s21, s22
	v_mov_b32_e32 v0, v136
	ds_read_b128 v[156:159], v139
	ds_read_b128 v[160:163], v139 offset:1024
	ds_read_b128 v[172:175], v139 offset:2048
	ds_read_b128 v[176:179], v139 offset:3072
	ds_read_b128 v[180:183], v139 offset:4096
	ds_read_b128 v[184:187], v139 offset:5120
	ds_read_b128 v[188:191], v139 offset:6144
	ds_read_b128 v[192:195], v139 offset:7168
	s_nop 0
	v_mov_b32_e32 v0, v137
	s_nop 0
	s_waitcnt lgkmcnt(8)
	s_barrier
	s_waitcnt lgkmcnt(0)
	v_mov_b64_e32 v[50:51], v[164:165]
	s_waitcnt lgkmcnt(0)
	v_mfma_scale_f32_16x16x128_f8f6f4 v[98:101], v[156:163], v[148:155], v[98:101], v202, v202 op_sel_hi:[0,0,0]
	v_mov_b64_e32 v[52:53], v[166:167]
	v_mfma_scale_f32_16x16x128_f8f6f4 v[164:167], v[172:179], v[140:147], v[118:121], v202, v202 op_sel_hi:[0,0,0]
	s_add_i32 m0, s1, 0xc000
	v_mfma_scale_f32_16x16x128_f8f6f4 v[90:93], v[180:187], v[148:155], v[90:93], v202, v202 op_sel_hi:[0,0,0]
	global_load_lds_dwordx4 v136, s[26:27]
	v_mfma_scale_f32_16x16x128_f8f6f4 v[130:133], v[156:163], v[140:147], v[126:129], v202, v202 op_sel_hi:[0,0,0]
	v_mfma_scale_f32_16x16x128_f8f6f4 v[168:171], v[172:179], v[148:155], v[86:89], v202, v202 op_sel_hi:[0,0,0]
	s_add_i32 m0, s1, 0xe000
	v_mfma_scale_f32_16x16x128_f8f6f4 v[196:199], v[180:187], v[140:147], v[122:125], v202, v202 op_sel_hi:[0,0,0]
	global_load_lds_dwordx4 v137, s[26:27]
	v_mfma_scale_f32_16x16x128_f8f6f4 v[206:209], v[188:195], v[140:147], v[114:117], v202, v202 op_sel_hi:[0,0,0]
	v_mfma_scale_f32_16x16x128_f8f6f4 v[210:213], v[188:195], v[148:155], v[82:85], v202, v202 op_sel_hi:[0,0,0]
	s_barrier
	s_add_i32 s31, 0, 0x14000
	v_add_u32_e32 v0, s31, v138
	s_nop 2
	ds_read_b128 v[82:85], v0
	ds_read_b128 v[86:89], v0 offset:1024
	ds_read_b128 v[114:117], v0 offset:2048
	ds_read_b128 v[118:121], v0 offset:3072
	v_mov_b32_e32 v0, v136
	s_add_i32 s33, s34, s73
	s_nop 0
	v_mov_b32_e32 v0, v137
	s_nop 0
	s_barrier
	s_waitcnt lgkmcnt(0)
	s_waitcnt lgkmcnt(0)
	v_mfma_scale_f32_16x16x128_f8f6f4 v[66:69], v[156:163], v[82:89], v[66:69], v202, v202 op_sel_hi:[0,0,0]
	v_mfma_scale_f32_16x16x128_f8f6f4 v[38:41], v[156:163], v[114:121], v[38:41], v202, v202 op_sel_hi:[0,0,0]
	s_mov_b32 m0, s33
	v_mfma_scale_f32_16x16x128_f8f6f4 v[58:61], v[180:187], v[82:89], v[58:61], v202, v202 op_sel_hi:[0,0,0]
	global_load_lds_dwordx4 v136, s[46:47]
	v_mfma_scale_f32_16x16x128_f8f6f4 v[214:217], v[172:179], v[82:89], v[54:57], v202, v202 op_sel_hi:[0,0,0]
	v_mfma_scale_f32_16x16x128_f8f6f4 v[172:175], v[172:179], v[114:121], v[22:25], v202, v202 op_sel_hi:[0,0,0]
	s_add_i32 m0, s33, 0x2000
	v_mfma_scale_f32_16x16x128_f8f6f4 v[176:179], v[180:187], v[114:121], v[30:33], v202, v202 op_sel_hi:[0,0,0]
	global_load_lds_dwordx4 v137, s[46:47]
	v_mfma_scale_f32_16x16x128_f8f6f4 v[180:183], v[188:195], v[82:89], v[18:21], v202, v202 op_sel_hi:[0,0,0]
	v_mfma_scale_f32_16x16x128_f8f6f4 v[184:187], v[188:195], v[114:121], v[50:53], v202, v202 op_sel_hi:[0,0,0]
	v_mov_b32_e32 v0, v136
	s_barrier
	s_nop 1
	ds_read_b128 v[18:21], v139 offset:16384
	ds_read_b128 v[22:25], v139 offset:17408
	ds_read_b128 v[50:53], v139 offset:18432
	ds_read_b128 v[54:57], v139 offset:19456
	ds_read_b128 v[122:125], v139 offset:20480
	ds_read_b128 v[126:129], v139 offset:21504
	ds_read_b128 v[156:159], v139 offset:22528
	ds_read_b128 v[160:163], v139 offset:23552
	s_nop 0
	v_mov_b32_e32 v0, v137
	s_nop 0
	s_barrier
	s_waitcnt lgkmcnt(0)
	s_waitcnt lgkmcnt(0)
	v_mfma_scale_f32_16x16x128_f8f6f4 v[110:113], v[18:25], v[140:147], v[110:113], v202, v202 op_sel_hi:[0,0,0]
	v_mfma_scale_f32_16x16x128_f8f6f4 v[78:81], v[18:25], v[148:155], v[78:81], v202, v202 op_sel_hi:[0,0,0]
	s_mov_b32 m0, s1
	v_mfma_scale_f32_16x16x128_f8f6f4 v[102:105], v[50:57], v[140:147], v[102:105], v202, v202 op_sel_hi:[0,0,0]
	global_load_lds_dwordx4 v136, s[48:49]
	v_mfma_scale_f32_16x16x128_f8f6f4 v[106:109], v[122:129], v[140:147], v[106:109], v202, v202 op_sel_hi:[0,0,0]
	v_mfma_scale_f32_16x16x128_f8f6f4 v[94:97], v[156:163], v[140:147], v[94:97], v202, v202 op_sel_hi:[0,0,0]
	s_mov_b32 m0, s13
	v_mfma_scale_f32_16x16x128_f8f6f4 v[62:65], v[156:163], v[148:155], v[62:65], v202, v202 op_sel_hi:[0,0,0]
	global_load_lds_dwordx4 v137, s[48:49]
	v_mfma_scale_f32_16x16x128_f8f6f4 v[218:221], v[50:57], v[148:155], v[70:73], v202, v202 op_sel_hi:[0,0,0]
	v_mfma_scale_f32_16x16x128_f8f6f4 v[222:225], v[122:129], v[148:155], v[74:77], v202, v202 op_sel_hi:[0,0,0]
	s_barrier
	s_add_u32 s34, s46, 0x40000
	s_addc_u32 s35, s47, 0
	v_mov_b32_e32 v0, v136
	s_add_i32 s31, s31, s73
	s_mov_b32 s100, s31
	s_nop 0
	v_mov_b32_e32 v0, v137
	s_add_i32 s101, s31, 0x2000
	s_nop 0
	s_waitcnt vmcnt(4)
	s_barrier
	v_mfma_scale_f32_16x16x128_f8f6f4 v[34:37], v[50:57], v[82:89], v[34:37], v202, v202 op_sel_hi:[0,0,0]
	v_mfma_scale_f32_16x16x128_f8f6f4 v[226:229], v[18:25], v[82:89], v[46:49], v202, v202 op_sel_hi:[0,0,0]
	s_mov_b32 m0, s100
	v_mfma_scale_f32_16x16x128_f8f6f4 v[230:233], v[18:25], v[114:121], v[14:17], v202, v202 op_sel_hi:[0,0,0]
	global_load_lds_dwordx4 v136, s[34:35]
	v_mfma_scale_f32_16x16x128_f8f6f4 v[234:237], v[50:57], v[114:121], v[6:9], v202, v202 op_sel_hi:[0,0,0]
	v_mfma_scale_f32_16x16x128_f8f6f4 v[238:241], v[122:129], v[82:89], v[42:45], v202, v202 op_sel_hi:[0,0,0]
	s_mov_b32 m0, s101
	v_mfma_scale_f32_16x16x128_f8f6f4 v[242:245], v[122:129], v[114:121], v[10:13], v202, v202 op_sel_hi:[0,0,0]
	global_load_lds_dwordx4 v137, s[34:35]
	v_mfma_scale_f32_16x16x128_f8f6f4 v[246:249], v[156:163], v[82:89], v[26:29], v202, v202 op_sel_hi:[0,0,0]
	v_mfma_scale_f32_16x16x128_f8f6f4 v[50:53], v[156:163], v[114:121], v[2:5], v202, v202 op_sel_hi:[0,0,0]
	s_add_i32 s31, 0, 0x18000
	v_add_u32_e32 v0, s31, v138
	s_barrier
	s_nop 2
	ds_read_b128 v[2:5], v0
	ds_read_b128 v[6:9], v0 offset:1024
	ds_read_b128 v[10:13], v0 offset:2048
	ds_read_b128 v[14:17], v0 offset:3072
	s_add_u32 s34, s48, 0x40000
	v_mov_b32_e32 v0, v136
	ds_read_b128 v[18:21], v139 offset:32768
	ds_read_b128 v[22:25], v139 offset:33792
	ds_read_b128 v[26:29], v139 offset:34816
	ds_read_b128 v[30:33], v139 offset:35840
	ds_read_b128 v[42:45], v139 offset:36864
	ds_read_b128 v[46:49], v139 offset:37888
	ds_read_b128 v[70:73], v139 offset:38912
	ds_read_b128 v[74:77], v139 offset:39936
	s_addc_u32 s35, s49, 0
	s_nop 0
	v_mov_b32_e32 v0, v137
	s_nop 0
	s_waitcnt lgkmcnt(8)
	s_barrier
	s_waitcnt lgkmcnt(0)
	s_waitcnt lgkmcnt(0)
	v_mfma_scale_f32_16x16x128_f8f6f4 v[126:129], v[18:25], v[2:9], v[130:133], v202, v202 op_sel_hi:[0,0,0]
	v_mfma_scale_f32_16x16x128_f8f6f4 v[98:101], v[18:25], v[10:17], v[98:101], v202, v202 op_sel_hi:[0,0,0]
	s_mov_b32 m0, s14
	v_mfma_scale_f32_16x16x128_f8f6f4 v[118:121], v[26:33], v[2:9], v[164:167], v202, v202 op_sel_hi:[0,0,0]
	global_load_lds_dwordx4 v136, s[34:35]
	v_mfma_scale_f32_16x16x128_f8f6f4 v[86:89], v[26:33], v[10:17], v[168:171], v202, v202 op_sel_hi:[0,0,0]
	v_mfma_scale_f32_16x16x128_f8f6f4 v[122:125], v[42:49], v[2:9], v[196:199], v202, v202 op_sel_hi:[0,0,0]
	s_mov_b32 m0, s15
	v_mfma_scale_f32_16x16x128_f8f6f4 v[90:93], v[42:49], v[10:17], v[90:93], v202, v202 op_sel_hi:[0,0,0]
	global_load_lds_dwordx4 v137, s[34:35]
	v_mfma_scale_f32_16x16x128_f8f6f4 v[114:117], v[70:77], v[2:9], v[206:209], v202, v202 op_sel_hi:[0,0,0]
	v_mfma_scale_f32_16x16x128_f8f6f4 v[82:85], v[70:77], v[10:17], v[210:213], v202, v202 op_sel_hi:[0,0,0]
	s_barrier
	s_add_i32 s33, 0, 0x1c000
	v_add_u32_e32 v0, s33, v138
	ds_read_b128 v[140:143], v0
	ds_read_b128 v[144:147], v0 offset:1024
	ds_read_b128 v[148:151], v0 offset:2048
	ds_read_b128 v[152:155], v0 offset:3072
	v_mov_b32_e32 v0, v136
	s_add_i32 s31, s31, s73
	v_lshl_add_u64 v[54:55], s[46:47], 0, v[0:1]
	v_lshl_add_u64 v[54:55], v[54:55], 0, s[66:67]
	v_mov_b32_e32 v0, v137
	v_lshl_add_u64 v[54:55], s[46:47], 0, v[0:1]
	v_lshl_add_u64 v[54:55], v[54:55], 0, s[66:67]
	s_barrier
	s_waitcnt lgkmcnt(0)
	s_waitcnt lgkmcnt(0)
	v_mfma_scale_f32_16x16x128_f8f6f4 v[66:69], v[18:25], v[140:147], v[66:69], v202, v202 op_sel_hi:[0,0,0]
	v_mfma_scale_f32_16x16x128_f8f6f4 v[38:41], v[18:25], v[148:155], v[38:41], v202, v202 op_sel_hi:[0,0,0]
	s_add_u32 s98, s46, s66
	s_addc_u32 s99, s47, s67
	s_mov_b32 m0, s31
	v_mfma_scale_f32_16x16x128_f8f6f4 v[54:57], v[26:33], v[140:147], v[214:217], v202, v202 op_sel_hi:[0,0,0]
	global_load_lds_dwordx4 v136, s[98:99]
	v_mfma_scale_f32_16x16x128_f8f6f4 v[22:25], v[26:33], v[148:155], v[172:175], v202, v202 op_sel_hi:[0,0,0]
	v_mfma_scale_f32_16x16x128_f8f6f4 v[58:61], v[42:49], v[140:147], v[58:61], v202, v202 op_sel_hi:[0,0,0]
	s_add_i32 m0, s31, 0x2000
	v_mfma_scale_f32_16x16x128_f8f6f4 v[30:33], v[42:49], v[148:155], v[176:179], v202, v202 op_sel_hi:[0,0,0]
	global_load_lds_dwordx4 v137, s[98:99]
	v_mfma_scale_f32_16x16x128_f8f6f4 v[18:21], v[70:77], v[140:147], v[180:183], v202, v202 op_sel_hi:[0,0,0]
	v_mfma_scale_f32_16x16x128_f8f6f4 v[164:167], v[70:77], v[148:155], v[184:187], v202, v202 op_sel_hi:[0,0,0]
	v_mov_b32_e32 v0, v136
	s_barrier
	ds_read_b128 v[156:159], v139 offset:49152
	ds_read_b128 v[160:163], v139 offset:50176
	ds_read_b128 v[172:175], v139 offset:51200
	ds_read_b128 v[176:179], v139 offset:52224
	ds_read_b128 v[180:183], v139 offset:53248
	ds_read_b128 v[184:187], v139 offset:54272
	ds_read_b128 v[188:191], v139 offset:55296
	ds_read_b128 v[192:195], v139 offset:56320
	v_lshl_add_u64 v[26:27], s[48:49], 0, v[0:1]
	v_lshl_add_u64 v[26:27], v[26:27], 0, s[66:67]
	v_mov_b32_e32 v0, v137
	v_lshl_add_u64 v[26:27], s[48:49], 0, v[0:1]
	v_lshl_add_u64 v[26:27], v[26:27], 0, s[66:67]
	s_barrier
	s_waitcnt lgkmcnt(0)
	s_waitcnt lgkmcnt(0)
	v_mfma_scale_f32_16x16x128_f8f6f4 v[110:113], v[156:163], v[2:9], v[110:113], v202, v202 op_sel_hi:[0,0,0]
	v_mfma_scale_f32_16x16x128_f8f6f4 v[78:81], v[156:163], v[10:17], v[78:81], v202, v202 op_sel_hi:[0,0,0]
	s_add_u32 s98, s48, s66
	s_addc_u32 s99, s49, s67
	s_mov_b32 m0, s17
	v_mfma_scale_f32_16x16x128_f8f6f4 v[102:105], v[172:179], v[2:9], v[102:105], v202, v202 op_sel_hi:[0,0,0]
	global_load_lds_dwordx4 v136, s[98:99]
	v_mfma_scale_f32_16x16x128_f8f6f4 v[70:73], v[172:179], v[10:17], v[218:221], v202, v202 op_sel_hi:[0,0,0]
	v_mfma_scale_f32_16x16x128_f8f6f4 v[106:109], v[180:187], v[2:9], v[106:109], v202, v202 op_sel_hi:[0,0,0]
	s_mov_b32 m0, s18
	v_mfma_scale_f32_16x16x128_f8f6f4 v[74:77], v[180:187], v[10:17], v[222:225], v202, v202 op_sel_hi:[0,0,0]
	global_load_lds_dwordx4 v137, s[98:99]
	v_mfma_scale_f32_16x16x128_f8f6f4 v[94:97], v[188:195], v[2:9], v[94:97], v202, v202 op_sel_hi:[0,0,0]
	v_mfma_scale_f32_16x16x128_f8f6f4 v[62:65], v[188:195], v[10:17], v[62:65], v202, v202 op_sel_hi:[0,0,0]
	s_barrier
	s_add_u32 s34, s46, 0x40080
	s_addc_u32 s35, s47, 0
	v_mov_b32_e32 v0, v136
	s_add_i32 s31, s33, s73
	s_nop 0
	v_mov_b32_e32 v0, v137
	s_nop 0
	s_waitcnt vmcnt(4)
	s_barrier
	v_mfma_scale_f32_16x16x128_f8f6f4 v[46:49], v[156:163], v[140:147], v[226:229], v202, v202 op_sel_hi:[0,0,0]
	v_mfma_scale_f32_16x16x128_f8f6f4 v[14:17], v[156:163], v[148:155], v[230:233], v202, v202 op_sel_hi:[0,0,0]
	s_mov_b32 m0, s31
	v_mfma_scale_f32_16x16x128_f8f6f4 v[34:37], v[172:179], v[140:147], v[34:37], v202, v202 op_sel_hi:[0,0,0]
	global_load_lds_dwordx4 v136, s[34:35]
	v_mfma_scale_f32_16x16x128_f8f6f4 v[6:9], v[172:179], v[148:155], v[234:237], v202, v202 op_sel_hi:[0,0,0]
	v_mfma_scale_f32_16x16x128_f8f6f4 v[42:45], v[180:187], v[140:147], v[238:241], v202, v202 op_sel_hi:[0,0,0]
	s_add_i32 m0, s31, 0x2000
	v_mfma_scale_f32_16x16x128_f8f6f4 v[10:13], v[180:187], v[148:155], v[242:245], v202, v202 op_sel_hi:[0,0,0]
	global_load_lds_dwordx4 v137, s[34:35]
	v_mfma_scale_f32_16x16x128_f8f6f4 v[26:29], v[188:195], v[140:147], v[246:249], v202, v202 op_sel_hi:[0,0,0]
	v_mfma_scale_f32_16x16x128_f8f6f4 v[2:5], v[188:195], v[148:155], v[50:53], v202, v202 op_sel_hi:[0,0,0]
	s_add_i32 s30, s30, 2
	s_add_u32 s26, s26, 0x100
	s_addc_u32 s27, s27, 0
	s_add_u32 s22, s22, 0x100
	s_addc_u32 s25, s25, 0
	s_cmp_gt_u32 s30, 13
	s_barrier
	s_cbranch_scc0 .LBB0_249

.LBB0_253:
	s_barrier
	s_setprio 0

.LBB0_265:
	v_lshlrev_b32_e32 v3, 4, v2
	v_add_u32_e32 v0, s73, v3
	v_ashrrev_i32_e32 v4, 31, v0
	v_lshrrev_b32_e32 v4, 22, v4
	v_add_u32_e32 v4, v0, v4
	v_ashrrev_i32_e32 v4, 10, v4
	v_mul_i32_i24_e32 v5, 0x400, v4
	v_sub_u32_e32 v5, v0, v5
	v_lshrrev_b32_e32 v6, 4, v5
	v_bitop3_b32 v5, v6, v5, 32 bitop3:0x6c
	v_ashrrev_i32_e32 v7, 31, v5
	v_lshrrev_b32_e32 v7, 26, v7
	v_add_u32_e32 v7, v5, v7
	s_waitcnt vmcnt(0)
	v_lshrrev_b32_e32 v8, 6, v7
	v_and_b32_e32 v7, 0xc0, v7
	v_lshlrev_b32_e32 v6, 3, v4
	v_lshlrev_b32_e32 v4, 5, v4
	v_sub_u32_e32 v5, v5, v7
	v_and_b32_e32 v6, 0x1ffff0, v6
	v_and_b32_e32 v4, 32, v4
	v_ashrrev_i16_sdwa v5, v203, sext(v5) dst_sel:DWORD dst_unused:UNUSED_PAD src0_sel:DWORD src1_sel:BYTE_0
	v_add_u32_sdwa v4, v4, sext(v5) dst_sel:DWORD dst_unused:UNUSED_PAD src0_sel:DWORD src1_sel:WORD_0
	v_add_lshl_u32 v5, v8, v6, 11
	v_add_u32_e32 v0, 0x2000, v0
	v_lshl_add_u32 v205, v4, 1, v5
	v_ashrrev_i32_e32 v4, 31, v0
	v_lshrrev_b32_e32 v4, 22, v4
	v_add_u32_e32 v4, v0, v4
	v_ashrrev_i32_e32 v4, 10, v4
	v_mul_i32_i24_e32 v5, 0x400, v4
	v_sub_u32_e32 v0, v0, v5
	v_lshrrev_b32_e32 v5, 4, v0
	v_bitop3_b32 v0, v5, v0, 32 bitop3:0x6c
	v_ashrrev_i32_e32 v6, 31, v0
	v_lshrrev_b32_e32 v6, 26, v6
	v_add_u32_e32 v6, v0, v6
	v_lshrrev_b32_e32 v7, 6, v6
	v_and_b32_e32 v6, 0xffc0, v6
	v_sub_u32_e32 v0, v0, v6
	v_lshrrev_b16_e32 v6, 7, v0
	v_and_b32_e32 v6, 1, v6
	v_lshlrev_b32_e32 v5, 3, v4
	v_lshlrev_b32_e32 v4, 5, v4
	v_add_u16_e32 v0, v0, v6
	v_and_b32_e32 v5, 0x1ffff0, v5
	v_and_b32_e32 v4, 32, v4
	v_ashrrev_i16_sdwa v0, v203, sext(v0) dst_sel:DWORD dst_unused:UNUSED_PAD src0_sel:DWORD src1_sel:BYTE_0
	v_add_u32_sdwa v0, v4, sext(v0) dst_sel:DWORD dst_unused:UNUSED_PAD src0_sel:DWORD src1_sel:WORD_0
	v_add_lshl_u32 v4, v7, v5, 11
	v_lshl_add_u32 v206, v0, 1, v4
	v_mov_b32_e32 v0, v205
	s_add_i32 s18, s73, 0
	s_add_i32 m0, s18, 0x10000
	s_add_i32 s19, s18, 0x2000
	global_load_lds_dwordx4 v0, s[6:7]
	v_mov_b32_e32 v0, v206
	s_add_i32 m0, s18, 0x12000
	s_add_u32 s2, s6, 0x40000
	global_load_lds_dwordx4 v0, s[6:7]
	v_mov_b32_e32 v0, v205
	s_mov_b32 m0, s18
	s_addc_u32 s3, s7, 0
	global_load_lds_dwordx4 v0, s[4:5]
	v_mov_b32_e32 v0, v206
	s_mov_b32 m0, s19
	s_nop 0
	global_load_lds_dwordx4 v0, s[4:5]
	v_mov_b32_e32 v0, v205
	s_add_i32 m0, s18, 0x14000
	s_nop 0
	global_load_lds_dwordx4 v0, s[2:3]
	v_mov_b32_e32 v0, v206
	s_add_i32 m0, s18, 0x16000
	s_nop 0
	global_load_lds_dwordx4 v0, s[2:3]
	s_add_u32 s2, s4, 0x40000
	s_addc_u32 s3, s5, 0
	v_mov_b32_e32 v0, v205
	s_add_i32 s20, s18, 0x4000
	s_mov_b32 m0, s20
	s_add_i32 s21, s18, 0x6000
	global_load_lds_dwordx4 v0, s[2:3]
	v_mov_b32_e32 v0, v206
	s_mov_b32 m0, s21
	s_nop 0
	global_load_lds_dwordx4 v0, s[2:3]
	v_readlane_b32 s2, v252, 48
	v_readlane_b32 s3, v252, 49
	s_andn2_b64 vcc, exec, s[2:3]
	s_cbranch_vccnz .LBB0_267
	s_setprio 1
	s_barrier

.Lpeel_1:
	s_add_u32 s6, s4, 0xfffc0080
	s_addc_u32 s7, s5, -1
	s_add_i32 s25, 0, 0x10000
	v_add_u32_e32 v0, s25, v207
	ds_read_b128 v[52:55], v0
	ds_read_b128 v[56:59], v0 offset:1024
	ds_read_b128 v[68:71], v0 offset:2048
	ds_read_b128 v[72:75], v0 offset:3072
	s_cmp_eq_u32 s17, 12
	s_cselect_b32 s11, s3, s7
	s_cselect_b32 s10, s9, s6
	s_cselect_b32 s7, s12, s16
	s_cselect_b32 s6, s13, s15
	v_mov_b32_e32 v0, v205
	ds_read_b128 v[84:87], v208
	ds_read_b128 v[88:91], v208 offset:1024
	ds_read_b128 v[92:95], v208 offset:2048
	ds_read_b128 v[96:99], v208 offset:3072
	ds_read_b128 v[172:175], v208 offset:4096
	ds_read_b128 v[176:179], v208 offset:5120
	ds_read_b128 v[180:183], v208 offset:6144
	ds_read_b128 v[184:187], v208 offset:7168
	s_nop 0
	v_mov_b32_e32 v0, v206
	s_nop 0
	s_waitcnt lgkmcnt(8)
	s_barrier
	s_waitcnt lgkmcnt(0)
	s_waitcnt lgkmcnt(0)
	v_mfma_scale_f32_16x16x128_f8f6f4 v[164:167], v[52:59], v[84:91], 0, v202, v202 op_sel_hi:[0,0,0]
	v_mfma_scale_f32_16x16x128_f8f6f4 v[160:163], v[68:75], v[84:91], 0, v202, v202 op_sel_hi:[0,0,0]
	s_add_i32 m0, s18, 0xc000
	v_mfma_scale_f32_16x16x128_f8f6f4 v[156:159], v[52:59], v[92:99], 0, v202, v202 op_sel_hi:[0,0,0]
	global_load_lds_dwordx4 v205, s[4:5]
	v_mfma_scale_f32_16x16x128_f8f6f4 v[152:155], v[68:75], v[92:99], 0, v202, v202 op_sel_hi:[0,0,0]
	v_mfma_scale_f32_16x16x128_f8f6f4 v[148:151], v[52:59], v[172:179], 0, v202, v202 op_sel_hi:[0,0,0]
	s_add_i32 m0, s18, 0xe000
	v_mfma_scale_f32_16x16x128_f8f6f4 v[188:191], v[68:75], v[172:179], 0, v202, v202 op_sel_hi:[0,0,0]
	global_load_lds_dwordx4 v206, s[4:5]
	v_mfma_scale_f32_16x16x128_f8f6f4 v[192:195], v[52:59], v[180:187], 0, v202, v202 op_sel_hi:[0,0,0]
	v_mfma_scale_f32_16x16x128_f8f6f4 v[196:199], v[68:75], v[180:187], 0, v202, v202 op_sel_hi:[0,0,0]
	s_barrier
	s_add_i32 s30, 0, 0x14000
	v_add_u32_e32 v0, s30, v207
	s_nop 2
	ds_read_b128 v[132:135], v0
	ds_read_b128 v[136:139], v0 offset:1024
	ds_read_b128 v[140:143], v0 offset:2048
	ds_read_b128 v[144:147], v0 offset:3072
	v_mov_b32_e32 v0, v205
	s_add_i32 s25, s25, s73
	s_nop 0
	v_mov_b32_e32 v0, v206
	s_nop 0
	s_barrier
	s_waitcnt lgkmcnt(0)
	s_waitcnt lgkmcnt(0)
	v_mfma_scale_f32_16x16x128_f8f6f4 v[128:131], v[132:139], v[84:91], 0, v202, v202 op_sel_hi:[0,0,0]
	v_mfma_scale_f32_16x16x128_f8f6f4 v[124:127], v[140:147], v[84:91], 0, v202, v202 op_sel_hi:[0,0,0]
	s_mov_b32 m0, s25
	v_mfma_scale_f32_16x16x128_f8f6f4 v[120:123], v[132:139], v[92:99], 0, v202, v202 op_sel_hi:[0,0,0]
	global_load_lds_dwordx4 v205, s[6:7]
	v_mfma_scale_f32_16x16x128_f8f6f4 v[116:119], v[140:147], v[92:99], 0, v202, v202 op_sel_hi:[0,0,0]
	v_mfma_scale_f32_16x16x128_f8f6f4 v[210:213], v[132:139], v[172:179], 0, v202, v202 op_sel_hi:[0,0,0]
	s_add_i32 m0, s25, 0x2000
	v_mfma_scale_f32_16x16x128_f8f6f4 v[172:175], v[140:147], v[172:179], 0, v202, v202 op_sel_hi:[0,0,0]
	global_load_lds_dwordx4 v206, s[6:7]
	v_mfma_scale_f32_16x16x128_f8f6f4 v[176:179], v[132:139], v[180:187], 0, v202, v202 op_sel_hi:[0,0,0]
	v_mfma_scale_f32_16x16x128_f8f6f4 v[180:183], v[140:147], v[180:187], 0, v202, v202 op_sel_hi:[0,0,0]
	v_mov_b32_e32 v0, v205
	s_barrier
	ds_read_b128 v[84:87], v208 offset:16384
	ds_read_b128 v[88:91], v208 offset:17408
	ds_read_b128 v[92:95], v208 offset:18432
	ds_read_b128 v[96:99], v208 offset:19456
	ds_read_b128 v[100:103], v208 offset:20480
	ds_read_b128 v[104:107], v208 offset:21504
	ds_read_b128 v[108:111], v208 offset:22528
	ds_read_b128 v[112:115], v208 offset:23552
	s_nop 0
	v_mov_b32_e32 v0, v206
	s_nop 0
	s_barrier
	s_waitcnt lgkmcnt(0)
	s_waitcnt lgkmcnt(0)
	v_mfma_scale_f32_16x16x128_f8f6f4 v[80:83], v[52:59], v[84:91], 0, v202, v202 op_sel_hi:[0,0,0]
	v_mfma_scale_f32_16x16x128_f8f6f4 v[76:79], v[68:75], v[84:91], 0, v202, v202 op_sel_hi:[0,0,0]
	s_mov_b32 m0, s18
	v_mfma_scale_f32_16x16x128_f8f6f4 v[64:67], v[52:59], v[92:99], 0, v202, v202 op_sel_hi:[0,0,0]
	global_load_lds_dwordx4 v205, s[10:11]
	v_mfma_scale_f32_16x16x128_f8f6f4 v[60:63], v[68:75], v[92:99], 0, v202, v202 op_sel_hi:[0,0,0]
	v_mfma_scale_f32_16x16x128_f8f6f4 v[184:187], v[52:59], v[100:107], 0, v202, v202 op_sel_hi:[0,0,0]
	s_mov_b32 m0, s19
	v_mfma_scale_f32_16x16x128_f8f6f4 v[214:217], v[68:75], v[100:107], 0, v202, v202 op_sel_hi:[0,0,0]
	global_load_lds_dwordx4 v206, s[10:11]
	v_mfma_scale_f32_16x16x128_f8f6f4 v[218:221], v[52:59], v[108:115], 0, v202, v202 op_sel_hi:[0,0,0]
	v_mfma_scale_f32_16x16x128_f8f6f4 v[222:225], v[68:75], v[108:115], 0, v202, v202 op_sel_hi:[0,0,0]
	s_barrier
	s_add_u32 s26, s6, 0x40000
	s_addc_u32 s27, s7, 0
	v_mov_b32_e32 v0, v205
	s_add_i32 s25, s30, s73
	s_mov_b32 s100, s25
	s_nop 0
	v_mov_b32_e32 v0, v206
	s_add_i32 s101, s25, 0x2000
	s_nop 0
	s_waitcnt vmcnt(4)
	s_barrier
	v_mfma_scale_f32_16x16x128_f8f6f4 v[226:229], v[132:139], v[84:91], 0, v202, v202 op_sel_hi:[0,0,0]
	v_mfma_scale_f32_16x16x128_f8f6f4 v[230:233], v[140:147], v[84:91], 0, v202, v202 op_sel_hi:[0,0,0]
	s_mov_b32 m0, s100
	v_mfma_scale_f32_16x16x128_f8f6f4 v[234:237], v[132:139], v[92:99], 0, v202, v202 op_sel_hi:[0,0,0]
	global_load_lds_dwordx4 v205, s[26:27]
	v_mfma_scale_f32_16x16x128_f8f6f4 v[238:241], v[140:147], v[92:99], 0, v202, v202 op_sel_hi:[0,0,0]
	v_mfma_scale_f32_16x16x128_f8f6f4 v[242:245], v[132:139], v[100:107], 0, v202, v202 op_sel_hi:[0,0,0]
	s_mov_b32 m0, s101
	v_mfma_scale_f32_16x16x128_f8f6f4 v[246:249], v[140:147], v[100:107], 0, v202, v202 op_sel_hi:[0,0,0]
	global_load_lds_dwordx4 v206, s[26:27]
	v_mfma_scale_f32_16x16x128_f8f6f4 v[168:171], v[132:139], v[108:115], 0, v202, v202 op_sel_hi:[0,0,0]
	v_mfma_scale_f32_16x16x128_f8f6f4 v[140:143], v[140:147], v[108:115], 0, v202, v202 op_sel_hi:[0,0,0]
	s_add_i32 s25, 0, 0x18000
	v_add_u32_e32 v0, s25, v207
	s_barrier
	s_nop 2
	ds_read_b128 v[2:5], v0
	ds_read_b128 v[6:9], v0 offset:1024
	ds_read_b128 v[10:13], v0 offset:2048
	ds_read_b128 v[14:17], v0 offset:3072
	s_add_u32 s26, s10, 0x40000
	v_mov_b32_e32 v0, v205
	ds_read_b128 v[18:21], v208 offset:32768
	ds_read_b128 v[22:25], v208 offset:33792
	ds_read_b128 v[26:29], v208 offset:34816
	ds_read_b128 v[30:33], v208 offset:35840
	ds_read_b128 v[34:37], v208 offset:36864
	ds_read_b128 v[38:41], v208 offset:37888
	ds_read_b128 v[42:45], v208 offset:38912
	ds_read_b128 v[46:49], v208 offset:39936
	s_addc_u32 s27, s11, 0
	s_nop 0
	v_mov_b32_e32 v0, v206
	s_nop 0
	s_waitcnt lgkmcnt(8)
	s_barrier
	s_waitcnt lgkmcnt(0)
	s_waitcnt lgkmcnt(0)
	v_mfma_scale_f32_16x16x128_f8f6f4 v[164:167], v[2:9], v[18:25], v[164:167], v202, v202 op_sel_hi:[0,0,0]
	v_mfma_scale_f32_16x16x128_f8f6f4 v[160:163], v[10:17], v[18:25], v[160:163], v202, v202 op_sel_hi:[0,0,0]
	s_mov_b32 m0, s20
	v_mfma_scale_f32_16x16x128_f8f6f4 v[156:159], v[2:9], v[26:33], v[156:159], v202, v202 op_sel_hi:[0,0,0]
	global_load_lds_dwordx4 v205, s[26:27]
	v_mfma_scale_f32_16x16x128_f8f6f4 v[152:155], v[10:17], v[26:33], v[152:155], v202, v202 op_sel_hi:[0,0,0]
	v_mfma_scale_f32_16x16x128_f8f6f4 v[148:151], v[2:9], v[34:41], v[148:151], v202, v202 op_sel_hi:[0,0,0]
	s_mov_b32 m0, s21
	v_mfma_scale_f32_16x16x128_f8f6f4 v[144:147], v[10:17], v[34:41], v[188:191], v202, v202 op_sel_hi:[0,0,0]
	global_load_lds_dwordx4 v206, s[26:27]
	v_mfma_scale_f32_16x16x128_f8f6f4 v[136:139], v[2:9], v[42:49], v[192:195], v202, v202 op_sel_hi:[0,0,0]
	v_mfma_scale_f32_16x16x128_f8f6f4 v[132:135], v[10:17], v[42:49], v[196:199], v202, v202 op_sel_hi:[0,0,0]
	s_barrier
	s_add_i32 s26, 0, 0x1c000
	v_add_u32_e32 v0, s26, v207
	ds_read_b128 v[52:55], v0
	ds_read_b128 v[56:59], v0 offset:1024
	ds_read_b128 v[68:71], v0 offset:2048
	ds_read_b128 v[72:75], v0 offset:3072
	v_mov_b32_e32 v0, v205
	s_add_i32 s25, s25, s73
	v_lshl_add_u64 v[50:51], s[6:7], 0, v[0:1]
	v_lshl_add_u64 v[50:51], v[50:51], 0, s[66:67]
	v_mov_b32_e32 v0, v206
	v_lshl_add_u64 v[50:51], s[6:7], 0, v[0:1]
	v_lshl_add_u64 v[50:51], v[50:51], 0, s[66:67]
	s_barrier
	s_waitcnt lgkmcnt(0)
	s_waitcnt lgkmcnt(0)
	v_mfma_scale_f32_16x16x128_f8f6f4 v[128:131], v[52:59], v[18:25], v[128:131], v202, v202 op_sel_hi:[0,0,0]
	v_mfma_scale_f32_16x16x128_f8f6f4 v[124:127], v[68:75], v[18:25], v[124:127], v202, v202 op_sel_hi:[0,0,0]
	s_add_u32 s98, s6, s66
	s_addc_u32 s99, s7, s67
	s_mov_b32 m0, s25
	v_mfma_scale_f32_16x16x128_f8f6f4 v[120:123], v[52:59], v[26:33], v[120:123], v202, v202 op_sel_hi:[0,0,0]
	global_load_lds_dwordx4 v205, s[98:99]
	v_mfma_scale_f32_16x16x128_f8f6f4 v[116:119], v[68:75], v[26:33], v[116:119], v202, v202 op_sel_hi:[0,0,0]
	v_mfma_scale_f32_16x16x128_f8f6f4 v[112:115], v[52:59], v[34:41], v[210:213], v202, v202 op_sel_hi:[0,0,0]
	s_add_i32 m0, s25, 0x2000
	v_mfma_scale_f32_16x16x128_f8f6f4 v[108:111], v[68:75], v[34:41], v[172:175], v202, v202 op_sel_hi:[0,0,0]
	global_load_lds_dwordx4 v206, s[98:99]
	v_mfma_scale_f32_16x16x128_f8f6f4 v[104:107], v[52:59], v[42:49], v[176:179], v202, v202 op_sel_hi:[0,0,0]
	v_mfma_scale_f32_16x16x128_f8f6f4 v[100:103], v[68:75], v[42:49], v[180:183], v202, v202 op_sel_hi:[0,0,0]
	v_mov_b32_e32 v0, v205
	s_barrier
	ds_read_b128 v[18:21], v208 offset:49152
	ds_read_b128 v[22:25], v208 offset:50176
	ds_read_b128 v[84:87], v208 offset:51200
	ds_read_b128 v[88:91], v208 offset:52224
	ds_read_b128 v[92:95], v208 offset:53248
	ds_read_b128 v[96:99], v208 offset:54272
	ds_read_b128 v[172:175], v208 offset:55296
	ds_read_b128 v[176:179], v208 offset:56320
	v_lshl_add_u64 v[26:27], s[10:11], 0, v[0:1]
	v_lshl_add_u64 v[26:27], v[26:27], 0, s[66:67]
	v_mov_b32_e32 v0, v206
	v_lshl_add_u64 v[26:27], s[10:11], 0, v[0:1]
	v_lshl_add_u64 v[26:27], v[26:27], 0, s[66:67]
	s_barrier
	s_waitcnt lgkmcnt(0)
	s_waitcnt lgkmcnt(0)
	v_mfma_scale_f32_16x16x128_f8f6f4 v[80:83], v[2:9], v[18:25], v[80:83], v202, v202 op_sel_hi:[0,0,0]
	v_mfma_scale_f32_16x16x128_f8f6f4 v[76:79], v[10:17], v[18:25], v[76:79], v202, v202 op_sel_hi:[0,0,0]
	s_add_u32 s98, s10, s66
	s_addc_u32 s99, s11, s67
	s_mov_b32 m0, s22
	v_mfma_scale_f32_16x16x128_f8f6f4 v[64:67], v[2:9], v[84:91], v[64:67], v202, v202 op_sel_hi:[0,0,0]
	global_load_lds_dwordx4 v205, s[98:99]
	v_mfma_scale_f32_16x16x128_f8f6f4 v[60:63], v[10:17], v[84:91], v[60:63], v202, v202 op_sel_hi:[0,0,0]
	v_mfma_scale_f32_16x16x128_f8f6f4 v[48:51], v[2:9], v[92:99], v[184:187], v202, v202 op_sel_hi:[0,0,0]
	s_mov_b32 m0, s34
	v_mfma_scale_f32_16x16x128_f8f6f4 v[44:47], v[10:17], v[92:99], v[214:217], v202, v202 op_sel_hi:[0,0,0]
	global_load_lds_dwordx4 v206, s[98:99]
	v_mfma_scale_f32_16x16x128_f8f6f4 v[40:43], v[2:9], v[172:179], v[218:221], v202, v202 op_sel_hi:[0,0,0]
	v_mfma_scale_f32_16x16x128_f8f6f4 v[36:39], v[10:17], v[172:179], v[222:225], v202, v202 op_sel_hi:[0,0,0]
	s_barrier
	s_add_u32 s6, s6, 0x40080
	s_addc_u32 s7, s7, 0
	v_mov_b32_e32 v0, v205
	s_add_i32 s10, s26, s73
	s_nop 0
	v_mov_b32_e32 v0, v206
	s_nop 0
	s_waitcnt vmcnt(4)
	s_barrier
	v_mfma_scale_f32_16x16x128_f8f6f4 v[32:35], v[52:59], v[18:25], v[226:229], v202, v202 op_sel_hi:[0,0,0]
	v_mfma_scale_f32_16x16x128_f8f6f4 v[28:31], v[68:75], v[18:25], v[230:233], v202, v202 op_sel_hi:[0,0,0]
	s_mov_b32 m0, s10
	v_mfma_scale_f32_16x16x128_f8f6f4 v[24:27], v[52:59], v[84:91], v[234:237], v202, v202 op_sel_hi:[0,0,0]
	global_load_lds_dwordx4 v205, s[6:7]
	v_mfma_scale_f32_16x16x128_f8f6f4 v[20:23], v[68:75], v[84:91], v[238:241], v202, v202 op_sel_hi:[0,0,0]
	v_mfma_scale_f32_16x16x128_f8f6f4 v[16:19], v[52:59], v[92:99], v[242:245], v202, v202 op_sel_hi:[0,0,0]
	s_add_i32 m0, s10, 0x2000
	v_mfma_scale_f32_16x16x128_f8f6f4 v[12:15], v[68:75], v[92:99], v[246:249], v202, v202 op_sel_hi:[0,0,0]
	global_load_lds_dwordx4 v206, s[6:7]
	v_mfma_scale_f32_16x16x128_f8f6f4 v[8:11], v[52:59], v[172:179], v[168:171], v202, v202 op_sel_hi:[0,0,0]
	v_mfma_scale_f32_16x16x128_f8f6f4 v[4:7], v[68:75], v[172:179], v[140:143], v202, v202 op_sel_hi:[0,0,0]
	s_add_i32 s17, s17, 2
	s_add_u32 s4, s4, 0x100
	s_addc_u32 s5, s5, 0
	s_add_u32 s15, s15, 0x100
	s_addc_u32 s16, s16, 0
	s_cmp_gt_u32 s17, 13
	s_barrier
	s_cbranch_scc0 .LBB0_278
	s_branch .Lpeel_exit_1
.LBB0_278:
	s_add_u32 s6, s4, 0xfffc0080
	s_addc_u32 s7, s5, -1
	s_add_i32 s25, 0, 0x10000
	v_add_u32_e32 v0, s25, v207
	ds_read_b128 v[52:55], v0
	ds_read_b128 v[56:59], v0 offset:1024
	ds_read_b128 v[68:71], v0 offset:2048
	ds_read_b128 v[72:75], v0 offset:3072
	s_cmp_eq_u32 s17, 12
	s_cselect_b32 s11, s3, s7
	s_cselect_b32 s10, s9, s6
	s_cselect_b32 s7, s12, s16
	s_cselect_b32 s6, s13, s15
	v_mov_b32_e32 v0, v205
	ds_read_b128 v[84:87], v208
	ds_read_b128 v[88:91], v208 offset:1024
	ds_read_b128 v[92:95], v208 offset:2048
	ds_read_b128 v[96:99], v208 offset:3072
	ds_read_b128 v[172:175], v208 offset:4096
	ds_read_b128 v[176:179], v208 offset:5120
	ds_read_b128 v[180:183], v208 offset:6144
	ds_read_b128 v[184:187], v208 offset:7168
	s_nop 0
	v_mov_b32_e32 v0, v206
	s_nop 0
	s_waitcnt lgkmcnt(8)
	s_barrier
	s_waitcnt lgkmcnt(0)
	s_waitcnt lgkmcnt(0)
	v_mfma_scale_f32_16x16x128_f8f6f4 v[164:167], v[52:59], v[84:91], v[164:167], v202, v202 op_sel_hi:[0,0,0]
	v_mfma_scale_f32_16x16x128_f8f6f4 v[160:163], v[68:75], v[84:91], v[160:163], v202, v202 op_sel_hi:[0,0,0]
	s_add_i32 m0, s18, 0xc000
	v_mfma_scale_f32_16x16x128_f8f6f4 v[156:159], v[52:59], v[92:99], v[156:159], v202, v202 op_sel_hi:[0,0,0]
	global_load_lds_dwordx4 v205, s[4:5]
	v_mfma_scale_f32_16x16x128_f8f6f4 v[152:155], v[68:75], v[92:99], v[152:155], v202, v202 op_sel_hi:[0,0,0]
	v_mfma_scale_f32_16x16x128_f8f6f4 v[148:151], v[52:59], v[172:179], v[148:151], v202, v202 op_sel_hi:[0,0,0]
	s_add_i32 m0, s18, 0xe000
	v_mfma_scale_f32_16x16x128_f8f6f4 v[188:191], v[68:75], v[172:179], v[144:147], v202, v202 op_sel_hi:[0,0,0]
	global_load_lds_dwordx4 v206, s[4:5]
	v_mfma_scale_f32_16x16x128_f8f6f4 v[192:195], v[52:59], v[180:187], v[136:139], v202, v202 op_sel_hi:[0,0,0]
	v_mfma_scale_f32_16x16x128_f8f6f4 v[196:199], v[68:75], v[180:187], v[132:135], v202, v202 op_sel_hi:[0,0,0]
	s_barrier
	s_add_i32 s30, 0, 0x14000
	v_add_u32_e32 v0, s30, v207
	s_nop 2
	ds_read_b128 v[132:135], v0
	ds_read_b128 v[136:139], v0 offset:1024
	ds_read_b128 v[140:143], v0 offset:2048
	ds_read_b128 v[144:147], v0 offset:3072
	v_mov_b32_e32 v0, v205
	s_add_i32 s25, s25, s73
	s_nop 0
	v_mov_b32_e32 v0, v206
	s_nop 0
	s_barrier
	s_waitcnt lgkmcnt(0)
	s_waitcnt lgkmcnt(0)
	v_mfma_scale_f32_16x16x128_f8f6f4 v[128:131], v[132:139], v[84:91], v[128:131], v202, v202 op_sel_hi:[0,0,0]
	v_mfma_scale_f32_16x16x128_f8f6f4 v[124:127], v[140:147], v[84:91], v[124:127], v202, v202 op_sel_hi:[0,0,0]
	s_mov_b32 m0, s25
	v_mfma_scale_f32_16x16x128_f8f6f4 v[120:123], v[132:139], v[92:99], v[120:123], v202, v202 op_sel_hi:[0,0,0]
	global_load_lds_dwordx4 v205, s[6:7]
	v_mfma_scale_f32_16x16x128_f8f6f4 v[116:119], v[140:147], v[92:99], v[116:119], v202, v202 op_sel_hi:[0,0,0]
	v_mfma_scale_f32_16x16x128_f8f6f4 v[210:213], v[132:139], v[172:179], v[112:115], v202, v202 op_sel_hi:[0,0,0]
	s_add_i32 m0, s25, 0x2000
	v_mfma_scale_f32_16x16x128_f8f6f4 v[172:175], v[140:147], v[172:179], v[108:111], v202, v202 op_sel_hi:[0,0,0]
	global_load_lds_dwordx4 v206, s[6:7]
	v_mfma_scale_f32_16x16x128_f8f6f4 v[176:179], v[132:139], v[180:187], v[104:107], v202, v202 op_sel_hi:[0,0,0]
	v_mfma_scale_f32_16x16x128_f8f6f4 v[180:183], v[140:147], v[180:187], v[100:103], v202, v202 op_sel_hi:[0,0,0]
	v_mov_b32_e32 v0, v205
	s_barrier
	ds_read_b128 v[84:87], v208 offset:16384
	ds_read_b128 v[88:91], v208 offset:17408
	ds_read_b128 v[92:95], v208 offset:18432
	ds_read_b128 v[96:99], v208 offset:19456
	ds_read_b128 v[100:103], v208 offset:20480
	ds_read_b128 v[104:107], v208 offset:21504
	ds_read_b128 v[108:111], v208 offset:22528
	ds_read_b128 v[112:115], v208 offset:23552
	s_nop 0
	v_mov_b32_e32 v0, v206
	s_nop 0
	s_barrier
	s_waitcnt lgkmcnt(0)
	s_waitcnt lgkmcnt(0)
	v_mfma_scale_f32_16x16x128_f8f6f4 v[80:83], v[52:59], v[84:91], v[80:83], v202, v202 op_sel_hi:[0,0,0]
	v_mfma_scale_f32_16x16x128_f8f6f4 v[76:79], v[68:75], v[84:91], v[76:79], v202, v202 op_sel_hi:[0,0,0]
	s_mov_b32 m0, s18
	v_mfma_scale_f32_16x16x128_f8f6f4 v[64:67], v[52:59], v[92:99], v[64:67], v202, v202 op_sel_hi:[0,0,0]
	global_load_lds_dwordx4 v205, s[10:11]
	v_mfma_scale_f32_16x16x128_f8f6f4 v[60:63], v[68:75], v[92:99], v[60:63], v202, v202 op_sel_hi:[0,0,0]
	v_mfma_scale_f32_16x16x128_f8f6f4 v[184:187], v[52:59], v[100:107], v[48:51], v202, v202 op_sel_hi:[0,0,0]
	s_mov_b32 m0, s19
	v_mfma_scale_f32_16x16x128_f8f6f4 v[214:217], v[68:75], v[100:107], v[44:47], v202, v202 op_sel_hi:[0,0,0]
	global_load_lds_dwordx4 v206, s[10:11]
	v_mfma_scale_f32_16x16x128_f8f6f4 v[218:221], v[52:59], v[108:115], v[40:43], v202, v202 op_sel_hi:[0,0,0]
	v_mfma_scale_f32_16x16x128_f8f6f4 v[222:225], v[68:75], v[108:115], v[36:39], v202, v202 op_sel_hi:[0,0,0]
	s_barrier
	s_add_u32 s26, s6, 0x40000
	s_addc_u32 s27, s7, 0
	v_mov_b32_e32 v0, v205
	s_add_i32 s25, s30, s73
	s_mov_b32 s100, s25
	s_nop 0
	v_mov_b32_e32 v0, v206
	s_add_i32 s101, s25, 0x2000
	s_nop 0
	s_waitcnt vmcnt(4)
	s_barrier
	v_mfma_scale_f32_16x16x128_f8f6f4 v[226:229], v[132:139], v[84:91], v[32:35], v202, v202 op_sel_hi:[0,0,0]
	v_mfma_scale_f32_16x16x128_f8f6f4 v[230:233], v[140:147], v[84:91], v[28:31], v202, v202 op_sel_hi:[0,0,0]
	s_mov_b32 m0, s100
	v_mfma_scale_f32_16x16x128_f8f6f4 v[234:237], v[132:139], v[92:99], v[24:27], v202, v202 op_sel_hi:[0,0,0]
	global_load_lds_dwordx4 v205, s[26:27]
	v_mfma_scale_f32_16x16x128_f8f6f4 v[238:241], v[140:147], v[92:99], v[20:23], v202, v202 op_sel_hi:[0,0,0]
	v_mfma_scale_f32_16x16x128_f8f6f4 v[242:245], v[132:139], v[100:107], v[16:19], v202, v202 op_sel_hi:[0,0,0]
	s_mov_b32 m0, s101
	v_mfma_scale_f32_16x16x128_f8f6f4 v[246:249], v[140:147], v[100:107], v[12:15], v202, v202 op_sel_hi:[0,0,0]
	global_load_lds_dwordx4 v206, s[26:27]
	v_mfma_scale_f32_16x16x128_f8f6f4 v[168:171], v[132:139], v[108:115], v[8:11], v202, v202 op_sel_hi:[0,0,0]
	v_mfma_scale_f32_16x16x128_f8f6f4 v[140:143], v[140:147], v[108:115], v[4:7], v202, v202 op_sel_hi:[0,0,0]
	s_add_i32 s25, 0, 0x18000
	v_add_u32_e32 v0, s25, v207
	s_barrier
	s_nop 2
	ds_read_b128 v[2:5], v0
	ds_read_b128 v[6:9], v0 offset:1024
	ds_read_b128 v[10:13], v0 offset:2048
	ds_read_b128 v[14:17], v0 offset:3072
	s_add_u32 s26, s10, 0x40000
	v_mov_b32_e32 v0, v205
	ds_read_b128 v[18:21], v208 offset:32768
	ds_read_b128 v[22:25], v208 offset:33792
	ds_read_b128 v[26:29], v208 offset:34816
	ds_read_b128 v[30:33], v208 offset:35840
	ds_read_b128 v[34:37], v208 offset:36864
	ds_read_b128 v[38:41], v208 offset:37888
	ds_read_b128 v[42:45], v208 offset:38912
	ds_read_b128 v[46:49], v208 offset:39936
	s_addc_u32 s27, s11, 0
	s_nop 0
	v_mov_b32_e32 v0, v206
	s_nop 0
	s_waitcnt lgkmcnt(8)
	s_barrier
	s_waitcnt lgkmcnt(0)
	s_waitcnt lgkmcnt(0)
	v_mfma_scale_f32_16x16x128_f8f6f4 v[164:167], v[2:9], v[18:25], v[164:167], v202, v202 op_sel_hi:[0,0,0]
	v_mfma_scale_f32_16x16x128_f8f6f4 v[160:163], v[10:17], v[18:25], v[160:163], v202, v202 op_sel_hi:[0,0,0]
	s_mov_b32 m0, s20
	v_mfma_scale_f32_16x16x128_f8f6f4 v[156:159], v[2:9], v[26:33], v[156:159], v202, v202 op_sel_hi:[0,0,0]
	global_load_lds_dwordx4 v205, s[26:27]
	v_mfma_scale_f32_16x16x128_f8f6f4 v[152:155], v[10:17], v[26:33], v[152:155], v202, v202 op_sel_hi:[0,0,0]
	v_mfma_scale_f32_16x16x128_f8f6f4 v[148:151], v[2:9], v[34:41], v[148:151], v202, v202 op_sel_hi:[0,0,0]
	s_mov_b32 m0, s21
	v_mfma_scale_f32_16x16x128_f8f6f4 v[144:147], v[10:17], v[34:41], v[188:191], v202, v202 op_sel_hi:[0,0,0]
	global_load_lds_dwordx4 v206, s[26:27]
	v_mfma_scale_f32_16x16x128_f8f6f4 v[136:139], v[2:9], v[42:49], v[192:195], v202, v202 op_sel_hi:[0,0,0]
	v_mfma_scale_f32_16x16x128_f8f6f4 v[132:135], v[10:17], v[42:49], v[196:199], v202, v202 op_sel_hi:[0,0,0]
	s_barrier
	s_add_i32 s26, 0, 0x1c000
	v_add_u32_e32 v0, s26, v207
	ds_read_b128 v[52:55], v0
	ds_read_b128 v[56:59], v0 offset:1024
	ds_read_b128 v[68:71], v0 offset:2048
	ds_read_b128 v[72:75], v0 offset:3072
	v_mov_b32_e32 v0, v205
	s_add_i32 s25, s25, s73
	v_lshl_add_u64 v[50:51], s[6:7], 0, v[0:1]
	v_lshl_add_u64 v[50:51], v[50:51], 0, s[66:67]
	v_mov_b32_e32 v0, v206
	v_lshl_add_u64 v[50:51], s[6:7], 0, v[0:1]
	v_lshl_add_u64 v[50:51], v[50:51], 0, s[66:67]
	s_barrier
	s_waitcnt lgkmcnt(0)
	s_waitcnt lgkmcnt(0)
	v_mfma_scale_f32_16x16x128_f8f6f4 v[128:131], v[52:59], v[18:25], v[128:131], v202, v202 op_sel_hi:[0,0,0]
	v_mfma_scale_f32_16x16x128_f8f6f4 v[124:127], v[68:75], v[18:25], v[124:127], v202, v202 op_sel_hi:[0,0,0]
	s_add_u32 s98, s6, s66
	s_addc_u32 s99, s7, s67
	s_mov_b32 m0, s25
	v_mfma_scale_f32_16x16x128_f8f6f4 v[120:123], v[52:59], v[26:33], v[120:123], v202, v202 op_sel_hi:[0,0,0]
	global_load_lds_dwordx4 v205, s[98:99]
	v_mfma_scale_f32_16x16x128_f8f6f4 v[116:119], v[68:75], v[26:33], v[116:119], v202, v202 op_sel_hi:[0,0,0]
	v_mfma_scale_f32_16x16x128_f8f6f4 v[112:115], v[52:59], v[34:41], v[210:213], v202, v202 op_sel_hi:[0,0,0]
	s_add_i32 m0, s25, 0x2000
	v_mfma_scale_f32_16x16x128_f8f6f4 v[108:111], v[68:75], v[34:41], v[172:175], v202, v202 op_sel_hi:[0,0,0]
	global_load_lds_dwordx4 v206, s[98:99]
	v_mfma_scale_f32_16x16x128_f8f6f4 v[104:107], v[52:59], v[42:49], v[176:179], v202, v202 op_sel_hi:[0,0,0]
	v_mfma_scale_f32_16x16x128_f8f6f4 v[100:103], v[68:75], v[42:49], v[180:183], v202, v202 op_sel_hi:[0,0,0]
	v_mov_b32_e32 v0, v205
	s_barrier
	ds_read_b128 v[18:21], v208 offset:49152
	ds_read_b128 v[22:25], v208 offset:50176
	ds_read_b128 v[84:87], v208 offset:51200
	ds_read_b128 v[88:91], v208 offset:52224
	ds_read_b128 v[92:95], v208 offset:53248
	ds_read_b128 v[96:99], v208 offset:54272
	ds_read_b128 v[172:175], v208 offset:55296
	ds_read_b128 v[176:179], v208 offset:56320
	v_lshl_add_u64 v[26:27], s[10:11], 0, v[0:1]
	v_lshl_add_u64 v[26:27], v[26:27], 0, s[66:67]
	v_mov_b32_e32 v0, v206
	v_lshl_add_u64 v[26:27], s[10:11], 0, v[0:1]
	v_lshl_add_u64 v[26:27], v[26:27], 0, s[66:67]
	s_barrier
	s_waitcnt lgkmcnt(0)
	s_waitcnt lgkmcnt(0)
	v_mfma_scale_f32_16x16x128_f8f6f4 v[80:83], v[2:9], v[18:25], v[80:83], v202, v202 op_sel_hi:[0,0,0]
	v_mfma_scale_f32_16x16x128_f8f6f4 v[76:79], v[10:17], v[18:25], v[76:79], v202, v202 op_sel_hi:[0,0,0]
	s_add_u32 s98, s10, s66
	s_addc_u32 s99, s11, s67
	s_mov_b32 m0, s22
	v_mfma_scale_f32_16x16x128_f8f6f4 v[64:67], v[2:9], v[84:91], v[64:67], v202, v202 op_sel_hi:[0,0,0]
	global_load_lds_dwordx4 v205, s[98:99]
	v_mfma_scale_f32_16x16x128_f8f6f4 v[60:63], v[10:17], v[84:91], v[60:63], v202, v202 op_sel_hi:[0,0,0]
	v_mfma_scale_f32_16x16x128_f8f6f4 v[48:51], v[2:9], v[92:99], v[184:187], v202, v202 op_sel_hi:[0,0,0]
	s_mov_b32 m0, s34
	v_mfma_scale_f32_16x16x128_f8f6f4 v[44:47], v[10:17], v[92:99], v[214:217], v202, v202 op_sel_hi:[0,0,0]
	global_load_lds_dwordx4 v206, s[98:99]
	v_mfma_scale_f32_16x16x128_f8f6f4 v[40:43], v[2:9], v[172:179], v[218:221], v202, v202 op_sel_hi:[0,0,0]
	v_mfma_scale_f32_16x16x128_f8f6f4 v[36:39], v[10:17], v[172:179], v[222:225], v202, v202 op_sel_hi:[0,0,0]
	s_barrier
	s_add_u32 s6, s6, 0x40080
	s_addc_u32 s7, s7, 0
	v_mov_b32_e32 v0, v205
	s_add_i32 s10, s26, s73
	s_nop 0
	v_mov_b32_e32 v0, v206
	s_nop 0
	s_waitcnt vmcnt(4)
	s_barrier
	v_mfma_scale_f32_16x16x128_f8f6f4 v[32:35], v[52:59], v[18:25], v[226:229], v202, v202 op_sel_hi:[0,0,0]
	v_mfma_scale_f32_16x16x128_f8f6f4 v[28:31], v[68:75], v[18:25], v[230:233], v202, v202 op_sel_hi:[0,0,0]
	s_mov_b32 m0, s10
	v_mfma_scale_f32_16x16x128_f8f6f4 v[24:27], v[52:59], v[84:91], v[234:237], v202, v202 op_sel_hi:[0,0,0]
	global_load_lds_dwordx4 v205, s[6:7]
	v_mfma_scale_f32_16x16x128_f8f6f4 v[20:23], v[68:75], v[84:91], v[238:241], v202, v202 op_sel_hi:[0,0,0]
	v_mfma_scale_f32_16x16x128_f8f6f4 v[16:19], v[52:59], v[92:99], v[242:245], v202, v202 op_sel_hi:[0,0,0]
	s_add_i32 m0, s10, 0x2000
	v_mfma_scale_f32_16x16x128_f8f6f4 v[12:15], v[68:75], v[92:99], v[246:249], v202, v202 op_sel_hi:[0,0,0]
	global_load_lds_dwordx4 v206, s[6:7]
	v_mfma_scale_f32_16x16x128_f8f6f4 v[8:11], v[52:59], v[172:179], v[168:171], v202, v202 op_sel_hi:[0,0,0]
	v_mfma_scale_f32_16x16x128_f8f6f4 v[4:7], v[68:75], v[172:179], v[140:143], v202, v202 op_sel_hi:[0,0,0]
	s_add_i32 s17, s17, 2
	s_add_u32 s4, s4, 0x100
	s_addc_u32 s5, s5, 0
	s_add_u32 s15, s15, 0x100
	s_addc_u32 s16, s16, 0
	s_cmp_gt_u32 s17, 13
	s_barrier
	s_cbranch_scc0 .LBB0_278

.LBB0_834:
	s_barrier
	s_cmp_lt_i32 s8, 4
	s_cselect_b64 s[38:39], -1, 0
	s_and_b64 vcc, exec, s[38:39]
	s_cbranch_vccnz .LBB0_836
	s_setprio 1
	s_barrier

.LBB0_871:
	s_setprio 0
	s_nop 3
	v_rcp_f32_e32 v8, v82
	v_readlane_b32 s2, v254, 37
	v_readlane_b32 s3, v254, 38
	v_lshlrev_b32_e32 v0, 4, v17
	v_mov_b32_e32 v4, v1
	v_lshl_add_u64 v[2:3], s[2:3], 0, v[178:179]
	v_lshl_add_u64 v[6:7], v[2:3], 0, v[0:1]
	v_mul_f32_e32 v0, v66, v8
	v_mul_f32_e32 v3, v67, v8
	v_mov_b32_e32 v2, v1
	v_cvt_pk_fp8_f32 v2, v0, v3
	v_mul_f32_e32 v0, v70, v8
	v_mul_f32_e32 v3, v71, v8
	v_cvt_pk_fp8_f32 v4, v0, v3
	v_mul_f32_e32 v5, v68, v8
	v_mul_f32_e32 v9, v69, v8
	v_mul_f32_e32 v0, v72, v8
	v_mul_f32_e32 v3, v73, v8
	v_cvt_pk_fp8_f32 v2, v5, v9 op_sel:[0,0,1]
	v_cvt_pk_fp8_f32 v4, v0, v3 op_sel:[0,0,1]
	v_mul_f32_e32 v0, v74, v8
	v_mul_f32_e32 v5, v75, v8
	v_mov_b32_e32 v3, v1
	v_cvt_pk_fp8_f32 v3, v0, v5
	v_mul_f32_e32 v0, v78, v8
	v_mul_f32_e32 v11, v79, v8
	v_mov_b32_e32 v5, v1
	v_cvt_pk_fp8_f32 v5, v0, v11
	v_mul_f32_e32 v9, v76, v8
	v_mul_f32_e32 v10, v77, v8
	v_cvt_pk_fp8_f32 v3, v9, v10 op_sel:[0,0,1]
	v_mul_f32_e32 v0, v80, v8
	v_mul_f32_e32 v9, v81, v8
	v_cvt_pk_fp8_f32 v5, v0, v9 op_sel:[0,0,1]
	v_permlane32_swap_b32_e32 v2, v3
	v_mul_f32_e32 v0, v50, v8
	v_permlane32_swap_b32_e32 v4, v5
	global_store_dwordx4 v[6:7], v[2:5], off
	v_mul_f32_e32 v9, v53, v8
	v_mul_f32_e32 v11, v63, v8
	v_mul_f32_e32 v3, v51, v8
	v_mov_b32_e32 v2, v1
	v_cvt_pk_fp8_f32 v2, v0, v3
	v_mul_f32_e32 v0, v54, v8
	v_mul_f32_e32 v3, v55, v8
	v_mov_b32_e32 v4, v1
	v_cvt_pk_fp8_f32 v4, v0, v3
	v_mul_f32_e32 v5, v52, v8
	v_mul_f32_e32 v0, v56, v8
	v_mul_f32_e32 v3, v57, v8
	v_cvt_pk_fp8_f32 v2, v5, v9 op_sel:[0,0,1]
	v_cvt_pk_fp8_f32 v4, v0, v3 op_sel:[0,0,1]
	v_mul_f32_e32 v0, v58, v8
	v_mul_f32_e32 v5, v59, v8
	v_mov_b32_e32 v3, v1
	v_cvt_pk_fp8_f32 v3, v0, v5
	v_mul_f32_e32 v0, v62, v8
	v_mov_b32_e32 v5, v1
	v_cvt_pk_fp8_f32 v5, v0, v11
	v_mul_f32_e32 v9, v60, v8
	v_mul_f32_e32 v10, v61, v8
	v_cvt_pk_fp8_f32 v3, v9, v10 op_sel:[0,0,1]
	v_mul_f32_e32 v0, v64, v8
	v_mul_f32_e32 v9, v65, v8
	v_cvt_pk_fp8_f32 v5, v0, v9 op_sel:[0,0,1]
	v_permlane32_swap_b32_e32 v2, v3
	v_mul_f32_e32 v0, v34, v8
	v_permlane32_swap_b32_e32 v4, v5
	global_store_dwordx4 v[6:7], v[2:5], off offset:32
	v_mul_f32_e32 v9, v37, v8
	v_mul_f32_e32 v11, v47, v8
	v_mul_f32_e32 v3, v35, v8
	v_mov_b32_e32 v2, v1
	v_cvt_pk_fp8_f32 v2, v0, v3
	v_mul_f32_e32 v0, v38, v8
	v_mul_f32_e32 v3, v39, v8
	v_mov_b32_e32 v4, v1
	v_cvt_pk_fp8_f32 v4, v0, v3
	v_mul_f32_e32 v5, v36, v8
	v_mul_f32_e32 v0, v40, v8
	v_mul_f32_e32 v3, v41, v8
	v_cvt_pk_fp8_f32 v2, v5, v9 op_sel:[0,0,1]
	v_cvt_pk_fp8_f32 v4, v0, v3 op_sel:[0,0,1]
	v_mul_f32_e32 v0, v42, v8
	v_mul_f32_e32 v5, v43, v8
	v_mov_b32_e32 v3, v1
	v_cvt_pk_fp8_f32 v3, v0, v5
	v_mul_f32_e32 v0, v46, v8
	v_mov_b32_e32 v5, v1
	v_cvt_pk_fp8_f32 v5, v0, v11
	v_mul_f32_e32 v9, v44, v8
	v_mul_f32_e32 v10, v45, v8
	v_cvt_pk_fp8_f32 v3, v9, v10 op_sel:[0,0,1]
	v_mul_f32_e32 v0, v48, v8
	v_mul_f32_e32 v9, v49, v8
	v_cvt_pk_fp8_f32 v5, v0, v9 op_sel:[0,0,1]
	v_permlane32_swap_b32_e32 v2, v3
	v_mul_f32_e32 v0, v18, v8
	v_permlane32_swap_b32_e32 v4, v5
	global_store_dwordx4 v[6:7], v[2:5], off offset:64
	v_mul_f32_e32 v9, v21, v8
	v_mul_f32_e32 v11, v31, v8
	v_mul_f32_e32 v3, v19, v8
	v_mov_b32_e32 v2, v1
	v_cvt_pk_fp8_f32 v2, v0, v3
	v_mul_f32_e32 v0, v22, v8
	v_mul_f32_e32 v3, v23, v8
	v_mov_b32_e32 v4, v1
	v_cvt_pk_fp8_f32 v4, v0, v3
	v_mul_f32_e32 v5, v20, v8
	v_mul_f32_e32 v0, v24, v8
	v_mul_f32_e32 v3, v25, v8
	v_cvt_pk_fp8_f32 v2, v5, v9 op_sel:[0,0,1]
	v_cvt_pk_fp8_f32 v4, v0, v3 op_sel:[0,0,1]
	v_mul_f32_e32 v0, v26, v8
	v_mul_f32_e32 v5, v27, v8
	v_mov_b32_e32 v3, v1
	v_cvt_pk_fp8_f32 v3, v0, v5
	v_mul_f32_e32 v0, v30, v8
	v_mov_b32_e32 v5, v1
	v_cvt_pk_fp8_f32 v5, v0, v11
	v_mul_f32_e32 v9, v28, v8
	v_mul_f32_e32 v10, v29, v8
	v_mul_f32_e32 v0, v32, v8
	v_mul_f32_e32 v8, v33, v8
	v_cvt_pk_fp8_f32 v3, v9, v10 op_sel:[0,0,1]
	v_cvt_pk_fp8_f32 v5, v0, v8 op_sel:[0,0,1]
	s_nop 0
	v_permlane32_swap_b32_e32 v2, v3
	v_permlane32_swap_b32_e32 v4, v5
	global_store_dwordx4 v[6:7], v[2:5], off offset:96
	s_waitcnt vmcnt(0) lgkmcnt(0)
	s_barrier

.LBB0_884:
	s_barrier
	s_cmp_lt_i32 s24, 4
	s_cselect_b64 s[54:55], -1, 0
	s_and_b64 vcc, exec, s[54:55]
	s_cbranch_vccnz .LBB0_886
	s_setprio 1
	s_barrier

.LBB0_912:
	s_setprio 0
	s_nop 3
	v_rcp_f32_e32 v8, v96
	v_readlane_b32 s0, v254, 57
	v_readlane_b32 s1, v254, 58
	v_lshlrev_b32_e32 v0, 4, v209
	v_mov_b32_e32 v4, v1
	v_lshl_add_u64 v[2:3], s[0:1], 0, v[192:193]
	v_lshl_add_u64 v[6:7], v[2:3], 0, v[0:1]
	v_mul_f32_e32 v0, v80, v8
	v_mul_f32_e32 v3, v81, v8
	v_mov_b32_e32 v2, v1
	v_cvt_pk_fp8_f32 v2, v0, v3
	v_mul_f32_e32 v0, v84, v8
	v_mul_f32_e32 v3, v85, v8
	v_cvt_pk_fp8_f32 v4, v0, v3
	v_mul_f32_e32 v5, v82, v8
	v_mul_f32_e32 v9, v83, v8
	v_mul_f32_e32 v0, v86, v8
	v_mul_f32_e32 v3, v87, v8
	v_cvt_pk_fp8_f32 v2, v5, v9 op_sel:[0,0,1]
	v_cvt_pk_fp8_f32 v4, v0, v3 op_sel:[0,0,1]
	v_mul_f32_e32 v0, v88, v8
	v_mul_f32_e32 v5, v89, v8
	v_mov_b32_e32 v3, v1
	v_cvt_pk_fp8_f32 v3, v0, v5
	v_mul_f32_e32 v0, v92, v8
	v_mul_f32_e32 v11, v93, v8
	v_mov_b32_e32 v5, v1
	v_cvt_pk_fp8_f32 v5, v0, v11
	v_mul_f32_e32 v9, v90, v8
	v_mul_f32_e32 v10, v91, v8
	v_cvt_pk_fp8_f32 v3, v9, v10 op_sel:[0,0,1]
	v_mul_f32_e32 v0, v94, v8
	v_mul_f32_e32 v9, v95, v8
	v_cvt_pk_fp8_f32 v5, v0, v9 op_sel:[0,0,1]
	v_permlane32_swap_b32_e32 v2, v3
	v_mul_f32_e32 v0, v64, v8
	v_permlane32_swap_b32_e32 v4, v5
	global_store_dwordx4 v[6:7], v[2:5], off
	v_mul_f32_e32 v9, v67, v8
	v_mul_f32_e32 v11, v77, v8
	v_mul_f32_e32 v3, v65, v8
	v_mov_b32_e32 v2, v1
	v_cvt_pk_fp8_f32 v2, v0, v3
	v_mul_f32_e32 v0, v68, v8
	v_mul_f32_e32 v3, v69, v8
	v_mov_b32_e32 v4, v1
	v_cvt_pk_fp8_f32 v4, v0, v3
	v_mul_f32_e32 v5, v66, v8
	v_mul_f32_e32 v0, v70, v8
	v_mul_f32_e32 v3, v71, v8
	v_cvt_pk_fp8_f32 v2, v5, v9 op_sel:[0,0,1]
	v_cvt_pk_fp8_f32 v4, v0, v3 op_sel:[0,0,1]
	v_mul_f32_e32 v0, v72, v8
	v_mul_f32_e32 v5, v73, v8
	v_mov_b32_e32 v3, v1
	v_cvt_pk_fp8_f32 v3, v0, v5
	v_mul_f32_e32 v0, v76, v8
	v_mov_b32_e32 v5, v1
	v_cvt_pk_fp8_f32 v5, v0, v11
	v_mul_f32_e32 v9, v74, v8
	v_mul_f32_e32 v10, v75, v8
	v_cvt_pk_fp8_f32 v3, v9, v10 op_sel:[0,0,1]
	v_mul_f32_e32 v0, v78, v8
	v_mul_f32_e32 v9, v79, v8
	v_cvt_pk_fp8_f32 v5, v0, v9 op_sel:[0,0,1]
	v_permlane32_swap_b32_e32 v2, v3
	v_mul_f32_e32 v0, v48, v8
	v_permlane32_swap_b32_e32 v4, v5
	global_store_dwordx4 v[6:7], v[2:5], off offset:32
	v_mul_f32_e32 v9, v51, v8
	v_mul_f32_e32 v11, v61, v8
	v_mul_f32_e32 v3, v49, v8
	v_mov_b32_e32 v2, v1
	v_cvt_pk_fp8_f32 v2, v0, v3
	v_mul_f32_e32 v0, v52, v8
	v_mul_f32_e32 v3, v53, v8
	v_mov_b32_e32 v4, v1
	v_cvt_pk_fp8_f32 v4, v0, v3
	v_mul_f32_e32 v5, v50, v8
	v_mul_f32_e32 v0, v54, v8
	v_mul_f32_e32 v3, v55, v8
	v_cvt_pk_fp8_f32 v2, v5, v9 op_sel:[0,0,1]
	v_cvt_pk_fp8_f32 v4, v0, v3 op_sel:[0,0,1]
	v_mul_f32_e32 v0, v56, v8
	v_mul_f32_e32 v5, v57, v8
	v_mov_b32_e32 v3, v1
	v_cvt_pk_fp8_f32 v3, v0, v5
	v_mul_f32_e32 v0, v60, v8
	v_mov_b32_e32 v5, v1
	v_cvt_pk_fp8_f32 v5, v0, v11
	v_mul_f32_e32 v9, v58, v8
	v_mul_f32_e32 v10, v59, v8
	v_cvt_pk_fp8_f32 v3, v9, v10 op_sel:[0,0,1]
	v_mul_f32_e32 v0, v62, v8
	v_mul_f32_e32 v9, v63, v8
	v_cvt_pk_fp8_f32 v5, v0, v9 op_sel:[0,0,1]
	v_permlane32_swap_b32_e32 v2, v3
	v_mul_f32_e32 v0, v32, v8
	v_permlane32_swap_b32_e32 v4, v5
	global_store_dwordx4 v[6:7], v[2:5], off offset:64
	v_mul_f32_e32 v9, v35, v8
	v_mul_f32_e32 v11, v45, v8
	v_mul_f32_e32 v3, v33, v8
	v_mov_b32_e32 v2, v1
	v_cvt_pk_fp8_f32 v2, v0, v3
	v_mul_f32_e32 v0, v36, v8
	v_mul_f32_e32 v3, v37, v8
	v_mov_b32_e32 v4, v1
	v_cvt_pk_fp8_f32 v4, v0, v3
	v_mul_f32_e32 v5, v34, v8
	v_mul_f32_e32 v0, v38, v8
	v_mul_f32_e32 v3, v39, v8
	v_cvt_pk_fp8_f32 v2, v5, v9 op_sel:[0,0,1]
	v_cvt_pk_fp8_f32 v4, v0, v3 op_sel:[0,0,1]
	v_mul_f32_e32 v0, v40, v8
	v_mul_f32_e32 v5, v41, v8
	v_mov_b32_e32 v3, v1
	v_cvt_pk_fp8_f32 v3, v0, v5
	v_mul_f32_e32 v0, v44, v8
	v_mov_b32_e32 v5, v1
	v_cvt_pk_fp8_f32 v5, v0, v11
	v_mul_f32_e32 v9, v42, v8
	v_mul_f32_e32 v10, v43, v8
	v_mul_f32_e32 v0, v46, v8
	v_mul_f32_e32 v8, v47, v8
	v_cvt_pk_fp8_f32 v3, v9, v10 op_sel:[0,0,1]
	v_cvt_pk_fp8_f32 v5, v0, v8 op_sel:[0,0,1]
	s_mov_b64 s[54:55], 0x100
	v_permlane32_swap_b32_e32 v2, v3
	v_permlane32_swap_b32_e32 v4, v5
	global_store_dwordx4 v[6:7], v[2:5], off offset:96
	s_waitcnt vmcnt(0) lgkmcnt(0)
	s_barrier
	s_and_b64 vcc, exec, s[50:51]
	s_cbranch_vccnz .LBB0_873

.LBB0_1491:
	s_and_b64 vcc, exec, s[2:3]
	s_cbranch_vccz .LBB0_1228
	v_readlane_b32 s0, v254, 37
	v_readlane_b32 s1, v254, 38
	s_andn2_b64 vcc, exec, s[0:1]
	s_waitcnt vmcnt(0)
	v_mbcnt_lo_u32_b32 v0, -1, 0
	v_mbcnt_hi_u32_b32 v0, -1, v0
	s_cbranch_vccnz .LBB0_1228
	v_lshl_add_u32 v1, v0, 4, s21
	v_ashrrev_i32_e32 v2, 31, v1
	v_lshrrev_b32_e32 v2, 22, v2
	v_add_u32_e32 v2, v1, v2
	v_ashrrev_i32_e32 v2, 10, v2
	v_mul_i32_i24_e32 v3, 0x400, v2
	v_sub_u32_e32 v3, v1, v3
	v_lshrrev_b32_e32 v4, 4, v3
	v_bitop3_b32 v3, v4, v3, 32 bitop3:0x6c
	v_ashrrev_i32_e32 v5, 31, v3
	v_lshrrev_b32_e32 v5, 26, v5
	v_add_u32_e32 v5, v3, v5
	v_lshrrev_b32_e32 v6, 6, v5
	v_and_b32_e32 v5, 0xc0, v5
	v_lshlrev_b32_e32 v4, 3, v2
	v_lshlrev_b32_e32 v2, 5, v2
	v_sub_u32_e32 v3, v3, v5
	v_and_b32_e32 v4, 0x1ffff0, v4
	v_and_b32_e32 v2, 32, v2
	v_ashrrev_i16_sdwa v3, v147, sext(v3) dst_sel:DWORD dst_unused:UNUSED_PAD src0_sel:DWORD src1_sel:BYTE_0
	v_add_u32_sdwa v2, v2, sext(v3) dst_sel:DWORD dst_unused:UNUSED_PAD src0_sel:DWORD src1_sel:WORD_0
	v_add_lshl_u32 v3, v6, v4, 11
	v_add_u32_e32 v1, 0x2000, v1
	v_lshl_add_u32 v148, v2, 1, v3
	v_ashrrev_i32_e32 v2, 31, v1
	v_lshrrev_b32_e32 v2, 22, v2
	v_add_u32_e32 v2, v1, v2
	v_ashrrev_i32_e32 v2, 10, v2
	v_mul_i32_i24_e32 v3, 0x400, v2
	v_sub_u32_e32 v1, v1, v3
	v_lshrrev_b32_e32 v3, 4, v1
	v_bitop3_b32 v1, v3, v1, 32 bitop3:0x6c
	v_ashrrev_i32_e32 v4, 31, v1
	v_lshrrev_b32_e32 v4, 26, v4
	v_add_u32_e32 v4, v1, v4
	v_lshrrev_b32_e32 v5, 6, v4
	v_and_b32_e32 v4, 0xffc0, v4
	v_sub_u32_e32 v1, v1, v4
	v_lshrrev_b16_e32 v4, 7, v1
	v_and_b32_e32 v4, 1, v4
	v_lshlrev_b32_e32 v3, 3, v2
	v_lshlrev_b32_e32 v2, 5, v2
	v_add_u16_e32 v1, v1, v4
	v_and_b32_e32 v3, 0x1ffff0, v3
	v_and_b32_e32 v2, 32, v2
	v_ashrrev_i16_sdwa v1, v147, sext(v1) dst_sel:DWORD dst_unused:UNUSED_PAD src0_sel:DWORD src1_sel:BYTE_0
	v_add_u32_sdwa v1, v2, sext(v1) dst_sel:DWORD dst_unused:UNUSED_PAD src0_sel:DWORD src1_sel:WORD_0
	v_add_lshl_u32 v2, v5, v3, 11
	v_lshl_add_u32 v149, v1, 1, v2
	v_mov_b32_e32 v1, v148
	s_add_i32 s0, s21, 0
	v_readlane_b32 s2, v254, 61
	s_add_i32 m0, s0, 0x10000
	v_readlane_b32 s3, v254, 62
	s_add_i32 s1, s0, 0x2000
	s_add_i32 s8, s0, 0x4000
	s_add_i32 s9, s0, 0x6000
	s_nop 1
	global_load_lds_dwordx4 v1, s[2:3]
	v_mov_b32_e32 v1, v149
	s_add_i32 m0, s0, 0x12000
	s_nop 0
	global_load_lds_dwordx4 v1, s[2:3]
	v_mov_b32_e32 v1, v148
	v_readlane_b32 s2, v254, 59
	s_mov_b32 m0, s0
	v_readlane_b32 s3, v254, 60
	s_nop 4
	global_load_lds_dwordx4 v1, s[2:3]
	v_mov_b32_e32 v1, v149
	s_mov_b32 m0, s1
	s_nop 0
	global_load_lds_dwordx4 v1, s[2:3]
	v_mov_b32_e32 v1, v148
	v_readlane_b32 s2, v252, 28
	s_add_i32 m0, s0, 0x14000
	v_readlane_b32 s3, v252, 29
	s_nop 4
	global_load_lds_dwordx4 v1, s[2:3]
	v_mov_b32_e32 v1, v149
	s_add_i32 m0, s0, 0x16000
	s_nop 0
	global_load_lds_dwordx4 v1, s[2:3]
	v_mov_b32_e32 v1, v148
	v_readlane_b32 s2, v252, 44
	s_mov_b32 m0, s8
	v_readlane_b32 s3, v252, 45
	s_nop 4
	global_load_lds_dwordx4 v1, s[2:3]
	v_mov_b32_e32 v1, v149
	s_mov_b32 m0, s9
	s_nop 0
	global_load_lds_dwordx4 v1, s[2:3]
	v_readlane_b32 s2, v252, 20
	v_readlane_b32 s3, v252, 21
	s_andn2_b64 vcc, exec, s[2:3]
	s_cbranch_vccnz .LBB0_1495
	s_setprio 1
	s_barrier

.Lpeel_2:
	s_add_u32 s24, s2, 0xfffc0080
	s_addc_u32 s25, s3, -1
	s_add_i32 s28, 0, 0x10000
	v_add_u32_e32 v128, s28, v150
	ds_read_b128 v[136:139], v128
	ds_read_b128 v[140:143], v128 offset:1024
	ds_read_b128 v[152:155], v128 offset:2048
	ds_read_b128 v[156:159], v128 offset:3072
	s_cmp_eq_u32 s22, 12
	s_cselect_b32 s41, s49, s25
	s_cselect_b32 s40, s48, s24
	s_cselect_b32 s39, s59, s20
	s_cselect_b32 s38, s58, s7
	v_mov_b32_e32 v128, v148
	ds_read_b128 v[160:163], v151
	ds_read_b128 v[164:167], v151 offset:1024
	ds_read_b128 v[168:171], v151 offset:2048
	ds_read_b128 v[172:175], v151 offset:3072
	ds_read_b128 v[176:179], v151 offset:4096
	ds_read_b128 v[180:183], v151 offset:5120
	ds_read_b128 v[184:187], v151 offset:6144
	ds_read_b128 v[188:191], v151 offset:7168
	s_nop 0
	v_mov_b32_e32 v128, v149
	s_nop 0
	s_waitcnt lgkmcnt(8)
	s_barrier
	s_waitcnt lgkmcnt(0)
	s_waitcnt lgkmcnt(0)
	v_mfma_scale_f32_16x16x128_f8f6f4 v[124:127], v[136:143], v[160:167], 0, v146, v146 op_sel_hi:[0,0,0]
	v_mfma_scale_f32_16x16x128_f8f6f4 v[120:123], v[152:159], v[160:167], 0, v146, v146 op_sel_hi:[0,0,0]
	s_add_i32 m0, s0, 0xc000
	v_mfma_scale_f32_16x16x128_f8f6f4 v[116:119], v[136:143], v[168:175], 0, v146, v146 op_sel_hi:[0,0,0]
	global_load_lds_dwordx4 v148, s[2:3]
	v_mfma_scale_f32_16x16x128_f8f6f4 v[112:115], v[152:159], v[168:175], 0, v146, v146 op_sel_hi:[0,0,0]
	v_mfma_scale_f32_16x16x128_f8f6f4 v[128:131], v[136:143], v[176:183], 0, v146, v146 op_sel_hi:[0,0,0]
	s_add_i32 m0, s0, 0xe000
	v_mfma_scale_f32_16x16x128_f8f6f4 v[192:195], v[152:159], v[176:183], 0, v146, v146 op_sel_hi:[0,0,0]
	global_load_lds_dwordx4 v149, s[2:3]
	v_mfma_scale_f32_16x16x128_f8f6f4 v[196:199], v[136:143], v[184:191], 0, v146, v146 op_sel_hi:[0,0,0]
	v_mfma_scale_f32_16x16x128_f8f6f4 v[200:203], v[152:159], v[184:191], 0, v146, v146 op_sel_hi:[0,0,0]
	s_barrier
	s_add_i32 s29, 0, 0x14000
	s_nop 0
	v_add_u32_e32 v108, s29, v150
	v_mov_b32_e32 v132, v148
	s_add_i32 s24, s28, s21
	ds_read_b128 v[96:99], v108
	ds_read_b128 v[100:103], v108 offset:1024
	ds_read_b128 v[104:107], v108 offset:2048
	ds_read_b128 v[108:111], v108 offset:3072
	s_nop 0
	v_mov_b32_e32 v132, v149
	s_nop 0
	s_barrier
	s_waitcnt lgkmcnt(0)
	s_waitcnt lgkmcnt(0)
	v_mfma_scale_f32_16x16x128_f8f6f4 v[204:207], v[96:103], v[160:167], 0, v146, v146 op_sel_hi:[0,0,0]
	v_mfma_scale_f32_16x16x128_f8f6f4 v[160:163], v[104:111], v[160:167], 0, v146, v146 op_sel_hi:[0,0,0]
	s_mov_b32 m0, s24
	v_mfma_scale_f32_16x16x128_f8f6f4 v[164:167], v[96:103], v[168:175], 0, v146, v146 op_sel_hi:[0,0,0]
	global_load_lds_dwordx4 v148, s[38:39]
	v_mfma_scale_f32_16x16x128_f8f6f4 v[168:171], v[104:111], v[168:175], 0, v146, v146 op_sel_hi:[0,0,0]
	v_mfma_scale_f32_16x16x128_f8f6f4 v[172:175], v[96:103], v[176:183], 0, v146, v146 op_sel_hi:[0,0,0]
	s_add_i32 m0, s24, 0x2000
	v_mfma_scale_f32_16x16x128_f8f6f4 v[176:179], v[104:111], v[176:183], 0, v146, v146 op_sel_hi:[0,0,0]
	global_load_lds_dwordx4 v149, s[38:39]
	v_mfma_scale_f32_16x16x128_f8f6f4 v[180:183], v[96:103], v[184:191], 0, v146, v146 op_sel_hi:[0,0,0]
	v_mfma_scale_f32_16x16x128_f8f6f4 v[184:187], v[104:111], v[184:191], 0, v146, v146 op_sel_hi:[0,0,0]
	v_mov_b32_e32 v132, v148
	s_barrier
	s_nop 2
	ds_read_b128 v[32:35], v151 offset:16384
	ds_read_b128 v[36:39], v151 offset:17408
	ds_read_b128 v[40:43], v151 offset:18432
	ds_read_b128 v[44:47], v151 offset:19456
	ds_read_b128 v[48:51], v151 offset:20480
	ds_read_b128 v[52:55], v151 offset:21504
	ds_read_b128 v[56:59], v151 offset:22528
	ds_read_b128 v[60:63], v151 offset:23552
	s_nop 0
	v_mov_b32_e32 v132, v149
	s_nop 0
	s_barrier
	s_waitcnt lgkmcnt(0)
	s_waitcnt lgkmcnt(0)
	v_mfma_scale_f32_16x16x128_f8f6f4 v[92:95], v[136:143], v[32:39], 0, v146, v146 op_sel_hi:[0,0,0]
	v_mfma_scale_f32_16x16x128_f8f6f4 v[88:91], v[152:159], v[32:39], 0, v146, v146 op_sel_hi:[0,0,0]
	s_mov_b32 m0, s0
	v_mfma_scale_f32_16x16x128_f8f6f4 v[84:87], v[136:143], v[40:47], 0, v146, v146 op_sel_hi:[0,0,0]
	global_load_lds_dwordx4 v148, s[40:41]
	v_mfma_scale_f32_16x16x128_f8f6f4 v[80:83], v[152:159], v[40:47], 0, v146, v146 op_sel_hi:[0,0,0]
	v_mfma_scale_f32_16x16x128_f8f6f4 v[76:79], v[136:143], v[48:55], 0, v146, v146 op_sel_hi:[0,0,0]
	s_mov_b32 m0, s1
	v_mfma_scale_f32_16x16x128_f8f6f4 v[72:75], v[152:159], v[48:55], 0, v146, v146 op_sel_hi:[0,0,0]
	global_load_lds_dwordx4 v149, s[40:41]
	v_mfma_scale_f32_16x16x128_f8f6f4 v[188:191], v[136:143], v[56:63], 0, v146, v146 op_sel_hi:[0,0,0]
	v_mfma_scale_f32_16x16x128_f8f6f4 v[208:211], v[152:159], v[56:63], 0, v146, v146 op_sel_hi:[0,0,0]
	s_barrier
	s_add_u32 s24, s38, 0x40000
	s_addc_u32 s25, s39, 0
	s_nop 2
	v_mov_b32_e32 v64, v148
	s_add_i32 s28, s29, s21
	s_mov_b32 s100, s28
	s_nop 0
	v_mov_b32_e32 v64, v149
	s_add_i32 s101, s28, 0x2000
	s_nop 0
	s_waitcnt vmcnt(4)
	s_barrier
	v_mfma_scale_f32_16x16x128_f8f6f4 v[212:215], v[96:103], v[32:39], 0, v146, v146 op_sel_hi:[0,0,0]
	v_mfma_scale_f32_16x16x128_f8f6f4 v[216:219], v[104:111], v[32:39], 0, v146, v146 op_sel_hi:[0,0,0]
	s_mov_b32 m0, s100
	v_mfma_scale_f32_16x16x128_f8f6f4 v[220:223], v[96:103], v[40:47], 0, v146, v146 op_sel_hi:[0,0,0]
	global_load_lds_dwordx4 v148, s[24:25]
	v_mfma_scale_f32_16x16x128_f8f6f4 v[224:227], v[104:111], v[40:47], 0, v146, v146 op_sel_hi:[0,0,0]
	v_mfma_scale_f32_16x16x128_f8f6f4 v[228:231], v[96:103], v[48:55], 0, v146, v146 op_sel_hi:[0,0,0]
	s_mov_b32 m0, s101
	v_mfma_scale_f32_16x16x128_f8f6f4 v[232:235], v[104:111], v[48:55], 0, v146, v146 op_sel_hi:[0,0,0]
	global_load_lds_dwordx4 v149, s[24:25]
	v_mfma_scale_f32_16x16x128_f8f6f4 v[236:239], v[96:103], v[56:63], 0, v146, v146 op_sel_hi:[0,0,0]
	v_mfma_scale_f32_16x16x128_f8f6f4 v[240:243], v[104:111], v[56:63], 0, v146, v146 op_sel_hi:[0,0,0]
	s_add_i32 s28, 0, 0x18000
	s_nop 1
	v_add_u32_e32 v12, s28, v150
	s_barrier
	s_nop 0
	ds_read_b128 v[0:3], v12
	ds_read_b128 v[4:7], v12 offset:1024
	ds_read_b128 v[8:11], v12 offset:2048
	ds_read_b128 v[12:15], v12 offset:3072
	s_add_u32 s24, s40, 0x40000
	v_mov_b32_e32 v40, v148
	ds_read_b128 v[16:19], v151 offset:32768
	ds_read_b128 v[20:23], v151 offset:33792
	ds_read_b128 v[24:27], v151 offset:34816
	ds_read_b128 v[28:31], v151 offset:35840
	ds_read_b128 v[32:35], v151 offset:36864
	ds_read_b128 v[36:39], v151 offset:37888
	ds_read_b128 v[64:67], v151 offset:38912
	ds_read_b128 v[68:71], v151 offset:39936
	s_addc_u32 s25, s41, 0
	s_nop 0
	v_mov_b32_e32 v40, v149
	s_nop 0
	s_waitcnt lgkmcnt(8)
	s_barrier
	s_waitcnt lgkmcnt(0)
	s_waitcnt lgkmcnt(0)
	v_mfma_scale_f32_16x16x128_f8f6f4 v[124:127], v[0:7], v[16:23], v[124:127], v146, v146 op_sel_hi:[0,0,0]
	v_mfma_scale_f32_16x16x128_f8f6f4 v[120:123], v[8:15], v[16:23], v[120:123], v146, v146 op_sel_hi:[0,0,0]
	s_mov_b32 m0, s8
	v_mfma_scale_f32_16x16x128_f8f6f4 v[116:119], v[0:7], v[24:31], v[116:119], v146, v146 op_sel_hi:[0,0,0]
	global_load_lds_dwordx4 v148, s[24:25]
	v_mfma_scale_f32_16x16x128_f8f6f4 v[112:115], v[8:15], v[24:31], v[112:115], v146, v146 op_sel_hi:[0,0,0]
	v_mfma_scale_f32_16x16x128_f8f6f4 v[108:111], v[0:7], v[32:39], v[128:131], v146, v146 op_sel_hi:[0,0,0]
	s_mov_b32 m0, s9
	v_mfma_scale_f32_16x16x128_f8f6f4 v[104:107], v[8:15], v[32:39], v[192:195], v146, v146 op_sel_hi:[0,0,0]
	global_load_lds_dwordx4 v149, s[24:25]
	v_mfma_scale_f32_16x16x128_f8f6f4 v[100:103], v[0:7], v[64:71], v[196:199], v146, v146 op_sel_hi:[0,0,0]
	v_mfma_scale_f32_16x16x128_f8f6f4 v[96:99], v[8:15], v[64:71], v[200:203], v146, v146 op_sel_hi:[0,0,0]
	s_barrier
	s_add_i32 s29, 0, 0x1c000
	v_add_u32_e32 v40, s29, v150
	v_mov_b32_e32 v132, v148
	ds_read_b128 v[136:139], v40
	ds_read_b128 v[140:143], v40 offset:1024
	ds_read_b128 v[152:155], v40 offset:2048
	ds_read_b128 v[156:159], v40 offset:3072
	s_add_i32 s24, s28, s21
	v_lshl_add_u64 v[40:41], s[38:39], 0, v[132:133]
	v_lshl_add_u64 v[40:41], v[40:41], 0, s[52:53]
	v_mov_b32_e32 v132, v149
	v_lshl_add_u64 v[40:41], s[38:39], 0, v[132:133]
	v_lshl_add_u64 v[40:41], v[40:41], 0, s[52:53]
	s_barrier
	s_waitcnt lgkmcnt(0)
	s_waitcnt lgkmcnt(0)
	v_mfma_scale_f32_16x16x128_f8f6f4 v[60:63], v[136:143], v[16:23], v[204:207], v146, v146 op_sel_hi:[0,0,0]
	v_mfma_scale_f32_16x16x128_f8f6f4 v[56:59], v[152:159], v[16:23], v[160:163], v146, v146 op_sel_hi:[0,0,0]
	s_add_u32 s98, s38, s52
	s_addc_u32 s99, s39, s53
	s_mov_b32 m0, s24
	v_mfma_scale_f32_16x16x128_f8f6f4 v[52:55], v[136:143], v[24:31], v[164:167], v146, v146 op_sel_hi:[0,0,0]
	global_load_lds_dwordx4 v148, s[98:99]
	v_mfma_scale_f32_16x16x128_f8f6f4 v[48:51], v[152:159], v[24:31], v[168:171], v146, v146 op_sel_hi:[0,0,0]
	v_mfma_scale_f32_16x16x128_f8f6f4 v[44:47], v[136:143], v[32:39], v[172:175], v146, v146 op_sel_hi:[0,0,0]
	s_add_i32 m0, s24, 0x2000
	v_mfma_scale_f32_16x16x128_f8f6f4 v[40:43], v[152:159], v[32:39], v[176:179], v146, v146 op_sel_hi:[0,0,0]
	global_load_lds_dwordx4 v149, s[98:99]
	v_mfma_scale_f32_16x16x128_f8f6f4 v[36:39], v[136:143], v[64:71], v[180:183], v146, v146 op_sel_hi:[0,0,0]
	v_mfma_scale_f32_16x16x128_f8f6f4 v[32:35], v[152:159], v[64:71], v[184:187], v146, v146 op_sel_hi:[0,0,0]
	v_mov_b32_e32 v132, v148
	s_barrier
	ds_read_b128 v[16:19], v151 offset:49152
	ds_read_b128 v[20:23], v151 offset:50176
	ds_read_b128 v[160:163], v151 offset:51200
	ds_read_b128 v[164:167], v151 offset:52224
	ds_read_b128 v[168:171], v151 offset:53248
	ds_read_b128 v[172:175], v151 offset:54272
	ds_read_b128 v[176:179], v151 offset:55296
	ds_read_b128 v[180:183], v151 offset:56320
	v_lshl_add_u64 v[24:25], s[40:41], 0, v[132:133]
	v_lshl_add_u64 v[24:25], v[24:25], 0, s[52:53]
	v_mov_b32_e32 v132, v149
	v_lshl_add_u64 v[24:25], s[40:41], 0, v[132:133]
	v_lshl_add_u64 v[24:25], v[24:25], 0, s[52:53]
	s_barrier
	s_waitcnt lgkmcnt(0)
	s_waitcnt lgkmcnt(0)
	v_mfma_scale_f32_16x16x128_f8f6f4 v[92:95], v[0:7], v[16:23], v[92:95], v146, v146 op_sel_hi:[0,0,0]
	v_mfma_scale_f32_16x16x128_f8f6f4 v[88:91], v[8:15], v[16:23], v[88:91], v146, v146 op_sel_hi:[0,0,0]
	s_add_u32 s98, s40, s52
	s_addc_u32 s99, s41, s53
	s_mov_b32 m0, s10
	v_mfma_scale_f32_16x16x128_f8f6f4 v[84:87], v[0:7], v[160:167], v[84:87], v146, v146 op_sel_hi:[0,0,0]
	global_load_lds_dwordx4 v148, s[98:99]
	v_mfma_scale_f32_16x16x128_f8f6f4 v[80:83], v[8:15], v[160:167], v[80:83], v146, v146 op_sel_hi:[0,0,0]
	v_mfma_scale_f32_16x16x128_f8f6f4 v[76:79], v[0:7], v[168:175], v[76:79], v146, v146 op_sel_hi:[0,0,0]
	s_mov_b32 m0, s11
	v_mfma_scale_f32_16x16x128_f8f6f4 v[72:75], v[8:15], v[168:175], v[72:75], v146, v146 op_sel_hi:[0,0,0]
	global_load_lds_dwordx4 v149, s[98:99]
	v_mfma_scale_f32_16x16x128_f8f6f4 v[68:71], v[0:7], v[176:183], v[188:191], v146, v146 op_sel_hi:[0,0,0]
	v_mfma_scale_f32_16x16x128_f8f6f4 v[64:67], v[8:15], v[176:183], v[208:211], v146, v146 op_sel_hi:[0,0,0]
	s_barrier
	s_add_u32 s24, s38, 0x40080
	s_addc_u32 s25, s39, 0
	v_mov_b32_e32 v0, v148
	s_add_i32 s28, s29, s21
	s_nop 0
	v_mov_b32_e32 v0, v149
	s_nop 0
	s_waitcnt vmcnt(4)
	s_barrier
	v_mfma_scale_f32_16x16x128_f8f6f4 v[28:31], v[136:143], v[16:23], v[212:215], v146, v146 op_sel_hi:[0,0,0]
	v_mfma_scale_f32_16x16x128_f8f6f4 v[24:27], v[152:159], v[16:23], v[216:219], v146, v146 op_sel_hi:[0,0,0]
	s_mov_b32 m0, s28
	v_mfma_scale_f32_16x16x128_f8f6f4 v[20:23], v[136:143], v[160:167], v[220:223], v146, v146 op_sel_hi:[0,0,0]
	global_load_lds_dwordx4 v148, s[24:25]
	v_mfma_scale_f32_16x16x128_f8f6f4 v[16:19], v[152:159], v[160:167], v[224:227], v146, v146 op_sel_hi:[0,0,0]
	v_mfma_scale_f32_16x16x128_f8f6f4 v[12:15], v[136:143], v[168:175], v[228:231], v146, v146 op_sel_hi:[0,0,0]
	s_add_i32 m0, s28, 0x2000
	v_mfma_scale_f32_16x16x128_f8f6f4 v[8:11], v[152:159], v[168:175], v[232:235], v146, v146 op_sel_hi:[0,0,0]
	global_load_lds_dwordx4 v149, s[24:25]
	v_mfma_scale_f32_16x16x128_f8f6f4 v[4:7], v[136:143], v[176:183], v[236:239], v146, v146 op_sel_hi:[0,0,0]
	v_mfma_scale_f32_16x16x128_f8f6f4 v[0:3], v[152:159], v[176:183], v[240:243], v146, v146 op_sel_hi:[0,0,0]
	s_add_i32 s22, s22, 2
	s_add_u32 s2, s2, 0x100
	s_addc_u32 s3, s3, 0
	s_add_u32 s7, s7, 0x100
	s_addc_u32 s20, s20, 0
	s_cmp_gt_u32 s22, 13
	s_barrier
	s_cbranch_scc0 .LBB0_1503
	s_branch .Lpeel_exit_2
.LBB0_1503:
	s_add_u32 s24, s2, 0xfffc0080
	s_addc_u32 s25, s3, -1
	s_add_i32 s28, 0, 0x10000
	v_add_u32_e32 v128, s28, v150
	ds_read_b128 v[136:139], v128
	ds_read_b128 v[140:143], v128 offset:1024
	ds_read_b128 v[152:155], v128 offset:2048
	ds_read_b128 v[156:159], v128 offset:3072
	s_cmp_eq_u32 s22, 12
	s_cselect_b32 s41, s49, s25
	s_cselect_b32 s40, s48, s24
	s_cselect_b32 s39, s59, s20
	s_cselect_b32 s38, s58, s7
	v_mov_b32_e32 v128, v148
	ds_read_b128 v[160:163], v151
	ds_read_b128 v[164:167], v151 offset:1024
	ds_read_b128 v[168:171], v151 offset:2048
	ds_read_b128 v[172:175], v151 offset:3072
	ds_read_b128 v[176:179], v151 offset:4096
	ds_read_b128 v[180:183], v151 offset:5120
	ds_read_b128 v[184:187], v151 offset:6144
	ds_read_b128 v[188:191], v151 offset:7168
	s_nop 0
	v_mov_b32_e32 v128, v149
	s_nop 0
	s_waitcnt lgkmcnt(8)
	s_barrier
	s_waitcnt lgkmcnt(0)
	s_waitcnt lgkmcnt(0)
	v_mfma_scale_f32_16x16x128_f8f6f4 v[124:127], v[136:143], v[160:167], v[124:127], v146, v146 op_sel_hi:[0,0,0]
	v_mfma_scale_f32_16x16x128_f8f6f4 v[120:123], v[152:159], v[160:167], v[120:123], v146, v146 op_sel_hi:[0,0,0]
	s_add_i32 m0, s0, 0xc000
	v_mfma_scale_f32_16x16x128_f8f6f4 v[116:119], v[136:143], v[168:175], v[116:119], v146, v146 op_sel_hi:[0,0,0]
	global_load_lds_dwordx4 v148, s[2:3]
	v_mfma_scale_f32_16x16x128_f8f6f4 v[112:115], v[152:159], v[168:175], v[112:115], v146, v146 op_sel_hi:[0,0,0]
	v_mfma_scale_f32_16x16x128_f8f6f4 v[128:131], v[136:143], v[176:183], v[108:111], v146, v146 op_sel_hi:[0,0,0]
	s_add_i32 m0, s0, 0xe000
	v_mfma_scale_f32_16x16x128_f8f6f4 v[192:195], v[152:159], v[176:183], v[104:107], v146, v146 op_sel_hi:[0,0,0]
	global_load_lds_dwordx4 v149, s[2:3]
	v_mfma_scale_f32_16x16x128_f8f6f4 v[196:199], v[136:143], v[184:191], v[100:103], v146, v146 op_sel_hi:[0,0,0]
	v_mfma_scale_f32_16x16x128_f8f6f4 v[200:203], v[152:159], v[184:191], v[96:99], v146, v146 op_sel_hi:[0,0,0]
	s_barrier
	s_add_i32 s29, 0, 0x14000
	s_nop 0
	v_add_u32_e32 v108, s29, v150
	v_mov_b32_e32 v132, v148
	s_add_i32 s24, s28, s21
	ds_read_b128 v[96:99], v108
	ds_read_b128 v[100:103], v108 offset:1024
	ds_read_b128 v[104:107], v108 offset:2048
	ds_read_b128 v[108:111], v108 offset:3072
	s_nop 0
	v_mov_b32_e32 v132, v149
	s_nop 0
	s_barrier
	s_waitcnt lgkmcnt(0)
	s_waitcnt lgkmcnt(0)
	v_mfma_scale_f32_16x16x128_f8f6f4 v[204:207], v[96:103], v[160:167], v[60:63], v146, v146 op_sel_hi:[0,0,0]
	v_mfma_scale_f32_16x16x128_f8f6f4 v[160:163], v[104:111], v[160:167], v[56:59], v146, v146 op_sel_hi:[0,0,0]
	s_mov_b32 m0, s24
	v_mfma_scale_f32_16x16x128_f8f6f4 v[164:167], v[96:103], v[168:175], v[52:55], v146, v146 op_sel_hi:[0,0,0]
	global_load_lds_dwordx4 v148, s[38:39]
	v_mfma_scale_f32_16x16x128_f8f6f4 v[168:171], v[104:111], v[168:175], v[48:51], v146, v146 op_sel_hi:[0,0,0]
	v_mfma_scale_f32_16x16x128_f8f6f4 v[172:175], v[96:103], v[176:183], v[44:47], v146, v146 op_sel_hi:[0,0,0]
	s_add_i32 m0, s24, 0x2000
	v_mfma_scale_f32_16x16x128_f8f6f4 v[176:179], v[104:111], v[176:183], v[40:43], v146, v146 op_sel_hi:[0,0,0]
	global_load_lds_dwordx4 v149, s[38:39]
	v_mfma_scale_f32_16x16x128_f8f6f4 v[180:183], v[96:103], v[184:191], v[36:39], v146, v146 op_sel_hi:[0,0,0]
	v_mfma_scale_f32_16x16x128_f8f6f4 v[184:187], v[104:111], v[184:191], v[32:35], v146, v146 op_sel_hi:[0,0,0]
	v_mov_b32_e32 v132, v148
	s_barrier
	s_nop 2
	ds_read_b128 v[32:35], v151 offset:16384
	ds_read_b128 v[36:39], v151 offset:17408
	ds_read_b128 v[40:43], v151 offset:18432
	ds_read_b128 v[44:47], v151 offset:19456
	ds_read_b128 v[48:51], v151 offset:20480
	ds_read_b128 v[52:55], v151 offset:21504
	ds_read_b128 v[56:59], v151 offset:22528
	ds_read_b128 v[60:63], v151 offset:23552
	s_nop 0
	v_mov_b32_e32 v132, v149
	s_nop 0
	s_barrier
	s_waitcnt lgkmcnt(0)
	s_waitcnt lgkmcnt(0)
	v_mfma_scale_f32_16x16x128_f8f6f4 v[92:95], v[136:143], v[32:39], v[92:95], v146, v146 op_sel_hi:[0,0,0]
	v_mfma_scale_f32_16x16x128_f8f6f4 v[88:91], v[152:159], v[32:39], v[88:91], v146, v146 op_sel_hi:[0,0,0]
	s_mov_b32 m0, s0
	v_mfma_scale_f32_16x16x128_f8f6f4 v[84:87], v[136:143], v[40:47], v[84:87], v146, v146 op_sel_hi:[0,0,0]
	global_load_lds_dwordx4 v148, s[40:41]
	v_mfma_scale_f32_16x16x128_f8f6f4 v[80:83], v[152:159], v[40:47], v[80:83], v146, v146 op_sel_hi:[0,0,0]
	v_mfma_scale_f32_16x16x128_f8f6f4 v[76:79], v[136:143], v[48:55], v[76:79], v146, v146 op_sel_hi:[0,0,0]
	s_mov_b32 m0, s1
	v_mfma_scale_f32_16x16x128_f8f6f4 v[72:75], v[152:159], v[48:55], v[72:75], v146, v146 op_sel_hi:[0,0,0]
	global_load_lds_dwordx4 v149, s[40:41]
	v_mfma_scale_f32_16x16x128_f8f6f4 v[188:191], v[136:143], v[56:63], v[68:71], v146, v146 op_sel_hi:[0,0,0]
	v_mfma_scale_f32_16x16x128_f8f6f4 v[208:211], v[152:159], v[56:63], v[64:67], v146, v146 op_sel_hi:[0,0,0]
	s_barrier
	s_add_u32 s24, s38, 0x40000
	s_addc_u32 s25, s39, 0
	s_nop 2
	v_mov_b32_e32 v64, v148
	s_add_i32 s28, s29, s21
	s_mov_b32 s100, s28
	s_nop 0
	v_mov_b32_e32 v64, v149
	s_add_i32 s101, s28, 0x2000
	s_nop 0
	s_waitcnt vmcnt(4)
	s_barrier
	v_mfma_scale_f32_16x16x128_f8f6f4 v[212:215], v[96:103], v[32:39], v[28:31], v146, v146 op_sel_hi:[0,0,0]
	v_mfma_scale_f32_16x16x128_f8f6f4 v[216:219], v[104:111], v[32:39], v[24:27], v146, v146 op_sel_hi:[0,0,0]
	s_mov_b32 m0, s100
	v_mfma_scale_f32_16x16x128_f8f6f4 v[220:223], v[96:103], v[40:47], v[20:23], v146, v146 op_sel_hi:[0,0,0]
	global_load_lds_dwordx4 v148, s[24:25]
	v_mfma_scale_f32_16x16x128_f8f6f4 v[224:227], v[104:111], v[40:47], v[16:19], v146, v146 op_sel_hi:[0,0,0]
	v_mfma_scale_f32_16x16x128_f8f6f4 v[228:231], v[96:103], v[48:55], v[12:15], v146, v146 op_sel_hi:[0,0,0]
	s_mov_b32 m0, s101
	v_mfma_scale_f32_16x16x128_f8f6f4 v[232:235], v[104:111], v[48:55], v[8:11], v146, v146 op_sel_hi:[0,0,0]
	global_load_lds_dwordx4 v149, s[24:25]
	v_mfma_scale_f32_16x16x128_f8f6f4 v[236:239], v[96:103], v[56:63], v[4:7], v146, v146 op_sel_hi:[0,0,0]
	v_mfma_scale_f32_16x16x128_f8f6f4 v[240:243], v[104:111], v[56:63], v[0:3], v146, v146 op_sel_hi:[0,0,0]
	s_add_i32 s28, 0, 0x18000
	s_nop 1
	v_add_u32_e32 v12, s28, v150
	s_barrier
	s_nop 0
	ds_read_b128 v[0:3], v12
	ds_read_b128 v[4:7], v12 offset:1024
	ds_read_b128 v[8:11], v12 offset:2048
	ds_read_b128 v[12:15], v12 offset:3072
	s_add_u32 s24, s40, 0x40000
	v_mov_b32_e32 v40, v148
	ds_read_b128 v[16:19], v151 offset:32768
	ds_read_b128 v[20:23], v151 offset:33792
	ds_read_b128 v[24:27], v151 offset:34816
	ds_read_b128 v[28:31], v151 offset:35840
	ds_read_b128 v[32:35], v151 offset:36864
	ds_read_b128 v[36:39], v151 offset:37888
	ds_read_b128 v[64:67], v151 offset:38912
	ds_read_b128 v[68:71], v151 offset:39936
	s_addc_u32 s25, s41, 0
	s_nop 0
	v_mov_b32_e32 v40, v149
	s_nop 0
	s_waitcnt lgkmcnt(8)
	s_barrier
	s_waitcnt lgkmcnt(0)
	s_waitcnt lgkmcnt(0)
	v_mfma_scale_f32_16x16x128_f8f6f4 v[124:127], v[0:7], v[16:23], v[124:127], v146, v146 op_sel_hi:[0,0,0]
	v_mfma_scale_f32_16x16x128_f8f6f4 v[120:123], v[8:15], v[16:23], v[120:123], v146, v146 op_sel_hi:[0,0,0]
	s_mov_b32 m0, s8
	v_mfma_scale_f32_16x16x128_f8f6f4 v[116:119], v[0:7], v[24:31], v[116:119], v146, v146 op_sel_hi:[0,0,0]
	global_load_lds_dwordx4 v148, s[24:25]
	v_mfma_scale_f32_16x16x128_f8f6f4 v[112:115], v[8:15], v[24:31], v[112:115], v146, v146 op_sel_hi:[0,0,0]
	v_mfma_scale_f32_16x16x128_f8f6f4 v[108:111], v[0:7], v[32:39], v[128:131], v146, v146 op_sel_hi:[0,0,0]
	s_mov_b32 m0, s9
	v_mfma_scale_f32_16x16x128_f8f6f4 v[104:107], v[8:15], v[32:39], v[192:195], v146, v146 op_sel_hi:[0,0,0]
	global_load_lds_dwordx4 v149, s[24:25]
	v_mfma_scale_f32_16x16x128_f8f6f4 v[100:103], v[0:7], v[64:71], v[196:199], v146, v146 op_sel_hi:[0,0,0]
	v_mfma_scale_f32_16x16x128_f8f6f4 v[96:99], v[8:15], v[64:71], v[200:203], v146, v146 op_sel_hi:[0,0,0]
	s_barrier
	s_add_i32 s29, 0, 0x1c000
	v_add_u32_e32 v40, s29, v150
	v_mov_b32_e32 v132, v148
	ds_read_b128 v[136:139], v40
	ds_read_b128 v[140:143], v40 offset:1024
	ds_read_b128 v[152:155], v40 offset:2048
	ds_read_b128 v[156:159], v40 offset:3072
	s_add_i32 s24, s28, s21
	v_lshl_add_u64 v[40:41], s[38:39], 0, v[132:133]
	v_lshl_add_u64 v[40:41], v[40:41], 0, s[52:53]
	v_mov_b32_e32 v132, v149
	v_lshl_add_u64 v[40:41], s[38:39], 0, v[132:133]
	v_lshl_add_u64 v[40:41], v[40:41], 0, s[52:53]
	s_barrier
	s_waitcnt lgkmcnt(0)
	s_waitcnt lgkmcnt(0)
	v_mfma_scale_f32_16x16x128_f8f6f4 v[60:63], v[136:143], v[16:23], v[204:207], v146, v146 op_sel_hi:[0,0,0]
	v_mfma_scale_f32_16x16x128_f8f6f4 v[56:59], v[152:159], v[16:23], v[160:163], v146, v146 op_sel_hi:[0,0,0]
	s_add_u32 s98, s38, s52
	s_addc_u32 s99, s39, s53
	s_mov_b32 m0, s24
	v_mfma_scale_f32_16x16x128_f8f6f4 v[52:55], v[136:143], v[24:31], v[164:167], v146, v146 op_sel_hi:[0,0,0]
	global_load_lds_dwordx4 v148, s[98:99]
	v_mfma_scale_f32_16x16x128_f8f6f4 v[48:51], v[152:159], v[24:31], v[168:171], v146, v146 op_sel_hi:[0,0,0]
	v_mfma_scale_f32_16x16x128_f8f6f4 v[44:47], v[136:143], v[32:39], v[172:175], v146, v146 op_sel_hi:[0,0,0]
	s_add_i32 m0, s24, 0x2000
	v_mfma_scale_f32_16x16x128_f8f6f4 v[40:43], v[152:159], v[32:39], v[176:179], v146, v146 op_sel_hi:[0,0,0]
	global_load_lds_dwordx4 v149, s[98:99]
	v_mfma_scale_f32_16x16x128_f8f6f4 v[36:39], v[136:143], v[64:71], v[180:183], v146, v146 op_sel_hi:[0,0,0]
	v_mfma_scale_f32_16x16x128_f8f6f4 v[32:35], v[152:159], v[64:71], v[184:187], v146, v146 op_sel_hi:[0,0,0]
	v_mov_b32_e32 v132, v148
	s_barrier
	ds_read_b128 v[16:19], v151 offset:49152
	ds_read_b128 v[20:23], v151 offset:50176
	ds_read_b128 v[160:163], v151 offset:51200
	ds_read_b128 v[164:167], v151 offset:52224
	ds_read_b128 v[168:171], v151 offset:53248
	ds_read_b128 v[172:175], v151 offset:54272
	ds_read_b128 v[176:179], v151 offset:55296
	ds_read_b128 v[180:183], v151 offset:56320
	v_lshl_add_u64 v[24:25], s[40:41], 0, v[132:133]
	v_lshl_add_u64 v[24:25], v[24:25], 0, s[52:53]
	v_mov_b32_e32 v132, v149
	v_lshl_add_u64 v[24:25], s[40:41], 0, v[132:133]
	v_lshl_add_u64 v[24:25], v[24:25], 0, s[52:53]
	s_barrier
	s_waitcnt lgkmcnt(0)
	s_waitcnt lgkmcnt(0)
	v_mfma_scale_f32_16x16x128_f8f6f4 v[92:95], v[0:7], v[16:23], v[92:95], v146, v146 op_sel_hi:[0,0,0]
	v_mfma_scale_f32_16x16x128_f8f6f4 v[88:91], v[8:15], v[16:23], v[88:91], v146, v146 op_sel_hi:[0,0,0]
	s_add_u32 s98, s40, s52
	s_addc_u32 s99, s41, s53
	s_mov_b32 m0, s10
	v_mfma_scale_f32_16x16x128_f8f6f4 v[84:87], v[0:7], v[160:167], v[84:87], v146, v146 op_sel_hi:[0,0,0]
	global_load_lds_dwordx4 v148, s[98:99]
	v_mfma_scale_f32_16x16x128_f8f6f4 v[80:83], v[8:15], v[160:167], v[80:83], v146, v146 op_sel_hi:[0,0,0]
	v_mfma_scale_f32_16x16x128_f8f6f4 v[76:79], v[0:7], v[168:175], v[76:79], v146, v146 op_sel_hi:[0,0,0]
	s_mov_b32 m0, s11
	v_mfma_scale_f32_16x16x128_f8f6f4 v[72:75], v[8:15], v[168:175], v[72:75], v146, v146 op_sel_hi:[0,0,0]
	global_load_lds_dwordx4 v149, s[98:99]
	v_mfma_scale_f32_16x16x128_f8f6f4 v[68:71], v[0:7], v[176:183], v[188:191], v146, v146 op_sel_hi:[0,0,0]
	v_mfma_scale_f32_16x16x128_f8f6f4 v[64:67], v[8:15], v[176:183], v[208:211], v146, v146 op_sel_hi:[0,0,0]
	s_barrier
	s_add_u32 s24, s38, 0x40080
	s_addc_u32 s25, s39, 0
	v_mov_b32_e32 v0, v148
	s_add_i32 s28, s29, s21
	s_nop 0
	v_mov_b32_e32 v0, v149
	s_nop 0
	s_waitcnt vmcnt(4)
	s_barrier
	v_mfma_scale_f32_16x16x128_f8f6f4 v[28:31], v[136:143], v[16:23], v[212:215], v146, v146 op_sel_hi:[0,0,0]
	v_mfma_scale_f32_16x16x128_f8f6f4 v[24:27], v[152:159], v[16:23], v[216:219], v146, v146 op_sel_hi:[0,0,0]
	s_mov_b32 m0, s28
	v_mfma_scale_f32_16x16x128_f8f6f4 v[20:23], v[136:143], v[160:167], v[220:223], v146, v146 op_sel_hi:[0,0,0]
	global_load_lds_dwordx4 v148, s[24:25]
	v_mfma_scale_f32_16x16x128_f8f6f4 v[16:19], v[152:159], v[160:167], v[224:227], v146, v146 op_sel_hi:[0,0,0]
	v_mfma_scale_f32_16x16x128_f8f6f4 v[12:15], v[136:143], v[168:175], v[228:231], v146, v146 op_sel_hi:[0,0,0]
	s_add_i32 m0, s28, 0x2000
	v_mfma_scale_f32_16x16x128_f8f6f4 v[8:11], v[152:159], v[168:175], v[232:235], v146, v146 op_sel_hi:[0,0,0]
	global_load_lds_dwordx4 v149, s[24:25]
	v_mfma_scale_f32_16x16x128_f8f6f4 v[4:7], v[136:143], v[176:183], v[236:239], v146, v146 op_sel_hi:[0,0,0]
	v_mfma_scale_f32_16x16x128_f8f6f4 v[0:3], v[152:159], v[176:183], v[240:243], v146, v146 op_sel_hi:[0,0,0]
	s_add_i32 s22, s22, 2
	s_add_u32 s2, s2, 0x100
	s_addc_u32 s3, s3, 0
	s_add_u32 s7, s7, 0x100
	s_addc_u32 s20, s20, 0
	s_cmp_gt_u32 s22, 13
	s_barrier
	s_cbranch_scc0 .LBB0_1503

.LBB0_1932:
	s_mov_b64 s[98:99], exec
	s_mov_b64 exec, -1
	v_mbcnt_lo_u32_b32 v0, -1, 0
	v_mbcnt_hi_u32_b32 v0, -1, v0
	v_min_u32_e32 v0, 14, v0
	v_lshl_add_u32 v0, v0, 2, s3
	ds_read_b32 v0, v0
	s_waitcnt lgkmcnt(0)
	v_cmp_ge_i32_e32 vcc, s59, v0
	s_mov_b64 exec, s[98:99]
	s_and_b32 s8, vcc_lo, 0x7fff
	s_bcnt1_i32_b32 s8, s8
	s_add_i32 s3, s3, 60
	s_mov_b32 s2, 16
	s_cmp_eq_u32 s2, 16
	s_add_u32 s10, s14, 0x249c8000
	s_addc_u32 s11, s15, 0
	s_add_u32 s2, s14, 0x39c8000
	s_addc_u32 s3, s15, 0
	s_add_u32 s21, s14, 0x4c8000
	v_add_u32_e32 v0, s4, v176
	v_readlane_b32 s9, v252, 10
	s_addc_u32 s33, s15, 0
	v_readlane_b32 s5, v252, 2
	v_ashrrev_i32_e32 v1, 31, v0
	s_lshl_b32 s42, s9, 10
	s_mul_i32 s9, s59, -11
	s_lshr_b32 s5, s5, 8
	v_lshrrev_b32_e32 v1, 26, v1
	s_add_i32 s30, s9, s0
	s_mul_i32 s12, s8, 0x580000
	v_lshlrev_b32_e32 v2, 4, v0
	v_add_u32_e32 v1, v0, v1
	v_bfe_i32 v0, v0, 27, 1
	s_mul_hi_u32 s9, s8, 0x580000
	s_add_u32 s18, s2, s12
	v_lshrrev_b32_e32 v0, 22, v0
	s_addc_u32 s9, s3, s9
	s_ashr_i32 s31, s30, 31
	v_add_u32_e32 v0, v2, v0
	s_lshl_b64 s[12:13], s[30:31], 19
	v_and_b32_e32 v0, 0xfffffc00, v0
	s_add_u32 s36, s18, s12
	v_sub_u32_e32 v0, v2, v0
	v_add_u32_e32 v2, 0x2000, v2
	s_addc_u32 s37, s9, s13
	s_lshl_b32 s9, s8, 2
	v_ashrrev_i32_e32 v3, 31, v2
	s_add_i32 s9, s9, 0
	v_lshrrev_b32_e32 v3, 22, v3
	s_add_i32 s9, s9, 0x20100
	v_add_u32_e32 v3, v2, v3
	v_mov_b32_e32 v5, s9
	v_ashrrev_i32_e32 v15, 10, v3
	ds_read_b32 v5, v5
	v_mul_i32_i24_e32 v3, 0x400, v15
	v_ashrrev_i32_e32 v12, 6, v1
	v_lshrrev_b32_e32 v1, 4, v0
	v_sub_u32_e32 v2, v2, v3
	v_bitop3_b32 v13, v1, v0, 32 bitop3:0x6c
	v_lshrrev_b32_e32 v3, 4, v2
	v_ashrrev_i32_e32 v1, 31, v13
	v_bitop3_b32 v16, v3, v2, 32 bitop3:0x6c
	v_lshrrev_b32_e32 v1, 26, v1
	v_ashrrev_i32_e32 v3, 31, v16
	s_mov_b32 s9, 0
	s_waitcnt lgkmcnt(0)
	v_sub_u32_e32 v5, s59, v5
	v_lshlrev_b32_e32 v0, 3, v12
	v_add_u32_e32 v14, v13, v1
	v_lshrrev_b32_e32 v3, 26, v3
	s_lshl_b64 s[12:13], s[8:9], 16
	v_lshlrev_b32_e32 v8, 8, v5
	v_and_b32_e32 v0, -16, v0
	v_ashrrev_i32_e32 v1, 6, v14
	v_lshlrev_b32_e32 v2, 3, v15
	v_add_u32_e32 v17, v16, v3
	s_add_u32 s12, s21, s12
	v_ashrrev_i32_e32 v9, 31, v8
	v_add_u32_e32 v4, v1, v0
	v_and_b32_e32 v2, -16, v2
	v_ashrrev_i32_e32 v3, 6, v17
	s_addc_u32 s13, s33, s13
	v_lshlrev_b64 v[8:9], 2, v[8:9]
	v_add_u32_e32 v6, v3, v2
	v_lshl_add_u64 v[8:9], s[12:13], 0, v[8:9]
	v_ashrrev_i32_e32 v5, 31, v4
	v_lshl_add_u64 v[10:11], v[4:5], 2, v[8:9]
	v_ashrrev_i32_e32 v7, 31, v6
	v_lshl_add_u64 v[8:9], v[6:7], 2, v[8:9]
	global_load_dword v5, v[10:11], off
	global_load_dword v7, v[8:9], off
	global_load_dword v18, v[8:9], off offset:512
	global_load_dword v19, v[10:11], off offset:512
	v_and_b32_e32 v11, 0xc0, v14
	v_mov_b32_e32 v8, 1
	v_sub_u32_e32 v11, v13, v11
	v_lshlrev_b32_e32 v9, 5, v12
	v_ashrrev_i16_sdwa v11, v8, sext(v11) dst_sel:DWORD dst_unused:UNUSED_PAD src0_sel:DWORD src1_sel:BYTE_0
	v_and_b32_e32 v9, 32, v9
	v_bfe_i32 v11, v11, 0, 16
	v_and_b32_e32 v12, 0xc0, v17
	v_add_lshl_u32 v180, v9, v11, 1
	v_sub_u32_e32 v9, v16, v12
	v_lshlrev_b32_e32 v10, 5, v15
	v_lshl_add_u32 v181, v4, 11, v180
	v_ashrrev_i16_sdwa v4, v8, sext(v9) dst_sel:DWORD dst_unused:UNUSED_PAD src0_sel:DWORD src1_sel:BYTE_0
	v_and_b32_e32 v10, 32, v10
	v_bfe_i32 v4, v4, 0, 16
	s_add_i32 s31, s42, 0
	v_add_lshl_u32 v182, v10, v4, 1
	s_add_i32 s43, s31, 0x10000
	v_lshl_add_u32 v183, v6, 11, v182
	v_mov_b32_e32 v8, v181
	v_mov_b32_e32 v4, v183
	s_mov_b32 m0, s43
	s_add_i32 s44, s31, 0x12000
	s_add_i32 s45, s31, 0x2000
	global_load_lds_dwordx4 v8, s[36:37]
	s_mov_b32 m0, s44
	s_add_u32 s12, s36, 0x40000
	global_load_lds_dwordx4 v4, s[36:37]
	s_mov_b32 m0, s31
	s_addc_u32 s13, s37, 0
	s_add_i32 s46, s31, 0x4000
	s_add_i32 s47, s31, 0x6000
	s_waitcnt vmcnt(0)
	v_lshl_add_u32 v184, v5, 11, v180
	v_mov_b32_e32 v4, v184
	v_lshl_add_u32 v185, v7, 11, v182
	v_lshl_add_u32 v186, v19, 11, v180
	global_load_lds_dwordx4 v4, s[10:11]
	v_mov_b32_e32 v4, v185
	s_mov_b32 m0, s45
	v_lshl_add_u32 v187, v18, 11, v182
	global_load_lds_dwordx4 v4, s[10:11]
	v_mov_b32_e32 v4, v181
	s_add_i32 m0, s31, 0x14000
	s_nop 0
	global_load_lds_dwordx4 v4, s[12:13]
	v_mov_b32_e32 v4, v183
	s_add_i32 m0, s31, 0x16000
	s_cmp_eq_u32 s5, 1
	global_load_lds_dwordx4 v4, s[12:13]
	v_mov_b32_e32 v4, v186
	s_mov_b32 m0, s46
	s_nop 0
	global_load_lds_dwordx4 v4, s[10:11]
	v_mov_b32_e32 v4, v187
	s_mov_b32 m0, s47
	s_nop 0
	global_load_lds_dwordx4 v4, s[10:11]
	s_cbranch_scc0 .LBB0_1935
	s_setprio 1
	s_barrier

.LBB0_1944:
	s_add_u32 s40, s36, 0x80
	s_addc_u32 s41, s37, 0
	v_add_u32_e32 v178, s5, v188
	s_and_b64 s[38:39], s[38:39], exec
	ds_read_b128 v[196:199], v178
	ds_read_b128 v[200:203], v178 offset:1024
	ds_read_b128 v[204:207], v178 offset:2048
	ds_read_b128 v[208:211], v178 offset:3072
	v_mov_b32_e32 v178, v181
	s_mov_b32 m0, s43
	s_cselect_b32 s39, s27, s23
	s_cselect_b32 s38, s26, s8
	s_waitcnt lgkmcnt(0)
	v_mfma_scale_f32_16x16x128_f8f6f4 v[172:175], v[0:7], v[40:47], v[172:175], v195, v195 op_sel_hi:[0,0,0]
	global_load_lds_dwordx4 v178, s[38:39]
	v_mov_b32_e32 v178, v183
	s_mov_b32 m0, s44
	s_cselect_b32 s41, s11, s41
	global_load_lds_dwordx4 v178, s[38:39]
	v_mfma_scale_f32_16x16x128_f8f6f4 v[168:171], v[8:15], v[40:47], v[168:171], v195, v195 op_sel_hi:[0,0,0]
	s_barrier
	s_waitcnt lgkmcnt(0)
	s_cselect_b32 s40, s10, s40
	v_mfma_scale_f32_16x16x128_f8f6f4 v[164:167], v[0:7], v[32:39], v[164:167], v195, v195 op_sel_hi:[0,0,0]
	v_mfma_scale_f32_16x16x128_f8f6f4 v[156:159], v[8:15], v[32:39], v[156:159], v195, v195 op_sel_hi:[0,0,0]
	v_mfma_scale_f32_16x16x128_f8f6f4 v[140:143], v[0:7], v[24:31], v[140:143], v195, v195 op_sel_hi:[0,0,0]
	v_mfma_scale_f32_16x16x128_f8f6f4 v[132:135], v[8:15], v[24:31], v[132:135], v195, v195 op_sel_hi:[0,0,0]
	v_mfma_scale_f32_16x16x128_f8f6f4 v[120:123], v[0:7], v[16:23], v[120:123], v195, v195 op_sel_hi:[0,0,0]
	v_mfma_scale_f32_16x16x128_f8f6f4 v[112:115], v[8:15], v[16:23], v[112:115], v195, v195 op_sel_hi:[0,0,0]
	v_mfma_scale_f32_16x16x128_f8f6f4 v[160:163], v[196:203], v[40:47], v[160:163], v195, v195 op_sel_hi:[0,0,0]
	v_mfma_scale_f32_16x16x128_f8f6f4 v[152:155], v[204:211], v[40:47], v[152:155], v195, v195 op_sel_hi:[0,0,0]
	v_mfma_scale_f32_16x16x128_f8f6f4 v[148:151], v[196:203], v[32:39], v[148:151], v195, v195 op_sel_hi:[0,0,0]
	v_mfma_scale_f32_16x16x128_f8f6f4 v[144:147], v[204:211], v[32:39], v[144:147], v195, v195 op_sel_hi:[0,0,0]
	v_mfma_scale_f32_16x16x128_f8f6f4 v[136:139], v[196:203], v[24:31], v[136:139], v195, v195 op_sel_hi:[0,0,0]
	v_mfma_scale_f32_16x16x128_f8f6f4 v[128:131], v[204:211], v[24:31], v[128:131], v195, v195 op_sel_hi:[0,0,0]
	v_mfma_scale_f32_16x16x128_f8f6f4 v[124:127], v[196:203], v[16:23], v[124:127], v195, v195 op_sel_hi:[0,0,0]
	v_mfma_scale_f32_16x16x128_f8f6f4 v[116:119], v[204:211], v[16:23], v[116:119], v195, v195 op_sel_hi:[0,0,0]
	v_mov_b32_e32 v178, v184
	s_mov_b32 m0, s31
	s_barrier
	ds_read_b128 v[16:19], v194 offset:16384
	ds_read_b128 v[20:23], v194 offset:17408
	ds_read_b128 v[24:27], v194 offset:18432
	ds_read_b128 v[28:31], v194 offset:19456
	ds_read_b128 v[32:35], v194 offset:20480
	ds_read_b128 v[36:39], v194 offset:21504
	ds_read_b128 v[40:43], v194 offset:22528
	ds_read_b128 v[44:47], v194 offset:23552
	s_nop 0
	global_load_lds_dwordx4 v178, s[40:41]
	v_mov_b32_e32 v178, v185
	s_mov_b32 m0, s45
	s_nop 0
	global_load_lds_dwordx4 v178, s[40:41]
	s_barrier
	s_waitcnt lgkmcnt(0)
	s_waitcnt lgkmcnt(0)
	v_mfma_scale_f32_16x16x128_f8f6f4 v[108:111], v[0:7], v[16:23], v[108:111], v195, v195 op_sel_hi:[0,0,0]
	v_mfma_scale_f32_16x16x128_f8f6f4 v[100:103], v[8:15], v[16:23], v[100:103], v195, v195 op_sel_hi:[0,0,0]
	v_mfma_scale_f32_16x16x128_f8f6f4 v[92:95], v[0:7], v[24:31], v[92:95], v195, v195 op_sel_hi:[0,0,0]
	v_mfma_scale_f32_16x16x128_f8f6f4 v[84:87], v[8:15], v[24:31], v[84:87], v195, v195 op_sel_hi:[0,0,0]
	v_mfma_scale_f32_16x16x128_f8f6f4 v[76:79], v[0:7], v[32:39], v[76:79], v195, v195 op_sel_hi:[0,0,0]
	v_mfma_scale_f32_16x16x128_f8f6f4 v[68:71], v[8:15], v[32:39], v[68:71], v195, v195 op_sel_hi:[0,0,0]
	v_mfma_scale_f32_16x16x128_f8f6f4 v[60:63], v[0:7], v[40:47], v[60:63], v195, v195 op_sel_hi:[0,0,0]
	v_mfma_scale_f32_16x16x128_f8f6f4 v[52:55], v[8:15], v[40:47], v[52:55], v195, v195 op_sel_hi:[0,0,0]
	s_barrier
	s_add_u32 s62, s38, 0x40000
	s_addc_u32 s63, s39, 0
	v_mov_b32_e32 v0, v181
	s_add_i32 s61, s5, s42
	s_mov_b32 m0, s61
	s_nop 0
	global_load_lds_dwordx4 v0, s[62:63]
	v_mov_b32_e32 v0, v183
	s_add_i32 m0, s61, 0x2000
	s_nop 0
	global_load_lds_dwordx4 v0, s[62:63]
	s_waitcnt vmcnt(6)
	s_barrier
	v_mfma_scale_f32_16x16x128_f8f6f4 v[104:107], v[196:203], v[16:23], v[104:107], v195, v195 op_sel_hi:[0,0,0]
	v_mfma_scale_f32_16x16x128_f8f6f4 v[96:99], v[204:211], v[16:23], v[96:99], v195, v195 op_sel_hi:[0,0,0]
	v_mfma_scale_f32_16x16x128_f8f6f4 v[88:91], v[196:203], v[24:31], v[88:91], v195, v195 op_sel_hi:[0,0,0]
	v_mfma_scale_f32_16x16x128_f8f6f4 v[80:83], v[204:211], v[24:31], v[80:83], v195, v195 op_sel_hi:[0,0,0]
	v_mfma_scale_f32_16x16x128_f8f6f4 v[72:75], v[196:203], v[32:39], v[72:75], v195, v195 op_sel_hi:[0,0,0]
	v_mfma_scale_f32_16x16x128_f8f6f4 v[64:67], v[204:211], v[32:39], v[64:67], v195, v195 op_sel_hi:[0,0,0]
	v_mfma_scale_f32_16x16x128_f8f6f4 v[56:59], v[196:203], v[40:47], v[56:59], v195, v195 op_sel_hi:[0,0,0]
	v_mfma_scale_f32_16x16x128_f8f6f4 v[48:51], v[204:211], v[40:47], v[48:51], v195, v195 op_sel_hi:[0,0,0]
	s_add_i32 s61, 0, 0x18000
	v_add_u32_e32 v12, s61, v188
	s_barrier
	ds_read_b128 v[0:3], v12
	ds_read_b128 v[4:7], v12 offset:1024
	ds_read_b128 v[8:11], v12 offset:2048
	ds_read_b128 v[12:15], v12 offset:3072
	v_mov_b32_e32 v178, v186
	s_mov_b32 m0, s46
	ds_read_b128 v[16:19], v194 offset:32768
	ds_read_b128 v[20:23], v194 offset:33792
	ds_read_b128 v[24:27], v194 offset:34816
	ds_read_b128 v[28:31], v194 offset:35840
	ds_read_b128 v[32:35], v194 offset:36864
	ds_read_b128 v[36:39], v194 offset:37888
	ds_read_b128 v[40:43], v194 offset:38912
	ds_read_b128 v[44:47], v194 offset:39936
	s_nop 0
	global_load_lds_dwordx4 v178, s[40:41]
	v_mov_b32_e32 v178, v187
	s_mov_b32 m0, s47
	s_nop 0
	global_load_lds_dwordx4 v178, s[40:41]
	s_waitcnt lgkmcnt(8)
	s_barrier
	s_waitcnt lgkmcnt(0)
	s_waitcnt lgkmcnt(0)
	v_mfma_scale_f32_16x16x128_f8f6f4 v[172:175], v[0:7], v[16:23], v[172:175], v195, v195 op_sel_hi:[0,0,0]
	v_mfma_scale_f32_16x16x128_f8f6f4 v[168:171], v[8:15], v[16:23], v[168:171], v195, v195 op_sel_hi:[0,0,0]
	v_mfma_scale_f32_16x16x128_f8f6f4 v[164:167], v[0:7], v[24:31], v[164:167], v195, v195 op_sel_hi:[0,0,0]
	v_mfma_scale_f32_16x16x128_f8f6f4 v[156:159], v[8:15], v[24:31], v[156:159], v195, v195 op_sel_hi:[0,0,0]
	v_mfma_scale_f32_16x16x128_f8f6f4 v[140:143], v[0:7], v[32:39], v[140:143], v195, v195 op_sel_hi:[0,0,0]
	v_mfma_scale_f32_16x16x128_f8f6f4 v[132:135], v[8:15], v[32:39], v[132:135], v195, v195 op_sel_hi:[0,0,0]
	v_mfma_scale_f32_16x16x128_f8f6f4 v[120:123], v[0:7], v[40:47], v[120:123], v195, v195 op_sel_hi:[0,0,0]
	v_mfma_scale_f32_16x16x128_f8f6f4 v[112:115], v[8:15], v[40:47], v[112:115], v195, v195 op_sel_hi:[0,0,0]
	s_barrier
	s_add_i32 s62, 0, 0x1c000
	v_add_u32_e32 v178, s62, v188
	ds_read_b128 v[196:199], v178
	ds_read_b128 v[200:203], v178 offset:1024
	ds_read_b128 v[204:207], v178 offset:2048
	ds_read_b128 v[208:211], v178 offset:3072
	v_mov_b32_e32 v178, v181
	s_add_i32 s61, s61, s42
	v_lshl_add_u64 v[212:213], s[38:39], 0, v[178:179]
	v_lshl_add_u64 v[212:213], v[212:213], 0, s[12:13]
	s_mov_b32 m0, s61
	v_mov_b32_e32 v178, v183
	global_load_lds_dwordx4 v[212:213], off
	s_add_i32 m0, s61, 0x2000
	v_lshl_add_u64 v[212:213], s[38:39], 0, v[178:179]
	v_lshl_add_u64 v[212:213], v[212:213], 0, s[12:13]
	global_load_lds_dwordx4 v[212:213], off
	s_barrier
	s_waitcnt lgkmcnt(0)
	s_waitcnt lgkmcnt(0)
	v_mfma_scale_f32_16x16x128_f8f6f4 v[160:163], v[196:203], v[16:23], v[160:163], v195, v195 op_sel_hi:[0,0,0]
	v_mfma_scale_f32_16x16x128_f8f6f4 v[152:155], v[204:211], v[16:23], v[152:155], v195, v195 op_sel_hi:[0,0,0]
	v_mfma_scale_f32_16x16x128_f8f6f4 v[148:151], v[196:203], v[24:31], v[148:151], v195, v195 op_sel_hi:[0,0,0]
	v_mfma_scale_f32_16x16x128_f8f6f4 v[144:147], v[204:211], v[24:31], v[144:147], v195, v195 op_sel_hi:[0,0,0]
	v_mfma_scale_f32_16x16x128_f8f6f4 v[136:139], v[196:203], v[32:39], v[136:139], v195, v195 op_sel_hi:[0,0,0]
	v_mfma_scale_f32_16x16x128_f8f6f4 v[128:131], v[204:211], v[32:39], v[128:131], v195, v195 op_sel_hi:[0,0,0]
	v_mfma_scale_f32_16x16x128_f8f6f4 v[124:127], v[196:203], v[40:47], v[124:127], v195, v195 op_sel_hi:[0,0,0]
	v_mfma_scale_f32_16x16x128_f8f6f4 v[116:119], v[204:211], v[40:47], v[116:119], v195, v195 op_sel_hi:[0,0,0]
	v_mov_b32_e32 v178, v184
	s_barrier
	ds_read_b128 v[16:19], v194 offset:49152
	ds_read_b128 v[20:23], v194 offset:50176
	ds_read_b128 v[24:27], v194 offset:51200
	ds_read_b128 v[28:31], v194 offset:52224
	ds_read_b128 v[32:35], v194 offset:53248
	ds_read_b128 v[36:39], v194 offset:54272
	ds_read_b128 v[40:43], v194 offset:55296
	ds_read_b128 v[44:47], v194 offset:56320
	s_mov_b32 m0, s52
	v_lshl_add_u64 v[212:213], s[40:41], 0, v[178:179]
	v_lshl_add_u64 v[212:213], v[212:213], 0, s[12:13]
	v_mov_b32_e32 v178, v185
	global_load_lds_dwordx4 v[212:213], off
	s_mov_b32 m0, s53
	v_lshl_add_u64 v[212:213], s[40:41], 0, v[178:179]
	v_lshl_add_u64 v[212:213], v[212:213], 0, s[12:13]
	global_load_lds_dwordx4 v[212:213], off
	s_barrier
	s_waitcnt lgkmcnt(0)
	s_waitcnt lgkmcnt(0)
	v_mfma_scale_f32_16x16x128_f8f6f4 v[108:111], v[0:7], v[16:23], v[108:111], v195, v195 op_sel_hi:[0,0,0]
	v_mfma_scale_f32_16x16x128_f8f6f4 v[100:103], v[8:15], v[16:23], v[100:103], v195, v195 op_sel_hi:[0,0,0]
	v_mfma_scale_f32_16x16x128_f8f6f4 v[92:95], v[0:7], v[24:31], v[92:95], v195, v195 op_sel_hi:[0,0,0]
	v_mfma_scale_f32_16x16x128_f8f6f4 v[84:87], v[8:15], v[24:31], v[84:87], v195, v195 op_sel_hi:[0,0,0]
	v_mfma_scale_f32_16x16x128_f8f6f4 v[76:79], v[0:7], v[32:39], v[76:79], v195, v195 op_sel_hi:[0,0,0]
	v_mfma_scale_f32_16x16x128_f8f6f4 v[68:71], v[8:15], v[32:39], v[68:71], v195, v195 op_sel_hi:[0,0,0]
	v_mfma_scale_f32_16x16x128_f8f6f4 v[60:63], v[0:7], v[40:47], v[60:63], v195, v195 op_sel_hi:[0,0,0]
	v_mfma_scale_f32_16x16x128_f8f6f4 v[52:55], v[8:15], v[40:47], v[52:55], v195, v195 op_sel_hi:[0,0,0]
	s_barrier
	s_add_u32 s38, s38, 0x40080
	s_addc_u32 s39, s39, 0
	v_mov_b32_e32 v0, v181
	s_add_i32 s40, s62, s42
	s_mov_b32 m0, s40
	s_nop 0
	global_load_lds_dwordx4 v0, s[38:39]
	v_mov_b32_e32 v0, v183
	s_add_i32 m0, s40, 0x2000
	s_nop 0
	global_load_lds_dwordx4 v0, s[38:39]
	s_waitcnt vmcnt(6)
	s_barrier
	v_mfma_scale_f32_16x16x128_f8f6f4 v[104:107], v[196:203], v[16:23], v[104:107], v195, v195 op_sel_hi:[0,0,0]
	v_mfma_scale_f32_16x16x128_f8f6f4 v[96:99], v[204:211], v[16:23], v[96:99], v195, v195 op_sel_hi:[0,0,0]
	v_mfma_scale_f32_16x16x128_f8f6f4 v[88:91], v[196:203], v[24:31], v[88:91], v195, v195 op_sel_hi:[0,0,0]
	v_mfma_scale_f32_16x16x128_f8f6f4 v[80:83], v[204:211], v[24:31], v[80:83], v195, v195 op_sel_hi:[0,0,0]
	v_mfma_scale_f32_16x16x128_f8f6f4 v[72:75], v[196:203], v[32:39], v[72:75], v195, v195 op_sel_hi:[0,0,0]
	v_mfma_scale_f32_16x16x128_f8f6f4 v[64:67], v[204:211], v[32:39], v[64:67], v195, v195 op_sel_hi:[0,0,0]
	v_mfma_scale_f32_16x16x128_f8f6f4 v[56:59], v[196:203], v[40:47], v[56:59], v195, v195 op_sel_hi:[0,0,0]
	v_mfma_scale_f32_16x16x128_f8f6f4 v[48:51], v[204:211], v[40:47], v[48:51], v195, v195 op_sel_hi:[0,0,0]
	s_add_i32 s60, s60, 2
	s_add_u32 s36, s36, 0x100
	s_addc_u32 s37, s37, 0
	s_add_u32 s8, s8, 0x100
	s_addc_u32 s23, s23, 0
	s_cmp_gt_u32 s60, 13
	s_barrier
	s_cbranch_scc1 .LBB0_1936
.LBB0_1945:
	ds_read_b128 v[0:3], v193
	ds_read_b128 v[4:7], v193 offset:1024
	ds_read_b128 v[8:11], v193 offset:2048
	ds_read_b128 v[12:15], v193 offset:3072
	s_cmp_eq_u32 s60, 12
	s_cselect_b64 s[38:39], -1, 0
	v_mov_b32_e32 v178, v186
	ds_read_b128 v[40:43], v194
	ds_read_b128 v[44:47], v194 offset:1024
	ds_read_b128 v[32:35], v194 offset:2048
	ds_read_b128 v[36:39], v194 offset:3072
	ds_read_b128 v[24:27], v194 offset:4096
	ds_read_b128 v[28:31], v194 offset:5120
	ds_read_b128 v[16:19], v194 offset:6144
	ds_read_b128 v[20:23], v194 offset:7168
	s_add_i32 m0, s31, 0xc000
	s_nop 0
	global_load_lds_dwordx4 v178, s[36:37]
	v_mov_b32_e32 v178, v187
	s_add_i32 m0, s31, 0xe000
	s_nop 0
	global_load_lds_dwordx4 v178, s[36:37]
	s_waitcnt lgkmcnt(8)
	s_barrier
	s_waitcnt lgkmcnt(0)
	s_barrier
	s_and_b64 s[40:41], s[34:35], s[38:39]
	s_andn2_b64 vcc, exec, s[40:41]
	s_cbranch_vccnz .LBB0_1944
	ds_read_b32 v178, v189
	ds_read_b32 v185, v190
	ds_read_b32 v186, v191
	ds_read_b32 v187, v192
	s_waitcnt lgkmcnt(0)
	v_lshl_add_u32 v184, v178, 11, v180
	v_lshl_add_u32 v185, v185, 11, v182
	v_lshl_add_u32 v186, v186, 11, v180
	v_lshl_add_u32 v187, v187, 11, v182
	s_branch .LBB0_1944

.Lpeelg_t0:
	s_add_u32 s40, s36, 0x80
	s_addc_u32 s41, s37, 0
	v_add_u32_e32 v178, s5, v188
	s_and_b64 s[38:39], s[38:39], exec
	ds_read_b128 v[196:199], v178
	ds_read_b128 v[200:203], v178 offset:1024
	ds_read_b128 v[204:207], v178 offset:2048
	ds_read_b128 v[208:211], v178 offset:3072
	v_mov_b32_e32 v178, v181
	s_mov_b32 m0, s43
	s_cselect_b32 s39, s27, s23
	s_cselect_b32 s38, s26, s8
	s_waitcnt lgkmcnt(0)
	v_mfma_scale_f32_16x16x128_f8f6f4 v[172:175], v[0:7], v[40:47], 0, v195, v195 op_sel_hi:[0,0,0]
	global_load_lds_dwordx4 v178, s[38:39]
	v_mov_b32_e32 v178, v183
	s_mov_b32 m0, s44
	s_cselect_b32 s41, s11, s41
	global_load_lds_dwordx4 v178, s[38:39]
	v_mfma_scale_f32_16x16x128_f8f6f4 v[168:171], v[8:15], v[40:47], 0, v195, v195 op_sel_hi:[0,0,0]
	s_barrier
	s_waitcnt lgkmcnt(0)
	s_cselect_b32 s40, s10, s40
	v_mfma_scale_f32_16x16x128_f8f6f4 v[164:167], v[0:7], v[32:39], 0, v195, v195 op_sel_hi:[0,0,0]
	v_mfma_scale_f32_16x16x128_f8f6f4 v[156:159], v[8:15], v[32:39], 0, v195, v195 op_sel_hi:[0,0,0]
	v_mfma_scale_f32_16x16x128_f8f6f4 v[140:143], v[0:7], v[24:31], 0, v195, v195 op_sel_hi:[0,0,0]
	v_mfma_scale_f32_16x16x128_f8f6f4 v[132:135], v[8:15], v[24:31], 0, v195, v195 op_sel_hi:[0,0,0]
	v_mfma_scale_f32_16x16x128_f8f6f4 v[120:123], v[0:7], v[16:23], 0, v195, v195 op_sel_hi:[0,0,0]
	v_mfma_scale_f32_16x16x128_f8f6f4 v[112:115], v[8:15], v[16:23], 0, v195, v195 op_sel_hi:[0,0,0]
	v_mfma_scale_f32_16x16x128_f8f6f4 v[160:163], v[196:203], v[40:47], 0, v195, v195 op_sel_hi:[0,0,0]
	v_mfma_scale_f32_16x16x128_f8f6f4 v[152:155], v[204:211], v[40:47], 0, v195, v195 op_sel_hi:[0,0,0]
	v_mfma_scale_f32_16x16x128_f8f6f4 v[148:151], v[196:203], v[32:39], 0, v195, v195 op_sel_hi:[0,0,0]
	v_mfma_scale_f32_16x16x128_f8f6f4 v[144:147], v[204:211], v[32:39], 0, v195, v195 op_sel_hi:[0,0,0]
	v_mfma_scale_f32_16x16x128_f8f6f4 v[136:139], v[196:203], v[24:31], 0, v195, v195 op_sel_hi:[0,0,0]
	v_mfma_scale_f32_16x16x128_f8f6f4 v[128:131], v[204:211], v[24:31], 0, v195, v195 op_sel_hi:[0,0,0]
	v_mfma_scale_f32_16x16x128_f8f6f4 v[124:127], v[196:203], v[16:23], 0, v195, v195 op_sel_hi:[0,0,0]
	v_mfma_scale_f32_16x16x128_f8f6f4 v[116:119], v[204:211], v[16:23], 0, v195, v195 op_sel_hi:[0,0,0]
	v_mov_b32_e32 v178, v184
	s_mov_b32 m0, s31
	s_barrier
	ds_read_b128 v[16:19], v194 offset:16384
	ds_read_b128 v[20:23], v194 offset:17408
	ds_read_b128 v[24:27], v194 offset:18432
	ds_read_b128 v[28:31], v194 offset:19456
	ds_read_b128 v[32:35], v194 offset:20480
	ds_read_b128 v[36:39], v194 offset:21504
	ds_read_b128 v[40:43], v194 offset:22528
	ds_read_b128 v[44:47], v194 offset:23552
	s_nop 0
	global_load_lds_dwordx4 v178, s[40:41]
	v_mov_b32_e32 v178, v185
	s_mov_b32 m0, s45
	s_nop 0
	global_load_lds_dwordx4 v178, s[40:41]
	s_barrier
	s_waitcnt lgkmcnt(0)
	s_waitcnt lgkmcnt(0)
	v_mfma_scale_f32_16x16x128_f8f6f4 v[108:111], v[0:7], v[16:23], 0, v195, v195 op_sel_hi:[0,0,0]
	v_mfma_scale_f32_16x16x128_f8f6f4 v[100:103], v[8:15], v[16:23], 0, v195, v195 op_sel_hi:[0,0,0]
	v_mfma_scale_f32_16x16x128_f8f6f4 v[92:95], v[0:7], v[24:31], 0, v195, v195 op_sel_hi:[0,0,0]
	v_mfma_scale_f32_16x16x128_f8f6f4 v[84:87], v[8:15], v[24:31], 0, v195, v195 op_sel_hi:[0,0,0]
	v_mfma_scale_f32_16x16x128_f8f6f4 v[76:79], v[0:7], v[32:39], 0, v195, v195 op_sel_hi:[0,0,0]
	v_mfma_scale_f32_16x16x128_f8f6f4 v[68:71], v[8:15], v[32:39], 0, v195, v195 op_sel_hi:[0,0,0]
	v_mfma_scale_f32_16x16x128_f8f6f4 v[60:63], v[0:7], v[40:47], 0, v195, v195 op_sel_hi:[0,0,0]
	v_mfma_scale_f32_16x16x128_f8f6f4 v[52:55], v[8:15], v[40:47], 0, v195, v195 op_sel_hi:[0,0,0]
	s_barrier
	s_add_u32 s62, s38, 0x40000
	s_addc_u32 s63, s39, 0
	v_mov_b32_e32 v0, v181
	s_add_i32 s61, s5, s42
	s_mov_b32 m0, s61
	s_nop 0
	global_load_lds_dwordx4 v0, s[62:63]
	v_mov_b32_e32 v0, v183
	s_add_i32 m0, s61, 0x2000
	s_nop 0
	global_load_lds_dwordx4 v0, s[62:63]
	s_waitcnt vmcnt(6)
	s_barrier
	v_mfma_scale_f32_16x16x128_f8f6f4 v[104:107], v[196:203], v[16:23], 0, v195, v195 op_sel_hi:[0,0,0]
	v_mfma_scale_f32_16x16x128_f8f6f4 v[96:99], v[204:211], v[16:23], 0, v195, v195 op_sel_hi:[0,0,0]
	v_mfma_scale_f32_16x16x128_f8f6f4 v[88:91], v[196:203], v[24:31], 0, v195, v195 op_sel_hi:[0,0,0]
	v_mfma_scale_f32_16x16x128_f8f6f4 v[80:83], v[204:211], v[24:31], 0, v195, v195 op_sel_hi:[0,0,0]
	v_mfma_scale_f32_16x16x128_f8f6f4 v[72:75], v[196:203], v[32:39], 0, v195, v195 op_sel_hi:[0,0,0]
	v_mfma_scale_f32_16x16x128_f8f6f4 v[64:67], v[204:211], v[32:39], 0, v195, v195 op_sel_hi:[0,0,0]
	v_mfma_scale_f32_16x16x128_f8f6f4 v[56:59], v[196:203], v[40:47], 0, v195, v195 op_sel_hi:[0,0,0]
	v_mfma_scale_f32_16x16x128_f8f6f4 v[48:51], v[204:211], v[40:47], 0, v195, v195 op_sel_hi:[0,0,0]
	s_add_i32 s61, 0, 0x18000
	v_add_u32_e32 v12, s61, v188
	s_barrier
	ds_read_b128 v[0:3], v12
	ds_read_b128 v[4:7], v12 offset:1024
	ds_read_b128 v[8:11], v12 offset:2048
	ds_read_b128 v[12:15], v12 offset:3072
	v_mov_b32_e32 v178, v186
	s_mov_b32 m0, s46
	ds_read_b128 v[16:19], v194 offset:32768
	ds_read_b128 v[20:23], v194 offset:33792
	ds_read_b128 v[24:27], v194 offset:34816
	ds_read_b128 v[28:31], v194 offset:35840
	ds_read_b128 v[32:35], v194 offset:36864
	ds_read_b128 v[36:39], v194 offset:37888
	ds_read_b128 v[40:43], v194 offset:38912
	ds_read_b128 v[44:47], v194 offset:39936
	s_nop 0
	global_load_lds_dwordx4 v178, s[40:41]
	v_mov_b32_e32 v178, v187
	s_mov_b32 m0, s47
	s_nop 0
	global_load_lds_dwordx4 v178, s[40:41]
	s_waitcnt lgkmcnt(8)
	s_barrier
	s_waitcnt lgkmcnt(0)
	s_waitcnt lgkmcnt(0)
	v_mfma_scale_f32_16x16x128_f8f6f4 v[172:175], v[0:7], v[16:23], v[172:175], v195, v195 op_sel_hi:[0,0,0]
	v_mfma_scale_f32_16x16x128_f8f6f4 v[168:171], v[8:15], v[16:23], v[168:171], v195, v195 op_sel_hi:[0,0,0]
	v_mfma_scale_f32_16x16x128_f8f6f4 v[164:167], v[0:7], v[24:31], v[164:167], v195, v195 op_sel_hi:[0,0,0]
	v_mfma_scale_f32_16x16x128_f8f6f4 v[156:159], v[8:15], v[24:31], v[156:159], v195, v195 op_sel_hi:[0,0,0]
	v_mfma_scale_f32_16x16x128_f8f6f4 v[140:143], v[0:7], v[32:39], v[140:143], v195, v195 op_sel_hi:[0,0,0]
	v_mfma_scale_f32_16x16x128_f8f6f4 v[132:135], v[8:15], v[32:39], v[132:135], v195, v195 op_sel_hi:[0,0,0]
	v_mfma_scale_f32_16x16x128_f8f6f4 v[120:123], v[0:7], v[40:47], v[120:123], v195, v195 op_sel_hi:[0,0,0]
	v_mfma_scale_f32_16x16x128_f8f6f4 v[112:115], v[8:15], v[40:47], v[112:115], v195, v195 op_sel_hi:[0,0,0]
	s_barrier
	s_add_i32 s62, 0, 0x1c000
	v_add_u32_e32 v178, s62, v188
	ds_read_b128 v[196:199], v178
	ds_read_b128 v[200:203], v178 offset:1024
	ds_read_b128 v[204:207], v178 offset:2048
	ds_read_b128 v[208:211], v178 offset:3072
	v_mov_b32_e32 v178, v181
	s_add_i32 s61, s61, s42
	v_lshl_add_u64 v[212:213], s[38:39], 0, v[178:179]
	v_lshl_add_u64 v[212:213], v[212:213], 0, s[12:13]
	s_mov_b32 m0, s61
	v_mov_b32_e32 v178, v183
	global_load_lds_dwordx4 v[212:213], off
	s_add_i32 m0, s61, 0x2000
	v_lshl_add_u64 v[212:213], s[38:39], 0, v[178:179]
	v_lshl_add_u64 v[212:213], v[212:213], 0, s[12:13]
	global_load_lds_dwordx4 v[212:213], off
	s_barrier
	s_waitcnt lgkmcnt(0)
	s_waitcnt lgkmcnt(0)
	v_mfma_scale_f32_16x16x128_f8f6f4 v[160:163], v[196:203], v[16:23], v[160:163], v195, v195 op_sel_hi:[0,0,0]
	v_mfma_scale_f32_16x16x128_f8f6f4 v[152:155], v[204:211], v[16:23], v[152:155], v195, v195 op_sel_hi:[0,0,0]
	v_mfma_scale_f32_16x16x128_f8f6f4 v[148:151], v[196:203], v[24:31], v[148:151], v195, v195 op_sel_hi:[0,0,0]
	v_mfma_scale_f32_16x16x128_f8f6f4 v[144:147], v[204:211], v[24:31], v[144:147], v195, v195 op_sel_hi:[0,0,0]
	v_mfma_scale_f32_16x16x128_f8f6f4 v[136:139], v[196:203], v[32:39], v[136:139], v195, v195 op_sel_hi:[0,0,0]
	v_mfma_scale_f32_16x16x128_f8f6f4 v[128:131], v[204:211], v[32:39], v[128:131], v195, v195 op_sel_hi:[0,0,0]
	v_mfma_scale_f32_16x16x128_f8f6f4 v[124:127], v[196:203], v[40:47], v[124:127], v195, v195 op_sel_hi:[0,0,0]
	v_mfma_scale_f32_16x16x128_f8f6f4 v[116:119], v[204:211], v[40:47], v[116:119], v195, v195 op_sel_hi:[0,0,0]
	v_mov_b32_e32 v178, v184
	s_barrier
	ds_read_b128 v[16:19], v194 offset:49152
	ds_read_b128 v[20:23], v194 offset:50176
	ds_read_b128 v[24:27], v194 offset:51200
	ds_read_b128 v[28:31], v194 offset:52224
	ds_read_b128 v[32:35], v194 offset:53248
	ds_read_b128 v[36:39], v194 offset:54272
	ds_read_b128 v[40:43], v194 offset:55296
	ds_read_b128 v[44:47], v194 offset:56320
	s_mov_b32 m0, s52
	v_lshl_add_u64 v[212:213], s[40:41], 0, v[178:179]
	v_lshl_add_u64 v[212:213], v[212:213], 0, s[12:13]
	v_mov_b32_e32 v178, v185
	global_load_lds_dwordx4 v[212:213], off
	s_mov_b32 m0, s53
	v_lshl_add_u64 v[212:213], s[40:41], 0, v[178:179]
	v_lshl_add_u64 v[212:213], v[212:213], 0, s[12:13]
	global_load_lds_dwordx4 v[212:213], off
	s_barrier
	s_waitcnt lgkmcnt(0)
	s_waitcnt lgkmcnt(0)
	v_mfma_scale_f32_16x16x128_f8f6f4 v[108:111], v[0:7], v[16:23], v[108:111], v195, v195 op_sel_hi:[0,0,0]
	v_mfma_scale_f32_16x16x128_f8f6f4 v[100:103], v[8:15], v[16:23], v[100:103], v195, v195 op_sel_hi:[0,0,0]
	v_mfma_scale_f32_16x16x128_f8f6f4 v[92:95], v[0:7], v[24:31], v[92:95], v195, v195 op_sel_hi:[0,0,0]
	v_mfma_scale_f32_16x16x128_f8f6f4 v[84:87], v[8:15], v[24:31], v[84:87], v195, v195 op_sel_hi:[0,0,0]
	v_mfma_scale_f32_16x16x128_f8f6f4 v[76:79], v[0:7], v[32:39], v[76:79], v195, v195 op_sel_hi:[0,0,0]
	v_mfma_scale_f32_16x16x128_f8f6f4 v[68:71], v[8:15], v[32:39], v[68:71], v195, v195 op_sel_hi:[0,0,0]
	v_mfma_scale_f32_16x16x128_f8f6f4 v[60:63], v[0:7], v[40:47], v[60:63], v195, v195 op_sel_hi:[0,0,0]
	v_mfma_scale_f32_16x16x128_f8f6f4 v[52:55], v[8:15], v[40:47], v[52:55], v195, v195 op_sel_hi:[0,0,0]
	s_barrier
	s_add_u32 s38, s38, 0x40080
	s_addc_u32 s39, s39, 0
	v_mov_b32_e32 v0, v181
	s_add_i32 s40, s62, s42
	s_mov_b32 m0, s40
	s_nop 0
	global_load_lds_dwordx4 v0, s[38:39]
	v_mov_b32_e32 v0, v183
	s_add_i32 m0, s40, 0x2000
	s_nop 0
	global_load_lds_dwordx4 v0, s[38:39]
	s_waitcnt vmcnt(6)
	s_barrier
	v_mfma_scale_f32_16x16x128_f8f6f4 v[104:107], v[196:203], v[16:23], v[104:107], v195, v195 op_sel_hi:[0,0,0]
	v_mfma_scale_f32_16x16x128_f8f6f4 v[96:99], v[204:211], v[16:23], v[96:99], v195, v195 op_sel_hi:[0,0,0]
	v_mfma_scale_f32_16x16x128_f8f6f4 v[88:91], v[196:203], v[24:31], v[88:91], v195, v195 op_sel_hi:[0,0,0]
	v_mfma_scale_f32_16x16x128_f8f6f4 v[80:83], v[204:211], v[24:31], v[80:83], v195, v195 op_sel_hi:[0,0,0]
	v_mfma_scale_f32_16x16x128_f8f6f4 v[72:75], v[196:203], v[32:39], v[72:75], v195, v195 op_sel_hi:[0,0,0]
	v_mfma_scale_f32_16x16x128_f8f6f4 v[64:67], v[204:211], v[32:39], v[64:67], v195, v195 op_sel_hi:[0,0,0]
	v_mfma_scale_f32_16x16x128_f8f6f4 v[56:59], v[196:203], v[40:47], v[56:59], v195, v195 op_sel_hi:[0,0,0]
	v_mfma_scale_f32_16x16x128_f8f6f4 v[48:51], v[204:211], v[40:47], v[48:51], v195, v195 op_sel_hi:[0,0,0]
	s_add_i32 s60, s60, 2
	s_add_u32 s36, s36, 0x100
	s_addc_u32 s37, s37, 0
	s_add_u32 s8, s8, 0x100
	s_addc_u32 s23, s23, 0
	s_cmp_gt_u32 s60, 13
	s_barrier
	s_cbranch_scc1 .LBB0_1936
	s_branch .LBB0_1945

.LBB0_2373:
	s_mov_b64 s[98:99], exec
	s_mov_b64 exec, -1
	v_mbcnt_lo_u32_b32 v1, -1, 0
	v_mbcnt_hi_u32_b32 v1, -1, v1
	v_min_u32_e32 v1, 14, v1
	v_lshl_add_u32 v1, v1, 2, s7
	ds_read_b32 v1, v1
	s_waitcnt lgkmcnt(0)
	v_cmp_ge_i32_e32 vcc, s50, v1
	s_mov_b64 exec, s[98:99]
	s_and_b32 s10, vcc_lo, 0x7fff
	s_bcnt1_i32_b32 s10, s10
	s_add_i32 s7, s7, 60
	s_mov_b32 s8, 16
	s_cmp_eq_u32 s8, 16
	s_add_u32 s7, s4, 0x2f1c8000
	s_addc_u32 s9, s5, 0
	s_add_u32 s22, s4, 0xe9c8000
	v_readlane_b32 s11, v252, 10
	s_addc_u32 s23, s5, 0
	s_lshl_b32 s24, s11, 10
	v_lshl_add_u32 v1, v0, 4, s24
	v_ashrrev_i32_e32 v2, 31, v1
	v_lshrrev_b32_e32 v2, 22, v2
	v_add_u32_e32 v2, v1, v2
	v_ashrrev_i32_e32 v2, 10, v2
	v_mul_i32_i24_e32 v3, 0x400, v2
	v_sub_u32_e32 v3, v1, v3
	v_lshrrev_b32_e32 v4, 4, v3
	v_bitop3_b32 v3, v4, v3, 32 bitop3:0x6c
	v_ashrrev_i32_e32 v5, 31, v3
	v_lshrrev_b32_e32 v5, 26, v5
	v_add_u32_e32 v5, v3, v5
	v_lshlrev_b32_e32 v4, 3, v2
	v_lshrrev_b32_e32 v6, 6, v5
	v_and_b32_e32 v5, 0xc0, v5
	v_and_b32_e32 v4, 0x7ffff0, v4
	v_lshlrev_b32_e32 v2, 5, v2
	v_sub_u32_e32 v3, v3, v5
	v_mov_b32_e32 v5, 1
	v_add_u32_e32 v4, v6, v4
	v_and_b32_e32 v2, 32, v2
	v_ashrrev_i16_sdwa v3, v5, sext(v3) dst_sel:DWORD dst_unused:UNUSED_PAD src0_sel:DWORD src1_sel:BYTE_0
	s_movk_i32 s11, 0x600
	v_add_u32_sdwa v2, v2, sext(v3) dst_sel:DWORD dst_unused:UNUSED_PAD src0_sel:DWORD src1_sel:WORD_0
	v_mul_lo_u32 v3, v4, s11
	v_add_u32_e32 v1, 0x2000, v1
	v_lshl_add_u32 v132, v2, 1, v3
	v_ashrrev_i32_e32 v2, 31, v1
	v_lshrrev_b32_e32 v2, 22, v2
	v_add_u32_e32 v2, v1, v2
	v_ashrrev_i32_e32 v2, 10, v2
	v_mul_i32_i24_e32 v3, 0x400, v2
	v_sub_u32_e32 v1, v1, v3
	v_lshrrev_b32_e32 v3, 4, v1
	v_bitop3_b32 v1, v3, v1, 32 bitop3:0x6c
	v_ashrrev_i32_e32 v4, 31, v1
	v_lshrrev_b32_e32 v4, 26, v4
	v_add_u32_e32 v4, v1, v4
	v_lshrrev_b32_e32 v6, 6, v4
	v_and_b32_e32 v4, 0xffc0, v4
	v_sub_u32_e32 v1, v1, v4
	v_lshrrev_b16_e32 v4, 7, v1
	v_lshlrev_b32_e32 v3, 3, v2
	v_and_b32_e32 v4, 1, v4
	v_and_b32_e32 v3, 0x7ffff0, v3
	v_lshlrev_b32_e32 v2, 5, v2
	v_add_u16_e32 v1, v1, v4
	v_add_u32_e32 v3, v6, v3
	v_and_b32_e32 v2, 32, v2
	v_ashrrev_i16_sdwa v1, v5, sext(v1) dst_sel:DWORD dst_unused:UNUSED_PAD src0_sel:DWORD src1_sel:BYTE_0
	v_readlane_b32 s8, v252, 2
	v_add_u32_sdwa v1, v2, sext(v1) dst_sel:DWORD dst_unused:UNUSED_PAD src0_sel:DWORD src1_sel:WORD_0
	v_mul_lo_u32 v2, v3, s11
	s_lshl_b32 s11, s50, 3
	s_lshr_b32 s8, s8, 8
	s_sub_i32 s51, s0, s11
	s_mul_hi_u32 s11, s10, 0x300000
	s_mul_i32 s10, s10, 0x300000
	s_add_u32 s10, s22, s10
	s_addc_u32 s11, s23, s11
	s_mul_i32 s13, s51, 0x60000
	s_mul_hi_i32 s12, s51, 0x60000
	s_add_u32 s18, s10, s13
	s_addc_u32 s19, s11, s12
	s_mul_i32 s11, s50, 0x60000
	s_mul_hi_i32 s10, s50, 0x60000
	s_add_u32 s16, s7, s11
	v_lshl_add_u32 v133, v1, 1, v2
	s_addc_u32 s17, s9, s10
	s_add_i32 s25, s24, 0
	v_mov_b32_e32 v1, v132
	s_add_i32 m0, s25, 0x10000
	s_add_i32 s26, s25, 0x2000
	global_load_lds_dwordx4 v1, s[18:19]
	v_mov_b32_e32 v1, v133
	s_add_i32 m0, s25, 0x12000
	s_add_u32 s10, s18, 0x30000
	global_load_lds_dwordx4 v1, s[18:19]
	v_mov_b32_e32 v1, v132
	s_mov_b32 m0, s25
	s_addc_u32 s11, s19, 0
	global_load_lds_dwordx4 v1, s[16:17]
	v_mov_b32_e32 v1, v133
	s_mov_b32 m0, s26
	s_mov_b32 s29, 0
	global_load_lds_dwordx4 v1, s[16:17]
	v_mov_b32_e32 v1, v132
	s_add_i32 m0, s25, 0x14000
	s_mov_b32 s30, 0x10000
	global_load_lds_dwordx4 v1, s[10:11]
	v_mov_b32_e32 v1, v133
	s_add_i32 m0, s25, 0x16000
	s_nop 0
	global_load_lds_dwordx4 v1, s[10:11]
	s_add_u32 s10, s16, 0x30000
	s_addc_u32 s11, s17, 0
	s_add_i32 s27, s25, 0x4000
	v_mov_b32_e32 v1, v132
	s_mov_b32 m0, s27
	s_add_i32 s28, s25, 0x6000
	global_load_lds_dwordx4 v1, s[10:11]
	v_mov_b32_e32 v1, v133
	s_mov_b32 m0, s28
	s_cmp_eq_u32 s8, 1
	global_load_lds_dwordx4 v1, s[10:11]
	s_cbranch_scc0 .LBB0_2376
	s_setprio 1
	s_barrier

.Lpeel_4:
	ds_read_b128 v[140:143], v134
	ds_read_b128 v[144:147], v134 offset:1024
	ds_read_b128 v[148:151], v134 offset:2048
	ds_read_b128 v[152:155], v134 offset:3072
	s_add_u32 s18, s16, 0xfffd0080
	s_addc_u32 s19, s17, -1
	s_cmp_eq_u32 s54, 8
	s_cselect_b32 s21, s15, s19
	s_cselect_b32 s20, s14, s18
	s_cselect_b32 s19, s13, s53
	s_cselect_b32 s18, s12, s52
	v_mov_b32_e32 v128, v132
	ds_read_b128 v[156:159], v135
	ds_read_b128 v[160:163], v135 offset:1024
	ds_read_b128 v[164:167], v135 offset:2048
	ds_read_b128 v[168:171], v135 offset:3072
	ds_read_b128 v[172:175], v135 offset:4096
	ds_read_b128 v[176:179], v135 offset:5120
	ds_read_b128 v[180:183], v135 offset:6144
	ds_read_b128 v[184:187], v135 offset:7168
	s_nop 0
	v_mov_b32_e32 v128, v133
	s_nop 0
	s_waitcnt lgkmcnt(8)
	s_barrier
	s_waitcnt lgkmcnt(0)
	s_waitcnt lgkmcnt(0)
	v_mfma_scale_f32_16x16x128_f8f6f4 v[124:127], v[140:147], v[156:163], 0, v136, v136 op_sel_hi:[0,0,0]
	v_mfma_scale_f32_16x16x128_f8f6f4 v[120:123], v[148:155], v[156:163], 0, v136, v136 op_sel_hi:[0,0,0]
	s_mov_b32 m0, s39
	v_mfma_scale_f32_16x16x128_f8f6f4 v[116:119], v[140:147], v[164:171], 0, v136, v136 op_sel_hi:[0,0,0]
	global_load_lds_dwordx4 v132, s[16:17]
	v_mfma_scale_f32_16x16x128_f8f6f4 v[112:115], v[148:155], v[164:171], 0, v136, v136 op_sel_hi:[0,0,0]
	v_mfma_scale_f32_16x16x128_f8f6f4 v[188:191], v[140:147], v[172:179], 0, v136, v136 op_sel_hi:[0,0,0]
	s_mov_b32 m0, s40
	v_mfma_scale_f32_16x16x128_f8f6f4 v[192:195], v[148:155], v[172:179], 0, v136, v136 op_sel_hi:[0,0,0]
	global_load_lds_dwordx4 v133, s[16:17]
	v_mfma_scale_f32_16x16x128_f8f6f4 v[196:199], v[140:147], v[180:187], 0, v136, v136 op_sel_hi:[0,0,0]
	v_mfma_scale_f32_16x16x128_f8f6f4 v[200:203], v[148:155], v[180:187], 0, v136, v136 op_sel_hi:[0,0,0]
	s_barrier
	v_mov_b32_e32 v128, v132
	s_nop 2
	ds_read_b128 v[96:99], v137
	ds_read_b128 v[100:103], v137 offset:1024
	ds_read_b128 v[104:107], v137 offset:2048
	ds_read_b128 v[108:111], v137 offset:3072
	s_nop 0
	v_mov_b32_e32 v128, v133
	s_nop 0
	s_barrier
	s_waitcnt lgkmcnt(0)
	s_waitcnt lgkmcnt(0)
	v_mfma_scale_f32_16x16x128_f8f6f4 v[204:207], v[96:103], v[156:163], 0, v136, v136 op_sel_hi:[0,0,0]
	v_mfma_scale_f32_16x16x128_f8f6f4 v[156:159], v[104:111], v[156:163], 0, v136, v136 op_sel_hi:[0,0,0]
	s_mov_b32 m0, s41
	v_mfma_scale_f32_16x16x128_f8f6f4 v[160:163], v[96:103], v[164:171], 0, v136, v136 op_sel_hi:[0,0,0]
	global_load_lds_dwordx4 v132, s[18:19]
	v_mfma_scale_f32_16x16x128_f8f6f4 v[164:167], v[104:111], v[164:171], 0, v136, v136 op_sel_hi:[0,0,0]
	v_mfma_scale_f32_16x16x128_f8f6f4 v[168:171], v[96:103], v[172:179], 0, v136, v136 op_sel_hi:[0,0,0]
	s_mov_b32 m0, s42
	v_mfma_scale_f32_16x16x128_f8f6f4 v[172:175], v[104:111], v[172:179], 0, v136, v136 op_sel_hi:[0,0,0]
	global_load_lds_dwordx4 v133, s[18:19]
	v_mfma_scale_f32_16x16x128_f8f6f4 v[176:179], v[96:103], v[180:187], 0, v136, v136 op_sel_hi:[0,0,0]
	v_mfma_scale_f32_16x16x128_f8f6f4 v[180:183], v[104:111], v[180:187], 0, v136, v136 op_sel_hi:[0,0,0]
	v_mov_b32_e32 v128, v132
	s_barrier
	s_nop 2
	ds_read_b128 v[64:67], v135 offset:16384
	ds_read_b128 v[68:71], v135 offset:17408
	ds_read_b128 v[72:75], v135 offset:18432
	ds_read_b128 v[76:79], v135 offset:19456
	ds_read_b128 v[80:83], v135 offset:20480
	ds_read_b128 v[84:87], v135 offset:21504
	ds_read_b128 v[88:91], v135 offset:22528
	ds_read_b128 v[92:95], v135 offset:23552
	s_nop 0
	v_mov_b32_e32 v128, v133
	s_nop 0
	s_barrier
	s_waitcnt lgkmcnt(0)
	s_waitcnt lgkmcnt(0)
	v_mfma_scale_f32_16x16x128_f8f6f4 v[60:63], v[140:147], v[64:71], 0, v136, v136 op_sel_hi:[0,0,0]
	v_mfma_scale_f32_16x16x128_f8f6f4 v[56:59], v[148:155], v[64:71], 0, v136, v136 op_sel_hi:[0,0,0]
	s_mov_b32 m0, s25
	v_mfma_scale_f32_16x16x128_f8f6f4 v[52:55], v[140:147], v[72:79], 0, v136, v136 op_sel_hi:[0,0,0]
	global_load_lds_dwordx4 v132, s[20:21]
	v_mfma_scale_f32_16x16x128_f8f6f4 v[48:51], v[148:155], v[72:79], 0, v136, v136 op_sel_hi:[0,0,0]
	v_mfma_scale_f32_16x16x128_f8f6f4 v[184:187], v[140:147], v[80:87], 0, v136, v136 op_sel_hi:[0,0,0]
	s_mov_b32 m0, s26
	v_mfma_scale_f32_16x16x128_f8f6f4 v[208:211], v[148:155], v[80:87], 0, v136, v136 op_sel_hi:[0,0,0]
	global_load_lds_dwordx4 v133, s[20:21]
	v_mfma_scale_f32_16x16x128_f8f6f4 v[212:215], v[140:147], v[88:95], 0, v136, v136 op_sel_hi:[0,0,0]
	v_mfma_scale_f32_16x16x128_f8f6f4 v[216:219], v[148:155], v[88:95], 0, v136, v136 op_sel_hi:[0,0,0]
	s_barrier
	s_add_u32 s56, s18, 0x30000
	s_nop 3
	v_mov_b32_e32 v32, v132
	s_addc_u32 s57, s19, 0
	s_nop 0
	v_mov_b32_e32 v32, v133
	s_nop 0
	s_waitcnt vmcnt(4)
	s_barrier
	v_mfma_scale_f32_16x16x128_f8f6f4 v[220:223], v[96:103], v[64:71], 0, v136, v136 op_sel_hi:[0,0,0]
	v_mfma_scale_f32_16x16x128_f8f6f4 v[224:227], v[104:111], v[64:71], 0, v136, v136 op_sel_hi:[0,0,0]
	s_mov_b32 m0, s43
	v_mfma_scale_f32_16x16x128_f8f6f4 v[228:231], v[96:103], v[72:79], 0, v136, v136 op_sel_hi:[0,0,0]
	global_load_lds_dwordx4 v132, s[56:57]
	v_mfma_scale_f32_16x16x128_f8f6f4 v[232:235], v[104:111], v[72:79], 0, v136, v136 op_sel_hi:[0,0,0]
	v_mfma_scale_f32_16x16x128_f8f6f4 v[236:239], v[96:103], v[80:87], 0, v136, v136 op_sel_hi:[0,0,0]
	s_mov_b32 m0, s44
	v_mfma_scale_f32_16x16x128_f8f6f4 v[240:243], v[104:111], v[80:87], 0, v136, v136 op_sel_hi:[0,0,0]
	global_load_lds_dwordx4 v133, s[56:57]
	v_mfma_scale_f32_16x16x128_f8f6f4 v[244:247], v[96:103], v[88:95], 0, v136, v136 op_sel_hi:[0,0,0]
	v_mfma_scale_f32_16x16x128_f8f6f4 v[248:251], v[104:111], v[88:95], 0, v136, v136 op_sel_hi:[0,0,0]
	s_barrier
	s_nop 4
	ds_read_b128 v[0:3], v138
	ds_read_b128 v[4:7], v138 offset:1024
	ds_read_b128 v[8:11], v138 offset:2048
	ds_read_b128 v[12:15], v138 offset:3072
	s_add_u32 s56, s20, 0x30000
	v_mov_b32_e32 v64, v132
	ds_read_b128 v[16:19], v135 offset:32768
	ds_read_b128 v[20:23], v135 offset:33792
	ds_read_b128 v[24:27], v135 offset:34816
	ds_read_b128 v[28:31], v135 offset:35840
	ds_read_b128 v[32:35], v135 offset:36864
	ds_read_b128 v[36:39], v135 offset:37888
	ds_read_b128 v[40:43], v135 offset:38912
	ds_read_b128 v[44:47], v135 offset:39936
	s_addc_u32 s57, s21, 0
	s_nop 0
	v_mov_b32_e32 v64, v133
	s_nop 0
	s_waitcnt lgkmcnt(8)
	s_barrier
	s_waitcnt lgkmcnt(0)
	s_waitcnt lgkmcnt(0)
	v_mfma_scale_f32_16x16x128_f8f6f4 v[124:127], v[0:7], v[16:23], v[124:127], v136, v136 op_sel_hi:[0,0,0]
	v_mfma_scale_f32_16x16x128_f8f6f4 v[120:123], v[8:15], v[16:23], v[120:123], v136, v136 op_sel_hi:[0,0,0]
	s_mov_b32 m0, s27
	v_mfma_scale_f32_16x16x128_f8f6f4 v[116:119], v[0:7], v[24:31], v[116:119], v136, v136 op_sel_hi:[0,0,0]
	global_load_lds_dwordx4 v132, s[56:57]
	v_mfma_scale_f32_16x16x128_f8f6f4 v[112:115], v[8:15], v[24:31], v[112:115], v136, v136 op_sel_hi:[0,0,0]
	v_mfma_scale_f32_16x16x128_f8f6f4 v[108:111], v[0:7], v[32:39], v[188:191], v136, v136 op_sel_hi:[0,0,0]
	s_mov_b32 m0, s28
	v_mfma_scale_f32_16x16x128_f8f6f4 v[104:107], v[8:15], v[32:39], v[192:195], v136, v136 op_sel_hi:[0,0,0]
	global_load_lds_dwordx4 v133, s[56:57]
	v_mfma_scale_f32_16x16x128_f8f6f4 v[100:103], v[0:7], v[40:47], v[196:199], v136, v136 op_sel_hi:[0,0,0]
	v_mfma_scale_f32_16x16x128_f8f6f4 v[96:99], v[8:15], v[40:47], v[200:203], v136, v136 op_sel_hi:[0,0,0]
	s_barrier
	v_mov_b32_e32 v128, v132
	ds_read_b128 v[140:143], v139
	ds_read_b128 v[144:147], v139 offset:1024
	ds_read_b128 v[148:151], v139 offset:2048
	ds_read_b128 v[152:155], v139 offset:3072
	v_lshl_add_u64 v[64:65], s[18:19], 0, v[128:129]
	v_lshl_add_u64 v[64:65], v[64:65], 0, s[4:5]
	v_mov_b32_e32 v128, v133
	v_lshl_add_u64 v[64:65], s[18:19], 0, v[128:129]
	v_lshl_add_u64 v[64:65], v[64:65], 0, s[4:5]
	s_barrier
	s_waitcnt lgkmcnt(0)
	s_waitcnt lgkmcnt(0)
	v_mfma_scale_f32_16x16x128_f8f6f4 v[92:95], v[140:147], v[16:23], v[204:207], v136, v136 op_sel_hi:[0,0,0]
	v_mfma_scale_f32_16x16x128_f8f6f4 v[88:91], v[148:155], v[16:23], v[156:159], v136, v136 op_sel_hi:[0,0,0]
	s_add_u32 s98, s18, s4
	s_addc_u32 s99, s19, s5
	s_mov_b32 m0, s46
	v_mfma_scale_f32_16x16x128_f8f6f4 v[84:87], v[140:147], v[24:31], v[160:163], v136, v136 op_sel_hi:[0,0,0]
	global_load_lds_dwordx4 v132, s[98:99]
	v_mfma_scale_f32_16x16x128_f8f6f4 v[80:83], v[148:155], v[24:31], v[164:167], v136, v136 op_sel_hi:[0,0,0]
	v_mfma_scale_f32_16x16x128_f8f6f4 v[76:79], v[140:147], v[32:39], v[168:171], v136, v136 op_sel_hi:[0,0,0]
	s_mov_b32 m0, s47
	v_mfma_scale_f32_16x16x128_f8f6f4 v[72:75], v[148:155], v[32:39], v[172:175], v136, v136 op_sel_hi:[0,0,0]
	global_load_lds_dwordx4 v133, s[98:99]
	v_mfma_scale_f32_16x16x128_f8f6f4 v[68:71], v[140:147], v[40:47], v[176:179], v136, v136 op_sel_hi:[0,0,0]
	v_mfma_scale_f32_16x16x128_f8f6f4 v[64:67], v[148:155], v[40:47], v[180:183], v136, v136 op_sel_hi:[0,0,0]
	v_mov_b32_e32 v128, v132
	s_barrier
	ds_read_b128 v[16:19], v135 offset:49152
	ds_read_b128 v[20:23], v135 offset:50176
	ds_read_b128 v[156:159], v135 offset:51200
	ds_read_b128 v[160:163], v135 offset:52224
	ds_read_b128 v[164:167], v135 offset:53248
	ds_read_b128 v[168:171], v135 offset:54272
	ds_read_b128 v[172:175], v135 offset:55296
	ds_read_b128 v[176:179], v135 offset:56320
	v_lshl_add_u64 v[24:25], s[20:21], 0, v[128:129]
	v_lshl_add_u64 v[24:25], v[24:25], 0, s[4:5]
	v_mov_b32_e32 v128, v133
	v_lshl_add_u64 v[24:25], s[20:21], 0, v[128:129]
	v_lshl_add_u64 v[24:25], v[24:25], 0, s[4:5]
	s_barrier
	s_waitcnt lgkmcnt(0)
	s_waitcnt lgkmcnt(0)
	v_mfma_scale_f32_16x16x128_f8f6f4 v[60:63], v[0:7], v[16:23], v[60:63], v136, v136 op_sel_hi:[0,0,0]
	v_mfma_scale_f32_16x16x128_f8f6f4 v[56:59], v[8:15], v[16:23], v[56:59], v136, v136 op_sel_hi:[0,0,0]
	s_add_u32 s98, s20, s4
	s_addc_u32 s99, s21, s5
	s_mov_b32 m0, s36
	v_mfma_scale_f32_16x16x128_f8f6f4 v[52:55], v[0:7], v[156:163], v[52:55], v136, v136 op_sel_hi:[0,0,0]
	global_load_lds_dwordx4 v132, s[98:99]
	v_mfma_scale_f32_16x16x128_f8f6f4 v[48:51], v[8:15], v[156:163], v[48:51], v136, v136 op_sel_hi:[0,0,0]
	v_mfma_scale_f32_16x16x128_f8f6f4 v[44:47], v[0:7], v[164:171], v[184:187], v136, v136 op_sel_hi:[0,0,0]
	s_mov_b32 m0, s37
	v_mfma_scale_f32_16x16x128_f8f6f4 v[40:43], v[8:15], v[164:171], v[208:211], v136, v136 op_sel_hi:[0,0,0]
	global_load_lds_dwordx4 v133, s[98:99]
	v_mfma_scale_f32_16x16x128_f8f6f4 v[36:39], v[0:7], v[172:179], v[212:215], v136, v136 op_sel_hi:[0,0,0]
	v_mfma_scale_f32_16x16x128_f8f6f4 v[32:35], v[8:15], v[172:179], v[216:219], v136, v136 op_sel_hi:[0,0,0]
	s_barrier
	s_add_u32 s18, s18, 0x30080
	s_addc_u32 s19, s19, 0
	v_mov_b32_e32 v0, v132
	s_add_i32 s20, s45, s24
	s_nop 0
	v_mov_b32_e32 v0, v133
	s_nop 0
	s_waitcnt vmcnt(4)
	s_barrier
	v_mfma_scale_f32_16x16x128_f8f6f4 v[28:31], v[140:147], v[16:23], v[220:223], v136, v136 op_sel_hi:[0,0,0]
	v_mfma_scale_f32_16x16x128_f8f6f4 v[24:27], v[148:155], v[16:23], v[224:227], v136, v136 op_sel_hi:[0,0,0]
	s_mov_b32 m0, s20
	v_mfma_scale_f32_16x16x128_f8f6f4 v[20:23], v[140:147], v[156:163], v[228:231], v136, v136 op_sel_hi:[0,0,0]
	global_load_lds_dwordx4 v132, s[18:19]
	v_mfma_scale_f32_16x16x128_f8f6f4 v[16:19], v[148:155], v[156:163], v[232:235], v136, v136 op_sel_hi:[0,0,0]
	v_mfma_scale_f32_16x16x128_f8f6f4 v[12:15], v[140:147], v[164:171], v[236:239], v136, v136 op_sel_hi:[0,0,0]
	s_add_i32 m0, s20, 0x2000
	v_mfma_scale_f32_16x16x128_f8f6f4 v[8:11], v[148:155], v[164:171], v[240:243], v136, v136 op_sel_hi:[0,0,0]
	global_load_lds_dwordx4 v133, s[18:19]
	v_mfma_scale_f32_16x16x128_f8f6f4 v[4:7], v[140:147], v[172:179], v[244:247], v136, v136 op_sel_hi:[0,0,0]
	v_mfma_scale_f32_16x16x128_f8f6f4 v[0:3], v[148:155], v[172:179], v[248:251], v136, v136 op_sel_hi:[0,0,0]
	s_add_i32 s54, s54, 2
	s_add_u32 s16, s16, 0x100
	s_addc_u32 s17, s17, 0
	s_add_u32 s52, s52, 0x100
	s_addc_u32 s53, s53, 0
	s_cmp_gt_u32 s54, 9
	s_barrier
	s_cbranch_scc0 .LBB0_2382
	s_branch .Lpeel_exit_4
.LBB0_2382:
	ds_read_b128 v[140:143], v134
	ds_read_b128 v[144:147], v134 offset:1024
	ds_read_b128 v[148:151], v134 offset:2048
	ds_read_b128 v[152:155], v134 offset:3072
	s_add_u32 s18, s16, 0xfffd0080
	s_addc_u32 s19, s17, -1
	s_cmp_eq_u32 s54, 8
	s_cselect_b32 s21, s15, s19
	s_cselect_b32 s20, s14, s18
	s_cselect_b32 s19, s13, s53
	s_cselect_b32 s18, s12, s52
	v_mov_b32_e32 v128, v132
	ds_read_b128 v[156:159], v135
	ds_read_b128 v[160:163], v135 offset:1024
	ds_read_b128 v[164:167], v135 offset:2048
	ds_read_b128 v[168:171], v135 offset:3072
	ds_read_b128 v[172:175], v135 offset:4096
	ds_read_b128 v[176:179], v135 offset:5120
	ds_read_b128 v[180:183], v135 offset:6144
	ds_read_b128 v[184:187], v135 offset:7168
	s_nop 0
	v_mov_b32_e32 v128, v133
	s_nop 0
	s_waitcnt lgkmcnt(8)
	s_barrier
	s_waitcnt lgkmcnt(0)
	s_waitcnt lgkmcnt(0)
	v_mfma_scale_f32_16x16x128_f8f6f4 v[124:127], v[140:147], v[156:163], v[124:127], v136, v136 op_sel_hi:[0,0,0]
	v_mfma_scale_f32_16x16x128_f8f6f4 v[120:123], v[148:155], v[156:163], v[120:123], v136, v136 op_sel_hi:[0,0,0]
	s_mov_b32 m0, s39
	v_mfma_scale_f32_16x16x128_f8f6f4 v[116:119], v[140:147], v[164:171], v[116:119], v136, v136 op_sel_hi:[0,0,0]
	global_load_lds_dwordx4 v132, s[16:17]
	v_mfma_scale_f32_16x16x128_f8f6f4 v[112:115], v[148:155], v[164:171], v[112:115], v136, v136 op_sel_hi:[0,0,0]
	v_mfma_scale_f32_16x16x128_f8f6f4 v[188:191], v[140:147], v[172:179], v[108:111], v136, v136 op_sel_hi:[0,0,0]
	s_mov_b32 m0, s40
	v_mfma_scale_f32_16x16x128_f8f6f4 v[192:195], v[148:155], v[172:179], v[104:107], v136, v136 op_sel_hi:[0,0,0]
	global_load_lds_dwordx4 v133, s[16:17]
	v_mfma_scale_f32_16x16x128_f8f6f4 v[196:199], v[140:147], v[180:187], v[100:103], v136, v136 op_sel_hi:[0,0,0]
	v_mfma_scale_f32_16x16x128_f8f6f4 v[200:203], v[148:155], v[180:187], v[96:99], v136, v136 op_sel_hi:[0,0,0]
	s_barrier
	v_mov_b32_e32 v128, v132
	s_nop 2
	ds_read_b128 v[96:99], v137
	ds_read_b128 v[100:103], v137 offset:1024
	ds_read_b128 v[104:107], v137 offset:2048
	ds_read_b128 v[108:111], v137 offset:3072
	s_nop 0
	v_mov_b32_e32 v128, v133
	s_nop 0
	s_barrier
	s_waitcnt lgkmcnt(0)
	s_waitcnt lgkmcnt(0)
	v_mfma_scale_f32_16x16x128_f8f6f4 v[204:207], v[96:103], v[156:163], v[92:95], v136, v136 op_sel_hi:[0,0,0]
	v_mfma_scale_f32_16x16x128_f8f6f4 v[156:159], v[104:111], v[156:163], v[88:91], v136, v136 op_sel_hi:[0,0,0]
	s_mov_b32 m0, s41
	v_mfma_scale_f32_16x16x128_f8f6f4 v[160:163], v[96:103], v[164:171], v[84:87], v136, v136 op_sel_hi:[0,0,0]
	global_load_lds_dwordx4 v132, s[18:19]
	v_mfma_scale_f32_16x16x128_f8f6f4 v[164:167], v[104:111], v[164:171], v[80:83], v136, v136 op_sel_hi:[0,0,0]
	v_mfma_scale_f32_16x16x128_f8f6f4 v[168:171], v[96:103], v[172:179], v[76:79], v136, v136 op_sel_hi:[0,0,0]
	s_mov_b32 m0, s42
	v_mfma_scale_f32_16x16x128_f8f6f4 v[172:175], v[104:111], v[172:179], v[72:75], v136, v136 op_sel_hi:[0,0,0]
	global_load_lds_dwordx4 v133, s[18:19]
	v_mfma_scale_f32_16x16x128_f8f6f4 v[176:179], v[96:103], v[180:187], v[68:71], v136, v136 op_sel_hi:[0,0,0]
	v_mfma_scale_f32_16x16x128_f8f6f4 v[180:183], v[104:111], v[180:187], v[64:67], v136, v136 op_sel_hi:[0,0,0]
	v_mov_b32_e32 v128, v132
	s_barrier
	s_nop 2
	ds_read_b128 v[64:67], v135 offset:16384
	ds_read_b128 v[68:71], v135 offset:17408
	ds_read_b128 v[72:75], v135 offset:18432
	ds_read_b128 v[76:79], v135 offset:19456
	ds_read_b128 v[80:83], v135 offset:20480
	ds_read_b128 v[84:87], v135 offset:21504
	ds_read_b128 v[88:91], v135 offset:22528
	ds_read_b128 v[92:95], v135 offset:23552
	s_nop 0
	v_mov_b32_e32 v128, v133
	s_nop 0
	s_barrier
	s_waitcnt lgkmcnt(0)
	s_waitcnt lgkmcnt(0)
	v_mfma_scale_f32_16x16x128_f8f6f4 v[60:63], v[140:147], v[64:71], v[60:63], v136, v136 op_sel_hi:[0,0,0]
	v_mfma_scale_f32_16x16x128_f8f6f4 v[56:59], v[148:155], v[64:71], v[56:59], v136, v136 op_sel_hi:[0,0,0]
	s_mov_b32 m0, s25
	v_mfma_scale_f32_16x16x128_f8f6f4 v[52:55], v[140:147], v[72:79], v[52:55], v136, v136 op_sel_hi:[0,0,0]
	global_load_lds_dwordx4 v132, s[20:21]
	v_mfma_scale_f32_16x16x128_f8f6f4 v[48:51], v[148:155], v[72:79], v[48:51], v136, v136 op_sel_hi:[0,0,0]
	v_mfma_scale_f32_16x16x128_f8f6f4 v[184:187], v[140:147], v[80:87], v[44:47], v136, v136 op_sel_hi:[0,0,0]
	s_mov_b32 m0, s26
	v_mfma_scale_f32_16x16x128_f8f6f4 v[208:211], v[148:155], v[80:87], v[40:43], v136, v136 op_sel_hi:[0,0,0]
	global_load_lds_dwordx4 v133, s[20:21]
	v_mfma_scale_f32_16x16x128_f8f6f4 v[212:215], v[140:147], v[88:95], v[36:39], v136, v136 op_sel_hi:[0,0,0]
	v_mfma_scale_f32_16x16x128_f8f6f4 v[216:219], v[148:155], v[88:95], v[32:35], v136, v136 op_sel_hi:[0,0,0]
	s_barrier
	s_add_u32 s56, s18, 0x30000
	s_nop 3
	v_mov_b32_e32 v32, v132
	s_addc_u32 s57, s19, 0
	s_nop 0
	v_mov_b32_e32 v32, v133
	s_nop 0
	s_waitcnt vmcnt(4)
	s_barrier
	v_mfma_scale_f32_16x16x128_f8f6f4 v[220:223], v[96:103], v[64:71], v[28:31], v136, v136 op_sel_hi:[0,0,0]
	v_mfma_scale_f32_16x16x128_f8f6f4 v[224:227], v[104:111], v[64:71], v[24:27], v136, v136 op_sel_hi:[0,0,0]
	s_mov_b32 m0, s43
	v_mfma_scale_f32_16x16x128_f8f6f4 v[228:231], v[96:103], v[72:79], v[20:23], v136, v136 op_sel_hi:[0,0,0]
	global_load_lds_dwordx4 v132, s[56:57]
	v_mfma_scale_f32_16x16x128_f8f6f4 v[232:235], v[104:111], v[72:79], v[16:19], v136, v136 op_sel_hi:[0,0,0]
	v_mfma_scale_f32_16x16x128_f8f6f4 v[236:239], v[96:103], v[80:87], v[12:15], v136, v136 op_sel_hi:[0,0,0]
	s_mov_b32 m0, s44
	v_mfma_scale_f32_16x16x128_f8f6f4 v[240:243], v[104:111], v[80:87], v[8:11], v136, v136 op_sel_hi:[0,0,0]
	global_load_lds_dwordx4 v133, s[56:57]
	v_mfma_scale_f32_16x16x128_f8f6f4 v[244:247], v[96:103], v[88:95], v[4:7], v136, v136 op_sel_hi:[0,0,0]
	v_mfma_scale_f32_16x16x128_f8f6f4 v[248:251], v[104:111], v[88:95], v[0:3], v136, v136 op_sel_hi:[0,0,0]
	s_barrier
	s_nop 4
	ds_read_b128 v[0:3], v138
	ds_read_b128 v[4:7], v138 offset:1024
	ds_read_b128 v[8:11], v138 offset:2048
	ds_read_b128 v[12:15], v138 offset:3072
	s_add_u32 s56, s20, 0x30000
	v_mov_b32_e32 v64, v132
	ds_read_b128 v[16:19], v135 offset:32768
	ds_read_b128 v[20:23], v135 offset:33792
	ds_read_b128 v[24:27], v135 offset:34816
	ds_read_b128 v[28:31], v135 offset:35840
	ds_read_b128 v[32:35], v135 offset:36864
	ds_read_b128 v[36:39], v135 offset:37888
	ds_read_b128 v[40:43], v135 offset:38912
	ds_read_b128 v[44:47], v135 offset:39936
	s_addc_u32 s57, s21, 0
	s_nop 0
	v_mov_b32_e32 v64, v133
	s_nop 0
	s_waitcnt lgkmcnt(8)
	s_barrier
	s_waitcnt lgkmcnt(0)
	s_waitcnt lgkmcnt(0)
	v_mfma_scale_f32_16x16x128_f8f6f4 v[124:127], v[0:7], v[16:23], v[124:127], v136, v136 op_sel_hi:[0,0,0]
	v_mfma_scale_f32_16x16x128_f8f6f4 v[120:123], v[8:15], v[16:23], v[120:123], v136, v136 op_sel_hi:[0,0,0]
	s_mov_b32 m0, s27
	v_mfma_scale_f32_16x16x128_f8f6f4 v[116:119], v[0:7], v[24:31], v[116:119], v136, v136 op_sel_hi:[0,0,0]
	global_load_lds_dwordx4 v132, s[56:57]
	v_mfma_scale_f32_16x16x128_f8f6f4 v[112:115], v[8:15], v[24:31], v[112:115], v136, v136 op_sel_hi:[0,0,0]
	v_mfma_scale_f32_16x16x128_f8f6f4 v[108:111], v[0:7], v[32:39], v[188:191], v136, v136 op_sel_hi:[0,0,0]
	s_mov_b32 m0, s28
	v_mfma_scale_f32_16x16x128_f8f6f4 v[104:107], v[8:15], v[32:39], v[192:195], v136, v136 op_sel_hi:[0,0,0]
	global_load_lds_dwordx4 v133, s[56:57]
	v_mfma_scale_f32_16x16x128_f8f6f4 v[100:103], v[0:7], v[40:47], v[196:199], v136, v136 op_sel_hi:[0,0,0]
	v_mfma_scale_f32_16x16x128_f8f6f4 v[96:99], v[8:15], v[40:47], v[200:203], v136, v136 op_sel_hi:[0,0,0]
	s_barrier
	v_mov_b32_e32 v128, v132
	ds_read_b128 v[140:143], v139
	ds_read_b128 v[144:147], v139 offset:1024
	ds_read_b128 v[148:151], v139 offset:2048
	ds_read_b128 v[152:155], v139 offset:3072
	v_lshl_add_u64 v[64:65], s[18:19], 0, v[128:129]
	v_lshl_add_u64 v[64:65], v[64:65], 0, s[4:5]
	v_mov_b32_e32 v128, v133
	v_lshl_add_u64 v[64:65], s[18:19], 0, v[128:129]
	v_lshl_add_u64 v[64:65], v[64:65], 0, s[4:5]
	s_barrier
	s_waitcnt lgkmcnt(0)
	s_waitcnt lgkmcnt(0)
	v_mfma_scale_f32_16x16x128_f8f6f4 v[92:95], v[140:147], v[16:23], v[204:207], v136, v136 op_sel_hi:[0,0,0]
	v_mfma_scale_f32_16x16x128_f8f6f4 v[88:91], v[148:155], v[16:23], v[156:159], v136, v136 op_sel_hi:[0,0,0]
	s_add_u32 s98, s18, s4
	s_addc_u32 s99, s19, s5
	s_mov_b32 m0, s46
	v_mfma_scale_f32_16x16x128_f8f6f4 v[84:87], v[140:147], v[24:31], v[160:163], v136, v136 op_sel_hi:[0,0,0]
	global_load_lds_dwordx4 v132, s[98:99]
	v_mfma_scale_f32_16x16x128_f8f6f4 v[80:83], v[148:155], v[24:31], v[164:167], v136, v136 op_sel_hi:[0,0,0]
	v_mfma_scale_f32_16x16x128_f8f6f4 v[76:79], v[140:147], v[32:39], v[168:171], v136, v136 op_sel_hi:[0,0,0]
	s_mov_b32 m0, s47
	v_mfma_scale_f32_16x16x128_f8f6f4 v[72:75], v[148:155], v[32:39], v[172:175], v136, v136 op_sel_hi:[0,0,0]
	global_load_lds_dwordx4 v133, s[98:99]
	v_mfma_scale_f32_16x16x128_f8f6f4 v[68:71], v[140:147], v[40:47], v[176:179], v136, v136 op_sel_hi:[0,0,0]
	v_mfma_scale_f32_16x16x128_f8f6f4 v[64:67], v[148:155], v[40:47], v[180:183], v136, v136 op_sel_hi:[0,0,0]
	v_mov_b32_e32 v128, v132
	s_barrier
	ds_read_b128 v[16:19], v135 offset:49152
	ds_read_b128 v[20:23], v135 offset:50176
	ds_read_b128 v[156:159], v135 offset:51200
	ds_read_b128 v[160:163], v135 offset:52224
	ds_read_b128 v[164:167], v135 offset:53248
	ds_read_b128 v[168:171], v135 offset:54272
	ds_read_b128 v[172:175], v135 offset:55296
	ds_read_b128 v[176:179], v135 offset:56320
	v_lshl_add_u64 v[24:25], s[20:21], 0, v[128:129]
	v_lshl_add_u64 v[24:25], v[24:25], 0, s[4:5]
	v_mov_b32_e32 v128, v133
	v_lshl_add_u64 v[24:25], s[20:21], 0, v[128:129]
	v_lshl_add_u64 v[24:25], v[24:25], 0, s[4:5]
	s_barrier
	s_waitcnt lgkmcnt(0)
	s_waitcnt lgkmcnt(0)
	v_mfma_scale_f32_16x16x128_f8f6f4 v[60:63], v[0:7], v[16:23], v[60:63], v136, v136 op_sel_hi:[0,0,0]
	v_mfma_scale_f32_16x16x128_f8f6f4 v[56:59], v[8:15], v[16:23], v[56:59], v136, v136 op_sel_hi:[0,0,0]
	s_add_u32 s98, s20, s4
	s_addc_u32 s99, s21, s5
	s_mov_b32 m0, s36
	v_mfma_scale_f32_16x16x128_f8f6f4 v[52:55], v[0:7], v[156:163], v[52:55], v136, v136 op_sel_hi:[0,0,0]
	global_load_lds_dwordx4 v132, s[98:99]
	v_mfma_scale_f32_16x16x128_f8f6f4 v[48:51], v[8:15], v[156:163], v[48:51], v136, v136 op_sel_hi:[0,0,0]
	v_mfma_scale_f32_16x16x128_f8f6f4 v[44:47], v[0:7], v[164:171], v[184:187], v136, v136 op_sel_hi:[0,0,0]
	s_mov_b32 m0, s37
	v_mfma_scale_f32_16x16x128_f8f6f4 v[40:43], v[8:15], v[164:171], v[208:211], v136, v136 op_sel_hi:[0,0,0]
	global_load_lds_dwordx4 v133, s[98:99]
	v_mfma_scale_f32_16x16x128_f8f6f4 v[36:39], v[0:7], v[172:179], v[212:215], v136, v136 op_sel_hi:[0,0,0]
	v_mfma_scale_f32_16x16x128_f8f6f4 v[32:35], v[8:15], v[172:179], v[216:219], v136, v136 op_sel_hi:[0,0,0]
	s_barrier
	s_add_u32 s18, s18, 0x30080
	s_addc_u32 s19, s19, 0
	v_mov_b32_e32 v0, v132
	s_add_i32 s20, s45, s24
	s_nop 0
	v_mov_b32_e32 v0, v133
	s_nop 0
	s_waitcnt vmcnt(4)
	s_barrier
	v_mfma_scale_f32_16x16x128_f8f6f4 v[28:31], v[140:147], v[16:23], v[220:223], v136, v136 op_sel_hi:[0,0,0]
	v_mfma_scale_f32_16x16x128_f8f6f4 v[24:27], v[148:155], v[16:23], v[224:227], v136, v136 op_sel_hi:[0,0,0]
	s_mov_b32 m0, s20
	v_mfma_scale_f32_16x16x128_f8f6f4 v[20:23], v[140:147], v[156:163], v[228:231], v136, v136 op_sel_hi:[0,0,0]
	global_load_lds_dwordx4 v132, s[18:19]
	v_mfma_scale_f32_16x16x128_f8f6f4 v[16:19], v[148:155], v[156:163], v[232:235], v136, v136 op_sel_hi:[0,0,0]
	v_mfma_scale_f32_16x16x128_f8f6f4 v[12:15], v[140:147], v[164:171], v[236:239], v136, v136 op_sel_hi:[0,0,0]
	s_add_i32 m0, s20, 0x2000
	v_mfma_scale_f32_16x16x128_f8f6f4 v[8:11], v[148:155], v[164:171], v[240:243], v136, v136 op_sel_hi:[0,0,0]
	global_load_lds_dwordx4 v133, s[18:19]
	v_mfma_scale_f32_16x16x128_f8f6f4 v[4:7], v[140:147], v[172:179], v[244:247], v136, v136 op_sel_hi:[0,0,0]
	v_mfma_scale_f32_16x16x128_f8f6f4 v[0:3], v[148:155], v[172:179], v[248:251], v136, v136 op_sel_hi:[0,0,0]
	s_add_i32 s54, s54, 2
	s_add_u32 s16, s16, 0x100
	s_addc_u32 s17, s17, 0
	s_add_u32 s52, s52, 0x100
	s_addc_u32 s53, s53, 0
	s_cmp_gt_u32 s54, 9
	s_barrier
	s_cbranch_scc0 .LBB0_2382

.LBB0_3189:
	v_readlane_b32 s2, v252, 10
	s_lshl_b32 s2, s2, 10
	v_lshlrev_b32_e32 v1, 4, v0
	v_add_u32_e32 v2, s2, v1
	v_ashrrev_i32_e32 v3, 31, v2
	v_lshrrev_b32_e32 v3, 22, v3
	v_add_u32_e32 v3, v2, v3
	v_ashrrev_i32_e32 v3, 10, v3
	v_mul_i32_i24_e32 v4, 0x400, v3
	v_sub_u32_e32 v4, v2, v4
	v_lshrrev_b32_e32 v5, 4, v4
	v_bitop3_b32 v4, v5, v4, 32 bitop3:0x6c
	v_ashrrev_i32_e32 v6, 31, v4
	v_lshrrev_b32_e32 v6, 26, v6
	v_add_u32_e32 v6, v4, v6
	v_lshrrev_b32_e32 v7, 6, v6
	v_and_b32_e32 v6, 0xc0, v6
	v_lshlrev_b32_e32 v5, 3, v3
	v_lshlrev_b32_e32 v3, 5, v3
	v_sub_u32_e32 v4, v4, v6
	v_mov_b32_e32 v6, 1
	v_and_b32_e32 v5, 0x1ffff0, v5
	v_and_b32_e32 v3, 32, v3
	v_ashrrev_i16_sdwa v4, v6, sext(v4) dst_sel:DWORD dst_unused:UNUSED_PAD src0_sel:DWORD src1_sel:BYTE_0
	v_add_u32_sdwa v3, v3, sext(v4) dst_sel:DWORD dst_unused:UNUSED_PAD src0_sel:DWORD src1_sel:WORD_0
	v_add_lshl_u32 v4, v7, v5, 11
	v_add_u32_e32 v2, 0x2000, v2
	v_lshl_add_u32 v198, v3, 1, v4
	v_ashrrev_i32_e32 v3, 31, v2
	v_lshrrev_b32_e32 v3, 22, v3
	v_add_u32_e32 v3, v2, v3
	v_ashrrev_i32_e32 v3, 10, v3
	v_mul_i32_i24_e32 v4, 0x400, v3
	v_sub_u32_e32 v2, v2, v4
	v_lshrrev_b32_e32 v4, 4, v2
	v_bitop3_b32 v2, v4, v2, 32 bitop3:0x6c
	v_ashrrev_i32_e32 v5, 31, v2
	v_lshrrev_b32_e32 v5, 26, v5
	v_add_u32_e32 v5, v2, v5
	v_lshrrev_b32_e32 v7, 6, v5
	v_and_b32_e32 v5, 0xffc0, v5
	v_sub_u32_e32 v2, v2, v5
	v_lshrrev_b16_e32 v5, 7, v2
	v_and_b32_e32 v5, 1, v5
	v_lshlrev_b32_e32 v4, 3, v3
	v_lshlrev_b32_e32 v3, 5, v3
	v_add_u16_e32 v2, v2, v5
	v_and_b32_e32 v4, 0x1ffff0, v4
	v_and_b32_e32 v3, 32, v3
	v_ashrrev_i16_sdwa v2, v6, sext(v2) dst_sel:DWORD dst_unused:UNUSED_PAD src0_sel:DWORD src1_sel:BYTE_0
	v_add_u32_sdwa v2, v3, sext(v2) dst_sel:DWORD dst_unused:UNUSED_PAD src0_sel:DWORD src1_sel:WORD_0
	v_add_lshl_u32 v3, v7, v4, 11
	s_add_i32 s40, s2, 0
	v_lshl_add_u32 v199, v2, 1, v3
	s_add_i32 s41, s40, 0x10000
	v_mov_b32_e32 v2, v198
	s_mov_b32 m0, s41
	s_add_i32 s42, s40, 0x12000
	global_load_lds_dwordx4 v2, s[6:7]
	v_mov_b32_e32 v2, v199
	s_mov_b32 m0, s42
	v_readlane_b32 s3, v252, 2
	global_load_lds_dwordx4 v2, s[6:7]
	v_mov_b32_e32 v2, v198
	s_mov_b32 m0, s40
	s_lshr_b32 s10, s3, 8
	global_load_lds_dwordx4 v2, s[8:9]
	v_mov_b32_e32 v2, v199
	s_add_i32 s43, s40, 0x2000
	s_mov_b32 m0, s43
	s_add_u32 s2, s6, 0x40000
	global_load_lds_dwordx4 v2, s[8:9]
	s_addc_u32 s3, s7, 0
	s_add_i32 s44, s40, 0x14000
	v_mov_b32_e32 v2, v198
	s_mov_b32 m0, s44
	s_add_i32 s45, s40, 0x16000
	global_load_lds_dwordx4 v2, s[2:3]
	v_mov_b32_e32 v2, v199
	s_mov_b32 m0, s45
	s_movk_i32 s48, 0x2000
	global_load_lds_dwordx4 v2, s[2:3]
	s_add_u32 s2, s8, 0x40000
	s_addc_u32 s3, s9, 0
	s_add_i32 s46, s40, 0x4000
	v_mov_b32_e32 v2, v198
	s_mov_b32 m0, s46
	s_add_i32 s47, s40, 0x6000
	global_load_lds_dwordx4 v2, s[2:3]
	v_mov_b32_e32 v2, v199
	s_mov_b32 m0, s47
	s_cmp_lg_u32 s10, 1
	global_load_lds_dwordx4 v2, s[2:3]
	s_mov_b32 s49, 0
	s_cbranch_scc1 .LBB0_3191
	s_setprio 1
	s_barrier

.LBB0_3197:
	ds_read_b128 v[0:3], v201
	ds_read_b128 v[4:7], v201 offset:1024
	ds_read_b128 v[8:11], v201 offset:2048
	ds_read_b128 v[12:15], v201 offset:3072
	v_mov_b32_e32 v16, v198
	s_waitcnt lgkmcnt(0)
	ds_read_b128 v[32:35], v202
	ds_read_b128 v[36:39], v202 offset:1024
	ds_read_b128 v[40:43], v202 offset:2048
	ds_read_b128 v[44:47], v202 offset:3072
	ds_read_b128 v[48:51], v202 offset:4096
	ds_read_b128 v[52:55], v202 offset:5120
	ds_read_b128 v[56:59], v202 offset:6144
	ds_read_b128 v[60:63], v202 offset:7168
	s_add_i32 m0, s40, 0xc000
	v_cmp_ne_u32_e64 s[6:7], 1, v205
	global_load_lds_dwordx4 v16, s[34:35]
	v_mov_b32_e32 v16, v199
	s_add_i32 m0, s40, 0xe000
	s_andn2_b64 vcc, exec, s[30:31]
	global_load_lds_dwordx4 v16, s[34:35]
	s_waitcnt lgkmcnt(8)
	s_barrier
	s_waitcnt lgkmcnt(0)
	s_cbranch_vccnz .LBB0_3199
	s_waitcnt lgkmcnt(0)
	v_mfma_scale_f32_16x16x128_f8f6f4 v[192:195], v[0:7], v[32:39], v[192:195], v203, v203 op_sel_hi:[0,0,0]
	v_mfma_scale_f32_16x16x128_f8f6f4 v[188:191], v[8:15], v[32:39], v[188:191], v203, v203 op_sel_hi:[0,0,0]
	v_mfma_scale_f32_16x16x128_f8f6f4 v[176:179], v[0:7], v[40:47], v[176:179], v203, v203 op_sel_hi:[0,0,0]
	v_mfma_scale_f32_16x16x128_f8f6f4 v[172:175], v[8:15], v[40:47], v[172:175], v203, v203 op_sel_hi:[0,0,0]
	v_mfma_scale_f32_16x16x128_f8f6f4 v[160:163], v[0:7], v[48:55], v[160:163], v203, v203 op_sel_hi:[0,0,0]
	v_mfma_scale_f32_16x16x128_f8f6f4 v[156:159], v[8:15], v[48:55], v[156:159], v203, v203 op_sel_hi:[0,0,0]
	v_mfma_scale_f32_16x16x128_f8f6f4 v[144:147], v[0:7], v[56:63], v[144:147], v203, v203 op_sel_hi:[0,0,0]
	v_mfma_scale_f32_16x16x128_f8f6f4 v[140:143], v[8:15], v[56:63], v[140:143], v203, v203 op_sel_hi:[0,0,0]
.LBB0_3199:
	s_cmp_eq_u32 s69, 12
	s_cselect_b64 s[38:39], -1, 0
	s_and_b64 s[8:9], s[38:39], exec
	s_cselect_b32 s37, s25, s27
	s_cselect_b32 s36, s24, s21
	s_barrier
	v_add_u32_e32 v28, 0x14000, v200
	v_mov_b32_e32 v64, v198
	s_mov_b32 m0, s41
	ds_read_b128 v[16:19], v28
	ds_read_b128 v[20:23], v28 offset:1024
	ds_read_b128 v[24:27], v28 offset:2048
	ds_read_b128 v[28:31], v28 offset:3072
	s_andn2_b64 vcc, exec, s[28:29]
	global_load_lds_dwordx4 v64, s[36:37]
	v_mov_b32_e32 v64, v199
	s_mov_b32 m0, s42
	s_nop 0
	global_load_lds_dwordx4 v64, s[36:37]
	s_barrier
	s_waitcnt lgkmcnt(0)
	v_cndmask_b32_e64 v64, 0, 1, s[28:29]
	v_cmp_ne_u32_e64 s[8:9], 1, v64
	s_cbranch_vccnz .LBB0_3201
	s_waitcnt lgkmcnt(0)
	v_mfma_scale_f32_16x16x128_f8f6f4 v[184:187], v[16:23], v[32:39], v[184:187], v203, v203 op_sel_hi:[0,0,0]
	v_mfma_scale_f32_16x16x128_f8f6f4 v[180:183], v[24:31], v[32:39], v[180:183], v203, v203 op_sel_hi:[0,0,0]
	v_mfma_scale_f32_16x16x128_f8f6f4 v[168:171], v[16:23], v[40:47], v[168:171], v203, v203 op_sel_hi:[0,0,0]
	v_mfma_scale_f32_16x16x128_f8f6f4 v[164:167], v[24:31], v[40:47], v[164:167], v203, v203 op_sel_hi:[0,0,0]
	v_mfma_scale_f32_16x16x128_f8f6f4 v[152:155], v[16:23], v[48:55], v[152:155], v203, v203 op_sel_hi:[0,0,0]
	v_mfma_scale_f32_16x16x128_f8f6f4 v[148:151], v[24:31], v[48:55], v[148:151], v203, v203 op_sel_hi:[0,0,0]
	v_mfma_scale_f32_16x16x128_f8f6f4 v[136:139], v[16:23], v[56:63], v[136:139], v203, v203 op_sel_hi:[0,0,0]
	v_mfma_scale_f32_16x16x128_f8f6f4 v[132:135], v[24:31], v[56:63], v[132:135], v203, v203 op_sel_hi:[0,0,0]
.LBB0_3201:
	s_add_u32 s70, s34, 0xfffc0080
	s_addc_u32 s71, s35, -1
	s_and_b64 s[38:39], s[38:39], exec
	v_mov_b32_e32 v64, v198
	s_mov_b32 m0, s40
	s_cselect_b32 s39, s23, s71
	s_cselect_b32 s38, s22, s70
	s_barrier
	s_waitcnt lgkmcnt(0)
	ds_read_b128 v[32:35], v202 offset:16384
	ds_read_b128 v[36:39], v202 offset:17408
	ds_read_b128 v[40:43], v202 offset:18432
	ds_read_b128 v[44:47], v202 offset:19456
	ds_read_b128 v[48:51], v202 offset:20480
	ds_read_b128 v[52:55], v202 offset:21504
	ds_read_b128 v[56:59], v202 offset:22528
	ds_read_b128 v[60:63], v202 offset:23552
	s_and_b64 vcc, exec, s[6:7]
	global_load_lds_dwordx4 v64, s[38:39]
	v_mov_b32_e32 v64, v199
	s_mov_b32 m0, s43
	s_nop 0
	global_load_lds_dwordx4 v64, s[38:39]
	s_barrier
	s_waitcnt lgkmcnt(0)
	s_cbranch_vccnz .LBB0_3203
	s_waitcnt lgkmcnt(0)
	v_mfma_scale_f32_16x16x128_f8f6f4 v[128:131], v[0:7], v[32:39], v[128:131], v203, v203 op_sel_hi:[0,0,0]
	v_mfma_scale_f32_16x16x128_f8f6f4 v[124:127], v[8:15], v[32:39], v[124:127], v203, v203 op_sel_hi:[0,0,0]
	v_mfma_scale_f32_16x16x128_f8f6f4 v[112:115], v[0:7], v[40:47], v[112:115], v203, v203 op_sel_hi:[0,0,0]
	v_mfma_scale_f32_16x16x128_f8f6f4 v[108:111], v[8:15], v[40:47], v[108:111], v203, v203 op_sel_hi:[0,0,0]
	v_mfma_scale_f32_16x16x128_f8f6f4 v[96:99], v[0:7], v[48:55], v[96:99], v203, v203 op_sel_hi:[0,0,0]
	v_mfma_scale_f32_16x16x128_f8f6f4 v[92:95], v[8:15], v[48:55], v[92:95], v203, v203 op_sel_hi:[0,0,0]
	v_mfma_scale_f32_16x16x128_f8f6f4 v[80:83], v[0:7], v[56:63], v[80:83], v203, v203 op_sel_hi:[0,0,0]
	v_mfma_scale_f32_16x16x128_f8f6f4 v[76:79], v[8:15], v[56:63], v[76:79], v203, v203 op_sel_hi:[0,0,0]
.LBB0_3203:
	s_barrier
	s_add_u32 s70, s36, 0x40000
	v_mov_b32_e32 v0, v198
	s_mov_b32 m0, s44
	s_addc_u32 s71, s37, 0
	s_and_b64 vcc, exec, s[8:9]
	global_load_lds_dwordx4 v0, s[70:71]
	v_mov_b32_e32 v0, v199
	s_mov_b32 m0, s45
	s_nop 0
	global_load_lds_dwordx4 v0, s[70:71]
	s_waitcnt vmcnt(6)
	s_barrier
	s_cbranch_vccnz .LBB0_3205
	s_waitcnt lgkmcnt(0)
	v_mfma_scale_f32_16x16x128_f8f6f4 v[120:123], v[16:23], v[32:39], v[120:123], v203, v203 op_sel_hi:[0,0,0]
	v_mfma_scale_f32_16x16x128_f8f6f4 v[116:119], v[24:31], v[32:39], v[116:119], v203, v203 op_sel_hi:[0,0,0]
	v_mfma_scale_f32_16x16x128_f8f6f4 v[104:107], v[16:23], v[40:47], v[104:107], v203, v203 op_sel_hi:[0,0,0]
	v_mfma_scale_f32_16x16x128_f8f6f4 v[100:103], v[24:31], v[40:47], v[100:103], v203, v203 op_sel_hi:[0,0,0]
	v_mfma_scale_f32_16x16x128_f8f6f4 v[88:91], v[16:23], v[48:55], v[88:91], v203, v203 op_sel_hi:[0,0,0]
	v_mfma_scale_f32_16x16x128_f8f6f4 v[84:87], v[24:31], v[48:55], v[84:87], v203, v203 op_sel_hi:[0,0,0]
	v_mfma_scale_f32_16x16x128_f8f6f4 v[72:75], v[16:23], v[56:63], v[72:75], v203, v203 op_sel_hi:[0,0,0]
	v_mfma_scale_f32_16x16x128_f8f6f4 v[68:71], v[24:31], v[56:63], v[68:71], v203, v203 op_sel_hi:[0,0,0]
.LBB0_3205:
	v_add_u32_e32 v12, 0x18000, v200
	s_barrier
	ds_read_b128 v[0:3], v12
	ds_read_b128 v[4:7], v12 offset:1024
	ds_read_b128 v[8:11], v12 offset:2048
	ds_read_b128 v[12:15], v12 offset:3072
	s_add_u32 s70, s38, 0x40000
	v_mov_b32_e32 v16, v198
	s_mov_b32 m0, s46
	s_waitcnt lgkmcnt(0)
	ds_read_b128 v[32:35], v202 offset:32768
	ds_read_b128 v[36:39], v202 offset:33792
	ds_read_b128 v[40:43], v202 offset:34816
	ds_read_b128 v[44:47], v202 offset:35840
	ds_read_b128 v[48:51], v202 offset:36864
	ds_read_b128 v[52:55], v202 offset:37888
	ds_read_b128 v[56:59], v202 offset:38912
	ds_read_b128 v[60:63], v202 offset:39936
	s_addc_u32 s71, s39, 0
	s_and_b64 vcc, exec, s[6:7]
	global_load_lds_dwordx4 v16, s[70:71]
	v_mov_b32_e32 v16, v199
	s_mov_b32 m0, s47
	s_nop 0
	global_load_lds_dwordx4 v16, s[70:71]
	s_waitcnt lgkmcnt(8)
	s_barrier
	s_waitcnt lgkmcnt(0)
	s_cbranch_vccnz .LBB0_3207
	s_waitcnt lgkmcnt(0)
	v_mfma_scale_f32_16x16x128_f8f6f4 v[192:195], v[0:7], v[32:39], v[192:195], v203, v203 op_sel_hi:[0,0,0]
	v_mfma_scale_f32_16x16x128_f8f6f4 v[188:191], v[8:15], v[32:39], v[188:191], v203, v203 op_sel_hi:[0,0,0]
	v_mfma_scale_f32_16x16x128_f8f6f4 v[176:179], v[0:7], v[40:47], v[176:179], v203, v203 op_sel_hi:[0,0,0]
	v_mfma_scale_f32_16x16x128_f8f6f4 v[172:175], v[8:15], v[40:47], v[172:175], v203, v203 op_sel_hi:[0,0,0]
	v_mfma_scale_f32_16x16x128_f8f6f4 v[160:163], v[0:7], v[48:55], v[160:163], v203, v203 op_sel_hi:[0,0,0]
	v_mfma_scale_f32_16x16x128_f8f6f4 v[156:159], v[8:15], v[48:55], v[156:159], v203, v203 op_sel_hi:[0,0,0]
	v_mfma_scale_f32_16x16x128_f8f6f4 v[144:147], v[0:7], v[56:63], v[144:147], v203, v203 op_sel_hi:[0,0,0]
	v_mfma_scale_f32_16x16x128_f8f6f4 v[140:143], v[8:15], v[56:63], v[140:143], v203, v203 op_sel_hi:[0,0,0]
.LBB0_3207:
	s_barrier
	v_add_u32_e32 v28, 0x1c000, v200
	v_mov_b32_e32 v64, v198
	ds_read_b128 v[16:19], v28
	ds_read_b128 v[20:23], v28 offset:1024
	ds_read_b128 v[24:27], v28 offset:2048
	ds_read_b128 v[28:31], v28 offset:3072
	s_mov_b32 m0, s57
	v_lshl_add_u64 v[66:67], s[36:37], 0, v[64:65]
	v_lshl_add_u64 v[66:67], v[66:67], 0, s[2:3]
	v_mov_b32_e32 v64, v199
	global_load_lds_dwordx4 v[66:67], off
	s_mov_b32 m0, s58
	v_lshl_add_u64 v[66:67], s[36:37], 0, v[64:65]
	v_lshl_add_u64 v[66:67], v[66:67], 0, s[2:3]
	global_load_lds_dwordx4 v[66:67], off
	s_barrier
	s_waitcnt lgkmcnt(0)
	s_and_b64 vcc, exec, s[8:9]
	s_cbranch_vccnz .LBB0_3209
	s_waitcnt lgkmcnt(0)
	v_mfma_scale_f32_16x16x128_f8f6f4 v[184:187], v[16:23], v[32:39], v[184:187], v203, v203 op_sel_hi:[0,0,0]
	v_mfma_scale_f32_16x16x128_f8f6f4 v[180:183], v[24:31], v[32:39], v[180:183], v203, v203 op_sel_hi:[0,0,0]
	v_mfma_scale_f32_16x16x128_f8f6f4 v[168:171], v[16:23], v[40:47], v[168:171], v203, v203 op_sel_hi:[0,0,0]
	v_mfma_scale_f32_16x16x128_f8f6f4 v[164:167], v[24:31], v[40:47], v[164:167], v203, v203 op_sel_hi:[0,0,0]
	v_mfma_scale_f32_16x16x128_f8f6f4 v[152:155], v[16:23], v[48:55], v[152:155], v203, v203 op_sel_hi:[0,0,0]
	v_mfma_scale_f32_16x16x128_f8f6f4 v[148:151], v[24:31], v[48:55], v[148:151], v203, v203 op_sel_hi:[0,0,0]
	v_mfma_scale_f32_16x16x128_f8f6f4 v[136:139], v[16:23], v[56:63], v[136:139], v203, v203 op_sel_hi:[0,0,0]
	v_mfma_scale_f32_16x16x128_f8f6f4 v[132:135], v[24:31], v[56:63], v[132:135], v203, v203 op_sel_hi:[0,0,0]
.LBB0_3209:
	v_mov_b32_e32 v64, v198
	s_barrier
	s_waitcnt lgkmcnt(0)
	ds_read_b128 v[32:35], v202 offset:49152
	ds_read_b128 v[36:39], v202 offset:50176
	ds_read_b128 v[40:43], v202 offset:51200
	ds_read_b128 v[44:47], v202 offset:52224
	ds_read_b128 v[48:51], v202 offset:53248
	ds_read_b128 v[52:55], v202 offset:54272
	ds_read_b128 v[56:59], v202 offset:55296
	ds_read_b128 v[60:63], v202 offset:56320
	s_mov_b32 m0, s59
	v_lshl_add_u64 v[66:67], s[38:39], 0, v[64:65]
	v_lshl_add_u64 v[66:67], v[66:67], 0, s[2:3]
	v_mov_b32_e32 v64, v199
	global_load_lds_dwordx4 v[66:67], off
	s_mov_b32 m0, s60
	v_lshl_add_u64 v[66:67], s[38:39], 0, v[64:65]
	v_lshl_add_u64 v[66:67], v[66:67], 0, s[2:3]
	global_load_lds_dwordx4 v[66:67], off
	s_barrier
	s_waitcnt lgkmcnt(0)
	s_and_b64 vcc, exec, s[6:7]
	s_cbranch_vccnz .LBB0_3211
	s_waitcnt lgkmcnt(0)
	v_mfma_scale_f32_16x16x128_f8f6f4 v[128:131], v[0:7], v[32:39], v[128:131], v203, v203 op_sel_hi:[0,0,0]
	v_mfma_scale_f32_16x16x128_f8f6f4 v[124:127], v[8:15], v[32:39], v[124:127], v203, v203 op_sel_hi:[0,0,0]
	v_mfma_scale_f32_16x16x128_f8f6f4 v[112:115], v[0:7], v[40:47], v[112:115], v203, v203 op_sel_hi:[0,0,0]
	v_mfma_scale_f32_16x16x128_f8f6f4 v[108:111], v[8:15], v[40:47], v[108:111], v203, v203 op_sel_hi:[0,0,0]
	v_mfma_scale_f32_16x16x128_f8f6f4 v[96:99], v[0:7], v[48:55], v[96:99], v203, v203 op_sel_hi:[0,0,0]
	v_mfma_scale_f32_16x16x128_f8f6f4 v[92:95], v[8:15], v[48:55], v[92:95], v203, v203 op_sel_hi:[0,0,0]
	v_mfma_scale_f32_16x16x128_f8f6f4 v[80:83], v[0:7], v[56:63], v[80:83], v203, v203 op_sel_hi:[0,0,0]
	v_mfma_scale_f32_16x16x128_f8f6f4 v[76:79], v[8:15], v[56:63], v[76:79], v203, v203 op_sel_hi:[0,0,0]
.LBB0_3211:
	s_barrier
	s_add_u32 s6, s36, 0x40080
	v_mov_b32_e32 v0, v198
	s_mov_b32 m0, s61
	s_addc_u32 s7, s37, 0
	s_and_b64 vcc, exec, s[8:9]
	global_load_lds_dwordx4 v0, s[6:7]
	v_mov_b32_e32 v0, v199
	s_mov_b32 m0, s62
	s_nop 0
	global_load_lds_dwordx4 v0, s[6:7]
	s_waitcnt vmcnt(6)
	s_barrier
	s_cbranch_vccnz .LBB0_3196
	s_waitcnt lgkmcnt(0)
	v_mfma_scale_f32_16x16x128_f8f6f4 v[120:123], v[16:23], v[32:39], v[120:123], v203, v203 op_sel_hi:[0,0,0]
	v_mfma_scale_f32_16x16x128_f8f6f4 v[116:119], v[24:31], v[32:39], v[116:119], v203, v203 op_sel_hi:[0,0,0]
	v_mfma_scale_f32_16x16x128_f8f6f4 v[104:107], v[16:23], v[40:47], v[104:107], v203, v203 op_sel_hi:[0,0,0]
	v_mfma_scale_f32_16x16x128_f8f6f4 v[100:103], v[24:31], v[40:47], v[100:103], v203, v203 op_sel_hi:[0,0,0]
	v_mfma_scale_f32_16x16x128_f8f6f4 v[88:91], v[16:23], v[48:55], v[88:91], v203, v203 op_sel_hi:[0,0,0]
	v_mfma_scale_f32_16x16x128_f8f6f4 v[84:87], v[24:31], v[48:55], v[84:87], v203, v203 op_sel_hi:[0,0,0]
	v_mfma_scale_f32_16x16x128_f8f6f4 v[72:75], v[16:23], v[56:63], v[72:75], v203, v203 op_sel_hi:[0,0,0]
	v_mfma_scale_f32_16x16x128_f8f6f4 v[68:71], v[24:31], v[56:63], v[68:71], v203, v203 op_sel_hi:[0,0,0]
	s_branch .LBB0_3196

.LBB0_3983:
	s_andn2_b64 vcc, exec, s[8:9]
	s_cbranch_vccnz .LBB0_4047
	v_add_u32_e32 v1, s58, v0
	v_ashrrev_i32_e32 v2, 31, v1
	v_lshrrev_b32_e32 v2, 26, v2
	v_lshlrev_b32_e32 v3, 4, v1
	v_add_u32_e32 v2, v1, v2
	v_bfe_i32 v1, v1, 27, 1
	v_lshrrev_b32_e32 v1, 22, v1
	v_add_u32_e32 v1, v3, v1
	v_and_b32_e32 v1, 0xfffffc00, v1
	v_sub_u32_e32 v1, v3, v1
	s_waitcnt vmcnt(14)
	v_lshrrev_b32_e32 v4, 4, v1
	v_bitop3_b32 v1, v4, v1, 32 bitop3:0x6c
	v_ashrrev_i32_e32 v5, 31, v1
	v_ashrrev_i32_e32 v2, 6, v2
	v_lshrrev_b32_e32 v5, 26, v5
	v_lshlrev_b32_e32 v4, 3, v2
	v_add_u32_e32 v5, v1, v5
	v_and_b32_e32 v4, -16, v4
	v_ashrrev_i32_e32 v6, 6, v5
	v_and_b32_e32 v5, 0xc0, v5
	v_add_u32_e32 v4, v6, v4
	v_sub_u32_e32 v1, v1, v5
	v_mov_b32_e32 v6, 1
	v_lshlrev_b32_e32 v2, 5, v2
	v_ashrrev_i16_sdwa v1, v6, sext(v1) dst_sel:DWORD dst_unused:UNUSED_PAD src0_sel:DWORD src1_sel:BYTE_0
	v_and_b32_e32 v2, 32, v2
	v_bfe_i32 v1, v1, 0, 16
	v_add_lshl_u32 v2, v2, v1, 1
	v_add_u32_e32 v1, 0x2000, v3
	v_lshl_add_u32 v169, v4, 10, v2
	v_mad_u64_u32 v[180:181], s[8:9], v4, s42, v[2:3]
	v_ashrrev_i32_e32 v2, 31, v1
	v_lshrrev_b32_e32 v2, 22, v2
	v_add_u32_e32 v2, v1, v2
	v_ashrrev_i32_e32 v2, 10, v2
	v_mul_i32_i24_e32 v3, 0x400, v2
	v_sub_u32_e32 v1, v1, v3
	v_lshrrev_b32_e32 v3, 4, v1
	v_bitop3_b32 v1, v3, v1, 32 bitop3:0x6c
	v_ashrrev_i32_e32 v4, 31, v1
	v_lshrrev_b32_e32 v4, 26, v4
	v_add_u32_e32 v4, v1, v4
	v_ashrrev_i32_e32 v5, 6, v4
	v_and_b32_e32 v4, 0xc0, v4
	v_sub_u32_e32 v1, v1, v4
	v_lshlrev_b32_e32 v3, 3, v2
	v_lshlrev_b32_e32 v2, 5, v2
	v_ashrrev_i16_sdwa v1, v6, sext(v1) dst_sel:DWORD dst_unused:UNUSED_PAD src0_sel:DWORD src1_sel:BYTE_0
	v_and_b32_e32 v3, -16, v3
	v_and_b32_e32 v2, 32, v2
	v_bfe_i32 v1, v1, 0, 16
	v_add_u32_e32 v3, v5, v3
	v_add_lshl_u32 v2, v2, v1, 1
	v_mov_b32_e32 v1, v180
	s_add_i32 s3, s33, 0
	v_mad_u64_u32 v[212:213], s[8:9], v3, s42, v[2:3]
	s_add_i32 m0, s3, 0x10000
	v_lshl_add_u32 v181, v3, 10, v2
	global_load_lds_dwordx4 v1, s[6:7]
	v_mov_b32_e32 v1, v212
	s_add_i32 m0, s3, 0x12000
	s_add_i32 s11, s3, 0x2000
	global_load_lds_dwordx4 v1, s[6:7]
	v_mov_b32_e32 v1, v169
	s_mov_b32 m0, s3
	s_add_u32 s8, s6, s20
	global_load_lds_dwordx4 v1, s[4:5]
	v_mov_b32_e32 v1, v181
	s_mov_b32 m0, s11
	s_addc_u32 s9, s7, s21
	global_load_lds_dwordx4 v1, s[4:5]
	v_mov_b32_e32 v1, v180
	s_add_i32 m0, s3, 0x14000
	s_nop 0
	global_load_lds_dwordx4 v1, s[8:9]
	v_mov_b32_e32 v1, v212
	s_add_i32 m0, s3, 0x16000
	s_add_u32 s16, s4, 0x20000
	global_load_lds_dwordx4 v1, s[8:9]
	s_addc_u32 s17, s5, 0
	v_mov_b32_e32 v1, v169
	s_add_i32 s14, s3, 0x4000
	s_mov_b32 m0, s14
	s_add_i32 s15, s3, 0x6000
	global_load_lds_dwordx4 v1, s[16:17]
	v_mov_b32_e32 v1, v181
	s_mov_b32 m0, s15
	s_nop 0
	global_load_lds_dwordx4 v1, s[16:17]
	v_readlane_b32 s16, v252, 37
	v_readlane_b32 s17, v252, 38
	s_andn2_b64 vcc, exec, s[16:17]
	s_cbranch_vccnz .LBB0_3986
	s_setprio 1
	s_barrier

.Lpeel_5:
	s_add_i32 s34, s6, 2
	s_add_u32 s8, s4, 0xfffe0080
	s_addc_u32 s7, s5, -1
	s_add_i32 s30, 0, 0x10000
	v_add_u32_e32 v140, s30, v200
	ds_read_b128 v[128:131], v140
	ds_read_b128 v[132:135], v140 offset:1024
	ds_read_b128 v[136:139], v140 offset:2048
	ds_read_b128 v[140:143], v140 offset:3072
	s_cmp_eq_u32 s12, s6
	s_cselect_b32 s6, s52, s8
	s_cselect_b32 s7, s53, s7
	s_cselect_b32 s9, s55, s27
	s_cselect_b32 s8, s54, s25
	v_mov_b32_e32 v168, v169
	ds_read_b128 v[144:147], v182
	ds_read_b128 v[148:151], v182 offset:1024
	ds_read_b128 v[152:155], v182 offset:2048
	ds_read_b128 v[156:159], v182 offset:3072
	ds_read_b128 v[160:163], v182 offset:4096
	ds_read_b128 v[164:167], v182 offset:5120
	ds_read_b128 v[184:187], v182 offset:6144
	ds_read_b128 v[188:191], v182 offset:7168
	s_nop 0
	v_mov_b32_e32 v168, v181
	s_nop 0
	s_waitcnt lgkmcnt(8)
	s_barrier
	s_waitcnt lgkmcnt(0)
	s_waitcnt lgkmcnt(0)
	v_mfma_scale_f32_16x16x128_f8f6f4 v[120:123], v[128:135], v[144:151], 0, v183, v183 op_sel_hi:[0,0,0]
	v_mov_b32_e32 v170, v200
	v_mfma_scale_f32_16x16x128_f8f6f4 v[124:127], v[136:143], v[144:151], 0, v183, v183 op_sel_hi:[0,0,0]
	s_add_i32 m0, s3, 0xc000
	v_mfma_scale_f32_16x16x128_f8f6f4 v[200:203], v[136:143], v[160:167], 0, v183, v183 op_sel_hi:[0,0,0]
	global_load_lds_dwordx4 v169, s[4:5]
	v_mfma_scale_f32_16x16x128_f8f6f4 v[176:179], v[128:135], v[152:159], 0, v183, v183 op_sel_hi:[0,0,0]
	v_mfma_scale_f32_16x16x128_f8f6f4 v[192:195], v[136:143], v[152:159], 0, v183, v183 op_sel_hi:[0,0,0]
	s_add_i32 m0, s3, 0xe000
	v_mfma_scale_f32_16x16x128_f8f6f4 v[196:199], v[128:135], v[160:167], 0, v183, v183 op_sel_hi:[0,0,0]
	global_load_lds_dwordx4 v181, s[4:5]
	v_mfma_scale_f32_16x16x128_f8f6f4 v[204:207], v[128:135], v[184:191], 0, v183, v183 op_sel_hi:[0,0,0]
	v_mfma_scale_f32_16x16x128_f8f6f4 v[208:211], v[136:143], v[184:191], 0, v183, v183 op_sel_hi:[0,0,0]
	s_barrier
	s_add_i32 s35, 0, 0x14000
	s_nop 1
	v_add_u32_e32 v92, s35, v170
	v_mov_b32_e32 v104, v180
	s_add_i32 s30, s30, s33
	ds_read_b128 v[72:75], v92
	ds_read_b128 v[76:79], v92 offset:1024
	ds_read_b128 v[88:91], v92 offset:2048
	ds_read_b128 v[92:95], v92 offset:3072
	s_mov_b32 m0, s30
	s_nop 0
	global_load_lds_dwordx4 v104, s[8:9]
	v_mov_b32_e32 v104, v212
	s_add_i32 m0, s30, 0x2000
	s_nop 0
	global_load_lds_dwordx4 v104, s[8:9]
	s_barrier
	s_waitcnt lgkmcnt(0)
	s_waitcnt lgkmcnt(0)
	v_mfma_scale_f32_16x16x128_f8f6f4 v[116:119], v[144:151], v[72:79], 0, v183, v183 op_sel_hi:[0,0,0]
	v_mov_b32_e32 v168, v212
	v_mfma_scale_f32_16x16x128_f8f6f4 v[112:115], v[144:151], v[88:95], 0, v183, v183 op_sel_hi:[0,0,0]
	v_mfma_scale_f32_16x16x128_f8f6f4 v[212:215], v[152:159], v[72:79], 0, v183, v183 op_sel_hi:[0,0,0]
	v_mfma_scale_f32_16x16x128_f8f6f4 v[216:219], v[152:159], v[88:95], 0, v183, v183 op_sel_hi:[0,0,0]
	v_mfma_scale_f32_16x16x128_f8f6f4 v[220:223], v[160:167], v[72:79], 0, v183, v183 op_sel_hi:[0,0,0]
	v_mfma_scale_f32_16x16x128_f8f6f4 v[160:163], v[160:167], v[88:95], 0, v183, v183 op_sel_hi:[0,0,0]
	v_mfma_scale_f32_16x16x128_f8f6f4 v[164:167], v[184:191], v[72:79], 0, v183, v183 op_sel_hi:[0,0,0]
	v_mfma_scale_f32_16x16x128_f8f6f4 v[184:187], v[184:191], v[88:95], 0, v183, v183 op_sel_hi:[0,0,0]
	v_mov_b32_e32 v144, v169
	s_barrier
	s_nop 2
	ds_read_b128 v[64:67], v182 offset:16384
	ds_read_b128 v[68:71], v182 offset:17408
	ds_read_b128 v[80:83], v182 offset:18432
	ds_read_b128 v[84:87], v182 offset:19456
	ds_read_b128 v[96:99], v182 offset:20480
	ds_read_b128 v[100:103], v182 offset:21504
	ds_read_b128 v[104:107], v182 offset:22528
	ds_read_b128 v[108:111], v182 offset:23552
	s_nop 0
	v_mov_b32_e32 v144, v181
	s_nop 0
	s_barrier
	s_waitcnt lgkmcnt(0)
	s_waitcnt lgkmcnt(0)
	v_mfma_scale_f32_16x16x128_f8f6f4 v[224:227], v[128:135], v[64:71], 0, v183, v183 op_sel_hi:[0,0,0]
	v_mfma_scale_f32_16x16x128_f8f6f4 v[228:231], v[136:143], v[64:71], 0, v183, v183 op_sel_hi:[0,0,0]
	s_mov_b32 m0, s3
	v_mfma_scale_f32_16x16x128_f8f6f4 v[232:235], v[128:135], v[80:87], 0, v183, v183 op_sel_hi:[0,0,0]
	global_load_lds_dwordx4 v169, s[6:7]
	v_mfma_scale_f32_16x16x128_f8f6f4 v[236:239], v[136:143], v[80:87], 0, v183, v183 op_sel_hi:[0,0,0]
	v_mfma_scale_f32_16x16x128_f8f6f4 v[240:243], v[128:135], v[96:103], 0, v183, v183 op_sel_hi:[0,0,0]
	s_mov_b32 m0, s11
	v_mfma_scale_f32_16x16x128_f8f6f4 v[244:247], v[136:143], v[96:103], 0, v183, v183 op_sel_hi:[0,0,0]
	global_load_lds_dwordx4 v181, s[6:7]
	v_mfma_scale_f32_16x16x128_f8f6f4 v[248:251], v[128:135], v[104:111], 0, v183, v183 op_sel_hi:[0,0,0]
	v_mfma_scale_f32_16x16x128_f8f6f4 v[172:175], v[136:143], v[104:111], 0, v183, v183 op_sel_hi:[0,0,0]
	s_barrier
	s_add_u32 s30, s8, s20
	s_addc_u32 s31, s9, s21
	s_nop 2
	v_mov_b32_e32 v8, v180
	s_add_i32 s35, s35, s33
	s_mov_b32 s100, s35
	s_nop 0
	v_mov_b32_e32 v8, v168
	s_add_i32 s101, s35, 0x2000
	s_nop 0
	s_waitcnt vmcnt(4)
	s_barrier
	v_mfma_scale_f32_16x16x128_f8f6f4 v[52:55], v[64:71], v[72:79], 0, v183, v183 op_sel_hi:[0,0,0]
	v_mfma_scale_f32_16x16x128_f8f6f4 v[48:51], v[64:71], v[88:95], 0, v183, v183 op_sel_hi:[0,0,0]
	s_mov_b32 m0, s100
	v_mfma_scale_f32_16x16x128_f8f6f4 v[36:39], v[80:87], v[72:79], 0, v183, v183 op_sel_hi:[0,0,0]
	global_load_lds_dwordx4 v180, s[30:31]
	v_mfma_scale_f32_16x16x128_f8f6f4 v[32:35], v[80:87], v[88:95], 0, v183, v183 op_sel_hi:[0,0,0]
	v_mfma_scale_f32_16x16x128_f8f6f4 v[20:23], v[96:103], v[72:79], 0, v183, v183 op_sel_hi:[0,0,0]
	s_mov_b32 m0, s101
	v_mfma_scale_f32_16x16x128_f8f6f4 v[16:19], v[96:103], v[88:95], 0, v183, v183 op_sel_hi:[0,0,0]
	global_load_lds_dwordx4 v168, s[30:31]
	v_mfma_scale_f32_16x16x128_f8f6f4 v[4:7], v[104:111], v[72:79], 0, v183, v183 op_sel_hi:[0,0,0]
	v_mfma_scale_f32_16x16x128_f8f6f4 v[0:3], v[104:111], v[88:95], 0, v183, v183 op_sel_hi:[0,0,0]
	s_add_i32 s35, 0, 0x18000
	v_add_u32_e32 v24, s35, v170
	s_barrier
	ds_read_b128 v[8:11], v24
	ds_read_b128 v[12:15], v24 offset:1024
	ds_read_b128 v[128:131], v24 offset:2048
	ds_read_b128 v[132:135], v24 offset:3072
	s_add_u32 s36, s6, 0x20000
	v_mov_b32_e32 v64, v169
	ds_read_b128 v[24:27], v182 offset:32768
	ds_read_b128 v[28:31], v182 offset:33792
	ds_read_b128 v[40:43], v182 offset:34816
	ds_read_b128 v[44:47], v182 offset:35840
	ds_read_b128 v[56:59], v182 offset:36864
	ds_read_b128 v[60:63], v182 offset:37888
	ds_read_b128 v[136:139], v182 offset:38912
	ds_read_b128 v[140:143], v182 offset:39936
	s_addc_u32 s37, s7, 0
	s_nop 0
	v_mov_b32_e32 v64, v181
	s_nop 0
	s_waitcnt lgkmcnt(8)
	s_barrier
	s_waitcnt lgkmcnt(0)
	s_waitcnt lgkmcnt(0)
	v_mfma_scale_f32_16x16x128_f8f6f4 v[120:123], v[8:15], v[24:31], v[120:123], v183, v183 op_sel_hi:[0,0,0]
	v_mfma_scale_f32_16x16x128_f8f6f4 v[124:127], v[128:135], v[24:31], v[124:127], v183, v183 op_sel_hi:[0,0,0]
	s_mov_b32 m0, s14
	v_mfma_scale_f32_16x16x128_f8f6f4 v[108:111], v[8:15], v[40:47], v[176:179], v183, v183 op_sel_hi:[0,0,0]
	global_load_lds_dwordx4 v169, s[36:37]
	v_mfma_scale_f32_16x16x128_f8f6f4 v[104:107], v[128:135], v[40:47], v[192:195], v183, v183 op_sel_hi:[0,0,0]
	v_mfma_scale_f32_16x16x128_f8f6f4 v[92:95], v[8:15], v[56:63], v[196:199], v183, v183 op_sel_hi:[0,0,0]
	s_mov_b32 m0, s15
	v_mfma_scale_f32_16x16x128_f8f6f4 v[88:91], v[128:135], v[56:63], v[200:203], v183, v183 op_sel_hi:[0,0,0]
	global_load_lds_dwordx4 v181, s[36:37]
	v_mfma_scale_f32_16x16x128_f8f6f4 v[76:79], v[8:15], v[136:143], v[204:207], v183, v183 op_sel_hi:[0,0,0]
	s_nop 5
	v_mov_b32_e32 v200, v170
	v_mfma_scale_f32_16x16x128_f8f6f4 v[72:75], v[128:135], v[136:143], v[208:211], v183, v183 op_sel_hi:[0,0,0]
	s_barrier
	s_add_i32 s36, 0, 0x1c000
	v_add_u32_e32 v64, s36, v200
	v_mov_b32_e32 v170, v180
	ds_read_b128 v[144:147], v64
	ds_read_b128 v[148:151], v64 offset:1024
	ds_read_b128 v[152:155], v64 offset:2048
	ds_read_b128 v[156:159], v64 offset:3072
	s_add_i32 s35, s35, s33
	v_lshl_add_u64 v[64:65], s[8:9], 0, v[170:171]
	v_lshl_add_u64 v[64:65], v[64:65], 0, s[62:63]
	v_mov_b32_e32 v170, v168
	v_lshl_add_u64 v[64:65], s[8:9], 0, v[170:171]
	v_lshl_add_u64 v[64:65], v[64:65], 0, s[62:63]
	s_barrier
	s_waitcnt lgkmcnt(0)
	s_waitcnt lgkmcnt(0)
	v_mfma_scale_f32_16x16x128_f8f6f4 v[116:119], v[24:31], v[144:151], v[116:119], v183, v183 op_sel_hi:[0,0,0]
	v_mfma_scale_f32_16x16x128_f8f6f4 v[112:115], v[24:31], v[152:159], v[112:115], v183, v183 op_sel_hi:[0,0,0]
	s_add_u32 s98, s8, s62
	s_addc_u32 s99, s9, s63
	s_mov_b32 m0, s35
	v_mfma_scale_f32_16x16x128_f8f6f4 v[100:103], v[40:47], v[144:151], v[212:215], v183, v183 op_sel_hi:[0,0,0]
	global_load_lds_dwordx4 v180, s[98:99]
	v_mfma_scale_f32_16x16x128_f8f6f4 v[96:99], v[40:47], v[152:159], v[216:219], v183, v183 op_sel_hi:[0,0,0]
	s_nop 5
	v_mov_b32_e32 v212, v168
	v_mfma_scale_f32_16x16x128_f8f6f4 v[84:87], v[56:63], v[144:151], v[220:223], v183, v183 op_sel_hi:[0,0,0]
	s_add_i32 m0, s35, 0x2000
	v_mfma_scale_f32_16x16x128_f8f6f4 v[80:83], v[56:63], v[152:159], v[160:163], v183, v183 op_sel_hi:[0,0,0]
	global_load_lds_dwordx4 v168, s[98:99]
	v_mfma_scale_f32_16x16x128_f8f6f4 v[68:71], v[136:143], v[144:151], v[164:167], v183, v183 op_sel_hi:[0,0,0]
	v_mfma_scale_f32_16x16x128_f8f6f4 v[64:67], v[136:143], v[152:159], v[184:187], v183, v183 op_sel_hi:[0,0,0]
	v_mov_b32_e32 v170, v169
	s_barrier
	ds_read_b128 v[136:139], v182 offset:49152
	ds_read_b128 v[140:143], v182 offset:50176
	ds_read_b128 v[160:163], v182 offset:51200
	ds_read_b128 v[164:167], v182 offset:52224
	ds_read_b128 v[184:187], v182 offset:53248
	ds_read_b128 v[188:191], v182 offset:54272
	ds_read_b128 v[192:195], v182 offset:55296
	ds_read_b128 v[196:199], v182 offset:56320
	v_lshl_add_u64 v[24:25], s[6:7], 0, v[170:171]
	v_lshl_add_u64 v[24:25], v[24:25], 0, s[62:63]
	v_mov_b32_e32 v170, v181
	v_lshl_add_u64 v[24:25], s[6:7], 0, v[170:171]
	v_lshl_add_u64 v[24:25], v[24:25], 0, s[62:63]
	s_barrier
	s_waitcnt lgkmcnt(0)
	s_waitcnt lgkmcnt(0)
	v_mfma_scale_f32_16x16x128_f8f6f4 v[60:63], v[8:15], v[136:143], v[224:227], v183, v183 op_sel_hi:[0,0,0]
	v_mfma_scale_f32_16x16x128_f8f6f4 v[56:59], v[128:135], v[136:143], v[228:231], v183, v183 op_sel_hi:[0,0,0]
	s_add_u32 s98, s6, s62
	s_addc_u32 s99, s7, s63
	s_mov_b32 m0, s16
	v_mfma_scale_f32_16x16x128_f8f6f4 v[44:47], v[8:15], v[160:167], v[232:235], v183, v183 op_sel_hi:[0,0,0]
	global_load_lds_dwordx4 v169, s[98:99]
	v_mfma_scale_f32_16x16x128_f8f6f4 v[40:43], v[128:135], v[160:167], v[236:239], v183, v183 op_sel_hi:[0,0,0]
	v_mfma_scale_f32_16x16x128_f8f6f4 v[28:31], v[8:15], v[184:191], v[240:243], v183, v183 op_sel_hi:[0,0,0]
	s_mov_b32 m0, s17
	v_mfma_scale_f32_16x16x128_f8f6f4 v[24:27], v[128:135], v[184:191], v[244:247], v183, v183 op_sel_hi:[0,0,0]
	global_load_lds_dwordx4 v181, s[98:99]
	v_mfma_scale_f32_16x16x128_f8f6f4 v[12:15], v[8:15], v[192:199], v[248:251], v183, v183 op_sel_hi:[0,0,0]
	v_mfma_scale_f32_16x16x128_f8f6f4 v[8:11], v[128:135], v[192:199], v[172:175], v183, v183 op_sel_hi:[0,0,0]
	s_barrier
	v_mov_b32_e32 v170, v180
	s_add_i32 s6, s36, s33
	v_lshl_add_u64 v[128:129], s[30:31], 0, v[170:171]
	v_lshl_add_u64 v[128:129], v[128:129], 0, s[62:63]
	s_mov_b32 s100, s6
	v_mov_b32_e32 v170, v168
	s_add_i32 s101, s6, 0x2000
	v_lshl_add_u64 v[128:129], s[30:31], 0, v[170:171]
	v_lshl_add_u64 v[128:129], v[128:129], 0, s[62:63]
	s_waitcnt vmcnt(4)
	s_barrier
	v_mfma_scale_f32_16x16x128_f8f6f4 v[52:55], v[136:143], v[144:151], v[52:55], v183, v183 op_sel_hi:[0,0,0]
	v_mfma_scale_f32_16x16x128_f8f6f4 v[48:51], v[136:143], v[152:159], v[48:51], v183, v183 op_sel_hi:[0,0,0]
	s_add_u32 s98, s30, s62
	s_addc_u32 s99, s31, s63
	s_mov_b32 m0, s100
	v_mfma_scale_f32_16x16x128_f8f6f4 v[36:39], v[160:167], v[144:151], v[36:39], v183, v183 op_sel_hi:[0,0,0]
	global_load_lds_dwordx4 v180, s[98:99]
	v_mfma_scale_f32_16x16x128_f8f6f4 v[32:35], v[160:167], v[152:159], v[32:35], v183, v183 op_sel_hi:[0,0,0]
	v_mfma_scale_f32_16x16x128_f8f6f4 v[20:23], v[184:191], v[144:151], v[20:23], v183, v183 op_sel_hi:[0,0,0]
	s_mov_b32 m0, s101
	v_mfma_scale_f32_16x16x128_f8f6f4 v[16:19], v[184:191], v[152:159], v[16:19], v183, v183 op_sel_hi:[0,0,0]
	global_load_lds_dwordx4 v168, s[98:99]
	v_mfma_scale_f32_16x16x128_f8f6f4 v[4:7], v[192:199], v[144:151], v[4:7], v183, v183 op_sel_hi:[0,0,0]
	v_mfma_scale_f32_16x16x128_f8f6f4 v[0:3], v[192:199], v[152:159], v[0:3], v183, v183 op_sel_hi:[0,0,0]
	s_add_u32 s4, s4, 0x100
	s_addc_u32 s5, s5, 0
	s_add_u32 s25, s25, 0x100
	s_addc_u32 s27, s27, 0
	s_cmp_ge_i32 s34, s13
	s_mov_b32 s6, s34
	s_barrier
	s_cbranch_scc0 .LBB0_3995
	s_branch .Lpeel_exit_5
.LBB0_3995:
	s_add_i32 s34, s6, 2
	s_add_u32 s8, s4, 0xfffe0080
	s_addc_u32 s7, s5, -1
	s_add_i32 s30, 0, 0x10000
	v_add_u32_e32 v140, s30, v200
	ds_read_b128 v[128:131], v140
	ds_read_b128 v[132:135], v140 offset:1024
	ds_read_b128 v[136:139], v140 offset:2048
	ds_read_b128 v[140:143], v140 offset:3072
	s_cmp_eq_u32 s12, s6
	s_cselect_b32 s6, s52, s8
	s_cselect_b32 s7, s53, s7
	s_cselect_b32 s9, s55, s27
	s_cselect_b32 s8, s54, s25
	v_mov_b32_e32 v168, v169
	ds_read_b128 v[144:147], v182
	ds_read_b128 v[148:151], v182 offset:1024
	ds_read_b128 v[152:155], v182 offset:2048
	ds_read_b128 v[156:159], v182 offset:3072
	ds_read_b128 v[160:163], v182 offset:4096
	ds_read_b128 v[164:167], v182 offset:5120
	ds_read_b128 v[184:187], v182 offset:6144
	ds_read_b128 v[188:191], v182 offset:7168
	s_nop 0
	v_mov_b32_e32 v168, v181
	s_nop 0
	s_waitcnt lgkmcnt(8)
	s_barrier
	s_waitcnt lgkmcnt(0)
	s_waitcnt lgkmcnt(0)
	v_mfma_scale_f32_16x16x128_f8f6f4 v[120:123], v[128:135], v[144:151], v[120:123], v183, v183 op_sel_hi:[0,0,0]
	v_mov_b32_e32 v170, v200
	v_mfma_scale_f32_16x16x128_f8f6f4 v[124:127], v[136:143], v[144:151], v[124:127], v183, v183 op_sel_hi:[0,0,0]
	s_add_i32 m0, s3, 0xc000
	v_mfma_scale_f32_16x16x128_f8f6f4 v[200:203], v[136:143], v[160:167], v[88:91], v183, v183 op_sel_hi:[0,0,0]
	global_load_lds_dwordx4 v169, s[4:5]
	v_mfma_scale_f32_16x16x128_f8f6f4 v[176:179], v[128:135], v[152:159], v[108:111], v183, v183 op_sel_hi:[0,0,0]
	v_mfma_scale_f32_16x16x128_f8f6f4 v[192:195], v[136:143], v[152:159], v[104:107], v183, v183 op_sel_hi:[0,0,0]
	s_add_i32 m0, s3, 0xe000
	v_mfma_scale_f32_16x16x128_f8f6f4 v[196:199], v[128:135], v[160:167], v[92:95], v183, v183 op_sel_hi:[0,0,0]
	global_load_lds_dwordx4 v181, s[4:5]
	v_mfma_scale_f32_16x16x128_f8f6f4 v[204:207], v[128:135], v[184:191], v[76:79], v183, v183 op_sel_hi:[0,0,0]
	v_mfma_scale_f32_16x16x128_f8f6f4 v[208:211], v[136:143], v[184:191], v[72:75], v183, v183 op_sel_hi:[0,0,0]
	s_barrier
	s_add_i32 s35, 0, 0x14000
	s_nop 1
	v_add_u32_e32 v92, s35, v170
	v_mov_b32_e32 v104, v180
	s_add_i32 s30, s30, s33
	ds_read_b128 v[72:75], v92
	ds_read_b128 v[76:79], v92 offset:1024
	ds_read_b128 v[88:91], v92 offset:2048
	ds_read_b128 v[92:95], v92 offset:3072
	s_mov_b32 m0, s30
	s_nop 0
	global_load_lds_dwordx4 v104, s[8:9]
	v_mov_b32_e32 v104, v212
	s_add_i32 m0, s30, 0x2000
	s_nop 0
	global_load_lds_dwordx4 v104, s[8:9]
	s_barrier
	s_waitcnt lgkmcnt(0)
	s_waitcnt lgkmcnt(0)
	v_mfma_scale_f32_16x16x128_f8f6f4 v[116:119], v[144:151], v[72:79], v[116:119], v183, v183 op_sel_hi:[0,0,0]
	v_mov_b32_e32 v168, v212
	v_mfma_scale_f32_16x16x128_f8f6f4 v[112:115], v[144:151], v[88:95], v[112:115], v183, v183 op_sel_hi:[0,0,0]
	v_mfma_scale_f32_16x16x128_f8f6f4 v[212:215], v[152:159], v[72:79], v[100:103], v183, v183 op_sel_hi:[0,0,0]
	v_mfma_scale_f32_16x16x128_f8f6f4 v[216:219], v[152:159], v[88:95], v[96:99], v183, v183 op_sel_hi:[0,0,0]
	v_mfma_scale_f32_16x16x128_f8f6f4 v[220:223], v[160:167], v[72:79], v[84:87], v183, v183 op_sel_hi:[0,0,0]
	v_mfma_scale_f32_16x16x128_f8f6f4 v[160:163], v[160:167], v[88:95], v[80:83], v183, v183 op_sel_hi:[0,0,0]
	v_mfma_scale_f32_16x16x128_f8f6f4 v[164:167], v[184:191], v[72:79], v[68:71], v183, v183 op_sel_hi:[0,0,0]
	v_mfma_scale_f32_16x16x128_f8f6f4 v[184:187], v[184:191], v[88:95], v[64:67], v183, v183 op_sel_hi:[0,0,0]
	v_mov_b32_e32 v144, v169
	s_barrier
	s_nop 2
	ds_read_b128 v[64:67], v182 offset:16384
	ds_read_b128 v[68:71], v182 offset:17408
	ds_read_b128 v[80:83], v182 offset:18432
	ds_read_b128 v[84:87], v182 offset:19456
	ds_read_b128 v[96:99], v182 offset:20480
	ds_read_b128 v[100:103], v182 offset:21504
	ds_read_b128 v[104:107], v182 offset:22528
	ds_read_b128 v[108:111], v182 offset:23552
	s_nop 0
	v_mov_b32_e32 v144, v181
	s_nop 0
	s_barrier
	s_waitcnt lgkmcnt(0)
	s_waitcnt lgkmcnt(0)
	v_mfma_scale_f32_16x16x128_f8f6f4 v[224:227], v[128:135], v[64:71], v[60:63], v183, v183 op_sel_hi:[0,0,0]
	v_mfma_scale_f32_16x16x128_f8f6f4 v[228:231], v[136:143], v[64:71], v[56:59], v183, v183 op_sel_hi:[0,0,0]
	s_mov_b32 m0, s3
	v_mfma_scale_f32_16x16x128_f8f6f4 v[232:235], v[128:135], v[80:87], v[44:47], v183, v183 op_sel_hi:[0,0,0]
	global_load_lds_dwordx4 v169, s[6:7]
	v_mfma_scale_f32_16x16x128_f8f6f4 v[236:239], v[136:143], v[80:87], v[40:43], v183, v183 op_sel_hi:[0,0,0]
	v_mfma_scale_f32_16x16x128_f8f6f4 v[240:243], v[128:135], v[96:103], v[28:31], v183, v183 op_sel_hi:[0,0,0]
	s_mov_b32 m0, s11
	v_mfma_scale_f32_16x16x128_f8f6f4 v[244:247], v[136:143], v[96:103], v[24:27], v183, v183 op_sel_hi:[0,0,0]
	global_load_lds_dwordx4 v181, s[6:7]
	v_mfma_scale_f32_16x16x128_f8f6f4 v[248:251], v[128:135], v[104:111], v[12:15], v183, v183 op_sel_hi:[0,0,0]
	v_mfma_scale_f32_16x16x128_f8f6f4 v[172:175], v[136:143], v[104:111], v[8:11], v183, v183 op_sel_hi:[0,0,0]
	s_barrier
	s_add_u32 s30, s8, s20
	s_addc_u32 s31, s9, s21
	s_nop 2
	v_mov_b32_e32 v8, v180
	s_add_i32 s35, s35, s33
	s_mov_b32 s100, s35
	s_nop 0
	v_mov_b32_e32 v8, v168
	s_add_i32 s101, s35, 0x2000
	s_nop 0
	s_waitcnt vmcnt(4)
	s_barrier
	v_mfma_scale_f32_16x16x128_f8f6f4 v[52:55], v[64:71], v[72:79], v[52:55], v183, v183 op_sel_hi:[0,0,0]
	v_mfma_scale_f32_16x16x128_f8f6f4 v[48:51], v[64:71], v[88:95], v[48:51], v183, v183 op_sel_hi:[0,0,0]
	s_mov_b32 m0, s100
	v_mfma_scale_f32_16x16x128_f8f6f4 v[36:39], v[80:87], v[72:79], v[36:39], v183, v183 op_sel_hi:[0,0,0]
	global_load_lds_dwordx4 v180, s[30:31]
	v_mfma_scale_f32_16x16x128_f8f6f4 v[32:35], v[80:87], v[88:95], v[32:35], v183, v183 op_sel_hi:[0,0,0]
	v_mfma_scale_f32_16x16x128_f8f6f4 v[20:23], v[96:103], v[72:79], v[20:23], v183, v183 op_sel_hi:[0,0,0]
	s_mov_b32 m0, s101
	v_mfma_scale_f32_16x16x128_f8f6f4 v[16:19], v[96:103], v[88:95], v[16:19], v183, v183 op_sel_hi:[0,0,0]
	global_load_lds_dwordx4 v168, s[30:31]
	v_mfma_scale_f32_16x16x128_f8f6f4 v[4:7], v[104:111], v[72:79], v[4:7], v183, v183 op_sel_hi:[0,0,0]
	v_mfma_scale_f32_16x16x128_f8f6f4 v[0:3], v[104:111], v[88:95], v[0:3], v183, v183 op_sel_hi:[0,0,0]
	s_add_i32 s35, 0, 0x18000
	v_add_u32_e32 v24, s35, v170
	s_barrier
	ds_read_b128 v[8:11], v24
	ds_read_b128 v[12:15], v24 offset:1024
	ds_read_b128 v[128:131], v24 offset:2048
	ds_read_b128 v[132:135], v24 offset:3072
	s_add_u32 s36, s6, 0x20000
	v_mov_b32_e32 v64, v169
	ds_read_b128 v[24:27], v182 offset:32768
	ds_read_b128 v[28:31], v182 offset:33792
	ds_read_b128 v[40:43], v182 offset:34816
	ds_read_b128 v[44:47], v182 offset:35840
	ds_read_b128 v[56:59], v182 offset:36864
	ds_read_b128 v[60:63], v182 offset:37888
	ds_read_b128 v[136:139], v182 offset:38912
	ds_read_b128 v[140:143], v182 offset:39936
	s_addc_u32 s37, s7, 0
	s_nop 0
	v_mov_b32_e32 v64, v181
	s_nop 0
	s_waitcnt lgkmcnt(8)
	s_barrier
	s_waitcnt lgkmcnt(0)
	s_waitcnt lgkmcnt(0)
	v_mfma_scale_f32_16x16x128_f8f6f4 v[120:123], v[8:15], v[24:31], v[120:123], v183, v183 op_sel_hi:[0,0,0]
	v_mfma_scale_f32_16x16x128_f8f6f4 v[124:127], v[128:135], v[24:31], v[124:127], v183, v183 op_sel_hi:[0,0,0]
	s_mov_b32 m0, s14
	v_mfma_scale_f32_16x16x128_f8f6f4 v[108:111], v[8:15], v[40:47], v[176:179], v183, v183 op_sel_hi:[0,0,0]
	global_load_lds_dwordx4 v169, s[36:37]
	v_mfma_scale_f32_16x16x128_f8f6f4 v[104:107], v[128:135], v[40:47], v[192:195], v183, v183 op_sel_hi:[0,0,0]
	v_mfma_scale_f32_16x16x128_f8f6f4 v[92:95], v[8:15], v[56:63], v[196:199], v183, v183 op_sel_hi:[0,0,0]
	s_mov_b32 m0, s15
	v_mfma_scale_f32_16x16x128_f8f6f4 v[88:91], v[128:135], v[56:63], v[200:203], v183, v183 op_sel_hi:[0,0,0]
	global_load_lds_dwordx4 v181, s[36:37]
	v_mfma_scale_f32_16x16x128_f8f6f4 v[76:79], v[8:15], v[136:143], v[204:207], v183, v183 op_sel_hi:[0,0,0]
	s_nop 5
	v_mov_b32_e32 v200, v170
	v_mfma_scale_f32_16x16x128_f8f6f4 v[72:75], v[128:135], v[136:143], v[208:211], v183, v183 op_sel_hi:[0,0,0]
	s_barrier
	s_add_i32 s36, 0, 0x1c000
	v_add_u32_e32 v64, s36, v200
	v_mov_b32_e32 v170, v180
	ds_read_b128 v[144:147], v64
	ds_read_b128 v[148:151], v64 offset:1024
	ds_read_b128 v[152:155], v64 offset:2048
	ds_read_b128 v[156:159], v64 offset:3072
	s_add_i32 s35, s35, s33
	v_lshl_add_u64 v[64:65], s[8:9], 0, v[170:171]
	v_lshl_add_u64 v[64:65], v[64:65], 0, s[62:63]
	v_mov_b32_e32 v170, v168
	v_lshl_add_u64 v[64:65], s[8:9], 0, v[170:171]
	v_lshl_add_u64 v[64:65], v[64:65], 0, s[62:63]
	s_barrier
	s_waitcnt lgkmcnt(0)
	s_waitcnt lgkmcnt(0)
	v_mfma_scale_f32_16x16x128_f8f6f4 v[116:119], v[24:31], v[144:151], v[116:119], v183, v183 op_sel_hi:[0,0,0]
	v_mfma_scale_f32_16x16x128_f8f6f4 v[112:115], v[24:31], v[152:159], v[112:115], v183, v183 op_sel_hi:[0,0,0]
	s_add_u32 s98, s8, s62
	s_addc_u32 s99, s9, s63
	s_mov_b32 m0, s35
	v_mfma_scale_f32_16x16x128_f8f6f4 v[100:103], v[40:47], v[144:151], v[212:215], v183, v183 op_sel_hi:[0,0,0]
	global_load_lds_dwordx4 v180, s[98:99]
	v_mfma_scale_f32_16x16x128_f8f6f4 v[96:99], v[40:47], v[152:159], v[216:219], v183, v183 op_sel_hi:[0,0,0]
	s_nop 5
	v_mov_b32_e32 v212, v168
	v_mfma_scale_f32_16x16x128_f8f6f4 v[84:87], v[56:63], v[144:151], v[220:223], v183, v183 op_sel_hi:[0,0,0]
	s_add_i32 m0, s35, 0x2000
	v_mfma_scale_f32_16x16x128_f8f6f4 v[80:83], v[56:63], v[152:159], v[160:163], v183, v183 op_sel_hi:[0,0,0]
	global_load_lds_dwordx4 v168, s[98:99]
	v_mfma_scale_f32_16x16x128_f8f6f4 v[68:71], v[136:143], v[144:151], v[164:167], v183, v183 op_sel_hi:[0,0,0]
	v_mfma_scale_f32_16x16x128_f8f6f4 v[64:67], v[136:143], v[152:159], v[184:187], v183, v183 op_sel_hi:[0,0,0]
	v_mov_b32_e32 v170, v169
	s_barrier
	ds_read_b128 v[136:139], v182 offset:49152
	ds_read_b128 v[140:143], v182 offset:50176
	ds_read_b128 v[160:163], v182 offset:51200
	ds_read_b128 v[164:167], v182 offset:52224
	ds_read_b128 v[184:187], v182 offset:53248
	ds_read_b128 v[188:191], v182 offset:54272
	ds_read_b128 v[192:195], v182 offset:55296
	ds_read_b128 v[196:199], v182 offset:56320
	v_lshl_add_u64 v[24:25], s[6:7], 0, v[170:171]
	v_lshl_add_u64 v[24:25], v[24:25], 0, s[62:63]
	v_mov_b32_e32 v170, v181
	v_lshl_add_u64 v[24:25], s[6:7], 0, v[170:171]
	v_lshl_add_u64 v[24:25], v[24:25], 0, s[62:63]
	s_barrier
	s_waitcnt lgkmcnt(0)
	s_waitcnt lgkmcnt(0)
	v_mfma_scale_f32_16x16x128_f8f6f4 v[60:63], v[8:15], v[136:143], v[224:227], v183, v183 op_sel_hi:[0,0,0]
	v_mfma_scale_f32_16x16x128_f8f6f4 v[56:59], v[128:135], v[136:143], v[228:231], v183, v183 op_sel_hi:[0,0,0]
	s_add_u32 s98, s6, s62
	s_addc_u32 s99, s7, s63
	s_mov_b32 m0, s16
	v_mfma_scale_f32_16x16x128_f8f6f4 v[44:47], v[8:15], v[160:167], v[232:235], v183, v183 op_sel_hi:[0,0,0]
	global_load_lds_dwordx4 v169, s[98:99]
	v_mfma_scale_f32_16x16x128_f8f6f4 v[40:43], v[128:135], v[160:167], v[236:239], v183, v183 op_sel_hi:[0,0,0]
	v_mfma_scale_f32_16x16x128_f8f6f4 v[28:31], v[8:15], v[184:191], v[240:243], v183, v183 op_sel_hi:[0,0,0]
	s_mov_b32 m0, s17
	v_mfma_scale_f32_16x16x128_f8f6f4 v[24:27], v[128:135], v[184:191], v[244:247], v183, v183 op_sel_hi:[0,0,0]
	global_load_lds_dwordx4 v181, s[98:99]
	v_mfma_scale_f32_16x16x128_f8f6f4 v[12:15], v[8:15], v[192:199], v[248:251], v183, v183 op_sel_hi:[0,0,0]
	v_mfma_scale_f32_16x16x128_f8f6f4 v[8:11], v[128:135], v[192:199], v[172:175], v183, v183 op_sel_hi:[0,0,0]
	s_barrier
	v_mov_b32_e32 v170, v180
	s_add_i32 s6, s36, s33
	v_lshl_add_u64 v[128:129], s[30:31], 0, v[170:171]
	v_lshl_add_u64 v[128:129], v[128:129], 0, s[62:63]
	s_mov_b32 s100, s6
	v_mov_b32_e32 v170, v168
	s_add_i32 s101, s6, 0x2000
	v_lshl_add_u64 v[128:129], s[30:31], 0, v[170:171]
	v_lshl_add_u64 v[128:129], v[128:129], 0, s[62:63]
	s_waitcnt vmcnt(4)
	s_barrier
	v_mfma_scale_f32_16x16x128_f8f6f4 v[52:55], v[136:143], v[144:151], v[52:55], v183, v183 op_sel_hi:[0,0,0]
	v_mfma_scale_f32_16x16x128_f8f6f4 v[48:51], v[136:143], v[152:159], v[48:51], v183, v183 op_sel_hi:[0,0,0]
	s_add_u32 s98, s30, s62
	s_addc_u32 s99, s31, s63
	s_mov_b32 m0, s100
	v_mfma_scale_f32_16x16x128_f8f6f4 v[36:39], v[160:167], v[144:151], v[36:39], v183, v183 op_sel_hi:[0,0,0]
	global_load_lds_dwordx4 v180, s[98:99]
	v_mfma_scale_f32_16x16x128_f8f6f4 v[32:35], v[160:167], v[152:159], v[32:35], v183, v183 op_sel_hi:[0,0,0]
	v_mfma_scale_f32_16x16x128_f8f6f4 v[20:23], v[184:191], v[144:151], v[20:23], v183, v183 op_sel_hi:[0,0,0]
	s_mov_b32 m0, s101
	v_mfma_scale_f32_16x16x128_f8f6f4 v[16:19], v[184:191], v[152:159], v[16:19], v183, v183 op_sel_hi:[0,0,0]
	global_load_lds_dwordx4 v168, s[98:99]
	v_mfma_scale_f32_16x16x128_f8f6f4 v[4:7], v[192:199], v[144:151], v[4:7], v183, v183 op_sel_hi:[0,0,0]
	v_mfma_scale_f32_16x16x128_f8f6f4 v[0:3], v[192:199], v[152:159], v[0:3], v183, v183 op_sel_hi:[0,0,0]
	s_add_u32 s4, s4, 0x100
	s_addc_u32 s5, s5, 0
	s_add_u32 s25, s25, 0x100
	s_addc_u32 s27, s27, 0
	s_cmp_ge_i32 s34, s13
	s_mov_b32 s6, s34
	s_barrier
	s_cbranch_scc0 .LBB0_3995

.LBB0_4046:
	s_barrier
	s_setprio 0
	s_movk_i32 s57, 0x80

.LBB0_4054:
	s_andn2_b64 vcc, exec, s[8:9]
	s_cbranch_vccnz .LBB0_4118
	v_add_u32_e32 v1, s58, v0
	v_ashrrev_i32_e32 v2, 31, v1
	v_lshrrev_b32_e32 v2, 26, v2
	v_lshlrev_b32_e32 v3, 4, v1
	v_add_u32_e32 v2, v1, v2
	v_bfe_i32 v1, v1, 27, 1
	v_lshrrev_b32_e32 v1, 22, v1
	v_add_u32_e32 v1, v3, v1
	v_and_b32_e32 v1, 0xfffffc00, v1
	v_sub_u32_e32 v1, v3, v1
	s_waitcnt vmcnt(14)
	v_lshrrev_b32_e32 v4, 4, v1
	v_bitop3_b32 v1, v4, v1, 32 bitop3:0x6c
	v_ashrrev_i32_e32 v5, 31, v1
	v_ashrrev_i32_e32 v2, 6, v2
	v_lshrrev_b32_e32 v5, 26, v5
	v_lshlrev_b32_e32 v4, 3, v2
	v_add_u32_e32 v5, v1, v5
	v_and_b32_e32 v4, -16, v4
	v_ashrrev_i32_e32 v6, 6, v5
	v_and_b32_e32 v5, 0xc0, v5
	v_add_u32_e32 v4, v6, v4
	v_sub_u32_e32 v1, v1, v5
	v_mov_b32_e32 v6, 1
	v_lshlrev_b32_e32 v2, 5, v2
	v_ashrrev_i16_sdwa v1, v6, sext(v1) dst_sel:DWORD dst_unused:UNUSED_PAD src0_sel:DWORD src1_sel:BYTE_0
	v_and_b32_e32 v2, 32, v2
	v_bfe_i32 v1, v1, 0, 16
	v_add_lshl_u32 v2, v2, v1, 1
	v_add_u32_e32 v1, 0x2000, v3
	v_lshl_add_u32 v169, v4, 10, v2
	v_mad_u64_u32 v[216:217], s[8:9], v4, s42, v[2:3]
	v_ashrrev_i32_e32 v2, 31, v1
	v_lshrrev_b32_e32 v2, 22, v2
	v_add_u32_e32 v2, v1, v2
	v_ashrrev_i32_e32 v2, 10, v2
	v_mul_i32_i24_e32 v3, 0x400, v2
	v_sub_u32_e32 v1, v1, v3
	v_lshrrev_b32_e32 v3, 4, v1
	v_bitop3_b32 v1, v3, v1, 32 bitop3:0x6c
	v_ashrrev_i32_e32 v4, 31, v1
	v_lshrrev_b32_e32 v4, 26, v4
	v_add_u32_e32 v4, v1, v4
	v_ashrrev_i32_e32 v5, 6, v4
	v_and_b32_e32 v4, 0xc0, v4
	v_sub_u32_e32 v1, v1, v4
	v_lshlrev_b32_e32 v3, 3, v2
	v_lshlrev_b32_e32 v2, 5, v2
	v_ashrrev_i16_sdwa v1, v6, sext(v1) dst_sel:DWORD dst_unused:UNUSED_PAD src0_sel:DWORD src1_sel:BYTE_0
	v_and_b32_e32 v3, -16, v3
	v_and_b32_e32 v2, 32, v2
	v_bfe_i32 v1, v1, 0, 16
	v_add_u32_e32 v3, v5, v3
	v_add_lshl_u32 v2, v2, v1, 1
	v_mov_b32_e32 v1, v216
	s_add_i32 s3, s33, 0
	v_mad_u64_u32 v[180:181], s[8:9], v3, s42, v[2:3]
	s_add_i32 m0, s3, 0x10000
	v_lshl_add_u32 v200, v3, 10, v2
	global_load_lds_dwordx4 v1, s[6:7]
	v_mov_b32_e32 v1, v180
	s_add_i32 m0, s3, 0x12000
	s_add_i32 s11, s3, 0x2000
	global_load_lds_dwordx4 v1, s[6:7]
	v_mov_b32_e32 v1, v169
	s_mov_b32 m0, s3
	s_add_u32 s8, s6, s20
	global_load_lds_dwordx4 v1, s[4:5]
	v_mov_b32_e32 v1, v200
	s_mov_b32 m0, s11
	s_addc_u32 s9, s7, s21
	global_load_lds_dwordx4 v1, s[4:5]
	v_mov_b32_e32 v1, v216
	s_add_i32 m0, s3, 0x14000
	s_nop 0
	global_load_lds_dwordx4 v1, s[8:9]
	v_mov_b32_e32 v1, v180
	s_add_i32 m0, s3, 0x16000
	s_add_u32 s16, s4, 0x20000
	global_load_lds_dwordx4 v1, s[8:9]
	s_addc_u32 s17, s5, 0
	v_mov_b32_e32 v1, v169
	s_add_i32 s14, s3, 0x4000
	s_mov_b32 m0, s14
	s_add_i32 s15, s3, 0x6000
	global_load_lds_dwordx4 v1, s[16:17]
	v_mov_b32_e32 v1, v200
	s_mov_b32 m0, s15
	s_nop 0
	global_load_lds_dwordx4 v1, s[16:17]
	v_readlane_b32 s16, v252, 37
	v_readlane_b32 s17, v252, 38
	s_andn2_b64 vcc, exec, s[16:17]
	s_cbranch_vccnz .LBB0_4057
	s_setprio 1
	s_barrier

.Lpeel_6:
	s_add_i32 s34, s6, 2
	s_add_u32 s8, s4, 0xfffe0080
	s_addc_u32 s7, s5, -1
	s_add_i32 s30, 0, 0x10000
	v_add_u32_e32 v140, s30, v181
	ds_read_b128 v[128:131], v140
	ds_read_b128 v[132:135], v140 offset:1024
	ds_read_b128 v[136:139], v140 offset:2048
	ds_read_b128 v[140:143], v140 offset:3072
	s_cmp_eq_u32 s12, s6
	s_cselect_b32 s6, s52, s8
	s_cselect_b32 s7, s53, s7
	s_cselect_b32 s9, s55, s27
	s_cselect_b32 s8, s54, s25
	v_mov_b32_e32 v168, v169
	ds_read_b128 v[144:147], v182
	ds_read_b128 v[148:151], v182 offset:1024
	ds_read_b128 v[152:155], v182 offset:2048
	ds_read_b128 v[156:159], v182 offset:3072
	ds_read_b128 v[160:163], v182 offset:4096
	ds_read_b128 v[164:167], v182 offset:5120
	ds_read_b128 v[184:187], v182 offset:6144
	ds_read_b128 v[188:191], v182 offset:7168
	s_add_i32 m0, s3, 0xc000
	s_nop 0
	global_load_lds_dwordx4 v168, s[4:5]
	v_mov_b32_e32 v168, v200
	s_add_i32 m0, s3, 0xe000
	s_nop 0
	global_load_lds_dwordx4 v168, s[4:5]
	s_waitcnt lgkmcnt(8)
	s_barrier
	s_waitcnt lgkmcnt(0)
	s_waitcnt lgkmcnt(0)
	v_mfma_scale_f32_16x16x128_f8f6f4 v[120:123], v[128:135], v[144:151], 0, v183, v183 op_sel_hi:[0,0,0]
	v_mov_b32_e32 v170, v200
	v_mfma_scale_f32_16x16x128_f8f6f4 v[124:127], v[136:143], v[144:151], 0, v183, v183 op_sel_hi:[0,0,0]
	v_mfma_scale_f32_16x16x128_f8f6f4 v[200:203], v[128:135], v[160:167], 0, v183, v183 op_sel_hi:[0,0,0]
	v_mfma_scale_f32_16x16x128_f8f6f4 v[192:195], v[128:135], v[152:159], 0, v183, v183 op_sel_hi:[0,0,0]
	v_mfma_scale_f32_16x16x128_f8f6f4 v[196:199], v[136:143], v[152:159], 0, v183, v183 op_sel_hi:[0,0,0]
	v_mfma_scale_f32_16x16x128_f8f6f4 v[204:207], v[136:143], v[160:167], 0, v183, v183 op_sel_hi:[0,0,0]
	v_mfma_scale_f32_16x16x128_f8f6f4 v[208:211], v[128:135], v[184:191], 0, v183, v183 op_sel_hi:[0,0,0]
	v_mfma_scale_f32_16x16x128_f8f6f4 v[212:215], v[136:143], v[184:191], 0, v183, v183 op_sel_hi:[0,0,0]
	s_barrier
	s_add_i32 s35, 0, 0x14000
	v_add_u32_e32 v92, s35, v181
	v_mov_b32_e32 v104, v216
	s_add_i32 s30, s30, s33
	s_nop 0
	ds_read_b128 v[72:75], v92
	ds_read_b128 v[76:79], v92 offset:1024
	ds_read_b128 v[88:91], v92 offset:2048
	ds_read_b128 v[92:95], v92 offset:3072
	s_mov_b32 m0, s30
	s_nop 0
	global_load_lds_dwordx4 v104, s[8:9]
	v_mov_b32_e32 v104, v180
	s_add_i32 m0, s30, 0x2000
	s_nop 0
	global_load_lds_dwordx4 v104, s[8:9]
	s_barrier
	s_waitcnt lgkmcnt(0)
	s_waitcnt lgkmcnt(0)
	v_mfma_scale_f32_16x16x128_f8f6f4 v[116:119], v[72:79], v[144:151], 0, v183, v183 op_sel_hi:[0,0,0]
	v_mov_b32_e32 v168, v216
	v_mfma_scale_f32_16x16x128_f8f6f4 v[112:115], v[88:95], v[144:151], 0, v183, v183 op_sel_hi:[0,0,0]
	v_mfma_scale_f32_16x16x128_f8f6f4 v[216:219], v[72:79], v[152:159], 0, v183, v183 op_sel_hi:[0,0,0]
	v_mfma_scale_f32_16x16x128_f8f6f4 v[220:223], v[88:95], v[152:159], 0, v183, v183 op_sel_hi:[0,0,0]
	v_mfma_scale_f32_16x16x128_f8f6f4 v[224:227], v[72:79], v[160:167], 0, v183, v183 op_sel_hi:[0,0,0]
	v_mfma_scale_f32_16x16x128_f8f6f4 v[160:163], v[88:95], v[160:167], 0, v183, v183 op_sel_hi:[0,0,0]
	v_mfma_scale_f32_16x16x128_f8f6f4 v[164:167], v[72:79], v[184:191], 0, v183, v183 op_sel_hi:[0,0,0]
	v_mfma_scale_f32_16x16x128_f8f6f4 v[184:187], v[88:95], v[184:191], 0, v183, v183 op_sel_hi:[0,0,0]
	v_mov_b32_e32 v144, v169
	s_barrier
	s_nop 2
	ds_read_b128 v[64:67], v182 offset:16384
	ds_read_b128 v[68:71], v182 offset:17408
	ds_read_b128 v[80:83], v182 offset:18432
	ds_read_b128 v[84:87], v182 offset:19456
	ds_read_b128 v[96:99], v182 offset:20480
	ds_read_b128 v[100:103], v182 offset:21504
	ds_read_b128 v[104:107], v182 offset:22528
	ds_read_b128 v[108:111], v182 offset:23552
	s_nop 0
	v_mov_b32_e32 v144, v170
	s_nop 0
	s_barrier
	s_waitcnt lgkmcnt(0)
	s_waitcnt lgkmcnt(0)
	v_mfma_scale_f32_16x16x128_f8f6f4 v[228:231], v[128:135], v[64:71], 0, v183, v183 op_sel_hi:[0,0,0]
	v_mfma_scale_f32_16x16x128_f8f6f4 v[232:235], v[136:143], v[64:71], 0, v183, v183 op_sel_hi:[0,0,0]
	s_mov_b32 m0, s3
	v_mfma_scale_f32_16x16x128_f8f6f4 v[236:239], v[128:135], v[80:87], 0, v183, v183 op_sel_hi:[0,0,0]
	global_load_lds_dwordx4 v169, s[6:7]
	v_mfma_scale_f32_16x16x128_f8f6f4 v[240:243], v[136:143], v[80:87], 0, v183, v183 op_sel_hi:[0,0,0]
	v_mfma_scale_f32_16x16x128_f8f6f4 v[244:247], v[128:135], v[96:103], 0, v183, v183 op_sel_hi:[0,0,0]
	s_mov_b32 m0, s11
	v_mfma_scale_f32_16x16x128_f8f6f4 v[248:251], v[136:143], v[96:103], 0, v183, v183 op_sel_hi:[0,0,0]
	global_load_lds_dwordx4 v170, s[6:7]
	v_mfma_scale_f32_16x16x128_f8f6f4 v[172:175], v[128:135], v[104:111], 0, v183, v183 op_sel_hi:[0,0,0]
	v_mfma_scale_f32_16x16x128_f8f6f4 v[176:179], v[136:143], v[104:111], 0, v183, v183 op_sel_hi:[0,0,0]
	s_barrier
	s_add_u32 s30, s8, s20
	s_addc_u32 s31, s9, s21
	s_nop 2
	v_mov_b32_e32 v8, v168
	s_add_i32 s35, s35, s33
	s_mov_b32 s100, s35
	s_nop 0
	v_mov_b32_e32 v8, v180
	s_add_i32 s101, s35, 0x2000
	s_nop 0
	s_waitcnt vmcnt(4)
	s_barrier
	v_mfma_scale_f32_16x16x128_f8f6f4 v[52:55], v[72:79], v[64:71], 0, v183, v183 op_sel_hi:[0,0,0]
	v_mfma_scale_f32_16x16x128_f8f6f4 v[48:51], v[88:95], v[64:71], 0, v183, v183 op_sel_hi:[0,0,0]
	s_mov_b32 m0, s100
	v_mfma_scale_f32_16x16x128_f8f6f4 v[36:39], v[72:79], v[80:87], 0, v183, v183 op_sel_hi:[0,0,0]
	global_load_lds_dwordx4 v168, s[30:31]
	v_mfma_scale_f32_16x16x128_f8f6f4 v[32:35], v[88:95], v[80:87], 0, v183, v183 op_sel_hi:[0,0,0]
	v_mfma_scale_f32_16x16x128_f8f6f4 v[20:23], v[72:79], v[96:103], 0, v183, v183 op_sel_hi:[0,0,0]
	s_mov_b32 m0, s101
	v_mfma_scale_f32_16x16x128_f8f6f4 v[16:19], v[88:95], v[96:103], 0, v183, v183 op_sel_hi:[0,0,0]
	global_load_lds_dwordx4 v180, s[30:31]
	v_mfma_scale_f32_16x16x128_f8f6f4 v[4:7], v[72:79], v[104:111], 0, v183, v183 op_sel_hi:[0,0,0]
	v_mfma_scale_f32_16x16x128_f8f6f4 v[0:3], v[88:95], v[104:111], 0, v183, v183 op_sel_hi:[0,0,0]
	s_add_i32 s35, 0, 0x18000
	v_add_u32_e32 v24, s35, v181
	s_barrier
	ds_read_b128 v[8:11], v24
	ds_read_b128 v[12:15], v24 offset:1024
	ds_read_b128 v[128:131], v24 offset:2048
	ds_read_b128 v[132:135], v24 offset:3072
	s_add_u32 s36, s6, 0x20000
	v_mov_b32_e32 v64, v169
	ds_read_b128 v[24:27], v182 offset:32768
	ds_read_b128 v[28:31], v182 offset:33792
	ds_read_b128 v[40:43], v182 offset:34816
	ds_read_b128 v[44:47], v182 offset:35840
	ds_read_b128 v[56:59], v182 offset:36864
	ds_read_b128 v[60:63], v182 offset:37888
	ds_read_b128 v[136:139], v182 offset:38912
	ds_read_b128 v[140:143], v182 offset:39936
	s_addc_u32 s37, s7, 0
	s_nop 0
	v_mov_b32_e32 v64, v170
	s_nop 0
	s_waitcnt lgkmcnt(8)
	s_barrier
	s_waitcnt lgkmcnt(0)
	s_waitcnt lgkmcnt(0)
	v_mfma_scale_f32_16x16x128_f8f6f4 v[120:123], v[8:15], v[24:31], v[120:123], v183, v183 op_sel_hi:[0,0,0]
	v_mfma_scale_f32_16x16x128_f8f6f4 v[124:127], v[128:135], v[24:31], v[124:127], v183, v183 op_sel_hi:[0,0,0]
	s_mov_b32 m0, s14
	v_mfma_scale_f32_16x16x128_f8f6f4 v[108:111], v[8:15], v[40:47], v[192:195], v183, v183 op_sel_hi:[0,0,0]
	global_load_lds_dwordx4 v169, s[36:37]
	v_mfma_scale_f32_16x16x128_f8f6f4 v[104:107], v[128:135], v[40:47], v[196:199], v183, v183 op_sel_hi:[0,0,0]
	v_mfma_scale_f32_16x16x128_f8f6f4 v[92:95], v[8:15], v[56:63], v[200:203], v183, v183 op_sel_hi:[0,0,0]
	s_mov_b32 m0, s15
	v_mfma_scale_f32_16x16x128_f8f6f4 v[88:91], v[128:135], v[56:63], v[204:207], v183, v183 op_sel_hi:[0,0,0]
	global_load_lds_dwordx4 v170, s[36:37]
	s_nop 5
	v_mov_b32_e32 v200, v170
	v_mfma_scale_f32_16x16x128_f8f6f4 v[76:79], v[8:15], v[136:143], v[208:211], v183, v183 op_sel_hi:[0,0,0]
	v_mfma_scale_f32_16x16x128_f8f6f4 v[72:75], v[128:135], v[136:143], v[212:215], v183, v183 op_sel_hi:[0,0,0]
	s_barrier
	s_add_i32 s36, 0, 0x1c000
	v_add_u32_e32 v64, s36, v181
	v_mov_b32_e32 v170, v168
	ds_read_b128 v[144:147], v64
	ds_read_b128 v[148:151], v64 offset:1024
	ds_read_b128 v[152:155], v64 offset:2048
	ds_read_b128 v[156:159], v64 offset:3072
	s_add_i32 s35, s35, s33
	v_lshl_add_u64 v[64:65], s[8:9], 0, v[170:171]
	v_lshl_add_u64 v[64:65], v[64:65], 0, s[62:63]
	v_mov_b32_e32 v170, v180
	v_lshl_add_u64 v[64:65], s[8:9], 0, v[170:171]
	v_lshl_add_u64 v[64:65], v[64:65], 0, s[62:63]
	s_barrier
	s_waitcnt lgkmcnt(0)
	s_waitcnt lgkmcnt(0)
	v_mfma_scale_f32_16x16x128_f8f6f4 v[116:119], v[144:151], v[24:31], v[116:119], v183, v183 op_sel_hi:[0,0,0]
	v_mfma_scale_f32_16x16x128_f8f6f4 v[112:115], v[152:159], v[24:31], v[112:115], v183, v183 op_sel_hi:[0,0,0]
	s_add_u32 s98, s8, s62
	s_addc_u32 s99, s9, s63
	s_mov_b32 m0, s35
	v_mfma_scale_f32_16x16x128_f8f6f4 v[100:103], v[144:151], v[40:47], v[216:219], v183, v183 op_sel_hi:[0,0,0]
	global_load_lds_dwordx4 v168, s[98:99]
	v_mfma_scale_f32_16x16x128_f8f6f4 v[96:99], v[152:159], v[40:47], v[220:223], v183, v183 op_sel_hi:[0,0,0]
	s_nop 5
	v_mov_b32_e32 v216, v168
	v_mfma_scale_f32_16x16x128_f8f6f4 v[84:87], v[144:151], v[56:63], v[224:227], v183, v183 op_sel_hi:[0,0,0]
	s_add_i32 m0, s35, 0x2000
	v_mfma_scale_f32_16x16x128_f8f6f4 v[80:83], v[152:159], v[56:63], v[160:163], v183, v183 op_sel_hi:[0,0,0]
	global_load_lds_dwordx4 v180, s[98:99]
	v_mfma_scale_f32_16x16x128_f8f6f4 v[68:71], v[144:151], v[136:143], v[164:167], v183, v183 op_sel_hi:[0,0,0]
	v_mfma_scale_f32_16x16x128_f8f6f4 v[64:67], v[152:159], v[136:143], v[184:187], v183, v183 op_sel_hi:[0,0,0]
	v_mov_b32_e32 v170, v169
	s_barrier
	ds_read_b128 v[136:139], v182 offset:49152
	ds_read_b128 v[140:143], v182 offset:50176
	ds_read_b128 v[160:163], v182 offset:51200
	ds_read_b128 v[164:167], v182 offset:52224
	ds_read_b128 v[184:187], v182 offset:53248
	ds_read_b128 v[188:191], v182 offset:54272
	ds_read_b128 v[192:195], v182 offset:55296
	ds_read_b128 v[196:199], v182 offset:56320
	v_lshl_add_u64 v[24:25], s[6:7], 0, v[170:171]
	v_lshl_add_u64 v[24:25], v[24:25], 0, s[62:63]
	v_mov_b32_e32 v170, v200
	v_lshl_add_u64 v[24:25], s[6:7], 0, v[170:171]
	v_lshl_add_u64 v[24:25], v[24:25], 0, s[62:63]
	s_barrier
	s_waitcnt lgkmcnt(0)
	s_waitcnt lgkmcnt(0)
	v_mfma_scale_f32_16x16x128_f8f6f4 v[60:63], v[8:15], v[136:143], v[228:231], v183, v183 op_sel_hi:[0,0,0]
	v_mfma_scale_f32_16x16x128_f8f6f4 v[56:59], v[128:135], v[136:143], v[232:235], v183, v183 op_sel_hi:[0,0,0]
	s_add_u32 s98, s6, s62
	s_addc_u32 s99, s7, s63
	s_mov_b32 m0, s16
	v_mfma_scale_f32_16x16x128_f8f6f4 v[44:47], v[8:15], v[160:167], v[236:239], v183, v183 op_sel_hi:[0,0,0]
	global_load_lds_dwordx4 v169, s[98:99]
	v_mfma_scale_f32_16x16x128_f8f6f4 v[40:43], v[128:135], v[160:167], v[240:243], v183, v183 op_sel_hi:[0,0,0]
	v_mfma_scale_f32_16x16x128_f8f6f4 v[28:31], v[8:15], v[184:191], v[244:247], v183, v183 op_sel_hi:[0,0,0]
	s_mov_b32 m0, s17
	v_mfma_scale_f32_16x16x128_f8f6f4 v[24:27], v[128:135], v[184:191], v[248:251], v183, v183 op_sel_hi:[0,0,0]
	global_load_lds_dwordx4 v200, s[98:99]
	v_mfma_scale_f32_16x16x128_f8f6f4 v[12:15], v[8:15], v[192:199], v[172:175], v183, v183 op_sel_hi:[0,0,0]
	v_mfma_scale_f32_16x16x128_f8f6f4 v[8:11], v[128:135], v[192:199], v[176:179], v183, v183 op_sel_hi:[0,0,0]
	s_barrier
	v_mov_b32_e32 v170, v168
	s_add_i32 s6, s36, s33
	v_lshl_add_u64 v[128:129], s[30:31], 0, v[170:171]
	v_lshl_add_u64 v[128:129], v[128:129], 0, s[62:63]
	s_mov_b32 s100, s6
	v_mov_b32_e32 v170, v180
	s_add_i32 s101, s6, 0x2000
	v_lshl_add_u64 v[128:129], s[30:31], 0, v[170:171]
	v_lshl_add_u64 v[128:129], v[128:129], 0, s[62:63]
	s_waitcnt vmcnt(4)
	s_barrier
	v_mfma_scale_f32_16x16x128_f8f6f4 v[52:55], v[144:151], v[136:143], v[52:55], v183, v183 op_sel_hi:[0,0,0]
	v_mfma_scale_f32_16x16x128_f8f6f4 v[48:51], v[152:159], v[136:143], v[48:51], v183, v183 op_sel_hi:[0,0,0]
	s_add_u32 s98, s30, s62
	s_addc_u32 s99, s31, s63
	s_mov_b32 m0, s100
	v_mfma_scale_f32_16x16x128_f8f6f4 v[36:39], v[144:151], v[160:167], v[36:39], v183, v183 op_sel_hi:[0,0,0]
	global_load_lds_dwordx4 v168, s[98:99]
	v_mfma_scale_f32_16x16x128_f8f6f4 v[32:35], v[152:159], v[160:167], v[32:35], v183, v183 op_sel_hi:[0,0,0]
	v_mfma_scale_f32_16x16x128_f8f6f4 v[20:23], v[144:151], v[184:191], v[20:23], v183, v183 op_sel_hi:[0,0,0]
	s_mov_b32 m0, s101
	v_mfma_scale_f32_16x16x128_f8f6f4 v[16:19], v[152:159], v[184:191], v[16:19], v183, v183 op_sel_hi:[0,0,0]
	global_load_lds_dwordx4 v180, s[98:99]
	v_mfma_scale_f32_16x16x128_f8f6f4 v[4:7], v[144:151], v[192:199], v[4:7], v183, v183 op_sel_hi:[0,0,0]
	v_mfma_scale_f32_16x16x128_f8f6f4 v[0:3], v[152:159], v[192:199], v[0:3], v183, v183 op_sel_hi:[0,0,0]
	s_add_u32 s4, s4, 0x100
	s_addc_u32 s5, s5, 0
	s_add_u32 s25, s25, 0x100
	s_addc_u32 s27, s27, 0
	s_cmp_ge_i32 s34, s13
	s_mov_b32 s6, s34
	s_barrier
	s_cbranch_scc0 .LBB0_4066
	s_branch .Lpeel_exit_6
.LBB0_4066:
	s_add_i32 s34, s6, 2
	s_add_u32 s8, s4, 0xfffe0080
	s_addc_u32 s7, s5, -1
	s_add_i32 s30, 0, 0x10000
	v_add_u32_e32 v140, s30, v181
	ds_read_b128 v[128:131], v140
	ds_read_b128 v[132:135], v140 offset:1024
	ds_read_b128 v[136:139], v140 offset:2048
	ds_read_b128 v[140:143], v140 offset:3072
	s_cmp_eq_u32 s12, s6
	s_cselect_b32 s6, s52, s8
	s_cselect_b32 s7, s53, s7
	s_cselect_b32 s9, s55, s27
	s_cselect_b32 s8, s54, s25
	v_mov_b32_e32 v168, v169
	ds_read_b128 v[144:147], v182
	ds_read_b128 v[148:151], v182 offset:1024
	ds_read_b128 v[152:155], v182 offset:2048
	ds_read_b128 v[156:159], v182 offset:3072
	ds_read_b128 v[160:163], v182 offset:4096
	ds_read_b128 v[164:167], v182 offset:5120
	ds_read_b128 v[184:187], v182 offset:6144
	ds_read_b128 v[188:191], v182 offset:7168
	s_add_i32 m0, s3, 0xc000
	s_nop 0
	global_load_lds_dwordx4 v168, s[4:5]
	v_mov_b32_e32 v168, v200
	s_add_i32 m0, s3, 0xe000
	s_nop 0
	global_load_lds_dwordx4 v168, s[4:5]
	s_waitcnt lgkmcnt(8)
	s_barrier
	s_waitcnt lgkmcnt(0)
	s_waitcnt lgkmcnt(0)
	v_mfma_scale_f32_16x16x128_f8f6f4 v[120:123], v[128:135], v[144:151], v[120:123], v183, v183 op_sel_hi:[0,0,0]
	v_mov_b32_e32 v170, v200
	v_mfma_scale_f32_16x16x128_f8f6f4 v[124:127], v[136:143], v[144:151], v[124:127], v183, v183 op_sel_hi:[0,0,0]
	v_mfma_scale_f32_16x16x128_f8f6f4 v[200:203], v[128:135], v[160:167], v[92:95], v183, v183 op_sel_hi:[0,0,0]
	v_mfma_scale_f32_16x16x128_f8f6f4 v[192:195], v[128:135], v[152:159], v[108:111], v183, v183 op_sel_hi:[0,0,0]
	v_mfma_scale_f32_16x16x128_f8f6f4 v[196:199], v[136:143], v[152:159], v[104:107], v183, v183 op_sel_hi:[0,0,0]
	v_mfma_scale_f32_16x16x128_f8f6f4 v[204:207], v[136:143], v[160:167], v[88:91], v183, v183 op_sel_hi:[0,0,0]
	v_mfma_scale_f32_16x16x128_f8f6f4 v[208:211], v[128:135], v[184:191], v[76:79], v183, v183 op_sel_hi:[0,0,0]
	v_mfma_scale_f32_16x16x128_f8f6f4 v[212:215], v[136:143], v[184:191], v[72:75], v183, v183 op_sel_hi:[0,0,0]
	s_barrier
	s_add_i32 s35, 0, 0x14000
	v_add_u32_e32 v92, s35, v181
	v_mov_b32_e32 v104, v216
	s_add_i32 s30, s30, s33
	s_nop 0
	ds_read_b128 v[72:75], v92
	ds_read_b128 v[76:79], v92 offset:1024
	ds_read_b128 v[88:91], v92 offset:2048
	ds_read_b128 v[92:95], v92 offset:3072
	s_mov_b32 m0, s30
	s_nop 0
	global_load_lds_dwordx4 v104, s[8:9]
	v_mov_b32_e32 v104, v180
	s_add_i32 m0, s30, 0x2000
	s_nop 0
	global_load_lds_dwordx4 v104, s[8:9]
	s_barrier
	s_waitcnt lgkmcnt(0)
	s_waitcnt lgkmcnt(0)
	v_mfma_scale_f32_16x16x128_f8f6f4 v[116:119], v[72:79], v[144:151], v[116:119], v183, v183 op_sel_hi:[0,0,0]
	v_mov_b32_e32 v168, v216
	v_mfma_scale_f32_16x16x128_f8f6f4 v[112:115], v[88:95], v[144:151], v[112:115], v183, v183 op_sel_hi:[0,0,0]
	v_mfma_scale_f32_16x16x128_f8f6f4 v[216:219], v[72:79], v[152:159], v[100:103], v183, v183 op_sel_hi:[0,0,0]
	v_mfma_scale_f32_16x16x128_f8f6f4 v[220:223], v[88:95], v[152:159], v[96:99], v183, v183 op_sel_hi:[0,0,0]
	v_mfma_scale_f32_16x16x128_f8f6f4 v[224:227], v[72:79], v[160:167], v[84:87], v183, v183 op_sel_hi:[0,0,0]
	v_mfma_scale_f32_16x16x128_f8f6f4 v[160:163], v[88:95], v[160:167], v[80:83], v183, v183 op_sel_hi:[0,0,0]
	v_mfma_scale_f32_16x16x128_f8f6f4 v[164:167], v[72:79], v[184:191], v[68:71], v183, v183 op_sel_hi:[0,0,0]
	v_mfma_scale_f32_16x16x128_f8f6f4 v[184:187], v[88:95], v[184:191], v[64:67], v183, v183 op_sel_hi:[0,0,0]
	v_mov_b32_e32 v144, v169
	s_barrier
	s_nop 2
	ds_read_b128 v[64:67], v182 offset:16384
	ds_read_b128 v[68:71], v182 offset:17408
	ds_read_b128 v[80:83], v182 offset:18432
	ds_read_b128 v[84:87], v182 offset:19456
	ds_read_b128 v[96:99], v182 offset:20480
	ds_read_b128 v[100:103], v182 offset:21504
	ds_read_b128 v[104:107], v182 offset:22528
	ds_read_b128 v[108:111], v182 offset:23552
	s_nop 0
	v_mov_b32_e32 v144, v170
	s_nop 0
	s_barrier
	s_waitcnt lgkmcnt(0)
	s_waitcnt lgkmcnt(0)
	v_mfma_scale_f32_16x16x128_f8f6f4 v[228:231], v[128:135], v[64:71], v[60:63], v183, v183 op_sel_hi:[0,0,0]
	v_mfma_scale_f32_16x16x128_f8f6f4 v[232:235], v[136:143], v[64:71], v[56:59], v183, v183 op_sel_hi:[0,0,0]
	s_mov_b32 m0, s3
	v_mfma_scale_f32_16x16x128_f8f6f4 v[236:239], v[128:135], v[80:87], v[44:47], v183, v183 op_sel_hi:[0,0,0]
	global_load_lds_dwordx4 v169, s[6:7]
	v_mfma_scale_f32_16x16x128_f8f6f4 v[240:243], v[136:143], v[80:87], v[40:43], v183, v183 op_sel_hi:[0,0,0]
	v_mfma_scale_f32_16x16x128_f8f6f4 v[244:247], v[128:135], v[96:103], v[28:31], v183, v183 op_sel_hi:[0,0,0]
	s_mov_b32 m0, s11
	v_mfma_scale_f32_16x16x128_f8f6f4 v[248:251], v[136:143], v[96:103], v[24:27], v183, v183 op_sel_hi:[0,0,0]
	global_load_lds_dwordx4 v170, s[6:7]
	v_mfma_scale_f32_16x16x128_f8f6f4 v[172:175], v[128:135], v[104:111], v[12:15], v183, v183 op_sel_hi:[0,0,0]
	v_mfma_scale_f32_16x16x128_f8f6f4 v[176:179], v[136:143], v[104:111], v[8:11], v183, v183 op_sel_hi:[0,0,0]
	s_barrier
	s_add_u32 s30, s8, s20
	s_addc_u32 s31, s9, s21
	s_nop 2
	v_mov_b32_e32 v8, v168
	s_add_i32 s35, s35, s33
	s_mov_b32 s100, s35
	s_nop 0
	v_mov_b32_e32 v8, v180
	s_add_i32 s101, s35, 0x2000
	s_nop 0
	s_waitcnt vmcnt(4)
	s_barrier
	v_mfma_scale_f32_16x16x128_f8f6f4 v[52:55], v[72:79], v[64:71], v[52:55], v183, v183 op_sel_hi:[0,0,0]
	v_mfma_scale_f32_16x16x128_f8f6f4 v[48:51], v[88:95], v[64:71], v[48:51], v183, v183 op_sel_hi:[0,0,0]
	s_mov_b32 m0, s100
	v_mfma_scale_f32_16x16x128_f8f6f4 v[36:39], v[72:79], v[80:87], v[36:39], v183, v183 op_sel_hi:[0,0,0]
	global_load_lds_dwordx4 v168, s[30:31]
	v_mfma_scale_f32_16x16x128_f8f6f4 v[32:35], v[88:95], v[80:87], v[32:35], v183, v183 op_sel_hi:[0,0,0]
	v_mfma_scale_f32_16x16x128_f8f6f4 v[20:23], v[72:79], v[96:103], v[20:23], v183, v183 op_sel_hi:[0,0,0]
	s_mov_b32 m0, s101
	v_mfma_scale_f32_16x16x128_f8f6f4 v[16:19], v[88:95], v[96:103], v[16:19], v183, v183 op_sel_hi:[0,0,0]
	global_load_lds_dwordx4 v180, s[30:31]
	v_mfma_scale_f32_16x16x128_f8f6f4 v[4:7], v[72:79], v[104:111], v[4:7], v183, v183 op_sel_hi:[0,0,0]
	v_mfma_scale_f32_16x16x128_f8f6f4 v[0:3], v[88:95], v[104:111], v[0:3], v183, v183 op_sel_hi:[0,0,0]
	s_add_i32 s35, 0, 0x18000
	v_add_u32_e32 v24, s35, v181
	s_barrier
	ds_read_b128 v[8:11], v24
	ds_read_b128 v[12:15], v24 offset:1024
	ds_read_b128 v[128:131], v24 offset:2048
	ds_read_b128 v[132:135], v24 offset:3072
	s_add_u32 s36, s6, 0x20000
	v_mov_b32_e32 v64, v169
	ds_read_b128 v[24:27], v182 offset:32768
	ds_read_b128 v[28:31], v182 offset:33792
	ds_read_b128 v[40:43], v182 offset:34816
	ds_read_b128 v[44:47], v182 offset:35840
	ds_read_b128 v[56:59], v182 offset:36864
	ds_read_b128 v[60:63], v182 offset:37888
	ds_read_b128 v[136:139], v182 offset:38912
	ds_read_b128 v[140:143], v182 offset:39936
	s_addc_u32 s37, s7, 0
	s_nop 0
	v_mov_b32_e32 v64, v170
	s_nop 0
	s_waitcnt lgkmcnt(8)
	s_barrier
	s_waitcnt lgkmcnt(0)
	s_waitcnt lgkmcnt(0)
	v_mfma_scale_f32_16x16x128_f8f6f4 v[120:123], v[8:15], v[24:31], v[120:123], v183, v183 op_sel_hi:[0,0,0]
	v_mfma_scale_f32_16x16x128_f8f6f4 v[124:127], v[128:135], v[24:31], v[124:127], v183, v183 op_sel_hi:[0,0,0]
	s_mov_b32 m0, s14
	v_mfma_scale_f32_16x16x128_f8f6f4 v[108:111], v[8:15], v[40:47], v[192:195], v183, v183 op_sel_hi:[0,0,0]
	global_load_lds_dwordx4 v169, s[36:37]
	v_mfma_scale_f32_16x16x128_f8f6f4 v[104:107], v[128:135], v[40:47], v[196:199], v183, v183 op_sel_hi:[0,0,0]
	v_mfma_scale_f32_16x16x128_f8f6f4 v[92:95], v[8:15], v[56:63], v[200:203], v183, v183 op_sel_hi:[0,0,0]
	s_mov_b32 m0, s15
	v_mfma_scale_f32_16x16x128_f8f6f4 v[88:91], v[128:135], v[56:63], v[204:207], v183, v183 op_sel_hi:[0,0,0]
	global_load_lds_dwordx4 v170, s[36:37]
	s_nop 5
	v_mov_b32_e32 v200, v170
	v_mfma_scale_f32_16x16x128_f8f6f4 v[76:79], v[8:15], v[136:143], v[208:211], v183, v183 op_sel_hi:[0,0,0]
	v_mfma_scale_f32_16x16x128_f8f6f4 v[72:75], v[128:135], v[136:143], v[212:215], v183, v183 op_sel_hi:[0,0,0]
	s_barrier
	s_add_i32 s36, 0, 0x1c000
	v_add_u32_e32 v64, s36, v181
	v_mov_b32_e32 v170, v168
	ds_read_b128 v[144:147], v64
	ds_read_b128 v[148:151], v64 offset:1024
	ds_read_b128 v[152:155], v64 offset:2048
	ds_read_b128 v[156:159], v64 offset:3072
	s_add_i32 s35, s35, s33
	v_lshl_add_u64 v[64:65], s[8:9], 0, v[170:171]
	v_lshl_add_u64 v[64:65], v[64:65], 0, s[62:63]
	v_mov_b32_e32 v170, v180
	v_lshl_add_u64 v[64:65], s[8:9], 0, v[170:171]
	v_lshl_add_u64 v[64:65], v[64:65], 0, s[62:63]
	s_barrier
	s_waitcnt lgkmcnt(0)
	s_waitcnt lgkmcnt(0)
	v_mfma_scale_f32_16x16x128_f8f6f4 v[116:119], v[144:151], v[24:31], v[116:119], v183, v183 op_sel_hi:[0,0,0]
	v_mfma_scale_f32_16x16x128_f8f6f4 v[112:115], v[152:159], v[24:31], v[112:115], v183, v183 op_sel_hi:[0,0,0]
	s_add_u32 s98, s8, s62
	s_addc_u32 s99, s9, s63
	s_mov_b32 m0, s35
	v_mfma_scale_f32_16x16x128_f8f6f4 v[100:103], v[144:151], v[40:47], v[216:219], v183, v183 op_sel_hi:[0,0,0]
	global_load_lds_dwordx4 v168, s[98:99]
	v_mfma_scale_f32_16x16x128_f8f6f4 v[96:99], v[152:159], v[40:47], v[220:223], v183, v183 op_sel_hi:[0,0,0]
	s_nop 5
	v_mov_b32_e32 v216, v168
	v_mfma_scale_f32_16x16x128_f8f6f4 v[84:87], v[144:151], v[56:63], v[224:227], v183, v183 op_sel_hi:[0,0,0]
	s_add_i32 m0, s35, 0x2000
	v_mfma_scale_f32_16x16x128_f8f6f4 v[80:83], v[152:159], v[56:63], v[160:163], v183, v183 op_sel_hi:[0,0,0]
	global_load_lds_dwordx4 v180, s[98:99]
	v_mfma_scale_f32_16x16x128_f8f6f4 v[68:71], v[144:151], v[136:143], v[164:167], v183, v183 op_sel_hi:[0,0,0]
	v_mfma_scale_f32_16x16x128_f8f6f4 v[64:67], v[152:159], v[136:143], v[184:187], v183, v183 op_sel_hi:[0,0,0]
	v_mov_b32_e32 v170, v169
	s_barrier
	ds_read_b128 v[136:139], v182 offset:49152
	ds_read_b128 v[140:143], v182 offset:50176
	ds_read_b128 v[160:163], v182 offset:51200
	ds_read_b128 v[164:167], v182 offset:52224
	ds_read_b128 v[184:187], v182 offset:53248
	ds_read_b128 v[188:191], v182 offset:54272
	ds_read_b128 v[192:195], v182 offset:55296
	ds_read_b128 v[196:199], v182 offset:56320
	v_lshl_add_u64 v[24:25], s[6:7], 0, v[170:171]
	v_lshl_add_u64 v[24:25], v[24:25], 0, s[62:63]
	v_mov_b32_e32 v170, v200
	v_lshl_add_u64 v[24:25], s[6:7], 0, v[170:171]
	v_lshl_add_u64 v[24:25], v[24:25], 0, s[62:63]
	s_barrier
	s_waitcnt lgkmcnt(0)
	s_waitcnt lgkmcnt(0)
	v_mfma_scale_f32_16x16x128_f8f6f4 v[60:63], v[8:15], v[136:143], v[228:231], v183, v183 op_sel_hi:[0,0,0]
	v_mfma_scale_f32_16x16x128_f8f6f4 v[56:59], v[128:135], v[136:143], v[232:235], v183, v183 op_sel_hi:[0,0,0]
	s_add_u32 s98, s6, s62
	s_addc_u32 s99, s7, s63
	s_mov_b32 m0, s16
	v_mfma_scale_f32_16x16x128_f8f6f4 v[44:47], v[8:15], v[160:167], v[236:239], v183, v183 op_sel_hi:[0,0,0]
	global_load_lds_dwordx4 v169, s[98:99]
	v_mfma_scale_f32_16x16x128_f8f6f4 v[40:43], v[128:135], v[160:167], v[240:243], v183, v183 op_sel_hi:[0,0,0]
	v_mfma_scale_f32_16x16x128_f8f6f4 v[28:31], v[8:15], v[184:191], v[244:247], v183, v183 op_sel_hi:[0,0,0]
	s_mov_b32 m0, s17
	v_mfma_scale_f32_16x16x128_f8f6f4 v[24:27], v[128:135], v[184:191], v[248:251], v183, v183 op_sel_hi:[0,0,0]
	global_load_lds_dwordx4 v200, s[98:99]
	v_mfma_scale_f32_16x16x128_f8f6f4 v[12:15], v[8:15], v[192:199], v[172:175], v183, v183 op_sel_hi:[0,0,0]
	v_mfma_scale_f32_16x16x128_f8f6f4 v[8:11], v[128:135], v[192:199], v[176:179], v183, v183 op_sel_hi:[0,0,0]
	s_barrier
	v_mov_b32_e32 v170, v168
	s_add_i32 s6, s36, s33
	v_lshl_add_u64 v[128:129], s[30:31], 0, v[170:171]
	v_lshl_add_u64 v[128:129], v[128:129], 0, s[62:63]
	s_mov_b32 s100, s6
	v_mov_b32_e32 v170, v180
	s_add_i32 s101, s6, 0x2000
	v_lshl_add_u64 v[128:129], s[30:31], 0, v[170:171]
	v_lshl_add_u64 v[128:129], v[128:129], 0, s[62:63]
	s_waitcnt vmcnt(4)
	s_barrier
	v_mfma_scale_f32_16x16x128_f8f6f4 v[52:55], v[144:151], v[136:143], v[52:55], v183, v183 op_sel_hi:[0,0,0]
	v_mfma_scale_f32_16x16x128_f8f6f4 v[48:51], v[152:159], v[136:143], v[48:51], v183, v183 op_sel_hi:[0,0,0]
	s_add_u32 s98, s30, s62
	s_addc_u32 s99, s31, s63
	s_mov_b32 m0, s100
	v_mfma_scale_f32_16x16x128_f8f6f4 v[36:39], v[144:151], v[160:167], v[36:39], v183, v183 op_sel_hi:[0,0,0]
	global_load_lds_dwordx4 v168, s[98:99]
	v_mfma_scale_f32_16x16x128_f8f6f4 v[32:35], v[152:159], v[160:167], v[32:35], v183, v183 op_sel_hi:[0,0,0]
	v_mfma_scale_f32_16x16x128_f8f6f4 v[20:23], v[144:151], v[184:191], v[20:23], v183, v183 op_sel_hi:[0,0,0]
	s_mov_b32 m0, s101
	v_mfma_scale_f32_16x16x128_f8f6f4 v[16:19], v[152:159], v[184:191], v[16:19], v183, v183 op_sel_hi:[0,0,0]
	global_load_lds_dwordx4 v180, s[98:99]
	v_mfma_scale_f32_16x16x128_f8f6f4 v[4:7], v[144:151], v[192:199], v[4:7], v183, v183 op_sel_hi:[0,0,0]
	v_mfma_scale_f32_16x16x128_f8f6f4 v[0:3], v[152:159], v[192:199], v[0:3], v183, v183 op_sel_hi:[0,0,0]
	s_add_u32 s4, s4, 0x100
	s_addc_u32 s5, s5, 0
	s_add_u32 s25, s25, 0x100
	s_addc_u32 s27, s27, 0
	s_cmp_ge_i32 s34, s13
	s_mov_b32 s6, s34
	s_barrier
	s_cbranch_scc0 .LBB0_4066

.LBB0_4512:
	s_barrier
	s_cmp_lt_i32 s4, 4
	s_cselect_b64 s[80:81], -1, 0
	s_and_b64 vcc, exec, s[80:81]
	s_cbranch_vccnz .LBB0_4514
	s_setprio 1
	s_barrier

.LBB0_4533:
	s_setprio 0
	s_nop 6
	v_rcp_f32_e32 v8, v80
	v_lshlrev_b64 v[2:3], 11, v[186:187]
	v_lshl_add_u64 v[2:3], s[82:83], 0, v[2:3]
	v_lshlrev_b32_e32 v0, 4, v197
	v_lshl_add_u64 v[6:7], v[2:3], 0, v[0:1]
	v_mul_f32_e32 v0, v64, v8
	v_mul_f32_e32 v3, v65, v8
	v_mov_b32_e32 v2, v1
	v_cvt_pk_fp8_f32 v2, v0, v3
	v_mul_f32_e32 v0, v68, v8
	v_mul_f32_e32 v3, v69, v8
	v_mov_b32_e32 v4, v1
	v_cvt_pk_fp8_f32 v4, v0, v3
	v_mul_f32_e32 v5, v66, v8
	v_mul_f32_e32 v9, v67, v8
	v_mul_f32_e32 v0, v70, v8
	v_mul_f32_e32 v3, v71, v8
	v_cvt_pk_fp8_f32 v2, v5, v9 op_sel:[0,0,1]
	v_cvt_pk_fp8_f32 v4, v0, v3 op_sel:[0,0,1]
	v_mul_f32_e32 v0, v72, v8
	v_mul_f32_e32 v5, v73, v8
	v_mov_b32_e32 v3, v1
	v_cvt_pk_fp8_f32 v3, v0, v5
	v_mul_f32_e32 v0, v76, v8
	v_mul_f32_e32 v11, v77, v8
	v_mov_b32_e32 v5, v1
	v_cvt_pk_fp8_f32 v5, v0, v11
	v_mul_f32_e32 v9, v74, v8
	v_mul_f32_e32 v10, v75, v8
	v_cvt_pk_fp8_f32 v3, v9, v10 op_sel:[0,0,1]
	v_mul_f32_e32 v0, v78, v8
	v_mul_f32_e32 v9, v79, v8
	v_cvt_pk_fp8_f32 v5, v0, v9 op_sel:[0,0,1]
	v_permlane32_swap_b32_e32 v2, v3
	v_mul_f32_e32 v0, v48, v8
	v_permlane32_swap_b32_e32 v4, v5
	global_store_dwordx4 v[6:7], v[2:5], off
	v_mul_f32_e32 v9, v51, v8
	v_mul_f32_e32 v11, v61, v8
	v_mul_f32_e32 v3, v49, v8
	v_mov_b32_e32 v2, v1
	v_cvt_pk_fp8_f32 v2, v0, v3
	v_mul_f32_e32 v0, v52, v8
	v_mul_f32_e32 v3, v53, v8
	v_mov_b32_e32 v4, v1
	v_cvt_pk_fp8_f32 v4, v0, v3
	v_mul_f32_e32 v5, v50, v8
	v_mul_f32_e32 v0, v54, v8
	v_mul_f32_e32 v3, v55, v8
	v_cvt_pk_fp8_f32 v2, v5, v9 op_sel:[0,0,1]
	v_cvt_pk_fp8_f32 v4, v0, v3 op_sel:[0,0,1]
	v_mul_f32_e32 v0, v56, v8
	v_mul_f32_e32 v5, v57, v8
	v_mov_b32_e32 v3, v1
	v_cvt_pk_fp8_f32 v3, v0, v5
	v_mul_f32_e32 v0, v60, v8
	v_mov_b32_e32 v5, v1
	v_cvt_pk_fp8_f32 v5, v0, v11
	v_mul_f32_e32 v9, v58, v8
	v_mul_f32_e32 v10, v59, v8
	v_cvt_pk_fp8_f32 v3, v9, v10 op_sel:[0,0,1]
	v_mul_f32_e32 v0, v62, v8
	v_mul_f32_e32 v9, v63, v8
	v_cvt_pk_fp8_f32 v5, v0, v9 op_sel:[0,0,1]
	v_permlane32_swap_b32_e32 v2, v3
	v_mul_f32_e32 v0, v32, v8
	v_permlane32_swap_b32_e32 v4, v5
	global_store_dwordx4 v[6:7], v[2:5], off offset:32
	v_mul_f32_e32 v9, v35, v8
	v_mul_f32_e32 v11, v45, v8
	v_mul_f32_e32 v3, v33, v8
	v_mov_b32_e32 v2, v1
	v_cvt_pk_fp8_f32 v2, v0, v3
	v_mul_f32_e32 v0, v36, v8
	v_mul_f32_e32 v3, v37, v8
	v_mov_b32_e32 v4, v1
	v_cvt_pk_fp8_f32 v4, v0, v3
	v_mul_f32_e32 v5, v34, v8
	v_mul_f32_e32 v0, v38, v8
	v_mul_f32_e32 v3, v39, v8
	v_cvt_pk_fp8_f32 v2, v5, v9 op_sel:[0,0,1]
	v_cvt_pk_fp8_f32 v4, v0, v3 op_sel:[0,0,1]
	v_mul_f32_e32 v0, v40, v8
	v_mul_f32_e32 v5, v41, v8
	v_mov_b32_e32 v3, v1
	v_cvt_pk_fp8_f32 v3, v0, v5
	v_mul_f32_e32 v0, v44, v8
	v_mov_b32_e32 v5, v1
	v_cvt_pk_fp8_f32 v5, v0, v11
	v_mul_f32_e32 v9, v42, v8
	v_mul_f32_e32 v10, v43, v8
	v_cvt_pk_fp8_f32 v3, v9, v10 op_sel:[0,0,1]
	v_mul_f32_e32 v0, v46, v8
	v_mul_f32_e32 v9, v47, v8
	v_cvt_pk_fp8_f32 v5, v0, v9 op_sel:[0,0,1]
	v_permlane32_swap_b32_e32 v2, v3
	v_mul_f32_e32 v0, v16, v8
	v_permlane32_swap_b32_e32 v4, v5
	global_store_dwordx4 v[6:7], v[2:5], off offset:64
	v_mul_f32_e32 v9, v19, v8
	v_mul_f32_e32 v11, v29, v8
	v_mul_f32_e32 v3, v17, v8
	v_mov_b32_e32 v2, v1
	v_cvt_pk_fp8_f32 v2, v0, v3
	v_mul_f32_e32 v0, v20, v8
	v_mul_f32_e32 v3, v21, v8
	v_mov_b32_e32 v4, v1
	v_cvt_pk_fp8_f32 v4, v0, v3
	v_mul_f32_e32 v5, v18, v8
	v_mul_f32_e32 v0, v22, v8
	v_mul_f32_e32 v3, v23, v8
	v_cvt_pk_fp8_f32 v2, v5, v9 op_sel:[0,0,1]
	v_cvt_pk_fp8_f32 v4, v0, v3 op_sel:[0,0,1]
	v_mul_f32_e32 v0, v24, v8
	v_mul_f32_e32 v5, v25, v8
	v_mov_b32_e32 v3, v1
	v_cvt_pk_fp8_f32 v3, v0, v5
	v_mul_f32_e32 v0, v28, v8
	v_mov_b32_e32 v5, v1
	v_cvt_pk_fp8_f32 v5, v0, v11
	v_mul_f32_e32 v9, v26, v8
	v_mul_f32_e32 v10, v27, v8
	v_mul_f32_e32 v0, v30, v8
	v_mul_f32_e32 v8, v31, v8
	v_cvt_pk_fp8_f32 v3, v9, v10 op_sel:[0,0,1]
	v_cvt_pk_fp8_f32 v5, v0, v8 op_sel:[0,0,1]
	s_and_b64 vcc, exec, s[52:53]
	v_permlane32_swap_b32_e32 v2, v3
	v_permlane32_swap_b32_e32 v4, v5
	global_store_dwordx4 v[6:7], v[2:5], off offset:96
	s_waitcnt vmcnt(0) lgkmcnt(0)
	s_barrier
	s_cbranch_vccz .LBB0_4535
	v_readlane_b32 s4, v254, 57
	v_readlane_b32 s5, v254, 58
	s_and_b64 s[4:5], s[4:5], s[78:79]
	s_cbranch_execz .LBB0_4536
	s_branch .LBB0_4537

.LBB0_4922:
	v_readlane_b32 s6, v252, 3
	v_readlane_b32 s7, v252, 4
	s_load_dwordx2 s[6:7], s[6:7], 0xb8
	s_ashr_i32 s10, s1, 3
	s_mov_b32 s33, 0
	s_mov_b32 s34, 0x10000
	s_waitcnt lgkmcnt(0)
	s_add_u32 s6, s6, s4
	s_addc_u32 s5, s7, s5
	s_add_u32 s1, s6, 0x289c8000
	s_addc_u32 s9, s5, 0
	s_add_u32 s26, s6, 0x31c8000
	v_readlane_b32 s4, v252, 2
	s_addc_u32 s27, s5, 0
	s_lshr_b32 s7, s4, 8
	v_readlane_b32 s4, v252, 10
	s_lshl_b32 s28, s4, 10
	v_lshl_add_u32 v1, v0, 4, s28
	v_ashrrev_i32_e32 v2, 31, v1
	v_lshrrev_b32_e32 v2, 22, v2
	v_add_u32_e32 v2, v1, v2
	v_ashrrev_i32_e32 v2, 10, v2
	v_mul_i32_i24_e32 v3, 0x400, v2
	v_sub_u32_e32 v3, v1, v3
	v_lshrrev_b32_e32 v4, 4, v3
	v_bitop3_b32 v3, v4, v3, 32 bitop3:0x6c
	v_ashrrev_i32_e32 v5, 31, v3
	v_lshrrev_b32_e32 v5, 26, v5
	v_add_u32_e32 v5, v3, v5
	v_lshrrev_b32_e32 v6, 6, v5
	v_and_b32_e32 v5, 0xc0, v5
	v_lshlrev_b32_e32 v4, 3, v2
	v_lshlrev_b32_e32 v2, 5, v2
	v_sub_u32_e32 v3, v3, v5
	v_mov_b32_e32 v5, 1
	v_and_b32_e32 v4, 0x1ffff0, v4
	v_and_b32_e32 v2, 32, v2
	v_ashrrev_i16_sdwa v3, v5, sext(v3) dst_sel:DWORD dst_unused:UNUSED_PAD src0_sel:DWORD src1_sel:BYTE_0
	v_add_u32_sdwa v2, v2, sext(v3) dst_sel:DWORD dst_unused:UNUSED_PAD src0_sel:DWORD src1_sel:WORD_0
	v_add_lshl_u32 v3, v6, v4, 11
	v_add_u32_e32 v1, 0x2000, v1
	s_add_i32 s4, s8, s10
	v_lshl_add_u32 v138, v2, 1, v3
	v_ashrrev_i32_e32 v2, 31, v1
	s_ashr_i32 s8, s4, 31
	v_lshrrev_b32_e32 v2, 22, v2
	s_lshr_b32 s8, s8, 26
	v_add_u32_e32 v2, v1, v2
	s_add_i32 s8, s4, s8
	v_ashrrev_i32_e32 v2, 10, v2
	s_ashr_i32 s10, s8, 6
	s_andn2_b32 s8, s8, 63
	v_mul_i32_i24_e32 v3, 0x400, v2
	s_sub_i32 s8, s4, s8
	v_sub_u32_e32 v1, v1, v3
	s_bfe_i32 s4, s8, 0x80000
	v_lshrrev_b32_e32 v3, 4, v1
	s_bfe_u32 s4, s4, 0x3000c
	v_bitop3_b32 v1, v3, v1, 32 bitop3:0x6c
	s_add_i32 s11, s8, s4
	v_ashrrev_i32_e32 v4, 31, v1
	s_bfe_i32 s4, s11, 0x80000
	s_and_b32 s11, s11, 0xf8
	v_lshrrev_b32_e32 v4, 26, v4
	s_sub_i32 s8, s8, s11
	v_add_u32_e32 v4, v1, v4
	s_lshl_b32 s10, s10, 3
	s_sext_i32_i8 s8, s8
	v_lshrrev_b32_e32 v6, 6, v4
	v_and_b32_e32 v4, 0xffc0, v4
	s_add_i32 s18, s10, s8
	v_sub_u32_e32 v1, v1, v4
	s_sext_i32_i16 s4, s4
	s_ashr_i32 s19, s18, 31
	v_lshrrev_b16_e32 v4, 7, v1
	s_lshr_b32 s4, s4, 3
	s_lshl_b64 s[10:11], s[18:19], 19
	v_and_b32_e32 v4, 1, v4
	s_add_u32 s20, s1, s10
	v_lshlrev_b32_e32 v3, 3, v2
	v_lshlrev_b32_e32 v2, 5, v2
	v_add_u16_e32 v1, v1, v4
	s_addc_u32 s21, s9, s11
	s_bfe_i64 s[10:11], s[4:5], 0x100000
	v_and_b32_e32 v3, 0x1ffff0, v3
	v_and_b32_e32 v2, 32, v2
	v_ashrrev_i16_sdwa v1, v5, sext(v1) dst_sel:DWORD dst_unused:UNUSED_PAD src0_sel:DWORD src1_sel:BYTE_0
	s_lshl_b64 s[10:11], s[10:11], 19
	v_add_u32_sdwa v1, v2, sext(v1) dst_sel:DWORD dst_unused:UNUSED_PAD src0_sel:DWORD src1_sel:WORD_0
	v_add_lshl_u32 v2, v6, v3, 11
	s_add_u32 s22, s26, s10
	v_lshl_add_u32 v139, v1, 1, v2
	s_addc_u32 s23, s27, s11
	s_add_i32 s19, s28, 0
	v_mov_b32_e32 v1, v138
	s_add_i32 m0, s19, 0x10000
	s_add_i32 s29, s19, 0x2000
	global_load_lds_dwordx4 v1, s[22:23]
	v_mov_b32_e32 v1, v139
	s_add_i32 m0, s19, 0x12000
	s_add_u32 s10, s22, 0x40000
	global_load_lds_dwordx4 v1, s[22:23]
	v_mov_b32_e32 v1, v138
	s_mov_b32 m0, s19
	s_addc_u32 s11, s23, 0
	global_load_lds_dwordx4 v1, s[20:21]
	v_mov_b32_e32 v1, v139
	s_mov_b32 m0, s29
	s_nop 0
	global_load_lds_dwordx4 v1, s[20:21]
	v_mov_b32_e32 v1, v138
	s_add_i32 m0, s19, 0x14000
	s_nop 0
	global_load_lds_dwordx4 v1, s[10:11]
	v_mov_b32_e32 v1, v139
	s_add_i32 m0, s19, 0x16000
	s_nop 0
	global_load_lds_dwordx4 v1, s[10:11]
	s_add_u32 s10, s20, 0x40000
	s_addc_u32 s11, s21, 0
	s_add_i32 s30, s19, 0x4000
	v_mov_b32_e32 v1, v138
	s_mov_b32 m0, s30
	s_add_i32 s31, s19, 0x6000
	global_load_lds_dwordx4 v1, s[10:11]
	v_mov_b32_e32 v1, v139
	s_mov_b32 m0, s31
	s_cmp_lg_u32 s7, 1
	global_load_lds_dwordx4 v1, s[10:11]
	s_cbranch_scc1 .LBB0_4924
	s_setprio 1
	s_barrier

.Lpeel_7:
	ds_read_b128 v[146:149], v141
	ds_read_b128 v[150:153], v141 offset:1024
	ds_read_b128 v[154:157], v141 offset:2048
	ds_read_b128 v[158:161], v141 offset:3072
	s_add_u32 s22, s20, 0xfffc0080
	s_addc_u32 s23, s21, -1
	s_cmp_eq_u32 s50, 12
	s_cselect_b32 s25, s15, s23
	s_cselect_b32 s24, s14, s22
	s_cselect_b32 s23, s17, s13
	s_cselect_b32 s22, s16, s11
	v_mov_b32_e32 v128, v138
	ds_read_b128 v[162:165], v142
	ds_read_b128 v[166:169], v142 offset:1024
	ds_read_b128 v[170:173], v142 offset:2048
	ds_read_b128 v[174:177], v142 offset:3072
	ds_read_b128 v[178:181], v142 offset:4096
	ds_read_b128 v[182:185], v142 offset:5120
	ds_read_b128 v[186:189], v142 offset:6144
	ds_read_b128 v[190:193], v142 offset:7168
	s_nop 0
	v_mov_b32_e32 v128, v139
	s_nop 0
	s_waitcnt lgkmcnt(8)
	s_barrier
	s_waitcnt lgkmcnt(0)
	s_waitcnt lgkmcnt(0)
	v_mfma_scale_f32_16x16x128_f8f6f4 v[124:127], v[146:153], v[162:169], 0, v143, v143 op_sel_hi:[0,0,0]
	v_mfma_scale_f32_16x16x128_f8f6f4 v[120:123], v[154:161], v[162:169], 0, v143, v143 op_sel_hi:[0,0,0]
	s_add_i32 m0, s19, 0xc000
	v_mfma_scale_f32_16x16x128_f8f6f4 v[116:119], v[146:153], v[170:177], 0, v143, v143 op_sel_hi:[0,0,0]
	global_load_lds_dwordx4 v138, s[20:21]
	v_mfma_scale_f32_16x16x128_f8f6f4 v[112:115], v[154:161], v[170:177], 0, v143, v143 op_sel_hi:[0,0,0]
	v_mfma_scale_f32_16x16x128_f8f6f4 v[132:135], v[146:153], v[178:185], 0, v143, v143 op_sel_hi:[0,0,0]
	s_add_i32 m0, s19, 0xe000
	v_mfma_scale_f32_16x16x128_f8f6f4 v[194:197], v[154:161], v[178:185], 0, v143, v143 op_sel_hi:[0,0,0]
	global_load_lds_dwordx4 v139, s[20:21]
	v_mfma_scale_f32_16x16x128_f8f6f4 v[198:201], v[146:153], v[186:193], 0, v143, v143 op_sel_hi:[0,0,0]
	v_mfma_scale_f32_16x16x128_f8f6f4 v[202:205], v[154:161], v[186:193], 0, v143, v143 op_sel_hi:[0,0,0]
	s_barrier
	v_mov_b32_e32 v128, v138
	s_add_i32 s51, s44, s28
	s_nop 2
	ds_read_b128 v[96:99], v144
	ds_read_b128 v[100:103], v144 offset:1024
	ds_read_b128 v[104:107], v144 offset:2048
	ds_read_b128 v[108:111], v144 offset:3072
	s_nop 0
	v_mov_b32_e32 v128, v139
	s_nop 0
	s_barrier
	s_waitcnt lgkmcnt(0)
	s_waitcnt lgkmcnt(0)
	v_mfma_scale_f32_16x16x128_f8f6f4 v[206:209], v[96:103], v[162:169], 0, v143, v143 op_sel_hi:[0,0,0]
	v_mfma_scale_f32_16x16x128_f8f6f4 v[162:165], v[104:111], v[162:169], 0, v143, v143 op_sel_hi:[0,0,0]
	s_mov_b32 m0, s51
	v_mfma_scale_f32_16x16x128_f8f6f4 v[166:169], v[96:103], v[170:177], 0, v143, v143 op_sel_hi:[0,0,0]
	global_load_lds_dwordx4 v138, s[22:23]
	v_mfma_scale_f32_16x16x128_f8f6f4 v[170:173], v[104:111], v[170:177], 0, v143, v143 op_sel_hi:[0,0,0]
	v_mfma_scale_f32_16x16x128_f8f6f4 v[174:177], v[96:103], v[178:185], 0, v143, v143 op_sel_hi:[0,0,0]
	s_add_i32 m0, s51, 0x2000
	v_mfma_scale_f32_16x16x128_f8f6f4 v[178:181], v[104:111], v[178:185], 0, v143, v143 op_sel_hi:[0,0,0]
	global_load_lds_dwordx4 v139, s[22:23]
	v_mfma_scale_f32_16x16x128_f8f6f4 v[182:185], v[96:103], v[186:193], 0, v143, v143 op_sel_hi:[0,0,0]
	v_mfma_scale_f32_16x16x128_f8f6f4 v[186:189], v[104:111], v[186:193], 0, v143, v143 op_sel_hi:[0,0,0]
	v_mov_b32_e32 v128, v138
	s_barrier
	s_nop 2
	ds_read_b128 v[32:35], v142 offset:16384
	ds_read_b128 v[36:39], v142 offset:17408
	ds_read_b128 v[40:43], v142 offset:18432
	ds_read_b128 v[44:47], v142 offset:19456
	ds_read_b128 v[48:51], v142 offset:20480
	ds_read_b128 v[52:55], v142 offset:21504
	ds_read_b128 v[56:59], v142 offset:22528
	ds_read_b128 v[60:63], v142 offset:23552
	s_nop 0
	v_mov_b32_e32 v128, v139
	s_nop 0
	s_barrier
	s_waitcnt lgkmcnt(0)
	s_waitcnt lgkmcnt(0)
	v_mfma_scale_f32_16x16x128_f8f6f4 v[92:95], v[146:153], v[32:39], 0, v143, v143 op_sel_hi:[0,0,0]
	v_mfma_scale_f32_16x16x128_f8f6f4 v[88:91], v[154:161], v[32:39], 0, v143, v143 op_sel_hi:[0,0,0]
	s_mov_b32 m0, s19
	v_mfma_scale_f32_16x16x128_f8f6f4 v[84:87], v[146:153], v[40:47], 0, v143, v143 op_sel_hi:[0,0,0]
	global_load_lds_dwordx4 v138, s[24:25]
	v_mfma_scale_f32_16x16x128_f8f6f4 v[80:83], v[154:161], v[40:47], 0, v143, v143 op_sel_hi:[0,0,0]
	v_mfma_scale_f32_16x16x128_f8f6f4 v[76:79], v[146:153], v[48:55], 0, v143, v143 op_sel_hi:[0,0,0]
	s_mov_b32 m0, s29
	v_mfma_scale_f32_16x16x128_f8f6f4 v[72:75], v[154:161], v[48:55], 0, v143, v143 op_sel_hi:[0,0,0]
	global_load_lds_dwordx4 v139, s[24:25]
	v_mfma_scale_f32_16x16x128_f8f6f4 v[190:193], v[146:153], v[56:63], 0, v143, v143 op_sel_hi:[0,0,0]
	v_mfma_scale_f32_16x16x128_f8f6f4 v[210:213], v[154:161], v[56:63], 0, v143, v143 op_sel_hi:[0,0,0]
	s_barrier
	s_add_u32 s52, s22, 0x40000
	s_addc_u32 s53, s23, 0
	s_nop 2
	v_mov_b32_e32 v64, v138
	s_add_i32 s51, s45, s28
	s_mov_b32 s100, s51
	s_nop 0
	v_mov_b32_e32 v64, v139
	s_add_i32 s101, s51, 0x2000
	s_nop 0
	s_waitcnt vmcnt(4)
	s_barrier
	v_mfma_scale_f32_16x16x128_f8f6f4 v[214:217], v[96:103], v[32:39], 0, v143, v143 op_sel_hi:[0,0,0]
	v_mfma_scale_f32_16x16x128_f8f6f4 v[218:221], v[104:111], v[32:39], 0, v143, v143 op_sel_hi:[0,0,0]
	s_mov_b32 m0, s100
	v_mfma_scale_f32_16x16x128_f8f6f4 v[222:225], v[96:103], v[40:47], 0, v143, v143 op_sel_hi:[0,0,0]
	global_load_lds_dwordx4 v138, s[52:53]
	v_mfma_scale_f32_16x16x128_f8f6f4 v[226:229], v[104:111], v[40:47], 0, v143, v143 op_sel_hi:[0,0,0]
	v_mfma_scale_f32_16x16x128_f8f6f4 v[230:233], v[96:103], v[48:55], 0, v143, v143 op_sel_hi:[0,0,0]
	s_mov_b32 m0, s101
	v_mfma_scale_f32_16x16x128_f8f6f4 v[234:237], v[104:111], v[48:55], 0, v143, v143 op_sel_hi:[0,0,0]
	global_load_lds_dwordx4 v139, s[52:53]
	v_mfma_scale_f32_16x16x128_f8f6f4 v[238:241], v[96:103], v[56:63], 0, v143, v143 op_sel_hi:[0,0,0]
	v_mfma_scale_f32_16x16x128_f8f6f4 v[242:245], v[104:111], v[56:63], 0, v143, v143 op_sel_hi:[0,0,0]
	s_add_i32 s51, 0, 0x18000
	s_nop 1
	v_add_u32_e32 v12, s51, v140
	s_barrier
	s_nop 0
	ds_read_b128 v[0:3], v12
	ds_read_b128 v[4:7], v12 offset:1024
	ds_read_b128 v[8:11], v12 offset:2048
	ds_read_b128 v[12:15], v12 offset:3072
	s_add_u32 s52, s24, 0x40000
	v_mov_b32_e32 v40, v138
	ds_read_b128 v[16:19], v142 offset:32768
	ds_read_b128 v[20:23], v142 offset:33792
	ds_read_b128 v[24:27], v142 offset:34816
	ds_read_b128 v[28:31], v142 offset:35840
	ds_read_b128 v[32:35], v142 offset:36864
	ds_read_b128 v[36:39], v142 offset:37888
	ds_read_b128 v[64:67], v142 offset:38912
	ds_read_b128 v[68:71], v142 offset:39936
	s_addc_u32 s53, s25, 0
	s_nop 0
	v_mov_b32_e32 v40, v139
	s_nop 0
	s_waitcnt lgkmcnt(8)
	s_barrier
	s_waitcnt lgkmcnt(0)
	s_waitcnt lgkmcnt(0)
	v_mfma_scale_f32_16x16x128_f8f6f4 v[124:127], v[0:7], v[16:23], v[124:127], v143, v143 op_sel_hi:[0,0,0]
	v_mfma_scale_f32_16x16x128_f8f6f4 v[120:123], v[8:15], v[16:23], v[120:123], v143, v143 op_sel_hi:[0,0,0]
	s_mov_b32 m0, s30
	v_mfma_scale_f32_16x16x128_f8f6f4 v[116:119], v[0:7], v[24:31], v[116:119], v143, v143 op_sel_hi:[0,0,0]
	global_load_lds_dwordx4 v138, s[52:53]
	v_mfma_scale_f32_16x16x128_f8f6f4 v[112:115], v[8:15], v[24:31], v[112:115], v143, v143 op_sel_hi:[0,0,0]
	v_mfma_scale_f32_16x16x128_f8f6f4 v[108:111], v[0:7], v[32:39], v[132:135], v143, v143 op_sel_hi:[0,0,0]
	s_mov_b32 m0, s31
	v_mfma_scale_f32_16x16x128_f8f6f4 v[104:107], v[8:15], v[32:39], v[194:197], v143, v143 op_sel_hi:[0,0,0]
	global_load_lds_dwordx4 v139, s[52:53]
	v_mfma_scale_f32_16x16x128_f8f6f4 v[100:103], v[0:7], v[64:71], v[198:201], v143, v143 op_sel_hi:[0,0,0]
	v_mfma_scale_f32_16x16x128_f8f6f4 v[96:99], v[8:15], v[64:71], v[202:205], v143, v143 op_sel_hi:[0,0,0]
	s_barrier
	s_add_i32 s52, 0, 0x1c000
	v_add_u32_e32 v40, s52, v140
	v_mov_b32_e32 v128, v138
	ds_read_b128 v[146:149], v40
	ds_read_b128 v[150:153], v40 offset:1024
	ds_read_b128 v[154:157], v40 offset:2048
	ds_read_b128 v[158:161], v40 offset:3072
	s_add_i32 s51, s51, s28
	v_lshl_add_u64 v[40:41], s[22:23], 0, v[128:129]
	v_lshl_add_u64 v[40:41], v[40:41], 0, s[6:7]
	v_mov_b32_e32 v128, v139
	v_lshl_add_u64 v[40:41], s[22:23], 0, v[128:129]
	v_lshl_add_u64 v[40:41], v[40:41], 0, s[6:7]
	s_barrier
	s_waitcnt lgkmcnt(0)
	s_waitcnt lgkmcnt(0)
	v_mfma_scale_f32_16x16x128_f8f6f4 v[60:63], v[146:153], v[16:23], v[206:209], v143, v143 op_sel_hi:[0,0,0]
	v_mfma_scale_f32_16x16x128_f8f6f4 v[56:59], v[154:161], v[16:23], v[162:165], v143, v143 op_sel_hi:[0,0,0]
	s_add_u32 s98, s22, s6
	s_addc_u32 s99, s23, s7
	s_mov_b32 m0, s51
	v_mfma_scale_f32_16x16x128_f8f6f4 v[52:55], v[146:153], v[24:31], v[166:169], v143, v143 op_sel_hi:[0,0,0]
	global_load_lds_dwordx4 v138, s[98:99]
	v_mfma_scale_f32_16x16x128_f8f6f4 v[48:51], v[154:161], v[24:31], v[170:173], v143, v143 op_sel_hi:[0,0,0]
	v_mfma_scale_f32_16x16x128_f8f6f4 v[44:47], v[146:153], v[32:39], v[174:177], v143, v143 op_sel_hi:[0,0,0]
	s_add_i32 m0, s51, 0x2000
	v_mfma_scale_f32_16x16x128_f8f6f4 v[40:43], v[154:161], v[32:39], v[178:181], v143, v143 op_sel_hi:[0,0,0]
	global_load_lds_dwordx4 v139, s[98:99]
	v_mfma_scale_f32_16x16x128_f8f6f4 v[36:39], v[146:153], v[64:71], v[182:185], v143, v143 op_sel_hi:[0,0,0]
	v_mfma_scale_f32_16x16x128_f8f6f4 v[32:35], v[154:161], v[64:71], v[186:189], v143, v143 op_sel_hi:[0,0,0]
	v_mov_b32_e32 v128, v138
	s_barrier
	ds_read_b128 v[16:19], v142 offset:49152
	ds_read_b128 v[20:23], v142 offset:50176
	ds_read_b128 v[162:165], v142 offset:51200
	ds_read_b128 v[166:169], v142 offset:52224
	ds_read_b128 v[170:173], v142 offset:53248
	ds_read_b128 v[174:177], v142 offset:54272
	ds_read_b128 v[178:181], v142 offset:55296
	ds_read_b128 v[182:185], v142 offset:56320
	v_lshl_add_u64 v[24:25], s[24:25], 0, v[128:129]
	v_lshl_add_u64 v[24:25], v[24:25], 0, s[6:7]
	v_mov_b32_e32 v128, v139
	v_lshl_add_u64 v[24:25], s[24:25], 0, v[128:129]
	v_lshl_add_u64 v[24:25], v[24:25], 0, s[6:7]
	s_barrier
	s_waitcnt lgkmcnt(0)
	s_waitcnt lgkmcnt(0)
	v_mfma_scale_f32_16x16x128_f8f6f4 v[92:95], v[0:7], v[16:23], v[92:95], v143, v143 op_sel_hi:[0,0,0]
	v_mfma_scale_f32_16x16x128_f8f6f4 v[88:91], v[8:15], v[16:23], v[88:91], v143, v143 op_sel_hi:[0,0,0]
	s_add_u32 s98, s24, s6
	s_addc_u32 s99, s25, s7
	s_mov_b32 m0, s41
	v_mfma_scale_f32_16x16x128_f8f6f4 v[84:87], v[0:7], v[162:169], v[84:87], v143, v143 op_sel_hi:[0,0,0]
	global_load_lds_dwordx4 v138, s[98:99]
	v_mfma_scale_f32_16x16x128_f8f6f4 v[80:83], v[8:15], v[162:169], v[80:83], v143, v143 op_sel_hi:[0,0,0]
	v_mfma_scale_f32_16x16x128_f8f6f4 v[76:79], v[0:7], v[170:177], v[76:79], v143, v143 op_sel_hi:[0,0,0]
	s_mov_b32 m0, s42
	v_mfma_scale_f32_16x16x128_f8f6f4 v[72:75], v[8:15], v[170:177], v[72:75], v143, v143 op_sel_hi:[0,0,0]
	global_load_lds_dwordx4 v139, s[98:99]
	v_mfma_scale_f32_16x16x128_f8f6f4 v[68:71], v[0:7], v[178:185], v[190:193], v143, v143 op_sel_hi:[0,0,0]
	v_mfma_scale_f32_16x16x128_f8f6f4 v[64:67], v[8:15], v[178:185], v[210:213], v143, v143 op_sel_hi:[0,0,0]
	s_barrier
	s_add_u32 s22, s22, 0x40080
	s_addc_u32 s23, s23, 0
	v_mov_b32_e32 v0, v138
	s_add_i32 s24, s52, s28
	s_nop 0
	v_mov_b32_e32 v0, v139
	s_nop 0
	s_waitcnt vmcnt(4)
	s_barrier
	v_mfma_scale_f32_16x16x128_f8f6f4 v[28:31], v[146:153], v[16:23], v[214:217], v143, v143 op_sel_hi:[0,0,0]
	v_mfma_scale_f32_16x16x128_f8f6f4 v[24:27], v[154:161], v[16:23], v[218:221], v143, v143 op_sel_hi:[0,0,0]
	s_mov_b32 m0, s24
	v_mfma_scale_f32_16x16x128_f8f6f4 v[20:23], v[146:153], v[162:169], v[222:225], v143, v143 op_sel_hi:[0,0,0]
	global_load_lds_dwordx4 v138, s[22:23]
	v_mfma_scale_f32_16x16x128_f8f6f4 v[16:19], v[154:161], v[162:169], v[226:229], v143, v143 op_sel_hi:[0,0,0]
	v_mfma_scale_f32_16x16x128_f8f6f4 v[12:15], v[146:153], v[170:177], v[230:233], v143, v143 op_sel_hi:[0,0,0]
	s_add_i32 m0, s24, 0x2000
	v_mfma_scale_f32_16x16x128_f8f6f4 v[8:11], v[154:161], v[170:177], v[234:237], v143, v143 op_sel_hi:[0,0,0]
	global_load_lds_dwordx4 v139, s[22:23]
	v_mfma_scale_f32_16x16x128_f8f6f4 v[4:7], v[146:153], v[178:185], v[238:241], v143, v143 op_sel_hi:[0,0,0]
	v_mfma_scale_f32_16x16x128_f8f6f4 v[0:3], v[154:161], v[178:185], v[242:245], v143, v143 op_sel_hi:[0,0,0]
	s_add_i32 s50, s50, 2
	s_add_u32 s20, s20, 0x100
	s_addc_u32 s21, s21, 0
	s_add_u32 s11, s11, 0x100
	s_addc_u32 s13, s13, 0
	s_cmp_gt_u32 s50, 13
	s_barrier
	s_cbranch_scc0 .LBB0_4932
	s_branch .Lpeel_exit_7
.LBB0_4932:
	ds_read_b128 v[146:149], v141
	ds_read_b128 v[150:153], v141 offset:1024
	ds_read_b128 v[154:157], v141 offset:2048
	ds_read_b128 v[158:161], v141 offset:3072
	s_add_u32 s22, s20, 0xfffc0080
	s_addc_u32 s23, s21, -1
	s_cmp_eq_u32 s50, 12
	s_cselect_b32 s25, s15, s23
	s_cselect_b32 s24, s14, s22
	s_cselect_b32 s23, s17, s13
	s_cselect_b32 s22, s16, s11
	v_mov_b32_e32 v128, v138
	ds_read_b128 v[162:165], v142
	ds_read_b128 v[166:169], v142 offset:1024
	ds_read_b128 v[170:173], v142 offset:2048
	ds_read_b128 v[174:177], v142 offset:3072
	ds_read_b128 v[178:181], v142 offset:4096
	ds_read_b128 v[182:185], v142 offset:5120
	ds_read_b128 v[186:189], v142 offset:6144
	ds_read_b128 v[190:193], v142 offset:7168
	s_nop 0
	v_mov_b32_e32 v128, v139
	s_nop 0
	s_waitcnt lgkmcnt(8)
	s_barrier
	s_waitcnt lgkmcnt(0)
	s_waitcnt lgkmcnt(0)
	v_mfma_scale_f32_16x16x128_f8f6f4 v[124:127], v[146:153], v[162:169], v[124:127], v143, v143 op_sel_hi:[0,0,0]
	v_mfma_scale_f32_16x16x128_f8f6f4 v[120:123], v[154:161], v[162:169], v[120:123], v143, v143 op_sel_hi:[0,0,0]
	s_add_i32 m0, s19, 0xc000
	v_mfma_scale_f32_16x16x128_f8f6f4 v[116:119], v[146:153], v[170:177], v[116:119], v143, v143 op_sel_hi:[0,0,0]
	global_load_lds_dwordx4 v138, s[20:21]
	v_mfma_scale_f32_16x16x128_f8f6f4 v[112:115], v[154:161], v[170:177], v[112:115], v143, v143 op_sel_hi:[0,0,0]
	v_mfma_scale_f32_16x16x128_f8f6f4 v[132:135], v[146:153], v[178:185], v[108:111], v143, v143 op_sel_hi:[0,0,0]
	s_add_i32 m0, s19, 0xe000
	v_mfma_scale_f32_16x16x128_f8f6f4 v[194:197], v[154:161], v[178:185], v[104:107], v143, v143 op_sel_hi:[0,0,0]
	global_load_lds_dwordx4 v139, s[20:21]
	v_mfma_scale_f32_16x16x128_f8f6f4 v[198:201], v[146:153], v[186:193], v[100:103], v143, v143 op_sel_hi:[0,0,0]
	v_mfma_scale_f32_16x16x128_f8f6f4 v[202:205], v[154:161], v[186:193], v[96:99], v143, v143 op_sel_hi:[0,0,0]
	s_barrier
	v_mov_b32_e32 v128, v138
	s_add_i32 s51, s44, s28
	s_nop 2
	ds_read_b128 v[96:99], v144
	ds_read_b128 v[100:103], v144 offset:1024
	ds_read_b128 v[104:107], v144 offset:2048
	ds_read_b128 v[108:111], v144 offset:3072
	s_nop 0
	v_mov_b32_e32 v128, v139
	s_nop 0
	s_barrier
	s_waitcnt lgkmcnt(0)
	s_waitcnt lgkmcnt(0)
	v_mfma_scale_f32_16x16x128_f8f6f4 v[206:209], v[96:103], v[162:169], v[60:63], v143, v143 op_sel_hi:[0,0,0]
	v_mfma_scale_f32_16x16x128_f8f6f4 v[162:165], v[104:111], v[162:169], v[56:59], v143, v143 op_sel_hi:[0,0,0]
	s_mov_b32 m0, s51
	v_mfma_scale_f32_16x16x128_f8f6f4 v[166:169], v[96:103], v[170:177], v[52:55], v143, v143 op_sel_hi:[0,0,0]
	global_load_lds_dwordx4 v138, s[22:23]
	v_mfma_scale_f32_16x16x128_f8f6f4 v[170:173], v[104:111], v[170:177], v[48:51], v143, v143 op_sel_hi:[0,0,0]
	v_mfma_scale_f32_16x16x128_f8f6f4 v[174:177], v[96:103], v[178:185], v[44:47], v143, v143 op_sel_hi:[0,0,0]
	s_add_i32 m0, s51, 0x2000
	v_mfma_scale_f32_16x16x128_f8f6f4 v[178:181], v[104:111], v[178:185], v[40:43], v143, v143 op_sel_hi:[0,0,0]
	global_load_lds_dwordx4 v139, s[22:23]
	v_mfma_scale_f32_16x16x128_f8f6f4 v[182:185], v[96:103], v[186:193], v[36:39], v143, v143 op_sel_hi:[0,0,0]
	v_mfma_scale_f32_16x16x128_f8f6f4 v[186:189], v[104:111], v[186:193], v[32:35], v143, v143 op_sel_hi:[0,0,0]
	v_mov_b32_e32 v128, v138
	s_barrier
	s_nop 2
	ds_read_b128 v[32:35], v142 offset:16384
	ds_read_b128 v[36:39], v142 offset:17408
	ds_read_b128 v[40:43], v142 offset:18432
	ds_read_b128 v[44:47], v142 offset:19456
	ds_read_b128 v[48:51], v142 offset:20480
	ds_read_b128 v[52:55], v142 offset:21504
	ds_read_b128 v[56:59], v142 offset:22528
	ds_read_b128 v[60:63], v142 offset:23552
	s_nop 0
	v_mov_b32_e32 v128, v139
	s_nop 0
	s_barrier
	s_waitcnt lgkmcnt(0)
	s_waitcnt lgkmcnt(0)
	v_mfma_scale_f32_16x16x128_f8f6f4 v[92:95], v[146:153], v[32:39], v[92:95], v143, v143 op_sel_hi:[0,0,0]
	v_mfma_scale_f32_16x16x128_f8f6f4 v[88:91], v[154:161], v[32:39], v[88:91], v143, v143 op_sel_hi:[0,0,0]
	s_mov_b32 m0, s19
	v_mfma_scale_f32_16x16x128_f8f6f4 v[84:87], v[146:153], v[40:47], v[84:87], v143, v143 op_sel_hi:[0,0,0]
	global_load_lds_dwordx4 v138, s[24:25]
	v_mfma_scale_f32_16x16x128_f8f6f4 v[80:83], v[154:161], v[40:47], v[80:83], v143, v143 op_sel_hi:[0,0,0]
	v_mfma_scale_f32_16x16x128_f8f6f4 v[76:79], v[146:153], v[48:55], v[76:79], v143, v143 op_sel_hi:[0,0,0]
	s_mov_b32 m0, s29
	v_mfma_scale_f32_16x16x128_f8f6f4 v[72:75], v[154:161], v[48:55], v[72:75], v143, v143 op_sel_hi:[0,0,0]
	global_load_lds_dwordx4 v139, s[24:25]
	v_mfma_scale_f32_16x16x128_f8f6f4 v[190:193], v[146:153], v[56:63], v[68:71], v143, v143 op_sel_hi:[0,0,0]
	v_mfma_scale_f32_16x16x128_f8f6f4 v[210:213], v[154:161], v[56:63], v[64:67], v143, v143 op_sel_hi:[0,0,0]
	s_barrier
	s_add_u32 s52, s22, 0x40000
	s_addc_u32 s53, s23, 0
	s_nop 2
	v_mov_b32_e32 v64, v138
	s_add_i32 s51, s45, s28
	s_mov_b32 s100, s51
	s_nop 0
	v_mov_b32_e32 v64, v139
	s_add_i32 s101, s51, 0x2000
	s_nop 0
	s_waitcnt vmcnt(4)
	s_barrier
	v_mfma_scale_f32_16x16x128_f8f6f4 v[214:217], v[96:103], v[32:39], v[28:31], v143, v143 op_sel_hi:[0,0,0]
	v_mfma_scale_f32_16x16x128_f8f6f4 v[218:221], v[104:111], v[32:39], v[24:27], v143, v143 op_sel_hi:[0,0,0]
	s_mov_b32 m0, s100
	v_mfma_scale_f32_16x16x128_f8f6f4 v[222:225], v[96:103], v[40:47], v[20:23], v143, v143 op_sel_hi:[0,0,0]
	global_load_lds_dwordx4 v138, s[52:53]
	v_mfma_scale_f32_16x16x128_f8f6f4 v[226:229], v[104:111], v[40:47], v[16:19], v143, v143 op_sel_hi:[0,0,0]
	v_mfma_scale_f32_16x16x128_f8f6f4 v[230:233], v[96:103], v[48:55], v[12:15], v143, v143 op_sel_hi:[0,0,0]
	s_mov_b32 m0, s101
	v_mfma_scale_f32_16x16x128_f8f6f4 v[234:237], v[104:111], v[48:55], v[8:11], v143, v143 op_sel_hi:[0,0,0]
	global_load_lds_dwordx4 v139, s[52:53]
	v_mfma_scale_f32_16x16x128_f8f6f4 v[238:241], v[96:103], v[56:63], v[4:7], v143, v143 op_sel_hi:[0,0,0]
	v_mfma_scale_f32_16x16x128_f8f6f4 v[242:245], v[104:111], v[56:63], v[0:3], v143, v143 op_sel_hi:[0,0,0]
	s_add_i32 s51, 0, 0x18000
	s_nop 1
	v_add_u32_e32 v12, s51, v140
	s_barrier
	s_nop 0
	ds_read_b128 v[0:3], v12
	ds_read_b128 v[4:7], v12 offset:1024
	ds_read_b128 v[8:11], v12 offset:2048
	ds_read_b128 v[12:15], v12 offset:3072
	s_add_u32 s52, s24, 0x40000
	v_mov_b32_e32 v40, v138
	ds_read_b128 v[16:19], v142 offset:32768
	ds_read_b128 v[20:23], v142 offset:33792
	ds_read_b128 v[24:27], v142 offset:34816
	ds_read_b128 v[28:31], v142 offset:35840
	ds_read_b128 v[32:35], v142 offset:36864
	ds_read_b128 v[36:39], v142 offset:37888
	ds_read_b128 v[64:67], v142 offset:38912
	ds_read_b128 v[68:71], v142 offset:39936
	s_addc_u32 s53, s25, 0
	s_nop 0
	v_mov_b32_e32 v40, v139
	s_nop 0
	s_waitcnt lgkmcnt(8)
	s_barrier
	s_waitcnt lgkmcnt(0)
	s_waitcnt lgkmcnt(0)
	v_mfma_scale_f32_16x16x128_f8f6f4 v[124:127], v[0:7], v[16:23], v[124:127], v143, v143 op_sel_hi:[0,0,0]
	v_mfma_scale_f32_16x16x128_f8f6f4 v[120:123], v[8:15], v[16:23], v[120:123], v143, v143 op_sel_hi:[0,0,0]
	s_mov_b32 m0, s30
	v_mfma_scale_f32_16x16x128_f8f6f4 v[116:119], v[0:7], v[24:31], v[116:119], v143, v143 op_sel_hi:[0,0,0]
	global_load_lds_dwordx4 v138, s[52:53]
	v_mfma_scale_f32_16x16x128_f8f6f4 v[112:115], v[8:15], v[24:31], v[112:115], v143, v143 op_sel_hi:[0,0,0]
	v_mfma_scale_f32_16x16x128_f8f6f4 v[108:111], v[0:7], v[32:39], v[132:135], v143, v143 op_sel_hi:[0,0,0]
	s_mov_b32 m0, s31
	v_mfma_scale_f32_16x16x128_f8f6f4 v[104:107], v[8:15], v[32:39], v[194:197], v143, v143 op_sel_hi:[0,0,0]
	global_load_lds_dwordx4 v139, s[52:53]
	v_mfma_scale_f32_16x16x128_f8f6f4 v[100:103], v[0:7], v[64:71], v[198:201], v143, v143 op_sel_hi:[0,0,0]
	v_mfma_scale_f32_16x16x128_f8f6f4 v[96:99], v[8:15], v[64:71], v[202:205], v143, v143 op_sel_hi:[0,0,0]
	s_barrier
	s_add_i32 s52, 0, 0x1c000
	v_add_u32_e32 v40, s52, v140
	v_mov_b32_e32 v128, v138
	ds_read_b128 v[146:149], v40
	ds_read_b128 v[150:153], v40 offset:1024
	ds_read_b128 v[154:157], v40 offset:2048
	ds_read_b128 v[158:161], v40 offset:3072
	s_add_i32 s51, s51, s28
	v_lshl_add_u64 v[40:41], s[22:23], 0, v[128:129]
	v_lshl_add_u64 v[40:41], v[40:41], 0, s[6:7]
	v_mov_b32_e32 v128, v139
	v_lshl_add_u64 v[40:41], s[22:23], 0, v[128:129]
	v_lshl_add_u64 v[40:41], v[40:41], 0, s[6:7]
	s_barrier
	s_waitcnt lgkmcnt(0)
	s_waitcnt lgkmcnt(0)
	v_mfma_scale_f32_16x16x128_f8f6f4 v[60:63], v[146:153], v[16:23], v[206:209], v143, v143 op_sel_hi:[0,0,0]
	v_mfma_scale_f32_16x16x128_f8f6f4 v[56:59], v[154:161], v[16:23], v[162:165], v143, v143 op_sel_hi:[0,0,0]
	s_add_u32 s98, s22, s6
	s_addc_u32 s99, s23, s7
	s_mov_b32 m0, s51
	v_mfma_scale_f32_16x16x128_f8f6f4 v[52:55], v[146:153], v[24:31], v[166:169], v143, v143 op_sel_hi:[0,0,0]
	global_load_lds_dwordx4 v138, s[98:99]
	v_mfma_scale_f32_16x16x128_f8f6f4 v[48:51], v[154:161], v[24:31], v[170:173], v143, v143 op_sel_hi:[0,0,0]
	v_mfma_scale_f32_16x16x128_f8f6f4 v[44:47], v[146:153], v[32:39], v[174:177], v143, v143 op_sel_hi:[0,0,0]
	s_add_i32 m0, s51, 0x2000
	v_mfma_scale_f32_16x16x128_f8f6f4 v[40:43], v[154:161], v[32:39], v[178:181], v143, v143 op_sel_hi:[0,0,0]
	global_load_lds_dwordx4 v139, s[98:99]
	v_mfma_scale_f32_16x16x128_f8f6f4 v[36:39], v[146:153], v[64:71], v[182:185], v143, v143 op_sel_hi:[0,0,0]
	v_mfma_scale_f32_16x16x128_f8f6f4 v[32:35], v[154:161], v[64:71], v[186:189], v143, v143 op_sel_hi:[0,0,0]
	v_mov_b32_e32 v128, v138
	s_barrier
	ds_read_b128 v[16:19], v142 offset:49152
	ds_read_b128 v[20:23], v142 offset:50176
	ds_read_b128 v[162:165], v142 offset:51200
	ds_read_b128 v[166:169], v142 offset:52224
	ds_read_b128 v[170:173], v142 offset:53248
	ds_read_b128 v[174:177], v142 offset:54272
	ds_read_b128 v[178:181], v142 offset:55296
	ds_read_b128 v[182:185], v142 offset:56320
	v_lshl_add_u64 v[24:25], s[24:25], 0, v[128:129]
	v_lshl_add_u64 v[24:25], v[24:25], 0, s[6:7]
	v_mov_b32_e32 v128, v139
	v_lshl_add_u64 v[24:25], s[24:25], 0, v[128:129]
	v_lshl_add_u64 v[24:25], v[24:25], 0, s[6:7]
	s_barrier
	s_waitcnt lgkmcnt(0)
	s_waitcnt lgkmcnt(0)
	v_mfma_scale_f32_16x16x128_f8f6f4 v[92:95], v[0:7], v[16:23], v[92:95], v143, v143 op_sel_hi:[0,0,0]
	v_mfma_scale_f32_16x16x128_f8f6f4 v[88:91], v[8:15], v[16:23], v[88:91], v143, v143 op_sel_hi:[0,0,0]
	s_add_u32 s98, s24, s6
	s_addc_u32 s99, s25, s7
	s_mov_b32 m0, s41
	v_mfma_scale_f32_16x16x128_f8f6f4 v[84:87], v[0:7], v[162:169], v[84:87], v143, v143 op_sel_hi:[0,0,0]
	global_load_lds_dwordx4 v138, s[98:99]
	v_mfma_scale_f32_16x16x128_f8f6f4 v[80:83], v[8:15], v[162:169], v[80:83], v143, v143 op_sel_hi:[0,0,0]
	v_mfma_scale_f32_16x16x128_f8f6f4 v[76:79], v[0:7], v[170:177], v[76:79], v143, v143 op_sel_hi:[0,0,0]
	s_mov_b32 m0, s42
	v_mfma_scale_f32_16x16x128_f8f6f4 v[72:75], v[8:15], v[170:177], v[72:75], v143, v143 op_sel_hi:[0,0,0]
	global_load_lds_dwordx4 v139, s[98:99]
	v_mfma_scale_f32_16x16x128_f8f6f4 v[68:71], v[0:7], v[178:185], v[190:193], v143, v143 op_sel_hi:[0,0,0]
	v_mfma_scale_f32_16x16x128_f8f6f4 v[64:67], v[8:15], v[178:185], v[210:213], v143, v143 op_sel_hi:[0,0,0]
	s_barrier
	s_add_u32 s22, s22, 0x40080
	s_addc_u32 s23, s23, 0
	v_mov_b32_e32 v0, v138
	s_add_i32 s24, s52, s28
	s_nop 0
	v_mov_b32_e32 v0, v139
	s_nop 0
	s_waitcnt vmcnt(4)
	s_barrier
	v_mfma_scale_f32_16x16x128_f8f6f4 v[28:31], v[146:153], v[16:23], v[214:217], v143, v143 op_sel_hi:[0,0,0]
	v_mfma_scale_f32_16x16x128_f8f6f4 v[24:27], v[154:161], v[16:23], v[218:221], v143, v143 op_sel_hi:[0,0,0]
	s_mov_b32 m0, s24
	v_mfma_scale_f32_16x16x128_f8f6f4 v[20:23], v[146:153], v[162:169], v[222:225], v143, v143 op_sel_hi:[0,0,0]
	global_load_lds_dwordx4 v138, s[22:23]
	v_mfma_scale_f32_16x16x128_f8f6f4 v[16:19], v[154:161], v[162:169], v[226:229], v143, v143 op_sel_hi:[0,0,0]
	v_mfma_scale_f32_16x16x128_f8f6f4 v[12:15], v[146:153], v[170:177], v[230:233], v143, v143 op_sel_hi:[0,0,0]
	s_add_i32 m0, s24, 0x2000
	v_mfma_scale_f32_16x16x128_f8f6f4 v[8:11], v[154:161], v[170:177], v[234:237], v143, v143 op_sel_hi:[0,0,0]
	global_load_lds_dwordx4 v139, s[22:23]
	v_mfma_scale_f32_16x16x128_f8f6f4 v[4:7], v[146:153], v[178:185], v[238:241], v143, v143 op_sel_hi:[0,0,0]
	v_mfma_scale_f32_16x16x128_f8f6f4 v[0:3], v[154:161], v[178:185], v[242:245], v143, v143 op_sel_hi:[0,0,0]
	s_add_i32 s50, s50, 2
	s_add_u32 s20, s20, 0x100
	s_addc_u32 s21, s21, 0
	s_add_u32 s11, s11, 0x100
	s_addc_u32 s13, s13, 0
	s_cmp_gt_u32 s50, 13
	s_barrier
	s_cbranch_scc0 .LBB0_4932

.LBB0_5361:
	s_mov_b64 s[98:99], exec
	s_mov_b64 exec, -1
	v_mbcnt_lo_u32_b32 v0, -1, 0
	v_mbcnt_hi_u32_b32 v0, -1, v0
	v_min_u32_e32 v0, 14, v0
	v_lshl_add_u32 v0, v0, 2, s3
	ds_read_b32 v0, v0
	s_waitcnt lgkmcnt(0)
	v_cmp_ge_i32_e32 vcc, s59, v0
	s_mov_b64 exec, s[98:99]
	s_and_b32 s8, vcc_lo, 0x7fff
	s_bcnt1_i32_b32 s8, s8
	s_add_i32 s3, s3, 60
	s_mov_b32 s2, 16
	s_cmp_eq_u32 s2, 16
	s_add_u32 s10, s14, 0x249c8000
	s_addc_u32 s11, s15, 0
	s_add_u32 s2, s14, 0x91c8000
	s_addc_u32 s3, s15, 0
	s_add_u32 s21, s14, 0x4c8000
	v_add_u32_e32 v0, s4, v176
	v_readlane_b32 s9, v252, 10
	s_addc_u32 s33, s15, 0
	v_readlane_b32 s5, v252, 2
	v_ashrrev_i32_e32 v1, 31, v0
	s_lshl_b32 s42, s9, 10
	s_mul_i32 s9, s59, -11
	s_lshr_b32 s5, s5, 8
	v_lshrrev_b32_e32 v1, 26, v1
	s_add_i32 s30, s9, s0
	s_mul_i32 s12, s8, 0x580000
	v_lshlrev_b32_e32 v2, 4, v0
	v_add_u32_e32 v1, v0, v1
	v_bfe_i32 v0, v0, 27, 1
	s_mul_hi_u32 s9, s8, 0x580000
	s_add_u32 s18, s2, s12
	v_lshrrev_b32_e32 v0, 22, v0
	s_addc_u32 s9, s3, s9
	s_ashr_i32 s31, s30, 31
	v_add_u32_e32 v0, v2, v0
	s_lshl_b64 s[12:13], s[30:31], 19
	v_and_b32_e32 v0, 0xfffffc00, v0
	s_add_u32 s36, s18, s12
	v_sub_u32_e32 v0, v2, v0
	v_add_u32_e32 v2, 0x2000, v2
	s_addc_u32 s37, s9, s13
	s_lshl_b32 s9, s8, 2
	v_ashrrev_i32_e32 v3, 31, v2
	s_add_i32 s9, s9, 0
	v_lshrrev_b32_e32 v3, 22, v3
	s_add_i32 s9, s9, 0x20100
	v_add_u32_e32 v3, v2, v3
	v_mov_b32_e32 v5, s9
	v_ashrrev_i32_e32 v15, 10, v3
	ds_read_b32 v5, v5
	v_mul_i32_i24_e32 v3, 0x400, v15
	v_ashrrev_i32_e32 v12, 6, v1
	v_lshrrev_b32_e32 v1, 4, v0
	v_sub_u32_e32 v2, v2, v3
	v_bitop3_b32 v13, v1, v0, 32 bitop3:0x6c
	v_lshrrev_b32_e32 v3, 4, v2
	v_ashrrev_i32_e32 v1, 31, v13
	v_bitop3_b32 v16, v3, v2, 32 bitop3:0x6c
	v_lshrrev_b32_e32 v1, 26, v1
	v_ashrrev_i32_e32 v3, 31, v16
	s_mov_b32 s9, 0
	s_waitcnt lgkmcnt(0)
	v_sub_u32_e32 v5, s59, v5
	v_lshlrev_b32_e32 v0, 3, v12
	v_add_u32_e32 v14, v13, v1
	v_lshrrev_b32_e32 v3, 26, v3
	s_lshl_b64 s[12:13], s[8:9], 16
	v_lshlrev_b32_e32 v8, 8, v5
	v_and_b32_e32 v0, -16, v0
	v_ashrrev_i32_e32 v1, 6, v14
	v_lshlrev_b32_e32 v2, 3, v15
	v_add_u32_e32 v17, v16, v3
	s_add_u32 s12, s21, s12
	v_ashrrev_i32_e32 v9, 31, v8
	v_add_u32_e32 v4, v1, v0
	v_and_b32_e32 v2, -16, v2
	v_ashrrev_i32_e32 v3, 6, v17
	s_addc_u32 s13, s33, s13
	v_lshlrev_b64 v[8:9], 2, v[8:9]
	v_add_u32_e32 v6, v3, v2
	v_lshl_add_u64 v[8:9], s[12:13], 0, v[8:9]
	v_ashrrev_i32_e32 v5, 31, v4
	v_lshl_add_u64 v[10:11], v[4:5], 2, v[8:9]
	v_ashrrev_i32_e32 v7, 31, v6
	v_lshl_add_u64 v[8:9], v[6:7], 2, v[8:9]
	global_load_dword v5, v[10:11], off
	global_load_dword v7, v[8:9], off
	global_load_dword v18, v[8:9], off offset:512
	global_load_dword v19, v[10:11], off offset:512
	v_and_b32_e32 v11, 0xc0, v14
	v_mov_b32_e32 v8, 1
	v_sub_u32_e32 v11, v13, v11
	v_lshlrev_b32_e32 v9, 5, v12
	v_ashrrev_i16_sdwa v11, v8, sext(v11) dst_sel:DWORD dst_unused:UNUSED_PAD src0_sel:DWORD src1_sel:BYTE_0
	v_and_b32_e32 v9, 32, v9
	v_bfe_i32 v11, v11, 0, 16
	v_and_b32_e32 v12, 0xc0, v17
	v_add_lshl_u32 v180, v9, v11, 1
	v_sub_u32_e32 v9, v16, v12
	v_lshlrev_b32_e32 v10, 5, v15
	v_lshl_add_u32 v181, v4, 11, v180
	v_ashrrev_i16_sdwa v4, v8, sext(v9) dst_sel:DWORD dst_unused:UNUSED_PAD src0_sel:DWORD src1_sel:BYTE_0
	v_and_b32_e32 v10, 32, v10
	v_bfe_i32 v4, v4, 0, 16
	s_add_i32 s31, s42, 0
	v_add_lshl_u32 v182, v10, v4, 1
	s_add_i32 s43, s31, 0x10000
	v_lshl_add_u32 v183, v6, 11, v182
	v_mov_b32_e32 v8, v181
	v_mov_b32_e32 v4, v183
	s_mov_b32 m0, s43
	s_add_i32 s44, s31, 0x12000
	s_add_i32 s45, s31, 0x2000
	global_load_lds_dwordx4 v8, s[36:37]
	s_mov_b32 m0, s44
	s_add_u32 s12, s36, 0x40000
	global_load_lds_dwordx4 v4, s[36:37]
	s_mov_b32 m0, s31
	s_addc_u32 s13, s37, 0
	s_add_i32 s46, s31, 0x4000
	s_add_i32 s47, s31, 0x6000
	s_waitcnt vmcnt(0)
	v_lshl_add_u32 v184, v5, 11, v180
	v_mov_b32_e32 v4, v184
	v_lshl_add_u32 v185, v7, 11, v182
	v_lshl_add_u32 v186, v19, 11, v180
	global_load_lds_dwordx4 v4, s[10:11]
	v_mov_b32_e32 v4, v185
	s_mov_b32 m0, s45
	v_lshl_add_u32 v187, v18, 11, v182
	global_load_lds_dwordx4 v4, s[10:11]
	v_mov_b32_e32 v4, v181
	s_add_i32 m0, s31, 0x14000
	s_nop 0
	global_load_lds_dwordx4 v4, s[12:13]
	v_mov_b32_e32 v4, v183
	s_add_i32 m0, s31, 0x16000
	s_cmp_eq_u32 s5, 1
	global_load_lds_dwordx4 v4, s[12:13]
	v_mov_b32_e32 v4, v186
	s_mov_b32 m0, s46
	s_nop 0
	global_load_lds_dwordx4 v4, s[10:11]
	v_mov_b32_e32 v4, v187
	s_mov_b32 m0, s47
	s_nop 0
	global_load_lds_dwordx4 v4, s[10:11]
	s_cbranch_scc0 .LBB0_5364
	s_setprio 1
	s_barrier

.LBB0_5804:
	s_mov_b64 s[98:99], exec
	s_mov_b64 exec, -1
	v_mbcnt_lo_u32_b32 v1, -1, 0
	v_mbcnt_hi_u32_b32 v1, -1, v1
	v_min_u32_e32 v1, 14, v1
	v_lshl_add_u32 v1, v1, 2, s6
	ds_read_b32 v1, v1
	s_waitcnt lgkmcnt(0)
	v_cmp_ge_i32_e32 vcc, s49, v1
	s_mov_b64 exec, s[98:99]
	s_and_b32 s8, vcc_lo, 0x7fff
	s_bcnt1_i32_b32 s8, s8
	s_add_i32 s6, s6, 60
	s_mov_b32 s7, 16
	s_cmp_eq_u32 s7, 16
	s_add_u32 s7, s4, 0x2f1c8000
	s_addc_u32 s20, s5, 0
	s_add_u32 s21, s4, 0x119c8000
	v_readlane_b32 s9, v252, 10
	s_addc_u32 s22, s5, 0
	s_lshl_b32 s23, s9, 10
	v_lshl_add_u32 v1, v0, 4, s23
	v_ashrrev_i32_e32 v2, 31, v1
	v_lshrrev_b32_e32 v2, 22, v2
	v_add_u32_e32 v2, v1, v2
	v_ashrrev_i32_e32 v2, 10, v2
	v_mul_i32_i24_e32 v3, 0x400, v2
	v_sub_u32_e32 v3, v1, v3
	v_lshrrev_b32_e32 v4, 4, v3
	v_bitop3_b32 v3, v4, v3, 32 bitop3:0x6c
	v_ashrrev_i32_e32 v5, 31, v3
	v_lshrrev_b32_e32 v5, 26, v5
	v_add_u32_e32 v5, v3, v5
	v_lshlrev_b32_e32 v4, 3, v2
	v_lshrrev_b32_e32 v6, 6, v5
	v_and_b32_e32 v5, 0xc0, v5
	v_and_b32_e32 v4, 0x7ffff0, v4
	v_lshlrev_b32_e32 v2, 5, v2
	v_sub_u32_e32 v3, v3, v5
	v_mov_b32_e32 v5, 1
	v_add_u32_e32 v4, v6, v4
	v_and_b32_e32 v2, 32, v2
	v_ashrrev_i16_sdwa v3, v5, sext(v3) dst_sel:DWORD dst_unused:UNUSED_PAD src0_sel:DWORD src1_sel:BYTE_0
	s_movk_i32 s9, 0x600
	v_add_u32_sdwa v2, v2, sext(v3) dst_sel:DWORD dst_unused:UNUSED_PAD src0_sel:DWORD src1_sel:WORD_0
	v_mul_lo_u32 v3, v4, s9
	v_add_u32_e32 v1, 0x2000, v1
	v_lshl_add_u32 v132, v2, 1, v3
	v_ashrrev_i32_e32 v2, 31, v1
	v_lshrrev_b32_e32 v2, 22, v2
	v_add_u32_e32 v2, v1, v2
	v_ashrrev_i32_e32 v2, 10, v2
	v_mul_i32_i24_e32 v3, 0x400, v2
	v_sub_u32_e32 v1, v1, v3
	v_lshrrev_b32_e32 v3, 4, v1
	v_bitop3_b32 v1, v3, v1, 32 bitop3:0x6c
	v_ashrrev_i32_e32 v4, 31, v1
	v_lshrrev_b32_e32 v4, 26, v4
	v_add_u32_e32 v4, v1, v4
	v_lshrrev_b32_e32 v6, 6, v4
	v_and_b32_e32 v4, 0xffc0, v4
	v_sub_u32_e32 v1, v1, v4
	v_lshrrev_b16_e32 v4, 7, v1
	v_lshlrev_b32_e32 v3, 3, v2
	v_and_b32_e32 v4, 1, v4
	v_and_b32_e32 v3, 0x7ffff0, v3
	v_lshlrev_b32_e32 v2, 5, v2
	v_add_u16_e32 v1, v1, v4
	v_add_u32_e32 v3, v6, v3
	v_and_b32_e32 v2, 32, v2
	v_ashrrev_i16_sdwa v1, v5, sext(v1) dst_sel:DWORD dst_unused:UNUSED_PAD src0_sel:DWORD src1_sel:BYTE_0
	v_readlane_b32 s6, v252, 2
	v_add_u32_sdwa v1, v2, sext(v1) dst_sel:DWORD dst_unused:UNUSED_PAD src0_sel:DWORD src1_sel:WORD_0
	v_mul_lo_u32 v2, v3, s9
	s_lshl_b32 s9, s49, 3
	s_lshr_b32 s6, s6, 8
	s_sub_i32 s50, s0, s9
	s_mul_hi_u32 s9, s8, 0x300000
	s_mul_i32 s8, s8, 0x300000
	s_add_u32 s8, s21, s8
	s_addc_u32 s9, s22, s9
	s_mul_i32 s11, s50, 0x60000
	s_mul_hi_i32 s10, s50, 0x60000
	s_add_u32 s16, s8, s11
	s_addc_u32 s17, s9, s10
	s_mul_i32 s9, s49, 0x60000
	s_mul_hi_i32 s8, s49, 0x60000
	s_add_u32 s14, s7, s9
	v_lshl_add_u32 v133, v1, 1, v2
	s_addc_u32 s15, s20, s8
	s_add_i32 s24, s23, 0
	v_mov_b32_e32 v1, v132
	s_add_i32 m0, s24, 0x10000
	s_add_i32 s25, s24, 0x2000
	global_load_lds_dwordx4 v1, s[16:17]
	v_mov_b32_e32 v1, v133
	s_add_i32 m0, s24, 0x12000
	s_add_u32 s8, s16, 0x30000
	global_load_lds_dwordx4 v1, s[16:17]
	v_mov_b32_e32 v1, v132
	s_mov_b32 m0, s24
	s_addc_u32 s9, s17, 0
	global_load_lds_dwordx4 v1, s[14:15]
	v_mov_b32_e32 v1, v133
	s_mov_b32 m0, s25
	s_mov_b32 s28, 0
	global_load_lds_dwordx4 v1, s[14:15]
	v_mov_b32_e32 v1, v132
	s_add_i32 m0, s24, 0x14000
	s_mov_b32 s29, 0x10000
	global_load_lds_dwordx4 v1, s[8:9]
	v_mov_b32_e32 v1, v133
	s_add_i32 m0, s24, 0x16000
	s_nop 0
	global_load_lds_dwordx4 v1, s[8:9]
	s_add_u32 s8, s14, 0x30000
	s_addc_u32 s9, s15, 0
	s_add_i32 s26, s24, 0x4000
	v_mov_b32_e32 v1, v132
	s_mov_b32 m0, s26
	s_add_i32 s27, s24, 0x6000
	global_load_lds_dwordx4 v1, s[8:9]
	v_mov_b32_e32 v1, v133
	s_mov_b32 m0, s27
	s_cmp_eq_u32 s6, 1
	global_load_lds_dwordx4 v1, s[8:9]
	s_cbranch_scc0 .LBB0_5807
	s_setprio 1
	s_barrier

.Lpeel_9:
	ds_read_b128 v[140:143], v134
	ds_read_b128 v[144:147], v134 offset:1024
	ds_read_b128 v[148:151], v134 offset:2048
	ds_read_b128 v[152:155], v134 offset:3072
	s_add_u32 s16, s14, 0xfffd0080
	s_addc_u32 s17, s15, -1
	s_cmp_eq_u32 s53, 8
	s_cselect_b32 s19, s13, s17
	s_cselect_b32 s18, s12, s16
	s_cselect_b32 s17, s11, s52
	s_cselect_b32 s16, s10, s51
	v_mov_b32_e32 v128, v132
	ds_read_b128 v[156:159], v135
	ds_read_b128 v[160:163], v135 offset:1024
	ds_read_b128 v[164:167], v135 offset:2048
	ds_read_b128 v[168:171], v135 offset:3072
	ds_read_b128 v[172:175], v135 offset:4096
	ds_read_b128 v[176:179], v135 offset:5120
	ds_read_b128 v[180:183], v135 offset:6144
	ds_read_b128 v[184:187], v135 offset:7168
	s_nop 0
	v_mov_b32_e32 v128, v133
	s_nop 0
	s_waitcnt lgkmcnt(8)
	s_barrier
	s_waitcnt lgkmcnt(0)
	s_waitcnt lgkmcnt(0)
	v_mfma_scale_f32_16x16x128_f8f6f4 v[124:127], v[140:147], v[156:163], 0, v136, v136 op_sel_hi:[0,0,0]
	v_mfma_scale_f32_16x16x128_f8f6f4 v[120:123], v[148:155], v[156:163], 0, v136, v136 op_sel_hi:[0,0,0]
	s_mov_b32 m0, s38
	v_mfma_scale_f32_16x16x128_f8f6f4 v[116:119], v[140:147], v[164:171], 0, v136, v136 op_sel_hi:[0,0,0]
	global_load_lds_dwordx4 v132, s[14:15]
	v_mfma_scale_f32_16x16x128_f8f6f4 v[112:115], v[148:155], v[164:171], 0, v136, v136 op_sel_hi:[0,0,0]
	v_mfma_scale_f32_16x16x128_f8f6f4 v[188:191], v[140:147], v[172:179], 0, v136, v136 op_sel_hi:[0,0,0]
	s_mov_b32 m0, s39
	v_mfma_scale_f32_16x16x128_f8f6f4 v[192:195], v[148:155], v[172:179], 0, v136, v136 op_sel_hi:[0,0,0]
	global_load_lds_dwordx4 v133, s[14:15]
	v_mfma_scale_f32_16x16x128_f8f6f4 v[196:199], v[140:147], v[180:187], 0, v136, v136 op_sel_hi:[0,0,0]
	v_mfma_scale_f32_16x16x128_f8f6f4 v[200:203], v[148:155], v[180:187], 0, v136, v136 op_sel_hi:[0,0,0]
	s_barrier
	v_mov_b32_e32 v128, v132
	s_nop 2
	ds_read_b128 v[96:99], v137
	ds_read_b128 v[100:103], v137 offset:1024
	ds_read_b128 v[104:107], v137 offset:2048
	ds_read_b128 v[108:111], v137 offset:3072
	s_nop 0
	v_mov_b32_e32 v128, v133
	s_nop 0
	s_barrier
	s_waitcnt lgkmcnt(0)
	s_waitcnt lgkmcnt(0)
	v_mfma_scale_f32_16x16x128_f8f6f4 v[204:207], v[96:103], v[156:163], 0, v136, v136 op_sel_hi:[0,0,0]
	v_mfma_scale_f32_16x16x128_f8f6f4 v[156:159], v[104:111], v[156:163], 0, v136, v136 op_sel_hi:[0,0,0]
	s_mov_b32 m0, s40
	v_mfma_scale_f32_16x16x128_f8f6f4 v[160:163], v[96:103], v[164:171], 0, v136, v136 op_sel_hi:[0,0,0]
	global_load_lds_dwordx4 v132, s[16:17]
	v_mfma_scale_f32_16x16x128_f8f6f4 v[164:167], v[104:111], v[164:171], 0, v136, v136 op_sel_hi:[0,0,0]
	v_mfma_scale_f32_16x16x128_f8f6f4 v[168:171], v[96:103], v[172:179], 0, v136, v136 op_sel_hi:[0,0,0]
	s_mov_b32 m0, s41
	v_mfma_scale_f32_16x16x128_f8f6f4 v[172:175], v[104:111], v[172:179], 0, v136, v136 op_sel_hi:[0,0,0]
	global_load_lds_dwordx4 v133, s[16:17]
	v_mfma_scale_f32_16x16x128_f8f6f4 v[176:179], v[96:103], v[180:187], 0, v136, v136 op_sel_hi:[0,0,0]
	v_mfma_scale_f32_16x16x128_f8f6f4 v[180:183], v[104:111], v[180:187], 0, v136, v136 op_sel_hi:[0,0,0]
	v_mov_b32_e32 v128, v132
	s_barrier
	s_nop 2
	ds_read_b128 v[64:67], v135 offset:16384
	ds_read_b128 v[68:71], v135 offset:17408
	ds_read_b128 v[72:75], v135 offset:18432
	ds_read_b128 v[76:79], v135 offset:19456
	ds_read_b128 v[80:83], v135 offset:20480
	ds_read_b128 v[84:87], v135 offset:21504
	ds_read_b128 v[88:91], v135 offset:22528
	ds_read_b128 v[92:95], v135 offset:23552
	s_nop 0
	v_mov_b32_e32 v128, v133
	s_nop 0
	s_barrier
	s_waitcnt lgkmcnt(0)
	s_waitcnt lgkmcnt(0)
	v_mfma_scale_f32_16x16x128_f8f6f4 v[60:63], v[140:147], v[64:71], 0, v136, v136 op_sel_hi:[0,0,0]
	v_mfma_scale_f32_16x16x128_f8f6f4 v[56:59], v[148:155], v[64:71], 0, v136, v136 op_sel_hi:[0,0,0]
	s_mov_b32 m0, s24
	v_mfma_scale_f32_16x16x128_f8f6f4 v[52:55], v[140:147], v[72:79], 0, v136, v136 op_sel_hi:[0,0,0]
	global_load_lds_dwordx4 v132, s[18:19]
	v_mfma_scale_f32_16x16x128_f8f6f4 v[48:51], v[148:155], v[72:79], 0, v136, v136 op_sel_hi:[0,0,0]
	v_mfma_scale_f32_16x16x128_f8f6f4 v[184:187], v[140:147], v[80:87], 0, v136, v136 op_sel_hi:[0,0,0]
	s_mov_b32 m0, s25
	v_mfma_scale_f32_16x16x128_f8f6f4 v[208:211], v[148:155], v[80:87], 0, v136, v136 op_sel_hi:[0,0,0]
	global_load_lds_dwordx4 v133, s[18:19]
	v_mfma_scale_f32_16x16x128_f8f6f4 v[212:215], v[140:147], v[88:95], 0, v136, v136 op_sel_hi:[0,0,0]
	v_mfma_scale_f32_16x16x128_f8f6f4 v[216:219], v[148:155], v[88:95], 0, v136, v136 op_sel_hi:[0,0,0]
	s_barrier
	s_add_u32 s54, s16, 0x30000
	s_nop 3
	v_mov_b32_e32 v32, v132
	s_addc_u32 s55, s17, 0
	s_nop 0
	v_mov_b32_e32 v32, v133
	s_nop 0
	s_waitcnt vmcnt(4)
	s_barrier
	v_mfma_scale_f32_16x16x128_f8f6f4 v[220:223], v[96:103], v[64:71], 0, v136, v136 op_sel_hi:[0,0,0]
	v_mfma_scale_f32_16x16x128_f8f6f4 v[224:227], v[104:111], v[64:71], 0, v136, v136 op_sel_hi:[0,0,0]
	s_mov_b32 m0, s42
	v_mfma_scale_f32_16x16x128_f8f6f4 v[228:231], v[96:103], v[72:79], 0, v136, v136 op_sel_hi:[0,0,0]
	global_load_lds_dwordx4 v132, s[54:55]
	v_mfma_scale_f32_16x16x128_f8f6f4 v[232:235], v[104:111], v[72:79], 0, v136, v136 op_sel_hi:[0,0,0]
	v_mfma_scale_f32_16x16x128_f8f6f4 v[236:239], v[96:103], v[80:87], 0, v136, v136 op_sel_hi:[0,0,0]
	s_mov_b32 m0, s43
	v_mfma_scale_f32_16x16x128_f8f6f4 v[240:243], v[104:111], v[80:87], 0, v136, v136 op_sel_hi:[0,0,0]
	global_load_lds_dwordx4 v133, s[54:55]
	v_mfma_scale_f32_16x16x128_f8f6f4 v[244:247], v[96:103], v[88:95], 0, v136, v136 op_sel_hi:[0,0,0]
	v_mfma_scale_f32_16x16x128_f8f6f4 v[248:251], v[104:111], v[88:95], 0, v136, v136 op_sel_hi:[0,0,0]
	s_barrier
	s_nop 4
	ds_read_b128 v[0:3], v138
	ds_read_b128 v[4:7], v138 offset:1024
	ds_read_b128 v[8:11], v138 offset:2048
	ds_read_b128 v[12:15], v138 offset:3072
	s_add_u32 s54, s18, 0x30000
	v_mov_b32_e32 v64, v132
	ds_read_b128 v[16:19], v135 offset:32768
	ds_read_b128 v[20:23], v135 offset:33792
	ds_read_b128 v[24:27], v135 offset:34816
	ds_read_b128 v[28:31], v135 offset:35840
	ds_read_b128 v[32:35], v135 offset:36864
	ds_read_b128 v[36:39], v135 offset:37888
	ds_read_b128 v[40:43], v135 offset:38912
	ds_read_b128 v[44:47], v135 offset:39936
	s_addc_u32 s55, s19, 0
	s_nop 0
	v_mov_b32_e32 v64, v133
	s_nop 0
	s_waitcnt lgkmcnt(8)
	s_barrier
	s_waitcnt lgkmcnt(0)
	s_waitcnt lgkmcnt(0)
	v_mfma_scale_f32_16x16x128_f8f6f4 v[124:127], v[0:7], v[16:23], v[124:127], v136, v136 op_sel_hi:[0,0,0]
	v_mfma_scale_f32_16x16x128_f8f6f4 v[120:123], v[8:15], v[16:23], v[120:123], v136, v136 op_sel_hi:[0,0,0]
	s_mov_b32 m0, s26
	v_mfma_scale_f32_16x16x128_f8f6f4 v[116:119], v[0:7], v[24:31], v[116:119], v136, v136 op_sel_hi:[0,0,0]
	global_load_lds_dwordx4 v132, s[54:55]
	v_mfma_scale_f32_16x16x128_f8f6f4 v[112:115], v[8:15], v[24:31], v[112:115], v136, v136 op_sel_hi:[0,0,0]
	v_mfma_scale_f32_16x16x128_f8f6f4 v[108:111], v[0:7], v[32:39], v[188:191], v136, v136 op_sel_hi:[0,0,0]
	s_mov_b32 m0, s27
	v_mfma_scale_f32_16x16x128_f8f6f4 v[104:107], v[8:15], v[32:39], v[192:195], v136, v136 op_sel_hi:[0,0,0]
	global_load_lds_dwordx4 v133, s[54:55]
	v_mfma_scale_f32_16x16x128_f8f6f4 v[100:103], v[0:7], v[40:47], v[196:199], v136, v136 op_sel_hi:[0,0,0]
	v_mfma_scale_f32_16x16x128_f8f6f4 v[96:99], v[8:15], v[40:47], v[200:203], v136, v136 op_sel_hi:[0,0,0]
	s_barrier
	v_mov_b32_e32 v128, v132
	ds_read_b128 v[140:143], v139
	ds_read_b128 v[144:147], v139 offset:1024
	ds_read_b128 v[148:151], v139 offset:2048
	ds_read_b128 v[152:155], v139 offset:3072
	v_lshl_add_u64 v[64:65], s[16:17], 0, v[128:129]
	v_lshl_add_u64 v[64:65], v[64:65], 0, s[4:5]
	v_mov_b32_e32 v128, v133
	v_lshl_add_u64 v[64:65], s[16:17], 0, v[128:129]
	v_lshl_add_u64 v[64:65], v[64:65], 0, s[4:5]
	s_barrier
	s_waitcnt lgkmcnt(0)
	s_waitcnt lgkmcnt(0)
	v_mfma_scale_f32_16x16x128_f8f6f4 v[92:95], v[140:147], v[16:23], v[204:207], v136, v136 op_sel_hi:[0,0,0]
	v_mfma_scale_f32_16x16x128_f8f6f4 v[88:91], v[148:155], v[16:23], v[156:159], v136, v136 op_sel_hi:[0,0,0]
	s_add_u32 s98, s16, s4
	s_addc_u32 s99, s17, s5
	s_mov_b32 m0, s45
	v_mfma_scale_f32_16x16x128_f8f6f4 v[84:87], v[140:147], v[24:31], v[160:163], v136, v136 op_sel_hi:[0,0,0]
	global_load_lds_dwordx4 v132, s[98:99]
	v_mfma_scale_f32_16x16x128_f8f6f4 v[80:83], v[148:155], v[24:31], v[164:167], v136, v136 op_sel_hi:[0,0,0]
	v_mfma_scale_f32_16x16x128_f8f6f4 v[76:79], v[140:147], v[32:39], v[168:171], v136, v136 op_sel_hi:[0,0,0]
	s_mov_b32 m0, s46
	v_mfma_scale_f32_16x16x128_f8f6f4 v[72:75], v[148:155], v[32:39], v[172:175], v136, v136 op_sel_hi:[0,0,0]
	global_load_lds_dwordx4 v133, s[98:99]
	v_mfma_scale_f32_16x16x128_f8f6f4 v[68:71], v[140:147], v[40:47], v[176:179], v136, v136 op_sel_hi:[0,0,0]
	v_mfma_scale_f32_16x16x128_f8f6f4 v[64:67], v[148:155], v[40:47], v[180:183], v136, v136 op_sel_hi:[0,0,0]
	v_mov_b32_e32 v128, v132
	s_barrier
	ds_read_b128 v[16:19], v135 offset:49152
	ds_read_b128 v[20:23], v135 offset:50176
	ds_read_b128 v[156:159], v135 offset:51200
	ds_read_b128 v[160:163], v135 offset:52224
	ds_read_b128 v[164:167], v135 offset:53248
	ds_read_b128 v[168:171], v135 offset:54272
	ds_read_b128 v[172:175], v135 offset:55296
	ds_read_b128 v[176:179], v135 offset:56320
	v_lshl_add_u64 v[24:25], s[18:19], 0, v[128:129]
	v_lshl_add_u64 v[24:25], v[24:25], 0, s[4:5]
	v_mov_b32_e32 v128, v133
	v_lshl_add_u64 v[24:25], s[18:19], 0, v[128:129]
	v_lshl_add_u64 v[24:25], v[24:25], 0, s[4:5]
	s_barrier
	s_waitcnt lgkmcnt(0)
	s_waitcnt lgkmcnt(0)
	v_mfma_scale_f32_16x16x128_f8f6f4 v[60:63], v[0:7], v[16:23], v[60:63], v136, v136 op_sel_hi:[0,0,0]
	v_mfma_scale_f32_16x16x128_f8f6f4 v[56:59], v[8:15], v[16:23], v[56:59], v136, v136 op_sel_hi:[0,0,0]
	s_add_u32 s98, s18, s4
	s_addc_u32 s99, s19, s5
	s_mov_b32 m0, s35
	v_mfma_scale_f32_16x16x128_f8f6f4 v[52:55], v[0:7], v[156:163], v[52:55], v136, v136 op_sel_hi:[0,0,0]
	global_load_lds_dwordx4 v132, s[98:99]
	v_mfma_scale_f32_16x16x128_f8f6f4 v[48:51], v[8:15], v[156:163], v[48:51], v136, v136 op_sel_hi:[0,0,0]
	v_mfma_scale_f32_16x16x128_f8f6f4 v[44:47], v[0:7], v[164:171], v[184:187], v136, v136 op_sel_hi:[0,0,0]
	s_mov_b32 m0, s36
	v_mfma_scale_f32_16x16x128_f8f6f4 v[40:43], v[8:15], v[164:171], v[208:211], v136, v136 op_sel_hi:[0,0,0]
	global_load_lds_dwordx4 v133, s[98:99]
	v_mfma_scale_f32_16x16x128_f8f6f4 v[36:39], v[0:7], v[172:179], v[212:215], v136, v136 op_sel_hi:[0,0,0]
	v_mfma_scale_f32_16x16x128_f8f6f4 v[32:35], v[8:15], v[172:179], v[216:219], v136, v136 op_sel_hi:[0,0,0]
	s_barrier
	s_add_u32 s16, s16, 0x30080
	s_addc_u32 s17, s17, 0
	v_mov_b32_e32 v0, v132
	s_add_i32 s18, s44, s23
	s_nop 0
	v_mov_b32_e32 v0, v133
	s_nop 0
	s_waitcnt vmcnt(4)
	s_barrier
	v_mfma_scale_f32_16x16x128_f8f6f4 v[28:31], v[140:147], v[16:23], v[220:223], v136, v136 op_sel_hi:[0,0,0]
	v_mfma_scale_f32_16x16x128_f8f6f4 v[24:27], v[148:155], v[16:23], v[224:227], v136, v136 op_sel_hi:[0,0,0]
	s_mov_b32 m0, s18
	v_mfma_scale_f32_16x16x128_f8f6f4 v[20:23], v[140:147], v[156:163], v[228:231], v136, v136 op_sel_hi:[0,0,0]
	global_load_lds_dwordx4 v132, s[16:17]
	v_mfma_scale_f32_16x16x128_f8f6f4 v[16:19], v[148:155], v[156:163], v[232:235], v136, v136 op_sel_hi:[0,0,0]
	v_mfma_scale_f32_16x16x128_f8f6f4 v[12:15], v[140:147], v[164:171], v[236:239], v136, v136 op_sel_hi:[0,0,0]
	s_add_i32 m0, s18, 0x2000
	v_mfma_scale_f32_16x16x128_f8f6f4 v[8:11], v[148:155], v[164:171], v[240:243], v136, v136 op_sel_hi:[0,0,0]
	global_load_lds_dwordx4 v133, s[16:17]
	v_mfma_scale_f32_16x16x128_f8f6f4 v[4:7], v[140:147], v[172:179], v[244:247], v136, v136 op_sel_hi:[0,0,0]
	v_mfma_scale_f32_16x16x128_f8f6f4 v[0:3], v[148:155], v[172:179], v[248:251], v136, v136 op_sel_hi:[0,0,0]
	s_add_i32 s53, s53, 2
	s_add_u32 s14, s14, 0x100
	s_addc_u32 s15, s15, 0
	s_add_u32 s51, s51, 0x100
	s_addc_u32 s52, s52, 0
	s_cmp_gt_u32 s53, 9
	s_barrier
	s_cbranch_scc0 .LBB0_5813
	s_branch .Lpeel_exit_9
.LBB0_5813:
	ds_read_b128 v[140:143], v134
	ds_read_b128 v[144:147], v134 offset:1024
	ds_read_b128 v[148:151], v134 offset:2048
	ds_read_b128 v[152:155], v134 offset:3072
	s_add_u32 s16, s14, 0xfffd0080
	s_addc_u32 s17, s15, -1
	s_cmp_eq_u32 s53, 8
	s_cselect_b32 s19, s13, s17
	s_cselect_b32 s18, s12, s16
	s_cselect_b32 s17, s11, s52
	s_cselect_b32 s16, s10, s51
	v_mov_b32_e32 v128, v132
	ds_read_b128 v[156:159], v135
	ds_read_b128 v[160:163], v135 offset:1024
	ds_read_b128 v[164:167], v135 offset:2048
	ds_read_b128 v[168:171], v135 offset:3072
	ds_read_b128 v[172:175], v135 offset:4096
	ds_read_b128 v[176:179], v135 offset:5120
	ds_read_b128 v[180:183], v135 offset:6144
	ds_read_b128 v[184:187], v135 offset:7168
	s_nop 0
	v_mov_b32_e32 v128, v133
	s_nop 0
	s_waitcnt lgkmcnt(8)
	s_barrier
	s_waitcnt lgkmcnt(0)
	s_waitcnt lgkmcnt(0)
	v_mfma_scale_f32_16x16x128_f8f6f4 v[124:127], v[140:147], v[156:163], v[124:127], v136, v136 op_sel_hi:[0,0,0]
	v_mfma_scale_f32_16x16x128_f8f6f4 v[120:123], v[148:155], v[156:163], v[120:123], v136, v136 op_sel_hi:[0,0,0]
	s_mov_b32 m0, s38
	v_mfma_scale_f32_16x16x128_f8f6f4 v[116:119], v[140:147], v[164:171], v[116:119], v136, v136 op_sel_hi:[0,0,0]
	global_load_lds_dwordx4 v132, s[14:15]
	v_mfma_scale_f32_16x16x128_f8f6f4 v[112:115], v[148:155], v[164:171], v[112:115], v136, v136 op_sel_hi:[0,0,0]
	v_mfma_scale_f32_16x16x128_f8f6f4 v[188:191], v[140:147], v[172:179], v[108:111], v136, v136 op_sel_hi:[0,0,0]
	s_mov_b32 m0, s39
	v_mfma_scale_f32_16x16x128_f8f6f4 v[192:195], v[148:155], v[172:179], v[104:107], v136, v136 op_sel_hi:[0,0,0]
	global_load_lds_dwordx4 v133, s[14:15]
	v_mfma_scale_f32_16x16x128_f8f6f4 v[196:199], v[140:147], v[180:187], v[100:103], v136, v136 op_sel_hi:[0,0,0]
	v_mfma_scale_f32_16x16x128_f8f6f4 v[200:203], v[148:155], v[180:187], v[96:99], v136, v136 op_sel_hi:[0,0,0]
	s_barrier
	v_mov_b32_e32 v128, v132
	s_nop 2
	ds_read_b128 v[96:99], v137
	ds_read_b128 v[100:103], v137 offset:1024
	ds_read_b128 v[104:107], v137 offset:2048
	ds_read_b128 v[108:111], v137 offset:3072
	s_nop 0
	v_mov_b32_e32 v128, v133
	s_nop 0
	s_barrier
	s_waitcnt lgkmcnt(0)
	s_waitcnt lgkmcnt(0)
	v_mfma_scale_f32_16x16x128_f8f6f4 v[204:207], v[96:103], v[156:163], v[92:95], v136, v136 op_sel_hi:[0,0,0]
	v_mfma_scale_f32_16x16x128_f8f6f4 v[156:159], v[104:111], v[156:163], v[88:91], v136, v136 op_sel_hi:[0,0,0]
	s_mov_b32 m0, s40
	v_mfma_scale_f32_16x16x128_f8f6f4 v[160:163], v[96:103], v[164:171], v[84:87], v136, v136 op_sel_hi:[0,0,0]
	global_load_lds_dwordx4 v132, s[16:17]
	v_mfma_scale_f32_16x16x128_f8f6f4 v[164:167], v[104:111], v[164:171], v[80:83], v136, v136 op_sel_hi:[0,0,0]
	v_mfma_scale_f32_16x16x128_f8f6f4 v[168:171], v[96:103], v[172:179], v[76:79], v136, v136 op_sel_hi:[0,0,0]
	s_mov_b32 m0, s41
	v_mfma_scale_f32_16x16x128_f8f6f4 v[172:175], v[104:111], v[172:179], v[72:75], v136, v136 op_sel_hi:[0,0,0]
	global_load_lds_dwordx4 v133, s[16:17]
	v_mfma_scale_f32_16x16x128_f8f6f4 v[176:179], v[96:103], v[180:187], v[68:71], v136, v136 op_sel_hi:[0,0,0]
	v_mfma_scale_f32_16x16x128_f8f6f4 v[180:183], v[104:111], v[180:187], v[64:67], v136, v136 op_sel_hi:[0,0,0]
	v_mov_b32_e32 v128, v132
	s_barrier
	s_nop 2
	ds_read_b128 v[64:67], v135 offset:16384
	ds_read_b128 v[68:71], v135 offset:17408
	ds_read_b128 v[72:75], v135 offset:18432
	ds_read_b128 v[76:79], v135 offset:19456
	ds_read_b128 v[80:83], v135 offset:20480
	ds_read_b128 v[84:87], v135 offset:21504
	ds_read_b128 v[88:91], v135 offset:22528
	ds_read_b128 v[92:95], v135 offset:23552
	s_nop 0
	v_mov_b32_e32 v128, v133
	s_nop 0
	s_barrier
	s_waitcnt lgkmcnt(0)
	s_waitcnt lgkmcnt(0)
	v_mfma_scale_f32_16x16x128_f8f6f4 v[60:63], v[140:147], v[64:71], v[60:63], v136, v136 op_sel_hi:[0,0,0]
	v_mfma_scale_f32_16x16x128_f8f6f4 v[56:59], v[148:155], v[64:71], v[56:59], v136, v136 op_sel_hi:[0,0,0]
	s_mov_b32 m0, s24
	v_mfma_scale_f32_16x16x128_f8f6f4 v[52:55], v[140:147], v[72:79], v[52:55], v136, v136 op_sel_hi:[0,0,0]
	global_load_lds_dwordx4 v132, s[18:19]
	v_mfma_scale_f32_16x16x128_f8f6f4 v[48:51], v[148:155], v[72:79], v[48:51], v136, v136 op_sel_hi:[0,0,0]
	v_mfma_scale_f32_16x16x128_f8f6f4 v[184:187], v[140:147], v[80:87], v[44:47], v136, v136 op_sel_hi:[0,0,0]
	s_mov_b32 m0, s25
	v_mfma_scale_f32_16x16x128_f8f6f4 v[208:211], v[148:155], v[80:87], v[40:43], v136, v136 op_sel_hi:[0,0,0]
	global_load_lds_dwordx4 v133, s[18:19]
	v_mfma_scale_f32_16x16x128_f8f6f4 v[212:215], v[140:147], v[88:95], v[36:39], v136, v136 op_sel_hi:[0,0,0]
	v_mfma_scale_f32_16x16x128_f8f6f4 v[216:219], v[148:155], v[88:95], v[32:35], v136, v136 op_sel_hi:[0,0,0]
	s_barrier
	s_add_u32 s54, s16, 0x30000
	s_nop 3
	v_mov_b32_e32 v32, v132
	s_addc_u32 s55, s17, 0
	s_nop 0
	v_mov_b32_e32 v32, v133
	s_nop 0
	s_waitcnt vmcnt(4)
	s_barrier
	v_mfma_scale_f32_16x16x128_f8f6f4 v[220:223], v[96:103], v[64:71], v[28:31], v136, v136 op_sel_hi:[0,0,0]
	v_mfma_scale_f32_16x16x128_f8f6f4 v[224:227], v[104:111], v[64:71], v[24:27], v136, v136 op_sel_hi:[0,0,0]
	s_mov_b32 m0, s42
	v_mfma_scale_f32_16x16x128_f8f6f4 v[228:231], v[96:103], v[72:79], v[20:23], v136, v136 op_sel_hi:[0,0,0]
	global_load_lds_dwordx4 v132, s[54:55]
	v_mfma_scale_f32_16x16x128_f8f6f4 v[232:235], v[104:111], v[72:79], v[16:19], v136, v136 op_sel_hi:[0,0,0]
	v_mfma_scale_f32_16x16x128_f8f6f4 v[236:239], v[96:103], v[80:87], v[12:15], v136, v136 op_sel_hi:[0,0,0]
	s_mov_b32 m0, s43
	v_mfma_scale_f32_16x16x128_f8f6f4 v[240:243], v[104:111], v[80:87], v[8:11], v136, v136 op_sel_hi:[0,0,0]
	global_load_lds_dwordx4 v133, s[54:55]
	v_mfma_scale_f32_16x16x128_f8f6f4 v[244:247], v[96:103], v[88:95], v[4:7], v136, v136 op_sel_hi:[0,0,0]
	v_mfma_scale_f32_16x16x128_f8f6f4 v[248:251], v[104:111], v[88:95], v[0:3], v136, v136 op_sel_hi:[0,0,0]
	s_barrier
	s_nop 4
	ds_read_b128 v[0:3], v138
	ds_read_b128 v[4:7], v138 offset:1024
	ds_read_b128 v[8:11], v138 offset:2048
	ds_read_b128 v[12:15], v138 offset:3072
	s_add_u32 s54, s18, 0x30000
	v_mov_b32_e32 v64, v132
	ds_read_b128 v[16:19], v135 offset:32768
	ds_read_b128 v[20:23], v135 offset:33792
	ds_read_b128 v[24:27], v135 offset:34816
	ds_read_b128 v[28:31], v135 offset:35840
	ds_read_b128 v[32:35], v135 offset:36864
	ds_read_b128 v[36:39], v135 offset:37888
	ds_read_b128 v[40:43], v135 offset:38912
	ds_read_b128 v[44:47], v135 offset:39936
	s_addc_u32 s55, s19, 0
	s_nop 0
	v_mov_b32_e32 v64, v133
	s_nop 0
	s_waitcnt lgkmcnt(8)
	s_barrier
	s_waitcnt lgkmcnt(0)
	s_waitcnt lgkmcnt(0)
	v_mfma_scale_f32_16x16x128_f8f6f4 v[124:127], v[0:7], v[16:23], v[124:127], v136, v136 op_sel_hi:[0,0,0]
	v_mfma_scale_f32_16x16x128_f8f6f4 v[120:123], v[8:15], v[16:23], v[120:123], v136, v136 op_sel_hi:[0,0,0]
	s_mov_b32 m0, s26
	v_mfma_scale_f32_16x16x128_f8f6f4 v[116:119], v[0:7], v[24:31], v[116:119], v136, v136 op_sel_hi:[0,0,0]
	global_load_lds_dwordx4 v132, s[54:55]
	v_mfma_scale_f32_16x16x128_f8f6f4 v[112:115], v[8:15], v[24:31], v[112:115], v136, v136 op_sel_hi:[0,0,0]
	v_mfma_scale_f32_16x16x128_f8f6f4 v[108:111], v[0:7], v[32:39], v[188:191], v136, v136 op_sel_hi:[0,0,0]
	s_mov_b32 m0, s27
	v_mfma_scale_f32_16x16x128_f8f6f4 v[104:107], v[8:15], v[32:39], v[192:195], v136, v136 op_sel_hi:[0,0,0]
	global_load_lds_dwordx4 v133, s[54:55]
	v_mfma_scale_f32_16x16x128_f8f6f4 v[100:103], v[0:7], v[40:47], v[196:199], v136, v136 op_sel_hi:[0,0,0]
	v_mfma_scale_f32_16x16x128_f8f6f4 v[96:99], v[8:15], v[40:47], v[200:203], v136, v136 op_sel_hi:[0,0,0]
	s_barrier
	v_mov_b32_e32 v128, v132
	ds_read_b128 v[140:143], v139
	ds_read_b128 v[144:147], v139 offset:1024
	ds_read_b128 v[148:151], v139 offset:2048
	ds_read_b128 v[152:155], v139 offset:3072
	v_lshl_add_u64 v[64:65], s[16:17], 0, v[128:129]
	v_lshl_add_u64 v[64:65], v[64:65], 0, s[4:5]
	v_mov_b32_e32 v128, v133
	v_lshl_add_u64 v[64:65], s[16:17], 0, v[128:129]
	v_lshl_add_u64 v[64:65], v[64:65], 0, s[4:5]
	s_barrier
	s_waitcnt lgkmcnt(0)
	s_waitcnt lgkmcnt(0)
	v_mfma_scale_f32_16x16x128_f8f6f4 v[92:95], v[140:147], v[16:23], v[204:207], v136, v136 op_sel_hi:[0,0,0]
	v_mfma_scale_f32_16x16x128_f8f6f4 v[88:91], v[148:155], v[16:23], v[156:159], v136, v136 op_sel_hi:[0,0,0]
	s_add_u32 s98, s16, s4
	s_addc_u32 s99, s17, s5
	s_mov_b32 m0, s45
	v_mfma_scale_f32_16x16x128_f8f6f4 v[84:87], v[140:147], v[24:31], v[160:163], v136, v136 op_sel_hi:[0,0,0]
	global_load_lds_dwordx4 v132, s[98:99]
	v_mfma_scale_f32_16x16x128_f8f6f4 v[80:83], v[148:155], v[24:31], v[164:167], v136, v136 op_sel_hi:[0,0,0]
	v_mfma_scale_f32_16x16x128_f8f6f4 v[76:79], v[140:147], v[32:39], v[168:171], v136, v136 op_sel_hi:[0,0,0]
	s_mov_b32 m0, s46
	v_mfma_scale_f32_16x16x128_f8f6f4 v[72:75], v[148:155], v[32:39], v[172:175], v136, v136 op_sel_hi:[0,0,0]
	global_load_lds_dwordx4 v133, s[98:99]
	v_mfma_scale_f32_16x16x128_f8f6f4 v[68:71], v[140:147], v[40:47], v[176:179], v136, v136 op_sel_hi:[0,0,0]
	v_mfma_scale_f32_16x16x128_f8f6f4 v[64:67], v[148:155], v[40:47], v[180:183], v136, v136 op_sel_hi:[0,0,0]
	v_mov_b32_e32 v128, v132
	s_barrier
	ds_read_b128 v[16:19], v135 offset:49152
	ds_read_b128 v[20:23], v135 offset:50176
	ds_read_b128 v[156:159], v135 offset:51200
	ds_read_b128 v[160:163], v135 offset:52224
	ds_read_b128 v[164:167], v135 offset:53248
	ds_read_b128 v[168:171], v135 offset:54272
	ds_read_b128 v[172:175], v135 offset:55296
	ds_read_b128 v[176:179], v135 offset:56320
	v_lshl_add_u64 v[24:25], s[18:19], 0, v[128:129]
	v_lshl_add_u64 v[24:25], v[24:25], 0, s[4:5]
	v_mov_b32_e32 v128, v133
	v_lshl_add_u64 v[24:25], s[18:19], 0, v[128:129]
	v_lshl_add_u64 v[24:25], v[24:25], 0, s[4:5]
	s_barrier
	s_waitcnt lgkmcnt(0)
	s_waitcnt lgkmcnt(0)
	v_mfma_scale_f32_16x16x128_f8f6f4 v[60:63], v[0:7], v[16:23], v[60:63], v136, v136 op_sel_hi:[0,0,0]
	v_mfma_scale_f32_16x16x128_f8f6f4 v[56:59], v[8:15], v[16:23], v[56:59], v136, v136 op_sel_hi:[0,0,0]
	s_add_u32 s98, s18, s4
	s_addc_u32 s99, s19, s5
	s_mov_b32 m0, s35
	v_mfma_scale_f32_16x16x128_f8f6f4 v[52:55], v[0:7], v[156:163], v[52:55], v136, v136 op_sel_hi:[0,0,0]
	global_load_lds_dwordx4 v132, s[98:99]
	v_mfma_scale_f32_16x16x128_f8f6f4 v[48:51], v[8:15], v[156:163], v[48:51], v136, v136 op_sel_hi:[0,0,0]
	v_mfma_scale_f32_16x16x128_f8f6f4 v[44:47], v[0:7], v[164:171], v[184:187], v136, v136 op_sel_hi:[0,0,0]
	s_mov_b32 m0, s36
	v_mfma_scale_f32_16x16x128_f8f6f4 v[40:43], v[8:15], v[164:171], v[208:211], v136, v136 op_sel_hi:[0,0,0]
	global_load_lds_dwordx4 v133, s[98:99]
	v_mfma_scale_f32_16x16x128_f8f6f4 v[36:39], v[0:7], v[172:179], v[212:215], v136, v136 op_sel_hi:[0,0,0]
	v_mfma_scale_f32_16x16x128_f8f6f4 v[32:35], v[8:15], v[172:179], v[216:219], v136, v136 op_sel_hi:[0,0,0]
	s_barrier
	s_add_u32 s16, s16, 0x30080
	s_addc_u32 s17, s17, 0
	v_mov_b32_e32 v0, v132
	s_add_i32 s18, s44, s23
	s_nop 0
	v_mov_b32_e32 v0, v133
	s_nop 0
	s_waitcnt vmcnt(4)
	s_barrier
	v_mfma_scale_f32_16x16x128_f8f6f4 v[28:31], v[140:147], v[16:23], v[220:223], v136, v136 op_sel_hi:[0,0,0]
	v_mfma_scale_f32_16x16x128_f8f6f4 v[24:27], v[148:155], v[16:23], v[224:227], v136, v136 op_sel_hi:[0,0,0]
	s_mov_b32 m0, s18
	v_mfma_scale_f32_16x16x128_f8f6f4 v[20:23], v[140:147], v[156:163], v[228:231], v136, v136 op_sel_hi:[0,0,0]
	global_load_lds_dwordx4 v132, s[16:17]
	v_mfma_scale_f32_16x16x128_f8f6f4 v[16:19], v[148:155], v[156:163], v[232:235], v136, v136 op_sel_hi:[0,0,0]
	v_mfma_scale_f32_16x16x128_f8f6f4 v[12:15], v[140:147], v[164:171], v[236:239], v136, v136 op_sel_hi:[0,0,0]
	s_add_i32 m0, s18, 0x2000
	v_mfma_scale_f32_16x16x128_f8f6f4 v[8:11], v[148:155], v[164:171], v[240:243], v136, v136 op_sel_hi:[0,0,0]
	global_load_lds_dwordx4 v133, s[16:17]
	v_mfma_scale_f32_16x16x128_f8f6f4 v[4:7], v[140:147], v[172:179], v[244:247], v136, v136 op_sel_hi:[0,0,0]
	v_mfma_scale_f32_16x16x128_f8f6f4 v[0:3], v[148:155], v[172:179], v[248:251], v136, v136 op_sel_hi:[0,0,0]
	s_add_i32 s53, s53, 2
	s_add_u32 s14, s14, 0x100
	s_addc_u32 s15, s15, 0
	s_add_u32 s51, s51, 0x100
	s_addc_u32 s52, s52, 0
	s_cmp_gt_u32 s53, 9
	s_barrier
	s_cbranch_scc0 .LBB0_5813
